# 109 back-to-back duplicate lgkmcnt(0) waits deleted (nothing but s_setprio between the pair), on top of the DMA-rebalanced K-loops version
# speedup vs baseline: 1.0011x; 1.0011x over previous
.LBB0_21:
	ds_write_b128 v53, v[34:37]
	ds_write_b128 v53, v[30:33] offset:1024
	ds_write_b128 v53, v[26:29] offset:2048
	ds_write_b128 v53, v[22:25] offset:3072
	ds_write_b128 v53, v[18:21] offset:4096
	ds_write_b128 v53, v[14:17] offset:5120
	ds_write_b128 v53, v[10:13] offset:6144
	ds_write_b128 v53, v[6:9] offset:7168
	ds_write_b128 v53, v[2:5] offset:8192
	s_waitcnt lgkmcnt(0)
	s_barrier
	s_and_saveexec_b64 s[6:7], s[4:5]
	s_cbranch_execz .LBB0_15
	s_load_dwordx2 s[8:9], s[20:21], 0x28
	s_ashr_i32 s29, s28, 31
	s_mul_i32 s11, s46, 0xc000
	s_mul_hi_i32 s10, s46, 0xc000
	v_mov_b32_e32 v41, v0
	s_waitcnt lgkmcnt(0)
	s_add_u32 s8, s8, s11
	s_addc_u32 s9, s9, s10
	s_lshl_b64 s[10:11], s[28:29], 2
	s_add_u32 s16, s8, s10
	s_addc_u32 s17, s9, s11
	s_mul_hi_i32 s9, s46, 9
	s_mul_i32 s8, s46, 9
	v_lshl_add_u64 v[2:3], s[16:17], 0, v[40:41]
	v_lshl_add_u64 v[4:5], v[38:39], 0, s[10:11]
	s_mov_b64 s[10:11], 0
	v_mov_b32_e32 v1, v50

.LBB0_220:
	s_add_u32 s40, s10, s38
	s_addc_u32 s41, s11, s39
	s_add_u32 s42, s40, 0x49800100
	ds_read_b128 v[144:147], v154
	ds_read_b128 v[170:173], v154 offset:2048
	ds_read_b128 v[148:151], v155
	ds_read_b128 v[174:177], v155 offset:2048
	s_addc_u32 s43, s41, 0
	s_add_u32 s67, s1, s38
	s_addc_u32 s68, s56, s39
	s_cmpk_eq_i32 s38, 0x700
	s_cselect_b64 vcc, -1, 0
	s_and_b64 s[40:41], vcc, exec
	ds_read_b128 v[178:181], v152
	ds_read_b128 v[186:189], v152 offset:2048
	ds_read_b128 v[182:185], v153
	ds_read_b128 v[190:193], v153 offset:2048
	ds_read_b128 v[196:199], v152 offset:4096
	ds_read_b128 v[204:207], v152 offset:6144
	ds_read_b128 v[200:203], v153 offset:4096
	ds_read_b128 v[208:211], v153 offset:6144
	s_waitcnt vmcnt(6)
	s_waitcnt lgkmcnt(8)
	s_barrier
	s_waitcnt lgkmcnt(0)
	s_setprio 1
	v_mfma_f32_16x16x128_f8f6f4 v[124:127], v[144:151], v[178:185], v[124:127]
	v_mfma_f32_16x16x128_f8f6f4 v[120:123], v[170:177], v[178:185], v[120:123]
	v_mfma_f32_16x16x128_f8f6f4 v[108:111], v[144:151], v[186:193], v[108:111]
	v_mfma_f32_16x16x128_f8f6f4 v[104:107], v[170:177], v[186:193], v[104:107]
	v_mfma_f32_16x16x128_f8f6f4 v[92:95], v[144:151], v[196:203], v[92:95]
	v_mfma_f32_16x16x128_f8f6f4 v[88:91], v[170:177], v[196:203], v[88:91]
	v_mfma_f32_16x16x128_f8f6f4 v[76:79], v[144:151], v[204:211], v[76:79]
	v_mfma_f32_16x16x128_f8f6f4 v[72:75], v[170:177], v[204:211], v[72:75]
	s_setprio 0
	s_barrier
	ds_read_b128 v[222:225], v154 offset:16384
	ds_read_b128 v[230:233], v154 offset:18432
	ds_read_b128 v[226:229], v155 offset:16384
	ds_read_b128 v[234:237], v155 offset:18432
	v_cndmask_b32_e32 v132, v135, v165, vcc
	s_cselect_b32 s43, s13, s43
	s_cselect_b32 s42, s12, s42
	s_cselect_b32 s41, s37, s68
	s_cselect_b32 s40, s36, s67
	v_cndmask_b32_e32 v137, v136, v167, vcc
	v_lshl_add_u64 v[212:213], v[142:143], 0, s[38:39]
	s_add_i32 m0, s33, 0xc000
	s_nop 0
	global_load_lds_dwordx4 v[212:213], off
	v_lshl_add_u64 v[212:213], v[140:141], 0, s[38:39]
	s_add_i32 m0, s33, 0xe000
	v_cndmask_b32_e32 v220, v134, v166, vcc
	global_load_lds_dwordx4 v[212:213], off
	s_barrier
	s_waitcnt lgkmcnt(0)
	s_setprio 1
	v_mfma_f32_16x16x128_f8f6f4 v[116:119], v[222:229], v[178:185], v[116:119]
	v_mfma_f32_16x16x128_f8f6f4 v[112:115], v[230:237], v[178:185], v[112:115]
	v_mfma_f32_16x16x128_f8f6f4 v[100:103], v[222:229], v[186:193], v[100:103]
	v_mfma_f32_16x16x128_f8f6f4 v[96:99], v[230:237], v[186:193], v[96:99]
	v_mfma_f32_16x16x128_f8f6f4 v[84:87], v[222:229], v[196:203], v[84:87]
	v_mfma_f32_16x16x128_f8f6f4 v[80:83], v[230:237], v[196:203], v[80:83]
	v_mfma_f32_16x16x128_f8f6f4 v[68:71], v[222:229], v[204:211], v[68:71]
	v_mfma_f32_16x16x128_f8f6f4 v[64:67], v[230:237], v[204:211], v[64:67]
	s_setprio 0
	s_barrier
	s_mov_b32 m0, s33
	ds_read_b128 v[186:189], v152 offset:16384
	ds_read_b128 v[196:199], v152 offset:18432
	ds_read_b128 v[190:193], v153 offset:16384
	ds_read_b128 v[200:203], v153 offset:18432
	ds_read_b128 v[204:207], v152 offset:20480
	ds_read_b128 v[212:215], v152 offset:22528
	ds_read_b128 v[208:211], v153 offset:20480
	ds_read_b128 v[216:219], v153 offset:22528
	global_load_lds_dwordx4 v132, s[42:43]
	s_mov_b32 m0, s46
	v_mov_b32_e32 v221, v133
	global_load_lds_dwordx4 v220, s[42:43]
	s_waitcnt lgkmcnt(8)
	s_barrier
	s_waitcnt lgkmcnt(0)
	v_lshl_add_u64 v[246:247], s[42:43], 0, v[132:133]
	v_lshl_add_u64 v[244:245], s[42:43], 0, v[220:221]
	s_setprio 1
	s_waitcnt lgkmcnt(0)
	v_mfma_f32_16x16x128_f8f6f4 v[60:63], v[144:151], v[186:193], v[60:63]
	v_mfma_f32_16x16x128_f8f6f4 v[56:59], v[170:177], v[186:193], v[56:59]
	v_mfma_f32_16x16x128_f8f6f4 v[44:47], v[144:151], v[196:203], v[44:47]
	v_mfma_f32_16x16x128_f8f6f4 v[40:43], v[170:177], v[196:203], v[40:43]
	v_mfma_f32_16x16x128_f8f6f4 v[28:31], v[144:151], v[204:211], v[28:31]
	v_mfma_f32_16x16x128_f8f6f4 v[24:27], v[170:177], v[204:211], v[24:27]
	v_mfma_f32_16x16x128_f8f6f4 v[12:15], v[144:151], v[212:219], v[12:15]
	v_mfma_f32_16x16x128_f8f6f4 v[8:11], v[170:177], v[212:219], v[8:11]
	s_setprio 0
	s_barrier
	s_mov_b32 m0, s44
	v_lshl_add_u64 v[144:145], s[40:41], 0, v[128:129]
	global_load_lds_dwordx4 v[144:145], off
	v_lshl_add_u64 v[146:147], s[40:41], 0, v[130:131]
	s_mov_b32 m0, s45
	s_nop 0
	global_load_lds_dwordx4 v[146:147], off
	s_waitcnt vmcnt(8)
	s_waitcnt lgkmcnt(0)
	s_barrier
	s_setprio 1
	s_waitcnt lgkmcnt(0)
	v_mfma_f32_16x16x128_f8f6f4 v[52:55], v[222:229], v[186:193], v[52:55]
	v_mfma_f32_16x16x128_f8f6f4 v[48:51], v[230:237], v[186:193], v[48:51]
	v_mfma_f32_16x16x128_f8f6f4 v[36:39], v[222:229], v[196:203], v[36:39]
	v_mfma_f32_16x16x128_f8f6f4 v[32:35], v[230:237], v[196:203], v[32:35]
	v_mfma_f32_16x16x128_f8f6f4 v[20:23], v[222:229], v[204:211], v[20:23]
	v_mfma_f32_16x16x128_f8f6f4 v[16:19], v[230:237], v[204:211], v[16:19]
	v_mfma_f32_16x16x128_f8f6f4 v[4:7], v[222:229], v[212:219], v[4:7]
	v_mfma_f32_16x16x128_f8f6f4 v[0:3], v[230:237], v[212:219], v[0:3]
	s_setprio 0
	s_barrier
	ds_read_b128 v[170:173], v154 offset:32768
	ds_read_b128 v[178:181], v154 offset:34816
	ds_read_b128 v[174:177], v155 offset:32768
	ds_read_b128 v[182:185], v155 offset:34816
	s_mov_b32 m0, s49
	ds_read_b128 v[186:189], v152 offset:32768
	ds_read_b128 v[196:199], v152 offset:34816
	ds_read_b128 v[190:193], v153 offset:32768
	ds_read_b128 v[200:203], v153 offset:34816
	ds_read_b128 v[204:207], v152 offset:36864
	ds_read_b128 v[212:215], v152 offset:38912
	ds_read_b128 v[208:211], v153 offset:36864
	ds_read_b128 v[216:219], v153 offset:38912
	v_cndmask_b32_e32 v132, v138, v168, vcc
	global_load_lds_dwordx4 v137, s[42:43]
	s_mov_b32 m0, s50
	s_nop 0
	global_load_lds_dwordx4 v132, s[42:43]
	s_waitcnt vmcnt(8)
	s_waitcnt lgkmcnt(8)
	s_barrier
	s_waitcnt lgkmcnt(0)
	s_setprio 1
	v_mfma_f32_16x16x128_f8f6f4 v[124:127], v[170:177], v[186:193], v[124:127]
	v_mfma_f32_16x16x128_f8f6f4 v[120:123], v[178:185], v[186:193], v[120:123]
	v_mfma_f32_16x16x128_f8f6f4 v[108:111], v[170:177], v[196:203], v[108:111]
	v_mfma_f32_16x16x128_f8f6f4 v[104:107], v[178:185], v[196:203], v[104:107]
	v_mfma_f32_16x16x128_f8f6f4 v[92:95], v[170:177], v[204:211], v[92:95]
	v_mfma_f32_16x16x128_f8f6f4 v[88:91], v[178:185], v[204:211], v[88:91]
	v_mfma_f32_16x16x128_f8f6f4 v[76:79], v[170:177], v[212:219], v[76:79]
	v_mfma_f32_16x16x128_f8f6f4 v[72:75], v[178:185], v[212:219], v[72:75]
	s_setprio 0
	s_barrier
	ds_read_b128 v[222:225], v154 offset:49152
	ds_read_b128 v[230:233], v154 offset:51200
	ds_read_b128 v[226:229], v155 offset:49152
	ds_read_b128 v[234:237], v155 offset:51200
	s_add_u32 s42, s40, 0x4000
	s_addc_u32 s43, s41, 0
	v_lshl_add_u64 v[220:221], s[42:43], 0, v[128:129]
	s_mov_b32 m0, s47
	s_nop 0
	global_load_lds_dwordx4 v[220:221], off
	v_lshl_add_u64 v[220:221], s[42:43], 0, v[130:131]
	s_mov_b32 m0, s48
	s_nop 0
	global_load_lds_dwordx4 v[220:221], off
	s_waitcnt vmcnt(8)
	s_barrier
	s_waitcnt lgkmcnt(0)
	s_setprio 1
	v_mfma_f32_16x16x128_f8f6f4 v[116:119], v[222:229], v[186:193], v[116:119]
	v_mfma_f32_16x16x128_f8f6f4 v[112:115], v[230:237], v[186:193], v[112:115]
	v_mfma_f32_16x16x128_f8f6f4 v[100:103], v[222:229], v[196:203], v[100:103]
	v_mfma_f32_16x16x128_f8f6f4 v[96:99], v[230:237], v[196:203], v[96:99]
	v_mfma_f32_16x16x128_f8f6f4 v[84:87], v[222:229], v[204:211], v[84:87]
	v_mfma_f32_16x16x128_f8f6f4 v[80:83], v[230:237], v[204:211], v[80:83]
	v_mfma_f32_16x16x128_f8f6f4 v[68:71], v[222:229], v[212:219], v[68:71]
	v_mfma_f32_16x16x128_f8f6f4 v[64:67], v[230:237], v[212:219], v[64:67]
	s_setprio 0
	s_barrier
	s_mov_b32 m0, s54
	v_lshl_add_u64 v[246:247], v[246:247], 0, s[24:25]
	ds_read_b128 v[186:189], v152 offset:49152
	ds_read_b128 v[196:199], v152 offset:51200
	ds_read_b128 v[190:193], v153 offset:49152
	ds_read_b128 v[200:203], v153 offset:51200
	ds_read_b128 v[204:207], v152 offset:53248
	ds_read_b128 v[212:215], v152 offset:55296
	ds_read_b128 v[208:211], v153 offset:53248
	ds_read_b128 v[216:219], v153 offset:55296
	global_load_lds_dwordx4 v[246:247], off
	v_lshl_add_u64 v[244:245], v[244:245], 0, s[24:25]
	s_mov_b32 m0, s55
	s_nop 0
	global_load_lds_dwordx4 v[244:245], off
	s_waitcnt lgkmcnt(8)
	s_barrier
	s_waitcnt lgkmcnt(0)
	s_setprio 1
	v_mfma_f32_16x16x128_f8f6f4 v[60:63], v[170:177], v[186:193], v[60:63]
	v_mfma_f32_16x16x128_f8f6f4 v[56:59], v[178:185], v[186:193], v[56:59]
	v_mfma_f32_16x16x128_f8f6f4 v[44:47], v[170:177], v[196:203], v[44:47]
	v_mfma_f32_16x16x128_f8f6f4 v[40:43], v[178:185], v[196:203], v[40:43]
	v_mfma_f32_16x16x128_f8f6f4 v[28:31], v[170:177], v[204:211], v[28:31]
	v_mfma_f32_16x16x128_f8f6f4 v[24:27], v[178:185], v[204:211], v[24:27]
	v_mfma_f32_16x16x128_f8f6f4 v[12:15], v[170:177], v[212:219], v[12:15]
	v_mfma_f32_16x16x128_f8f6f4 v[8:11], v[178:185], v[212:219], v[8:11]
	s_setprio 0
	s_barrier
	s_mov_b32 m0, s52
	v_lshl_add_u64 v[144:145], v[144:145], 0, s[24:25]
	global_load_lds_dwordx4 v[144:145], off
	v_lshl_add_u64 v[144:145], v[146:147], 0, s[24:25]
	s_mov_b32 m0, s53
	s_nop 0
	global_load_lds_dwordx4 v[144:145], off
	s_waitcnt vmcnt(8)
	s_waitcnt lgkmcnt(0)
	s_barrier
	s_setprio 1
	s_waitcnt lgkmcnt(0)
	v_mfma_f32_16x16x128_f8f6f4 v[52:55], v[222:229], v[186:193], v[52:55]
	v_mfma_f32_16x16x128_f8f6f4 v[48:51], v[230:237], v[186:193], v[48:51]
	v_mfma_f32_16x16x128_f8f6f4 v[36:39], v[222:229], v[196:203], v[36:39]
	v_mfma_f32_16x16x128_f8f6f4 v[32:35], v[230:237], v[196:203], v[32:35]
	v_mfma_f32_16x16x128_f8f6f4 v[20:23], v[222:229], v[204:211], v[20:23]
	v_mfma_f32_16x16x128_f8f6f4 v[16:19], v[230:237], v[204:211], v[16:19]
	v_mfma_f32_16x16x128_f8f6f4 v[4:7], v[222:229], v[212:219], v[4:7]
	v_mfma_f32_16x16x128_f8f6f4 v[0:3], v[230:237], v[212:219], v[0:3]
	s_setprio 0
	s_barrier
	s_add_u32 s40, s40, 0x4080
	s_addc_u32 s41, s41, 0
	s_mov_b32 m0, s58
	v_lshl_add_u64 v[144:145], s[40:41], 0, v[128:129]
	global_load_lds_dwordx4 v[144:145], off
	v_lshl_add_u64 v[144:145], s[40:41], 0, v[130:131]
	s_mov_b32 m0, s59
	s_add_i32 s57, s57, 2
	global_load_lds_dwordx4 v[144:145], off
	s_add_u32 s38, s38, 0x100
	s_addc_u32 s39, s39, 0
	s_cmp_gt_u32 s57, 13
	s_cbranch_scc0 .LBB0_220
	s_and_b64 vcc, exec, s[28:29]
	s_cbranch_vccz .LBB0_223
	s_barrier

.LBB0_313:
	s_add_u32 s36, s6, s34
	s_addc_u32 s37, s7, s35
	s_add_u32 s38, s36, 0x4e000100
	ds_read_b128 v[158:161], v167
	ds_read_b128 v[172:175], v167 offset:2048
	ds_read_b128 v[162:165], v168
	ds_read_b128 v[176:179], v168 offset:2048
	s_addc_u32 s39, s37, 0
	s_add_u32 s70, s67, s34
	s_addc_u32 s71, s68, s35
	s_cmpk_eq_i32 s34, 0x200
	s_cselect_b64 vcc, -1, 0
	s_and_b64 s[36:37], vcc, exec
	ds_read_b128 v[180:183], v129
	ds_read_b128 v[196:199], v129 offset:2048
	ds_read_b128 v[184:187], v131
	ds_read_b128 v[200:203], v131 offset:2048
	ds_read_b128 v[204:207], v129 offset:4096
	ds_read_b128 v[212:215], v129 offset:6144
	ds_read_b128 v[208:211], v131 offset:4096
	ds_read_b128 v[216:219], v131 offset:6144
	s_waitcnt vmcnt(6)
	s_waitcnt lgkmcnt(8)
	s_barrier
	s_waitcnt lgkmcnt(0)
	v_cndmask_b32_e32 v188, v148, v140, vcc
	s_setprio 1
	s_waitcnt lgkmcnt(0)
	v_mfma_f32_16x16x128_f8f6f4 v[124:127], v[158:165], v[180:187], v[124:127]
	v_mfma_f32_16x16x128_f8f6f4 v[120:123], v[172:179], v[180:187], v[120:123]
	v_mfma_f32_16x16x128_f8f6f4 v[112:115], v[158:165], v[196:203], v[112:115]
	v_mfma_f32_16x16x128_f8f6f4 v[104:107], v[172:179], v[196:203], v[104:107]
	v_mfma_f32_16x16x128_f8f6f4 v[96:99], v[158:165], v[204:211], v[96:99]
	v_mfma_f32_16x16x128_f8f6f4 v[88:91], v[172:179], v[204:211], v[88:91]
	v_mfma_f32_16x16x128_f8f6f4 v[80:83], v[158:165], v[212:219], v[80:83]
	v_mfma_f32_16x16x128_f8f6f4 v[72:75], v[172:179], v[212:219], v[72:75]
	s_setprio 0
	s_barrier
	ds_read_b128 v[228:231], v167 offset:16384
	ds_read_b128 v[236:239], v167 offset:18432
	ds_read_b128 v[232:235], v168 offset:16384
	ds_read_b128 v[240:243], v168 offset:18432
	v_cndmask_b32_e32 v136, v146, v138, vcc
	s_cselect_b32 s39, s9, s39
	s_cselect_b32 s38, s8, s38
	s_cselect_b32 s37, s31, s71
	s_cselect_b32 s36, s30, s70
	v_cndmask_b32_e32 v139, v150, v142, vcc
	v_lshl_add_u64 v[252:253], v[156:157], 0, s[34:35]
	s_add_i32 m0, s46, 0xc000
	s_nop 0
	global_load_lds_dwordx4 v[252:253], off
	v_lshl_add_u64 v[252:253], v[154:155], 0, s[34:35]
	s_add_i32 m0, s46, 0xe000
	s_nop 0
	global_load_lds_dwordx4 v[252:253], off
	s_barrier
	s_waitcnt lgkmcnt(0)
	s_setprio 1
	v_mfma_f32_16x16x128_f8f6f4 v[116:119], v[228:235], v[180:187], v[116:119]
	v_mfma_f32_16x16x128_f8f6f4 v[108:111], v[236:243], v[180:187], v[108:111]
	v_mfma_f32_16x16x128_f8f6f4 v[100:103], v[228:235], v[196:203], v[100:103]
	v_mfma_f32_16x16x128_f8f6f4 v[92:95], v[236:243], v[196:203], v[92:95]
	v_mfma_f32_16x16x128_f8f6f4 v[84:87], v[228:235], v[204:211], v[84:87]
	v_mfma_f32_16x16x128_f8f6f4 v[76:79], v[236:243], v[204:211], v[76:79]
	v_mfma_f32_16x16x128_f8f6f4 v[68:71], v[228:235], v[212:219], v[68:71]
	v_mfma_f32_16x16x128_f8f6f4 v[64:67], v[236:243], v[212:219], v[64:67]
	s_setprio 0
	s_barrier
	s_mov_b32 m0, s46
	ds_read_b128 v[196:199], v129 offset:16384
	ds_read_b128 v[204:207], v129 offset:18432
	ds_read_b128 v[200:203], v131 offset:16384
	ds_read_b128 v[208:211], v131 offset:18432
	ds_read_b128 v[212:215], v129 offset:20480
	ds_read_b128 v[220:223], v129 offset:22528
	ds_read_b128 v[216:219], v131 offset:20480
	ds_read_b128 v[224:227], v131 offset:22528
	global_load_lds_dwordx4 v136, s[38:39]
	s_mov_b32 m0, s49
	v_mov_b32_e32 v189, v137
	global_load_lds_dwordx4 v188, s[38:39]
	s_waitcnt lgkmcnt(8)
	s_barrier
	s_waitcnt lgkmcnt(0)
	v_lshl_add_u64 v[246:247], s[38:39], 0, v[136:137]
	v_lshl_add_u64 v[244:245], s[38:39], 0, v[188:189]
	s_setprio 1
	s_waitcnt lgkmcnt(0)
	v_mfma_f32_16x16x128_f8f6f4 v[60:63], v[158:165], v[196:203], v[60:63]
	v_mfma_f32_16x16x128_f8f6f4 v[56:59], v[172:179], v[196:203], v[56:59]
	v_mfma_f32_16x16x128_f8f6f4 v[48:51], v[158:165], v[204:211], v[48:51]
	v_mfma_f32_16x16x128_f8f6f4 v[40:43], v[172:179], v[204:211], v[40:43]
	v_mfma_f32_16x16x128_f8f6f4 v[32:35], v[158:165], v[212:219], v[32:35]
	v_mfma_f32_16x16x128_f8f6f4 v[24:27], v[172:179], v[212:219], v[24:27]
	v_mfma_f32_16x16x128_f8f6f4 v[16:19], v[158:165], v[220:227], v[16:19]
	v_mfma_f32_16x16x128_f8f6f4 v[8:11], v[172:179], v[220:227], v[8:11]
	s_setprio 0
	s_barrier
	s_mov_b32 m0, s47
	v_lshl_add_u64 v[158:159], s[36:37], 0, v[134:135]
	global_load_lds_dwordx4 v[158:159], off
	v_lshl_add_u64 v[160:161], s[36:37], 0, v[132:133]
	s_mov_b32 m0, s48
	s_nop 0
	global_load_lds_dwordx4 v[160:161], off
	s_waitcnt vmcnt(8)
	s_waitcnt lgkmcnt(0)
	s_barrier
	s_setprio 1
	s_waitcnt lgkmcnt(0)
	v_mfma_f32_16x16x128_f8f6f4 v[52:55], v[228:235], v[196:203], v[52:55]
	v_mfma_f32_16x16x128_f8f6f4 v[44:47], v[236:243], v[196:203], v[44:47]
	v_mfma_f32_16x16x128_f8f6f4 v[36:39], v[228:235], v[204:211], v[36:39]
	v_mfma_f32_16x16x128_f8f6f4 v[28:31], v[236:243], v[204:211], v[28:31]
	v_mfma_f32_16x16x128_f8f6f4 v[20:23], v[228:235], v[212:219], v[20:23]
	v_mfma_f32_16x16x128_f8f6f4 v[12:15], v[236:243], v[212:219], v[12:15]
	v_mfma_f32_16x16x128_f8f6f4 v[4:7], v[228:235], v[220:227], v[4:7]
	v_mfma_f32_16x16x128_f8f6f4 v[0:3], v[236:243], v[220:227], v[0:3]
	s_setprio 0
	s_barrier
	ds_read_b128 v[172:175], v167 offset:32768
	ds_read_b128 v[180:183], v167 offset:34816
	ds_read_b128 v[176:179], v168 offset:32768
	ds_read_b128 v[184:187], v168 offset:34816
	s_mov_b32 m0, s52
	ds_read_b128 v[196:199], v129 offset:32768
	ds_read_b128 v[204:207], v129 offset:34816
	ds_read_b128 v[200:203], v131 offset:32768
	ds_read_b128 v[208:211], v131 offset:34816
	ds_read_b128 v[212:215], v129 offset:36864
	ds_read_b128 v[220:223], v129 offset:38912
	ds_read_b128 v[216:219], v131 offset:36864
	ds_read_b128 v[224:227], v131 offset:38912
	v_cndmask_b32_e32 v136, v152, v144, vcc
	global_load_lds_dwordx4 v139, s[38:39]
	s_mov_b32 m0, s53
	s_nop 0
	global_load_lds_dwordx4 v136, s[38:39]
	s_waitcnt vmcnt(8)
	s_waitcnt lgkmcnt(8)
	s_barrier
	s_waitcnt lgkmcnt(0)
	s_setprio 1
	v_mfma_f32_16x16x128_f8f6f4 v[124:127], v[172:179], v[196:203], v[124:127]
	v_mfma_f32_16x16x128_f8f6f4 v[120:123], v[180:187], v[196:203], v[120:123]
	v_mfma_f32_16x16x128_f8f6f4 v[112:115], v[172:179], v[204:211], v[112:115]
	v_mfma_f32_16x16x128_f8f6f4 v[104:107], v[180:187], v[204:211], v[104:107]
	v_mfma_f32_16x16x128_f8f6f4 v[96:99], v[172:179], v[212:219], v[96:99]
	v_mfma_f32_16x16x128_f8f6f4 v[88:91], v[180:187], v[212:219], v[88:91]
	v_mfma_f32_16x16x128_f8f6f4 v[80:83], v[172:179], v[220:227], v[80:83]
	v_mfma_f32_16x16x128_f8f6f4 v[72:75], v[180:187], v[220:227], v[72:75]
	s_setprio 0
	s_barrier
	ds_read_b128 v[228:231], v167 offset:49152
	ds_read_b128 v[236:239], v167 offset:51200
	ds_read_b128 v[232:235], v168 offset:49152
	ds_read_b128 v[240:243], v168 offset:51200
	s_add_u32 s38, s36, 0x1800
	s_addc_u32 s39, s37, 0
	v_lshl_add_u64 v[188:189], s[38:39], 0, v[134:135]
	s_mov_b32 m0, s50
	s_nop 0
	global_load_lds_dwordx4 v[188:189], off
	v_lshl_add_u64 v[188:189], s[38:39], 0, v[132:133]
	s_mov_b32 m0, s51
	s_nop 0
	global_load_lds_dwordx4 v[188:189], off
	s_waitcnt vmcnt(8)
	s_barrier
	s_waitcnt lgkmcnt(0)
	s_setprio 1
	v_mfma_f32_16x16x128_f8f6f4 v[116:119], v[228:235], v[196:203], v[116:119]
	v_mfma_f32_16x16x128_f8f6f4 v[108:111], v[236:243], v[196:203], v[108:111]
	v_mfma_f32_16x16x128_f8f6f4 v[100:103], v[228:235], v[204:211], v[100:103]
	v_mfma_f32_16x16x128_f8f6f4 v[92:95], v[236:243], v[204:211], v[92:95]
	v_mfma_f32_16x16x128_f8f6f4 v[84:87], v[228:235], v[212:219], v[84:87]
	v_mfma_f32_16x16x128_f8f6f4 v[76:79], v[236:243], v[212:219], v[76:79]
	v_mfma_f32_16x16x128_f8f6f4 v[68:71], v[228:235], v[220:227], v[68:71]
	v_mfma_f32_16x16x128_f8f6f4 v[64:67], v[236:243], v[220:227], v[64:67]
	s_setprio 0
	s_barrier
	s_mov_b32 m0, s56
	v_lshl_add_u64 v[246:247], v[246:247], 0, s[18:19]
	ds_read_b128 v[196:199], v129 offset:49152
	ds_read_b128 v[204:207], v129 offset:51200
	ds_read_b128 v[200:203], v131 offset:49152
	ds_read_b128 v[208:211], v131 offset:51200
	ds_read_b128 v[212:215], v129 offset:53248
	ds_read_b128 v[220:223], v129 offset:55296
	ds_read_b128 v[216:219], v131 offset:53248
	ds_read_b128 v[224:227], v131 offset:55296
	global_load_lds_dwordx4 v[246:247], off
	v_lshl_add_u64 v[244:245], v[244:245], 0, s[18:19]
	s_mov_b32 m0, s57
	s_nop 0
	global_load_lds_dwordx4 v[244:245], off
	s_waitcnt lgkmcnt(8)
	s_barrier
	s_waitcnt lgkmcnt(0)
	s_setprio 1
	v_mfma_f32_16x16x128_f8f6f4 v[60:63], v[172:179], v[196:203], v[60:63]
	v_mfma_f32_16x16x128_f8f6f4 v[56:59], v[180:187], v[196:203], v[56:59]
	v_mfma_f32_16x16x128_f8f6f4 v[48:51], v[172:179], v[204:211], v[48:51]
	v_mfma_f32_16x16x128_f8f6f4 v[40:43], v[180:187], v[204:211], v[40:43]
	v_mfma_f32_16x16x128_f8f6f4 v[32:35], v[172:179], v[212:219], v[32:35]
	v_mfma_f32_16x16x128_f8f6f4 v[24:27], v[180:187], v[212:219], v[24:27]
	v_mfma_f32_16x16x128_f8f6f4 v[16:19], v[172:179], v[220:227], v[16:19]
	v_mfma_f32_16x16x128_f8f6f4 v[8:11], v[180:187], v[220:227], v[8:11]
	s_setprio 0
	s_barrier
	s_mov_b32 m0, s54
	v_lshl_add_u64 v[158:159], v[158:159], 0, s[18:19]
	global_load_lds_dwordx4 v[158:159], off
	v_lshl_add_u64 v[158:159], v[160:161], 0, s[18:19]
	s_mov_b32 m0, s55
	s_nop 0
	global_load_lds_dwordx4 v[158:159], off
	s_waitcnt vmcnt(8)
	s_waitcnt lgkmcnt(0)
	s_barrier
	s_setprio 1
	s_waitcnt lgkmcnt(0)
	v_mfma_f32_16x16x128_f8f6f4 v[52:55], v[228:235], v[196:203], v[52:55]
	v_mfma_f32_16x16x128_f8f6f4 v[44:47], v[236:243], v[196:203], v[44:47]
	v_mfma_f32_16x16x128_f8f6f4 v[36:39], v[228:235], v[204:211], v[36:39]
	v_mfma_f32_16x16x128_f8f6f4 v[28:31], v[236:243], v[204:211], v[28:31]
	v_mfma_f32_16x16x128_f8f6f4 v[20:23], v[228:235], v[212:219], v[20:23]
	v_mfma_f32_16x16x128_f8f6f4 v[12:15], v[236:243], v[212:219], v[12:15]
	v_mfma_f32_16x16x128_f8f6f4 v[4:7], v[228:235], v[220:227], v[4:7]
	v_mfma_f32_16x16x128_f8f6f4 v[0:3], v[236:243], v[220:227], v[0:3]
	s_setprio 0
	s_barrier
	s_add_u32 s36, s36, 0x1880
	s_addc_u32 s37, s37, 0
	s_mov_b32 m0, s58
	v_lshl_add_u64 v[158:159], s[36:37], 0, v[134:135]
	global_load_lds_dwordx4 v[158:159], off
	v_lshl_add_u64 v[158:159], s[36:37], 0, v[132:133]
	s_mov_b32 m0, s59
	s_add_i32 s69, s69, 2
	global_load_lds_dwordx4 v[158:159], off
	s_add_u32 s34, s34, 0x100
	s_addc_u32 s35, s35, 0
	s_cmp_gt_u32 s69, 3
	s_cbranch_scc0 .LBB0_313
	s_and_b64 vcc, exec, s[24:25]
	s_cbranch_vccz .LBB0_316
	s_barrier

.LBB0_334:
	v_mov_b32_e32 v161, v137
	v_mov_b32_e32 v163, v137
	s_mov_b64 s[44:45], 0
	s_mov_b64 s[10:11], -1
	s_mov_b64 s[42:43], 0
	s_add_u32 s52, s14, s44
	s_addc_u32 s53, s15, s45
	s_add_u32 s46, s52, 0x100
	s_addc_u32 s47, s53, 0
	s_and_b64 s[0:1], s[42:43], exec
	s_cselect_b32 s46, s14, s46
	s_cselect_b32 s47, s15, s47
	s_add_u32 s0, s40, s44
	s_addc_u32 s1, s41, s45
	s_add_u32 s44, s0, 0x100
	s_addc_u32 s45, s1, 0
	ds_read_b128 v[196:199], v170
	ds_read_b128 v[204:207], v170 offset:2048
	ds_read_b128 v[200:203], v171
	ds_read_b128 v[208:211], v171 offset:2048
	s_and_b64 s[0:1], s[42:43], exec
	s_cselect_b32 s51, s37, s45
	s_cselect_b32 s50, s36, s44
	s_waitcnt lgkmcnt(0)
	ds_read_b128 v[212:215], v129
	ds_read_b128 v[220:223], v129 offset:2048
	ds_read_b128 v[216:219], v133
	ds_read_b128 v[224:227], v133 offset:2048
	ds_read_b128 v[228:231], v129 offset:4096
	ds_read_b128 v[236:239], v129 offset:6144
	ds_read_b128 v[232:235], v133 offset:4096
	ds_read_b128 v[240:243], v133 offset:6144
	s_waitcnt vmcnt(6)
	s_waitcnt lgkmcnt(8)
	s_barrier
	s_waitcnt lgkmcnt(0)
	v_cndmask_b32_e64 v164, v158, v150, s[42:43]
	s_setprio 1
	s_waitcnt lgkmcnt(0)
	v_mfma_f32_16x16x128_f8f6f4 v[124:127], v[196:203], v[212:219], 0
	v_mfma_f32_16x16x128_f8f6f4 v[120:123], v[204:211], v[212:219], 0
	v_mfma_f32_16x16x128_f8f6f4 v[108:111], v[196:203], v[220:227], 0
	v_mfma_f32_16x16x128_f8f6f4 v[104:107], v[204:211], v[220:227], 0
	v_mfma_f32_16x16x128_f8f6f4 v[92:95], v[196:203], v[228:235], 0
	v_mfma_f32_16x16x128_f8f6f4 v[88:91], v[204:211], v[228:235], 0
	v_mfma_f32_16x16x128_f8f6f4 v[76:79], v[196:203], v[236:243], 0
	v_mfma_f32_16x16x128_f8f6f4 v[72:75], v[204:211], v[236:243], 0
	s_setprio 0
	s_barrier
	ds_read_b128 v[196:199], v170 offset:16384
	ds_read_b128 v[204:207], v170 offset:18432
	ds_read_b128 v[200:203], v171 offset:16384
	ds_read_b128 v[208:211], v171 offset:18432
	s_add_i32 m0, s58, 0xc000
	s_add_i32 s0, s58, 0xe000
	s_add_u32 s48, s50, 0x1000
	s_addc_u32 s49, s51, 0
	s_add_u32 s44, s50, 0x1080
	s_addc_u32 s45, s51, 0
	v_cndmask_b32_e64 v136, v156, v148, s[42:43]
	v_cndmask_b32_e64 v149, v160, v152, s[42:43]
	v_lshl_add_u64 v[252:253], s[52:53], 0, v[160:161]
	v_lshl_add_u64 v[252:253], v[252:253], 0, s[26:27]
	global_load_lds_dwordx4 v[252:253], off
	v_lshl_add_u64 v[252:253], s[52:53], 0, v[162:163]
	v_lshl_add_u64 v[252:253], v[252:253], 0, s[26:27]
	s_mov_b32 m0, s0
	s_nop 0
	global_load_lds_dwordx4 v[252:253], off
	s_barrier
	s_waitcnt lgkmcnt(0)
	s_setprio 1
	v_mfma_f32_16x16x128_f8f6f4 v[116:119], v[196:203], v[212:219], 0
	v_mfma_f32_16x16x128_f8f6f4 v[112:115], v[204:211], v[212:219], 0
	v_mfma_f32_16x16x128_f8f6f4 v[100:103], v[196:203], v[220:227], 0
	v_mfma_f32_16x16x128_f8f6f4 v[96:99], v[204:211], v[220:227], 0
	v_mfma_f32_16x16x128_f8f6f4 v[84:87], v[196:203], v[228:235], 0
	v_mfma_f32_16x16x128_f8f6f4 v[80:83], v[204:211], v[228:235], 0
	v_mfma_f32_16x16x128_f8f6f4 v[68:71], v[196:203], v[236:243], 0
	v_mfma_f32_16x16x128_f8f6f4 v[64:67], v[204:211], v[236:243], 0
	s_setprio 0
	s_barrier
	ds_read_b128 v[196:199], v170
	ds_read_b128 v[204:207], v170 offset:2048
	ds_read_b128 v[200:203], v171
	ds_read_b128 v[208:211], v171 offset:2048
	s_mov_b32 m0, s58
	ds_read_b128 v[212:215], v129 offset:16384
	ds_read_b128 v[220:223], v129 offset:18432
	ds_read_b128 v[216:219], v133 offset:16384
	ds_read_b128 v[224:227], v133 offset:18432
	ds_read_b128 v[228:231], v129 offset:20480
	ds_read_b128 v[236:239], v129 offset:22528
	ds_read_b128 v[232:235], v133 offset:20480
	ds_read_b128 v[240:243], v133 offset:22528
	global_load_lds_dwordx4 v136, s[46:47]
	s_mov_b32 m0, s61
	v_mov_b32_e32 v165, v137
	global_load_lds_dwordx4 v164, s[46:47]
	s_waitcnt lgkmcnt(8)
	s_barrier
	s_waitcnt lgkmcnt(0)
	v_lshl_add_u64 v[168:169], s[46:47], 0, v[136:137]
	v_lshl_add_u64 v[190:191], s[46:47], 0, v[164:165]
	s_setprio 1
	s_waitcnt lgkmcnt(0)
	v_mfma_f32_16x16x128_f8f6f4 v[60:63], v[196:203], v[212:219], 0
	v_mfma_f32_16x16x128_f8f6f4 v[56:59], v[204:211], v[212:219], 0
	v_mfma_f32_16x16x128_f8f6f4 v[44:47], v[196:203], v[220:227], 0
	v_mfma_f32_16x16x128_f8f6f4 v[40:43], v[204:211], v[220:227], 0
	v_mfma_f32_16x16x128_f8f6f4 v[28:31], v[196:203], v[228:235], 0
	v_mfma_f32_16x16x128_f8f6f4 v[24:27], v[204:211], v[228:235], 0
	v_mfma_f32_16x16x128_f8f6f4 v[12:15], v[196:203], v[236:243], 0
	v_mfma_f32_16x16x128_f8f6f4 v[8:11], v[204:211], v[236:243], 0
	s_setprio 0
	s_barrier
	s_mov_b32 m0, s59
	v_lshl_add_u64 v[164:165], s[50:51], 0, v[130:131]
	ds_read_b128 v[196:199], v170 offset:16384
	ds_read_b128 v[204:207], v170 offset:18432
	ds_read_b128 v[200:203], v171 offset:16384
	ds_read_b128 v[208:211], v171 offset:18432
	global_load_lds_dwordx4 v[164:165], off
	v_lshl_add_u64 v[166:167], s[50:51], 0, v[134:135]
	s_mov_b32 m0, s60
	s_nop 0
	global_load_lds_dwordx4 v[166:167], off
	s_waitcnt vmcnt(8)
	s_waitcnt lgkmcnt(0)
	s_barrier
	s_setprio 1
	s_waitcnt lgkmcnt(0)
	v_mfma_f32_16x16x128_f8f6f4 v[52:55], v[196:203], v[212:219], 0
	v_mfma_f32_16x16x128_f8f6f4 v[48:51], v[204:211], v[212:219], 0
	v_mfma_f32_16x16x128_f8f6f4 v[36:39], v[196:203], v[220:227], 0
	v_mfma_f32_16x16x128_f8f6f4 v[32:35], v[204:211], v[220:227], 0
	v_mfma_f32_16x16x128_f8f6f4 v[20:23], v[196:203], v[228:235], 0
	v_mfma_f32_16x16x128_f8f6f4 v[16:19], v[204:211], v[228:235], 0
	v_mfma_f32_16x16x128_f8f6f4 v[4:7], v[196:203], v[236:243], 0
	v_mfma_f32_16x16x128_f8f6f4 v[0:3], v[204:211], v[236:243], 0
	s_setprio 0
	s_barrier
	ds_read_b128 v[196:199], v170 offset:32768
	ds_read_b128 v[204:207], v170 offset:34816
	ds_read_b128 v[200:203], v171 offset:32768
	ds_read_b128 v[208:211], v171 offset:34816
	s_mov_b32 m0, s64
	ds_read_b128 v[212:215], v129 offset:32768
	ds_read_b128 v[220:223], v129 offset:34816
	ds_read_b128 v[216:219], v133 offset:32768
	ds_read_b128 v[224:227], v133 offset:34816
	ds_read_b128 v[228:231], v129 offset:36864
	ds_read_b128 v[236:239], v129 offset:38912
	ds_read_b128 v[232:235], v133 offset:36864
	ds_read_b128 v[240:243], v133 offset:38912
	v_cndmask_b32_e64 v136, v162, v154, s[42:43]
	global_load_lds_dwordx4 v149, s[46:47]
	s_mov_b32 m0, s65
	s_nop 0
	global_load_lds_dwordx4 v136, s[46:47]
	s_waitcnt vmcnt(8)
	s_waitcnt lgkmcnt(8)
	s_barrier
	s_waitcnt lgkmcnt(0)
	s_setprio 1
	v_mfma_f32_16x16x128_f8f6f4 v[124:127], v[196:203], v[212:219], v[124:127]
	v_mfma_f32_16x16x128_f8f6f4 v[120:123], v[204:211], v[212:219], v[120:123]
	v_mfma_f32_16x16x128_f8f6f4 v[108:111], v[196:203], v[220:227], v[108:111]
	v_mfma_f32_16x16x128_f8f6f4 v[104:107], v[204:211], v[220:227], v[104:107]
	v_mfma_f32_16x16x128_f8f6f4 v[92:95], v[196:203], v[228:235], v[92:95]
	v_mfma_f32_16x16x128_f8f6f4 v[88:91], v[204:211], v[228:235], v[88:91]
	v_mfma_f32_16x16x128_f8f6f4 v[76:79], v[196:203], v[236:243], v[76:79]
	v_mfma_f32_16x16x128_f8f6f4 v[72:75], v[204:211], v[236:243], v[72:75]
	s_setprio 0
	s_barrier
	ds_read_b128 v[196:199], v170 offset:49152
	ds_read_b128 v[204:207], v170 offset:51200
	ds_read_b128 v[200:203], v171 offset:49152
	ds_read_b128 v[208:211], v171 offset:51200
	v_lshl_add_u64 v[192:193], s[48:49], 0, v[130:131]
	s_mov_b32 m0, s62
	s_nop 0
	global_load_lds_dwordx4 v[192:193], off
	v_lshl_add_u64 v[192:193], s[48:49], 0, v[134:135]
	s_mov_b32 m0, s63
	s_nop 0
	global_load_lds_dwordx4 v[192:193], off
	s_waitcnt vmcnt(8)
	s_barrier
	s_waitcnt lgkmcnt(0)
	s_setprio 1
	v_mfma_f32_16x16x128_f8f6f4 v[116:119], v[196:203], v[212:219], v[116:119]
	v_mfma_f32_16x16x128_f8f6f4 v[112:115], v[204:211], v[212:219], v[112:115]
	v_mfma_f32_16x16x128_f8f6f4 v[100:103], v[196:203], v[220:227], v[100:103]
	v_mfma_f32_16x16x128_f8f6f4 v[96:99], v[204:211], v[220:227], v[96:99]
	v_mfma_f32_16x16x128_f8f6f4 v[84:87], v[196:203], v[228:235], v[84:87]
	v_mfma_f32_16x16x128_f8f6f4 v[80:83], v[204:211], v[228:235], v[80:83]
	v_mfma_f32_16x16x128_f8f6f4 v[68:71], v[196:203], v[236:243], v[68:71]
	v_mfma_f32_16x16x128_f8f6f4 v[64:67], v[204:211], v[236:243], v[64:67]
	s_setprio 0
	s_barrier
	ds_read_b128 v[196:199], v170 offset:32768
	ds_read_b128 v[204:207], v170 offset:34816
	ds_read_b128 v[200:203], v171 offset:32768
	ds_read_b128 v[208:211], v171 offset:34816
	s_mov_b32 m0, s69
	v_lshl_add_u64 v[168:169], v[168:169], 0, s[26:27]
	ds_read_b128 v[212:215], v129 offset:49152
	ds_read_b128 v[220:223], v129 offset:51200
	ds_read_b128 v[216:219], v133 offset:49152
	ds_read_b128 v[224:227], v133 offset:51200
	ds_read_b128 v[228:231], v129 offset:53248
	ds_read_b128 v[236:239], v129 offset:55296
	ds_read_b128 v[232:235], v133 offset:53248
	ds_read_b128 v[240:243], v133 offset:55296
	global_load_lds_dwordx4 v[168:169], off
	v_lshl_add_u64 v[168:169], v[190:191], 0, s[26:27]
	s_mov_b32 m0, s70
	s_nop 0
	global_load_lds_dwordx4 v[168:169], off
	s_waitcnt lgkmcnt(8)
	s_barrier
	s_waitcnt lgkmcnt(0)
	s_setprio 1
	v_mfma_f32_16x16x128_f8f6f4 v[60:63], v[196:203], v[212:219], v[60:63]
	v_mfma_f32_16x16x128_f8f6f4 v[56:59], v[204:211], v[212:219], v[56:59]
	v_mfma_f32_16x16x128_f8f6f4 v[44:47], v[196:203], v[220:227], v[44:47]
	v_mfma_f32_16x16x128_f8f6f4 v[40:43], v[204:211], v[220:227], v[40:43]
	v_mfma_f32_16x16x128_f8f6f4 v[28:31], v[196:203], v[228:235], v[28:31]
	v_mfma_f32_16x16x128_f8f6f4 v[24:27], v[204:211], v[228:235], v[24:27]
	v_mfma_f32_16x16x128_f8f6f4 v[12:15], v[196:203], v[236:243], v[12:15]
	v_mfma_f32_16x16x128_f8f6f4 v[8:11], v[204:211], v[236:243], v[8:11]
	s_setprio 0
	s_barrier
	s_mov_b32 m0, s67
	v_lshl_add_u64 v[164:165], v[164:165], 0, s[26:27]
	ds_read_b128 v[196:199], v170 offset:49152
	ds_read_b128 v[204:207], v170 offset:51200
	ds_read_b128 v[200:203], v171 offset:49152
	ds_read_b128 v[208:211], v171 offset:51200
	global_load_lds_dwordx4 v[164:165], off
	v_lshl_add_u64 v[164:165], v[166:167], 0, s[26:27]
	s_mov_b32 m0, s68
	s_nop 0
	global_load_lds_dwordx4 v[164:165], off
	s_waitcnt vmcnt(8)
	s_waitcnt lgkmcnt(0)
	s_barrier
	s_setprio 1
	s_waitcnt lgkmcnt(0)
	v_mfma_f32_16x16x128_f8f6f4 v[52:55], v[196:203], v[212:219], v[52:55]
	v_mfma_f32_16x16x128_f8f6f4 v[48:51], v[204:211], v[212:219], v[48:51]
	v_mfma_f32_16x16x128_f8f6f4 v[36:39], v[196:203], v[220:227], v[36:39]
	v_mfma_f32_16x16x128_f8f6f4 v[32:35], v[204:211], v[220:227], v[32:35]
	v_mfma_f32_16x16x128_f8f6f4 v[20:23], v[196:203], v[228:235], v[20:23]
	v_mfma_f32_16x16x128_f8f6f4 v[16:19], v[204:211], v[228:235], v[16:19]
	v_mfma_f32_16x16x128_f8f6f4 v[4:7], v[196:203], v[236:243], v[4:7]
	v_mfma_f32_16x16x128_f8f6f4 v[0:3], v[204:211], v[236:243], v[0:3]
	s_setprio 0
	s_barrier
	s_mov_b32 m0, s71
	v_lshl_add_u64 v[164:165], s[44:45], 0, v[130:131]
	global_load_lds_dwordx4 v[164:165], off
	v_lshl_add_u64 v[164:165], s[44:45], 0, v[134:135]
	s_mov_b32 m0, s72
	s_andn2_b64 vcc, exec, s[10:11]
	global_load_lds_dwordx4 v[164:165], off
	s_mov_b64 s[42:43], -1
	s_mov_b64 s[10:11], 0
	s_mov_b64 s[44:45], 0x100
	s_cbranch_vccz .LBB0_335
	s_branch .Lpeel_after_335
.LBB0_335:
	s_add_u32 s52, s14, s44
	s_addc_u32 s53, s15, s45
	s_add_u32 s46, s52, 0x100
	s_addc_u32 s47, s53, 0
	s_and_b64 s[0:1], s[42:43], exec
	s_cselect_b32 s46, s14, s46
	s_cselect_b32 s47, s15, s47
	s_add_u32 s0, s40, s44
	s_addc_u32 s1, s41, s45
	s_add_u32 s44, s0, 0x100
	s_addc_u32 s45, s1, 0
	ds_read_b128 v[196:199], v170
	ds_read_b128 v[204:207], v170 offset:2048
	ds_read_b128 v[200:203], v171
	ds_read_b128 v[208:211], v171 offset:2048
	s_and_b64 s[0:1], s[42:43], exec
	s_cselect_b32 s51, s37, s45
	s_cselect_b32 s50, s36, s44
	s_waitcnt lgkmcnt(0)
	ds_read_b128 v[212:215], v129
	ds_read_b128 v[220:223], v129 offset:2048
	ds_read_b128 v[216:219], v133
	ds_read_b128 v[224:227], v133 offset:2048
	ds_read_b128 v[228:231], v129 offset:4096
	ds_read_b128 v[236:239], v129 offset:6144
	ds_read_b128 v[232:235], v133 offset:4096
	ds_read_b128 v[240:243], v133 offset:6144
	s_waitcnt vmcnt(6)
	s_waitcnt lgkmcnt(8)
	s_barrier
	s_waitcnt lgkmcnt(0)
	v_cndmask_b32_e64 v164, v158, v150, s[42:43]
	s_setprio 1
	s_waitcnt lgkmcnt(0)
	v_mfma_f32_16x16x128_f8f6f4 v[124:127], v[196:203], v[212:219], v[124:127]
	v_mfma_f32_16x16x128_f8f6f4 v[120:123], v[204:211], v[212:219], v[120:123]
	v_mfma_f32_16x16x128_f8f6f4 v[108:111], v[196:203], v[220:227], v[108:111]
	v_mfma_f32_16x16x128_f8f6f4 v[104:107], v[204:211], v[220:227], v[104:107]
	v_mfma_f32_16x16x128_f8f6f4 v[92:95], v[196:203], v[228:235], v[92:95]
	v_mfma_f32_16x16x128_f8f6f4 v[88:91], v[204:211], v[228:235], v[88:91]
	v_mfma_f32_16x16x128_f8f6f4 v[76:79], v[196:203], v[236:243], v[76:79]
	v_mfma_f32_16x16x128_f8f6f4 v[72:75], v[204:211], v[236:243], v[72:75]
	s_setprio 0
	s_barrier
	ds_read_b128 v[196:199], v170 offset:16384
	ds_read_b128 v[204:207], v170 offset:18432
	ds_read_b128 v[200:203], v171 offset:16384
	ds_read_b128 v[208:211], v171 offset:18432
	s_add_i32 m0, s58, 0xc000
	s_add_i32 s0, s58, 0xe000
	s_add_u32 s48, s50, 0x1000
	s_addc_u32 s49, s51, 0
	s_add_u32 s44, s50, 0x1080
	s_addc_u32 s45, s51, 0
	v_cndmask_b32_e64 v136, v156, v148, s[42:43]
	v_cndmask_b32_e64 v149, v160, v152, s[42:43]
	v_lshl_add_u64 v[252:253], s[52:53], 0, v[160:161]
	v_lshl_add_u64 v[252:253], v[252:253], 0, s[26:27]
	global_load_lds_dwordx4 v[252:253], off
	v_lshl_add_u64 v[252:253], s[52:53], 0, v[162:163]
	v_lshl_add_u64 v[252:253], v[252:253], 0, s[26:27]
	s_mov_b32 m0, s0
	s_nop 0
	global_load_lds_dwordx4 v[252:253], off
	s_barrier
	s_waitcnt lgkmcnt(0)
	s_setprio 1
	v_mfma_f32_16x16x128_f8f6f4 v[116:119], v[196:203], v[212:219], v[116:119]
	v_mfma_f32_16x16x128_f8f6f4 v[112:115], v[204:211], v[212:219], v[112:115]
	v_mfma_f32_16x16x128_f8f6f4 v[100:103], v[196:203], v[220:227], v[100:103]
	v_mfma_f32_16x16x128_f8f6f4 v[96:99], v[204:211], v[220:227], v[96:99]
	v_mfma_f32_16x16x128_f8f6f4 v[84:87], v[196:203], v[228:235], v[84:87]
	v_mfma_f32_16x16x128_f8f6f4 v[80:83], v[204:211], v[228:235], v[80:83]
	v_mfma_f32_16x16x128_f8f6f4 v[68:71], v[196:203], v[236:243], v[68:71]
	v_mfma_f32_16x16x128_f8f6f4 v[64:67], v[204:211], v[236:243], v[64:67]
	s_setprio 0
	s_barrier
	ds_read_b128 v[196:199], v170
	ds_read_b128 v[204:207], v170 offset:2048
	ds_read_b128 v[200:203], v171
	ds_read_b128 v[208:211], v171 offset:2048
	s_mov_b32 m0, s58
	ds_read_b128 v[212:215], v129 offset:16384
	ds_read_b128 v[220:223], v129 offset:18432
	ds_read_b128 v[216:219], v133 offset:16384
	ds_read_b128 v[224:227], v133 offset:18432
	ds_read_b128 v[228:231], v129 offset:20480
	ds_read_b128 v[236:239], v129 offset:22528
	ds_read_b128 v[232:235], v133 offset:20480
	ds_read_b128 v[240:243], v133 offset:22528
	global_load_lds_dwordx4 v136, s[46:47]
	s_mov_b32 m0, s61
	v_mov_b32_e32 v165, v137
	global_load_lds_dwordx4 v164, s[46:47]
	s_waitcnt lgkmcnt(8)
	s_barrier
	s_waitcnt lgkmcnt(0)
	v_lshl_add_u64 v[168:169], s[46:47], 0, v[136:137]
	v_lshl_add_u64 v[190:191], s[46:47], 0, v[164:165]
	s_setprio 1
	s_waitcnt lgkmcnt(0)
	v_mfma_f32_16x16x128_f8f6f4 v[60:63], v[196:203], v[212:219], v[60:63]
	v_mfma_f32_16x16x128_f8f6f4 v[56:59], v[204:211], v[212:219], v[56:59]
	v_mfma_f32_16x16x128_f8f6f4 v[44:47], v[196:203], v[220:227], v[44:47]
	v_mfma_f32_16x16x128_f8f6f4 v[40:43], v[204:211], v[220:227], v[40:43]
	v_mfma_f32_16x16x128_f8f6f4 v[28:31], v[196:203], v[228:235], v[28:31]
	v_mfma_f32_16x16x128_f8f6f4 v[24:27], v[204:211], v[228:235], v[24:27]
	v_mfma_f32_16x16x128_f8f6f4 v[12:15], v[196:203], v[236:243], v[12:15]
	v_mfma_f32_16x16x128_f8f6f4 v[8:11], v[204:211], v[236:243], v[8:11]
	s_setprio 0
	s_barrier
	s_mov_b32 m0, s59
	v_lshl_add_u64 v[164:165], s[50:51], 0, v[130:131]
	ds_read_b128 v[196:199], v170 offset:16384
	ds_read_b128 v[204:207], v170 offset:18432
	ds_read_b128 v[200:203], v171 offset:16384
	ds_read_b128 v[208:211], v171 offset:18432
	global_load_lds_dwordx4 v[164:165], off
	v_lshl_add_u64 v[166:167], s[50:51], 0, v[134:135]
	s_mov_b32 m0, s60
	s_nop 0
	global_load_lds_dwordx4 v[166:167], off
	s_waitcnt vmcnt(8)
	s_waitcnt lgkmcnt(0)
	s_barrier
	s_setprio 1
	s_waitcnt lgkmcnt(0)
	v_mfma_f32_16x16x128_f8f6f4 v[52:55], v[196:203], v[212:219], v[52:55]
	v_mfma_f32_16x16x128_f8f6f4 v[48:51], v[204:211], v[212:219], v[48:51]
	v_mfma_f32_16x16x128_f8f6f4 v[36:39], v[196:203], v[220:227], v[36:39]
	v_mfma_f32_16x16x128_f8f6f4 v[32:35], v[204:211], v[220:227], v[32:35]
	v_mfma_f32_16x16x128_f8f6f4 v[20:23], v[196:203], v[228:235], v[20:23]
	v_mfma_f32_16x16x128_f8f6f4 v[16:19], v[204:211], v[228:235], v[16:19]
	v_mfma_f32_16x16x128_f8f6f4 v[4:7], v[196:203], v[236:243], v[4:7]
	v_mfma_f32_16x16x128_f8f6f4 v[0:3], v[204:211], v[236:243], v[0:3]
	s_setprio 0
	s_barrier
	ds_read_b128 v[196:199], v170 offset:32768
	ds_read_b128 v[204:207], v170 offset:34816
	ds_read_b128 v[200:203], v171 offset:32768
	ds_read_b128 v[208:211], v171 offset:34816
	s_mov_b32 m0, s64
	ds_read_b128 v[212:215], v129 offset:32768
	ds_read_b128 v[220:223], v129 offset:34816
	ds_read_b128 v[216:219], v133 offset:32768
	ds_read_b128 v[224:227], v133 offset:34816
	ds_read_b128 v[228:231], v129 offset:36864
	ds_read_b128 v[236:239], v129 offset:38912
	ds_read_b128 v[232:235], v133 offset:36864
	ds_read_b128 v[240:243], v133 offset:38912
	v_cndmask_b32_e64 v136, v162, v154, s[42:43]
	global_load_lds_dwordx4 v149, s[46:47]
	s_mov_b32 m0, s65
	s_nop 0
	global_load_lds_dwordx4 v136, s[46:47]
	s_waitcnt vmcnt(8)
	s_waitcnt lgkmcnt(8)
	s_barrier
	s_waitcnt lgkmcnt(0)
	s_setprio 1
	v_mfma_f32_16x16x128_f8f6f4 v[124:127], v[196:203], v[212:219], v[124:127]
	v_mfma_f32_16x16x128_f8f6f4 v[120:123], v[204:211], v[212:219], v[120:123]
	v_mfma_f32_16x16x128_f8f6f4 v[108:111], v[196:203], v[220:227], v[108:111]
	v_mfma_f32_16x16x128_f8f6f4 v[104:107], v[204:211], v[220:227], v[104:107]
	v_mfma_f32_16x16x128_f8f6f4 v[92:95], v[196:203], v[228:235], v[92:95]
	v_mfma_f32_16x16x128_f8f6f4 v[88:91], v[204:211], v[228:235], v[88:91]
	v_mfma_f32_16x16x128_f8f6f4 v[76:79], v[196:203], v[236:243], v[76:79]
	v_mfma_f32_16x16x128_f8f6f4 v[72:75], v[204:211], v[236:243], v[72:75]
	s_setprio 0
	s_barrier
	ds_read_b128 v[196:199], v170 offset:49152
	ds_read_b128 v[204:207], v170 offset:51200
	ds_read_b128 v[200:203], v171 offset:49152
	ds_read_b128 v[208:211], v171 offset:51200
	v_lshl_add_u64 v[192:193], s[48:49], 0, v[130:131]
	s_mov_b32 m0, s62
	s_nop 0
	global_load_lds_dwordx4 v[192:193], off
	v_lshl_add_u64 v[192:193], s[48:49], 0, v[134:135]
	s_mov_b32 m0, s63
	s_nop 0
	global_load_lds_dwordx4 v[192:193], off
	s_waitcnt vmcnt(8)
	s_barrier
	s_waitcnt lgkmcnt(0)
	s_setprio 1
	v_mfma_f32_16x16x128_f8f6f4 v[116:119], v[196:203], v[212:219], v[116:119]
	v_mfma_f32_16x16x128_f8f6f4 v[112:115], v[204:211], v[212:219], v[112:115]
	v_mfma_f32_16x16x128_f8f6f4 v[100:103], v[196:203], v[220:227], v[100:103]
	v_mfma_f32_16x16x128_f8f6f4 v[96:99], v[204:211], v[220:227], v[96:99]
	v_mfma_f32_16x16x128_f8f6f4 v[84:87], v[196:203], v[228:235], v[84:87]
	v_mfma_f32_16x16x128_f8f6f4 v[80:83], v[204:211], v[228:235], v[80:83]
	v_mfma_f32_16x16x128_f8f6f4 v[68:71], v[196:203], v[236:243], v[68:71]
	v_mfma_f32_16x16x128_f8f6f4 v[64:67], v[204:211], v[236:243], v[64:67]
	s_setprio 0
	s_barrier
	ds_read_b128 v[196:199], v170 offset:32768
	ds_read_b128 v[204:207], v170 offset:34816
	ds_read_b128 v[200:203], v171 offset:32768
	ds_read_b128 v[208:211], v171 offset:34816
	s_mov_b32 m0, s69
	v_lshl_add_u64 v[168:169], v[168:169], 0, s[26:27]
	ds_read_b128 v[212:215], v129 offset:49152
	ds_read_b128 v[220:223], v129 offset:51200
	ds_read_b128 v[216:219], v133 offset:49152
	ds_read_b128 v[224:227], v133 offset:51200
	ds_read_b128 v[228:231], v129 offset:53248
	ds_read_b128 v[236:239], v129 offset:55296
	ds_read_b128 v[232:235], v133 offset:53248
	ds_read_b128 v[240:243], v133 offset:55296
	global_load_lds_dwordx4 v[168:169], off
	v_lshl_add_u64 v[168:169], v[190:191], 0, s[26:27]
	s_mov_b32 m0, s70
	s_nop 0
	global_load_lds_dwordx4 v[168:169], off
	s_waitcnt lgkmcnt(8)
	s_barrier
	s_waitcnt lgkmcnt(0)
	s_setprio 1
	v_mfma_f32_16x16x128_f8f6f4 v[60:63], v[196:203], v[212:219], v[60:63]
	v_mfma_f32_16x16x128_f8f6f4 v[56:59], v[204:211], v[212:219], v[56:59]
	v_mfma_f32_16x16x128_f8f6f4 v[44:47], v[196:203], v[220:227], v[44:47]
	v_mfma_f32_16x16x128_f8f6f4 v[40:43], v[204:211], v[220:227], v[40:43]
	v_mfma_f32_16x16x128_f8f6f4 v[28:31], v[196:203], v[228:235], v[28:31]
	v_mfma_f32_16x16x128_f8f6f4 v[24:27], v[204:211], v[228:235], v[24:27]
	v_mfma_f32_16x16x128_f8f6f4 v[12:15], v[196:203], v[236:243], v[12:15]
	v_mfma_f32_16x16x128_f8f6f4 v[8:11], v[204:211], v[236:243], v[8:11]
	s_setprio 0
	s_barrier
	s_mov_b32 m0, s67
	v_lshl_add_u64 v[164:165], v[164:165], 0, s[26:27]
	ds_read_b128 v[196:199], v170 offset:49152
	ds_read_b128 v[204:207], v170 offset:51200
	ds_read_b128 v[200:203], v171 offset:49152
	ds_read_b128 v[208:211], v171 offset:51200
	global_load_lds_dwordx4 v[164:165], off
	v_lshl_add_u64 v[164:165], v[166:167], 0, s[26:27]
	s_mov_b32 m0, s68
	s_nop 0
	global_load_lds_dwordx4 v[164:165], off
	s_waitcnt vmcnt(8)
	s_waitcnt lgkmcnt(0)
	s_barrier
	s_setprio 1
	s_waitcnt lgkmcnt(0)
	v_mfma_f32_16x16x128_f8f6f4 v[52:55], v[196:203], v[212:219], v[52:55]
	v_mfma_f32_16x16x128_f8f6f4 v[48:51], v[204:211], v[212:219], v[48:51]
	v_mfma_f32_16x16x128_f8f6f4 v[36:39], v[196:203], v[220:227], v[36:39]
	v_mfma_f32_16x16x128_f8f6f4 v[32:35], v[204:211], v[220:227], v[32:35]
	v_mfma_f32_16x16x128_f8f6f4 v[20:23], v[196:203], v[228:235], v[20:23]
	v_mfma_f32_16x16x128_f8f6f4 v[16:19], v[204:211], v[228:235], v[16:19]
	v_mfma_f32_16x16x128_f8f6f4 v[4:7], v[196:203], v[236:243], v[4:7]
	v_mfma_f32_16x16x128_f8f6f4 v[0:3], v[204:211], v[236:243], v[0:3]
	s_setprio 0
	s_barrier
	s_mov_b32 m0, s71
	v_lshl_add_u64 v[164:165], s[44:45], 0, v[130:131]
	global_load_lds_dwordx4 v[164:165], off
	v_lshl_add_u64 v[164:165], s[44:45], 0, v[134:135]
	s_mov_b32 m0, s72
	s_andn2_b64 vcc, exec, s[10:11]
	global_load_lds_dwordx4 v[164:165], off
	s_mov_b64 s[42:43], -1
	s_mov_b64 s[10:11], 0
	s_mov_b64 s[44:45], 0x100
	s_cbranch_vccz .LBB0_335

.LBB0_462:
	s_and_b32 s33, s33, 63
	s_lshl_b32 s33, s33, s44
	s_and_b32 s33, s33, s43
	v_add_u32_e32 v64, s33, v98
	v_add_u32_e32 v66, s33, v99
	v_mad_i64_i32 v[64:65], s[44:45], s42, v64, 0
	s_lshl_b32 s39, s39, 2
	s_lshl_b32 s36, s36, 9
	v_mad_i64_i32 v[66:67], s[44:45], s42, v66, 0
	v_lshl_add_u64 v[64:65], v[64:65], 2, s[40:41]
	s_and_b32 s36, s36, s39
	v_lshl_add_u64 v[66:67], v[66:67], 2, s[40:41]
	v_lshl_add_u64 v[64:65], v[64:65], 0, s[36:37]
	v_lshl_add_u64 v[66:67], v[66:67], 0, s[36:37]
	v_lshl_add_u64 v[64:65], v[64:65], 0, v[152:153]
	v_lshl_add_u64 v[66:67], v[66:67], 0, v[152:153]
	global_load_dwordx4 v[92:95], v[64:65], off nt
	global_load_dwordx4 v[88:91], v[66:67], off nt
	v_add_u32_e32 v64, s33, v100
	v_add_u32_e32 v66, s33, v101
	v_mad_i64_i32 v[64:65], s[44:45], s42, v64, 0
	v_mad_i64_i32 v[66:67], s[44:45], s42, v66, 0
	v_lshl_add_u64 v[64:65], v[64:65], 2, s[40:41]
	v_lshl_add_u64 v[66:67], v[66:67], 2, s[40:41]
	v_lshl_add_u64 v[64:65], v[64:65], 0, s[36:37]
	v_lshl_add_u64 v[66:67], v[66:67], 0, s[36:37]
	v_lshl_add_u64 v[64:65], v[64:65], 0, v[152:153]
	v_lshl_add_u64 v[66:67], v[66:67], 0, v[152:153]
	global_load_dwordx4 v[84:87], v[64:65], off nt
	global_load_dwordx4 v[80:83], v[66:67], off nt
	v_add_u32_e32 v64, s33, v102
	v_add_u32_e32 v66, s33, v103
	v_mad_i64_i32 v[64:65], s[44:45], s42, v64, 0
	v_mad_i64_i32 v[66:67], s[44:45], s42, v66, 0
	v_lshl_add_u64 v[64:65], v[64:65], 2, s[40:41]
	v_lshl_add_u64 v[66:67], v[66:67], 2, s[40:41]
	v_lshl_add_u64 v[64:65], v[64:65], 0, s[36:37]
	v_lshl_add_u64 v[66:67], v[66:67], 0, s[36:37]
	v_lshl_add_u64 v[64:65], v[64:65], 0, v[152:153]
	v_lshl_add_u64 v[66:67], v[66:67], 0, v[152:153]
	global_load_dwordx4 v[76:79], v[64:65], off nt
	global_load_dwordx4 v[72:75], v[66:67], off nt
	v_add_u32_e32 v64, s33, v104
	v_add_u32_e32 v66, s33, v105
	v_mad_i64_i32 v[64:65], s[44:45], s42, v64, 0
	v_mad_i64_i32 v[66:67], s[42:43], s42, v66, 0
	v_lshl_add_u64 v[64:65], v[64:65], 2, s[40:41]
	v_lshl_add_u64 v[66:67], v[66:67], 2, s[40:41]
	v_lshl_add_u64 v[64:65], v[64:65], 0, s[36:37]
	v_lshl_add_u64 v[66:67], v[66:67], 0, s[36:37]
	v_lshl_add_u64 v[64:65], v[64:65], 0, v[152:153]
	v_lshl_add_u64 v[66:67], v[66:67], 0, v[152:153]
	global_load_dwordx4 v[68:71], v[64:65], off nt
	s_nop 0
	global_load_dwordx4 v[64:67], v[66:67], off nt
	s_waitcnt lgkmcnt(0)
	s_barrier
	ds_read2st64_b32 v[180:181], v188 offset1:2
	ds_read2st64_b32 v[182:183], v188 offset0:4 offset1:6
	ds_read2st64_b32 v[184:185], v188 offset0:8 offset1:10
	ds_read2st64_b32 v[186:187], v188 offset0:12 offset1:14
	ds_read2st64_b32 v[206:207], v188 offset0:16 offset1:18
	ds_read2st64_b32 v[208:209], v188 offset0:20 offset1:22
	ds_read2st64_b32 v[210:211], v188 offset0:24 offset1:26
	ds_read2st64_b32 v[212:213], v188 offset0:28 offset1:30
	ds_read_b32 v188, v189
	ds_read_b32 v189, v190
	ds_read_b32 v190, v191
	ds_read_b32 v191, v192
	ds_read_b32 v192, v193
	ds_read_b32 v193, v195
	ds_read_b32 v195, v196
	ds_read_b32 v196, v197
	ds_read_b32 v197, v198
	ds_read_b32 v198, v199
	ds_read_b32 v199, v200
	ds_read_b32 v200, v201
	ds_read_b32 v201, v202
	ds_read_b32 v202, v203
	ds_read_b32 v203, v204
	ds_read_b32 v204, v205
	s_waitcnt lgkmcnt(14)
	v_med3_f32 v205, v180, s70, v178
	v_med3_f32 v181, v181, s70, v178
	v_mov_b32_e32 v180, v153
	v_cvt_pk_fp8_f32 v180, v205, v181
	v_med3_f32 v184, v184, s70, v178
	v_med3_f32 v185, v185, s70, v178
	v_mov_b32_e32 v181, v153
	v_cvt_pk_fp8_f32 v181, v184, v185
	v_med3_f32 v182, v182, s70, v178
	v_med3_f32 v183, v183, s70, v178
	v_cvt_pk_fp8_f32 v180, v182, v183 op_sel:[0,0,1]
	v_med3_f32 v182, v186, s70, v178
	v_med3_f32 v183, v187, s70, v178
	v_cvt_pk_fp8_f32 v181, v182, v183 op_sel:[0,0,1]
	v_med3_f32 v183, v206, s70, v178
	v_med3_f32 v184, v207, s70, v178
	v_mov_b32_e32 v182, v153
	v_cvt_pk_fp8_f32 v182, v183, v184
	v_med3_f32 v184, v210, s70, v178
	v_med3_f32 v187, v211, s70, v178
	v_mov_b32_e32 v183, v153
	v_cvt_pk_fp8_f32 v183, v184, v187
	v_med3_f32 v185, v208, s70, v178
	v_med3_f32 v186, v209, s70, v178
	v_cvt_pk_fp8_f32 v182, v185, v186 op_sel:[0,0,1]
	v_med3_f32 v184, v212, s70, v178
	v_med3_f32 v185, v213, s70, v178
	v_cvt_pk_fp8_f32 v183, v184, v185 op_sel:[0,0,1]
	v_med3_f32 v185, v188, s70, v178
	v_med3_f32 v186, v189, s70, v178
	v_mov_b32_e32 v184, v153
	v_cvt_pk_fp8_f32 v184, v185, v186
	s_waitcnt lgkmcnt(11)
	v_med3_f32 v186, v192, s70, v178
	s_waitcnt lgkmcnt(10)
	v_med3_f32 v189, v193, s70, v178
	v_mov_b32_e32 v185, v153
	v_cvt_pk_fp8_f32 v185, v186, v189
	v_med3_f32 v187, v190, s70, v178
	v_med3_f32 v188, v191, s70, v178
	v_cvt_pk_fp8_f32 v184, v187, v188 op_sel:[0,0,1]
	s_waitcnt lgkmcnt(9)
	v_med3_f32 v186, v195, s70, v178
	s_waitcnt lgkmcnt(8)
	v_med3_f32 v187, v196, s70, v178
	v_cvt_pk_fp8_f32 v185, v186, v187 op_sel:[0,0,1]
	s_waitcnt lgkmcnt(7)
	v_med3_f32 v187, v197, s70, v178
	s_waitcnt lgkmcnt(6)
	v_med3_f32 v188, v198, s70, v178
	v_mov_b32_e32 v186, v153
	v_cvt_pk_fp8_f32 v186, v187, v188
	s_waitcnt lgkmcnt(3)
	v_med3_f32 v188, v201, s70, v178
	s_waitcnt lgkmcnt(2)
	v_med3_f32 v191, v202, s70, v178
	v_mov_b32_e32 v187, v153
	v_cvt_pk_fp8_f32 v187, v188, v191
	v_med3_f32 v189, v199, s70, v178
	v_med3_f32 v190, v200, s70, v178
	v_cvt_pk_fp8_f32 v186, v189, v190 op_sel:[0,0,1]
	s_waitcnt lgkmcnt(1)
	v_med3_f32 v188, v203, s70, v178
	s_waitcnt lgkmcnt(0)
	v_med3_f32 v189, v204, s70, v178
	s_cmp_lt_i32 s5, 0
	v_cvt_pk_fp8_f32 v187, v188, v189 op_sel:[0,0,1]
	v_add_u32_e32 v188, s5, v107
	s_cselect_b64 vcc, -1, 0
	v_cndmask_b32_e32 v190, v188, v106, vcc
	v_mov_b64_e32 v[188:189], s[6:7]
	v_mad_i64_i32 v[188:189], s[6:7], s38, v190, v[188:189]
	s_mov_b32 s5, s37
	v_lshl_add_u64 v[188:189], v[188:189], 0, s[4:5]
	s_add_i32 s19, s19, 3
	v_lshl_add_u64 v[188:189], v[188:189], 0, v[96:97]
	s_cmp_ge_i32 s19, s84
	global_store_dwordx4 v[188:189], v[180:183], off nt
	global_store_dwordx4 v[188:189], v[184:187], off offset:16 nt
	s_cbranch_scc1 .LBB0_492

.LBB0_473:
	s_and_b32 s36, s36, 63
	s_lshl_b32 s36, s36, s45
	s_and_b32 s46, s36, s44
	v_add_u32_e32 v0, s46, v98
	v_add_u32_e32 v2, s46, v99
	v_add_u32_e32 v8, s46, v100
	v_add_u32_e32 v10, s46, v101
	v_add_u32_e32 v16, s46, v102
	v_add_u32_e32 v18, s46, v103
	v_add_u32_e32 v24, s46, v104
	v_add_u32_e32 v26, s46, v105
	v_mad_i64_i32 v[0:1], s[44:45], s42, v0, 0
	s_lshl_b32 s36, s43, 2
	s_lshl_b32 s39, s39, 9
	v_mad_i64_i32 v[2:3], s[44:45], s42, v2, 0
	v_mad_i64_i32 v[8:9], s[44:45], s42, v8, 0
	v_mad_i64_i32 v[10:11], s[44:45], s42, v10, 0
	v_mad_i64_i32 v[16:17], s[44:45], s42, v16, 0
	v_mad_i64_i32 v[18:19], s[44:45], s42, v18, 0
	v_mad_i64_i32 v[24:25], s[44:45], s42, v24, 0
	v_mad_i64_i32 v[26:27], s[42:43], s42, v26, 0
	v_lshl_add_u64 v[0:1], v[0:1], 2, s[40:41]
	s_and_b32 s36, s39, s36
	v_lshl_add_u64 v[2:3], v[2:3], 2, s[40:41]
	v_lshl_add_u64 v[8:9], v[8:9], 2, s[40:41]
	v_lshl_add_u64 v[10:11], v[10:11], 2, s[40:41]
	v_lshl_add_u64 v[16:17], v[16:17], 2, s[40:41]
	v_lshl_add_u64 v[18:19], v[18:19], 2, s[40:41]
	v_lshl_add_u64 v[24:25], v[24:25], 2, s[40:41]
	v_lshl_add_u64 v[26:27], v[26:27], 2, s[40:41]
	v_lshl_add_u64 v[0:1], v[0:1], 0, s[36:37]
	v_lshl_add_u64 v[2:3], v[2:3], 0, s[36:37]
	v_lshl_add_u64 v[8:9], v[8:9], 0, s[36:37]
	v_lshl_add_u64 v[10:11], v[10:11], 0, s[36:37]
	v_lshl_add_u64 v[16:17], v[16:17], 0, s[36:37]
	v_lshl_add_u64 v[18:19], v[18:19], 0, s[36:37]
	v_lshl_add_u64 v[24:25], v[24:25], 0, s[36:37]
	v_lshl_add_u64 v[26:27], v[26:27], 0, s[36:37]
	v_lshl_add_u64 v[0:1], v[0:1], 0, v[152:153]
	v_lshl_add_u64 v[2:3], v[2:3], 0, v[152:153]
	v_lshl_add_u64 v[8:9], v[8:9], 0, v[152:153]
	v_lshl_add_u64 v[10:11], v[10:11], 0, v[152:153]
	v_lshl_add_u64 v[16:17], v[16:17], 0, v[152:153]
	v_lshl_add_u64 v[18:19], v[18:19], 0, v[152:153]
	v_lshl_add_u64 v[24:25], v[24:25], 0, v[152:153]
	v_lshl_add_u64 v[26:27], v[26:27], 0, v[152:153]
	global_load_dwordx4 v[4:7], v[0:1], off nt
	s_nop 0
	global_load_dwordx4 v[0:3], v[2:3], off nt
	s_nop 0
	global_load_dwordx4 v[12:15], v[8:9], off nt
	s_nop 0
	global_load_dwordx4 v[8:11], v[10:11], off nt
	s_nop 0
	global_load_dwordx4 v[20:23], v[16:17], off nt
	s_nop 0
	global_load_dwordx4 v[16:19], v[18:19], off nt
	s_nop 0
	global_load_dwordx4 v[28:31], v[24:25], off nt
	s_nop 0
	global_load_dwordx4 v[24:27], v[26:27], off nt
	v_add3_u32 v188, s33, v108, v141
	s_waitcnt lgkmcnt(0)
	s_barrier
	ds_read2st64_b32 v[206:207], v188 offset1:2
	ds_read2st64_b32 v[208:209], v188 offset0:4 offset1:6
	ds_read2st64_b32 v[210:211], v188 offset0:8 offset1:10
	ds_read2st64_b32 v[212:213], v188 offset0:12 offset1:14
	ds_read2st64_b32 v[214:215], v188 offset0:16 offset1:18
	ds_read2st64_b32 v[216:217], v188 offset0:20 offset1:22
	ds_read2st64_b32 v[218:219], v188 offset0:24 offset1:26
	ds_read2st64_b32 v[220:221], v188 offset0:28 offset1:30
	s_waitcnt lgkmcnt(7)
	v_med3_f32 v238, v206, s70, v178
	v_med3_f32 v207, v207, s70, v178
	v_mov_b32_e32 v206, v153
	v_cvt_pk_fp8_f32 v206, v238, v207
	s_waitcnt lgkmcnt(5)
	v_med3_f32 v210, v210, s70, v178
	v_med3_f32 v211, v211, s70, v178
	v_mov_b32_e32 v207, v153
	v_cvt_pk_fp8_f32 v207, v210, v211
	v_med3_f32 v208, v208, s70, v178
	v_med3_f32 v209, v209, s70, v178
	v_cvt_pk_fp8_f32 v206, v208, v209 op_sel:[0,0,1]
	s_waitcnt lgkmcnt(4)
	v_med3_f32 v208, v212, s70, v178
	v_med3_f32 v209, v213, s70, v178
	v_cvt_pk_fp8_f32 v207, v208, v209 op_sel:[0,0,1]
	s_waitcnt lgkmcnt(3)
	v_med3_f32 v209, v214, s70, v178
	v_med3_f32 v210, v215, s70, v178
	v_mov_b32_e32 v208, v153
	v_cvt_pk_fp8_f32 v208, v209, v210
	s_waitcnt lgkmcnt(1)
	v_med3_f32 v210, v218, s70, v178
	v_med3_f32 v213, v219, s70, v178
	v_mov_b32_e32 v209, v153
	v_cvt_pk_fp8_f32 v209, v210, v213
	v_add3_u32 v189, s33, v117, v142
	v_add3_u32 v190, s33, v118, v143
	v_add3_u32 v191, s33, v119, v144
	v_add3_u32 v192, s33, v120, v145
	v_add3_u32 v193, s33, v121, v146
	v_add3_u32 v195, s33, v122, v147
	v_add3_u32 v196, s33, v123, v148
	v_add3_u32 v197, s33, v124, v149
	ds_read_b32 v222, v189
	ds_read_b32 v223, v190
	ds_read_b32 v224, v191
	ds_read_b32 v225, v192
	ds_read_b32 v226, v193
	ds_read_b32 v227, v195
	ds_read_b32 v228, v196
	ds_read_b32 v229, v197
	v_med3_f32 v211, v216, s70, v178
	v_med3_f32 v212, v217, s70, v178
	v_cvt_pk_fp8_f32 v208, v211, v212 op_sel:[0,0,1]
	s_waitcnt lgkmcnt(8)
	v_med3_f32 v210, v220, s70, v178
	v_med3_f32 v211, v221, s70, v178
	v_cvt_pk_fp8_f32 v209, v210, v211 op_sel:[0,0,1]
	s_waitcnt lgkmcnt(7)
	v_med3_f32 v211, v222, s70, v178
	s_waitcnt lgkmcnt(6)
	v_med3_f32 v212, v223, s70, v178
	v_mov_b32_e32 v210, v153
	v_cvt_pk_fp8_f32 v210, v211, v212
	s_waitcnt lgkmcnt(3)
	v_med3_f32 v212, v226, s70, v178
	s_waitcnt lgkmcnt(2)
	v_med3_f32 v215, v227, s70, v178
	v_mov_b32_e32 v211, v153
	v_cvt_pk_fp8_f32 v211, v212, v215
	v_add3_u32 v198, s33, v125, v150
	v_add3_u32 v199, s33, v126, v151
	v_add3_u32 v200, s33, v127, v154
	v_add3_u32 v201, s33, v128, v155
	v_add3_u32 v202, s33, v129, v156
	v_add3_u32 v203, s33, v130, v157
	v_add3_u32 v204, s33, v131, v158
	v_add3_u32 v205, s33, v132, v159
	ds_read_b32 v230, v198
	ds_read_b32 v231, v199
	ds_read_b32 v232, v200
	ds_read_b32 v233, v201
	ds_read_b32 v234, v202
	ds_read_b32 v235, v203
	ds_read_b32 v236, v204
	ds_read_b32 v237, v205
	v_med3_f32 v213, v224, s70, v178
	v_med3_f32 v214, v225, s70, v178
	v_cvt_pk_fp8_f32 v210, v213, v214 op_sel:[0,0,1]
	s_waitcnt lgkmcnt(9)
	v_med3_f32 v212, v228, s70, v178
	s_waitcnt lgkmcnt(8)
	v_med3_f32 v213, v229, s70, v178
	v_cvt_pk_fp8_f32 v211, v212, v213 op_sel:[0,0,1]
	s_waitcnt lgkmcnt(7)
	v_med3_f32 v213, v230, s70, v178
	s_waitcnt lgkmcnt(6)
	v_med3_f32 v214, v231, s70, v178
	v_mov_b32_e32 v212, v153
	v_cvt_pk_fp8_f32 v212, v213, v214
	s_waitcnt lgkmcnt(3)
	v_med3_f32 v214, v234, s70, v178
	s_waitcnt lgkmcnt(2)
	v_med3_f32 v217, v235, s70, v178
	v_mov_b32_e32 v213, v153
	v_cvt_pk_fp8_f32 v213, v214, v217
	v_med3_f32 v215, v232, s70, v178
	v_med3_f32 v216, v233, s70, v178
	v_cvt_pk_fp8_f32 v212, v215, v216 op_sel:[0,0,1]
	s_waitcnt lgkmcnt(1)
	v_med3_f32 v214, v236, s70, v178
	s_waitcnt lgkmcnt(0)
	v_med3_f32 v215, v237, s70, v178
	s_cmp_lt_i32 s5, 0
	v_cvt_pk_fp8_f32 v213, v214, v215 op_sel:[0,0,1]
	v_add_u32_e32 v214, s5, v107
	s_cselect_b64 vcc, -1, 0
	v_cndmask_b32_e32 v216, v214, v106, vcc
	v_mov_b64_e32 v[214:215], s[6:7]
	v_mad_i64_i32 v[214:215], s[6:7], s38, v216, v[214:215]
	s_mov_b32 s5, s37
	v_lshl_add_u64 v[214:215], v[214:215], 0, s[4:5]
	s_add_i32 s4, s19, 1
	s_min_i32 s42, s4, s85
	s_lshl_b32 s4, s42, 1
	s_and_b32 s4, s4, 0xffffe000
	s_and_b32 s36, s42, 0xfff
	s_bfe_i32 s5, s42, 0x1001e
	s_or_b32 s4, s4, s36
	s_lshr_b32 s5, s5, 19
	s_add_i32 s5, s4, s5
	s_and_b32 s6, s5, 0xffffe000
	s_sub_i32 s6, s4, s6
	s_ashr_i32 s38, s6, 6
	s_and_b32 s33, s42, 63
	s_ashr_i32 s39, s38, 31
	v_lshl_add_u64 v[214:215], v[214:215], 0, v[96:97]
	s_cmpk_lt_i32 s4, 0x4000
	s_mov_b64 s[40:41], -1
	global_store_dwordx4 v[214:215], v[206:209], off nt
	global_store_dwordx4 v[214:215], v[210:213], off offset:16 nt
	s_cbranch_scc1 .LBB0_475
	s_lshl_b32 s4, s33, 3
	s_lshl_b32 s6, s36, 16
	s_and_b32 s4, s4, 0x180
	s_and_b32 s36, s6, 0xf0000
	s_lshl_b64 s[6:7], s[38:39], 20
	s_add_u32 s6, s73, s6
	s_addc_u32 s7, s74, s7
	s_add_u32 s6, s6, s36
	s_addc_u32 s7, s7, 0
	s_mov_b64 s[40:41], 0

.LBB0_483:
	s_and_b32 s36, s36, 63
	s_lshl_b32 s36, s36, s45
	s_and_b32 s46, s36, s44
	v_add_u32_e32 v32, s46, v98
	v_add_u32_e32 v34, s46, v99
	v_add_u32_e32 v40, s46, v100
	v_add_u32_e32 v42, s46, v101
	v_add_u32_e32 v48, s46, v102
	v_add_u32_e32 v50, s46, v103
	v_add_u32_e32 v56, s46, v104
	v_add_u32_e32 v58, s46, v105
	v_mad_i64_i32 v[32:33], s[44:45], s42, v32, 0
	s_lshl_b32 s36, s43, 2
	s_lshl_b32 s39, s39, 9
	v_mad_i64_i32 v[34:35], s[44:45], s42, v34, 0
	v_mad_i64_i32 v[40:41], s[44:45], s42, v40, 0
	v_mad_i64_i32 v[42:43], s[44:45], s42, v42, 0
	v_mad_i64_i32 v[48:49], s[44:45], s42, v48, 0
	v_mad_i64_i32 v[50:51], s[44:45], s42, v50, 0
	v_mad_i64_i32 v[56:57], s[44:45], s42, v56, 0
	v_mad_i64_i32 v[58:59], s[42:43], s42, v58, 0
	v_lshl_add_u64 v[32:33], v[32:33], 2, s[40:41]
	s_and_b32 s36, s39, s36
	v_lshl_add_u64 v[34:35], v[34:35], 2, s[40:41]
	v_lshl_add_u64 v[40:41], v[40:41], 2, s[40:41]
	v_lshl_add_u64 v[42:43], v[42:43], 2, s[40:41]
	v_lshl_add_u64 v[48:49], v[48:49], 2, s[40:41]
	v_lshl_add_u64 v[50:51], v[50:51], 2, s[40:41]
	v_lshl_add_u64 v[56:57], v[56:57], 2, s[40:41]
	v_lshl_add_u64 v[58:59], v[58:59], 2, s[40:41]
	v_lshl_add_u64 v[32:33], v[32:33], 0, s[36:37]
	v_lshl_add_u64 v[34:35], v[34:35], 0, s[36:37]
	v_lshl_add_u64 v[40:41], v[40:41], 0, s[36:37]
	v_lshl_add_u64 v[42:43], v[42:43], 0, s[36:37]
	v_lshl_add_u64 v[48:49], v[48:49], 0, s[36:37]
	v_lshl_add_u64 v[50:51], v[50:51], 0, s[36:37]
	v_lshl_add_u64 v[56:57], v[56:57], 0, s[36:37]
	v_lshl_add_u64 v[58:59], v[58:59], 0, s[36:37]
	v_lshl_add_u64 v[32:33], v[32:33], 0, v[152:153]
	v_lshl_add_u64 v[34:35], v[34:35], 0, v[152:153]
	v_lshl_add_u64 v[40:41], v[40:41], 0, v[152:153]
	v_lshl_add_u64 v[42:43], v[42:43], 0, v[152:153]
	v_lshl_add_u64 v[48:49], v[48:49], 0, v[152:153]
	v_lshl_add_u64 v[50:51], v[50:51], 0, v[152:153]
	v_lshl_add_u64 v[56:57], v[56:57], 0, v[152:153]
	v_lshl_add_u64 v[58:59], v[58:59], 0, v[152:153]
	global_load_dwordx4 v[36:39], v[32:33], off nt
	s_nop 0
	global_load_dwordx4 v[32:35], v[34:35], off nt
	s_nop 0
	global_load_dwordx4 v[44:47], v[40:41], off nt
	s_nop 0
	global_load_dwordx4 v[40:43], v[42:43], off nt
	s_nop 0
	global_load_dwordx4 v[52:55], v[48:49], off nt
	s_nop 0
	global_load_dwordx4 v[48:51], v[50:51], off nt
	s_nop 0
	global_load_dwordx4 v[60:63], v[56:57], off nt
	s_nop 0
	global_load_dwordx4 v[56:59], v[58:59], off nt
	v_add3_u32 v220, s33, v108, v141
	s_waitcnt lgkmcnt(0)
	s_barrier
	ds_read2st64_b32 v[206:207], v220 offset1:2
	ds_read2st64_b32 v[208:209], v220 offset0:4 offset1:6
	ds_read2st64_b32 v[210:211], v220 offset0:8 offset1:10
	ds_read2st64_b32 v[212:213], v220 offset0:12 offset1:14
	ds_read2st64_b32 v[214:215], v220 offset0:16 offset1:18
	ds_read2st64_b32 v[216:217], v220 offset0:20 offset1:22
	ds_read2st64_b32 v[218:219], v220 offset0:24 offset1:26
	ds_read2st64_b32 v[220:221], v220 offset0:28 offset1:30
	s_waitcnt lgkmcnt(7)
	v_med3_f32 v238, v206, s70, v178
	v_med3_f32 v207, v207, s70, v178
	v_mov_b32_e32 v206, v153
	v_cvt_pk_fp8_f32 v206, v238, v207
	s_waitcnt lgkmcnt(5)
	v_med3_f32 v210, v210, s70, v178
	v_med3_f32 v211, v211, s70, v178
	v_mov_b32_e32 v207, v153
	v_cvt_pk_fp8_f32 v207, v210, v211
	v_med3_f32 v208, v208, s70, v178
	v_med3_f32 v209, v209, s70, v178
	v_cvt_pk_fp8_f32 v206, v208, v209 op_sel:[0,0,1]
	s_waitcnt lgkmcnt(4)
	v_med3_f32 v208, v212, s70, v178
	v_med3_f32 v209, v213, s70, v178
	v_cvt_pk_fp8_f32 v207, v208, v209 op_sel:[0,0,1]
	s_waitcnt lgkmcnt(3)
	v_med3_f32 v209, v214, s70, v178
	v_med3_f32 v210, v215, s70, v178
	v_mov_b32_e32 v208, v153
	v_cvt_pk_fp8_f32 v208, v209, v210
	s_waitcnt lgkmcnt(1)
	v_med3_f32 v210, v218, s70, v178
	v_med3_f32 v213, v219, s70, v178
	v_mov_b32_e32 v209, v153
	v_cvt_pk_fp8_f32 v209, v210, v213
	v_add3_u32 v222, s33, v117, v142
	v_add3_u32 v223, s33, v118, v143
	v_add3_u32 v224, s33, v119, v144
	v_add3_u32 v225, s33, v120, v145
	v_add3_u32 v226, s33, v121, v146
	v_add3_u32 v227, s33, v122, v147
	v_add3_u32 v228, s33, v123, v148
	v_add3_u32 v229, s33, v124, v149
	ds_read_b32 v222, v222
	ds_read_b32 v223, v223
	ds_read_b32 v224, v224
	ds_read_b32 v225, v225
	ds_read_b32 v226, v226
	ds_read_b32 v227, v227
	ds_read_b32 v228, v228
	ds_read_b32 v229, v229
	v_med3_f32 v211, v216, s70, v178
	v_med3_f32 v212, v217, s70, v178
	v_cvt_pk_fp8_f32 v208, v211, v212 op_sel:[0,0,1]
	s_waitcnt lgkmcnt(8)
	v_med3_f32 v210, v220, s70, v178
	v_med3_f32 v211, v221, s70, v178
	v_cvt_pk_fp8_f32 v209, v210, v211 op_sel:[0,0,1]
	s_waitcnt lgkmcnt(7)
	v_med3_f32 v211, v222, s70, v178
	s_waitcnt lgkmcnt(6)
	v_med3_f32 v212, v223, s70, v178
	v_mov_b32_e32 v210, v153
	v_cvt_pk_fp8_f32 v210, v211, v212
	s_waitcnt lgkmcnt(3)
	v_med3_f32 v212, v226, s70, v178
	s_waitcnt lgkmcnt(2)
	v_med3_f32 v215, v227, s70, v178
	v_mov_b32_e32 v211, v153
	v_cvt_pk_fp8_f32 v211, v212, v215
	v_add3_u32 v230, s33, v125, v150
	v_add3_u32 v231, s33, v126, v151
	v_add3_u32 v232, s33, v127, v154
	v_add3_u32 v233, s33, v128, v155
	v_add3_u32 v234, s33, v129, v156
	v_add3_u32 v235, s33, v130, v157
	v_add3_u32 v236, s33, v131, v158
	v_add3_u32 v237, s33, v132, v159
	ds_read_b32 v230, v230
	ds_read_b32 v231, v231
	ds_read_b32 v232, v232
	ds_read_b32 v233, v233
	ds_read_b32 v234, v234
	ds_read_b32 v235, v235
	ds_read_b32 v236, v236
	ds_read_b32 v237, v237
	v_med3_f32 v213, v224, s70, v178
	v_med3_f32 v214, v225, s70, v178
	v_cvt_pk_fp8_f32 v210, v213, v214 op_sel:[0,0,1]
	s_waitcnt lgkmcnt(9)
	v_med3_f32 v212, v228, s70, v178
	s_waitcnt lgkmcnt(8)
	v_med3_f32 v213, v229, s70, v178
	v_cvt_pk_fp8_f32 v211, v212, v213 op_sel:[0,0,1]
	s_waitcnt lgkmcnt(7)
	v_med3_f32 v213, v230, s70, v178
	s_waitcnt lgkmcnt(6)
	v_med3_f32 v214, v231, s70, v178
	v_mov_b32_e32 v212, v153
	v_cvt_pk_fp8_f32 v212, v213, v214
	s_waitcnt lgkmcnt(3)
	v_med3_f32 v214, v234, s70, v178
	s_waitcnt lgkmcnt(2)
	v_med3_f32 v217, v235, s70, v178
	v_mov_b32_e32 v213, v153
	v_cvt_pk_fp8_f32 v213, v214, v217
	v_med3_f32 v215, v232, s70, v178
	v_med3_f32 v216, v233, s70, v178
	v_cvt_pk_fp8_f32 v212, v215, v216 op_sel:[0,0,1]
	s_waitcnt lgkmcnt(1)
	v_med3_f32 v214, v236, s70, v178
	s_waitcnt lgkmcnt(0)
	v_med3_f32 v215, v237, s70, v178
	s_cmp_lt_i32 s5, 0
	v_cvt_pk_fp8_f32 v213, v214, v215 op_sel:[0,0,1]
	v_add_u32_e32 v214, s5, v107
	s_cselect_b64 vcc, -1, 0
	v_cndmask_b32_e32 v216, v214, v106, vcc
	v_mov_b64_e32 v[214:215], s[6:7]
	v_mad_i64_i32 v[214:215], s[6:7], s38, v216, v[214:215]
	s_mov_b32 s5, s37
	v_lshl_add_u64 v[214:215], v[214:215], 0, s[4:5]
	s_add_i32 s4, s19, 2
	s_min_i32 s33, s4, s85
	s_lshl_b32 s4, s33, 1
	s_and_b32 s4, s4, 0xffffe000
	s_and_b32 s42, s33, 0xfff
	s_bfe_i32 s5, s33, 0x1001e
	s_or_b32 s4, s4, s42
	s_lshr_b32 s5, s5, 19
	s_add_i32 s5, s4, s5
	s_and_b32 s6, s5, 0xffffe000
	s_sub_i32 s6, s4, s6
	s_ashr_i32 s38, s6, 6
	s_and_b32 s36, s33, 63
	s_ashr_i32 s39, s38, 31
	v_lshl_add_u64 v[214:215], v[214:215], 0, v[96:97]
	s_cmpk_lt_i32 s4, 0x4000
	s_mov_b64 s[40:41], -1
	global_store_dwordx4 v[214:215], v[206:209], off nt
	global_store_dwordx4 v[214:215], v[210:213], off offset:16 nt
	s_cbranch_scc1 .LBB0_485
	s_lshl_b32 s4, s36, 3
	s_lshl_b32 s6, s42, 16
	s_and_b32 s4, s4, 0x180
	s_and_b32 s40, s6, 0xf0000
	s_lshl_b64 s[6:7], s[38:39], 20
	s_add_u32 s6, s73, s6
	s_addc_u32 s7, s74, s7
	s_add_u32 s6, s6, s40
	s_addc_u32 s7, s7, 0
	s_mov_b64 s[40:41], 0

.LBB0_502:
	v_mul_f32_e32 v0, v96, v0
	v_mul_f32_e32 v1, v96, v1
	v_mul_f32_e32 v21, v96, v21
	v_mul_f32_e32 v0, v0, v157
	v_mul_f32_e32 v1, v1, v156
	v_mul_f32_e32 v21, v21, v143
	v_med3_f32 v0, v0, s70, v178
	v_med3_f32 v1, v1, s70, v178
	v_mov_b32_e32 v143, v153
	v_cvt_pk_fp8_f32 v143, v0, v1
	v_mul_f32_e32 v2, v96, v2
	v_mul_f32_e32 v3, v96, v3
	v_mul_f32_e32 v2, v2, v155
	v_mul_f32_e32 v3, v3, v154
	v_mul_f32_e32 v20, v96, v20
	v_med3_f32 v0, v2, s70, v178
	v_med3_f32 v1, v3, s70, v178
	v_mul_f32_e32 v20, v20, v144
	v_mul_f32_e32 v10, v96, v10
	v_cvt_pk_fp8_f32 v143, v0, v1 op_sel:[0,0,1]
	v_med3_f32 v0, v94, s70, v178
	v_med3_f32 v1, v95, s70, v178
	v_mov_b32_e32 v144, v153
	v_mul_f32_e32 v10, v10, v145
	v_cvt_pk_fp8_f32 v144, v0, v1
	v_med3_f32 v0, v90, s70, v178
	v_med3_f32 v1, v91, s70, v178
	v_mov_b32_e32 v145, v153
	v_cvt_pk_fp8_f32 v145, v0, v1
	v_mul_f32_e32 v9, v96, v9
	v_med3_f32 v0, v88, s70, v178
	v_med3_f32 v1, v89, s70, v178
	v_mul_f32_e32 v8, v96, v8
	v_mul_f32_e32 v9, v9, v146
	v_cvt_pk_fp8_f32 v145, v0, v1 op_sel:[0,0,1]
	v_med3_f32 v0, v86, s70, v178
	v_med3_f32 v1, v87, s70, v178
	v_mov_b32_e32 v146, v153
	v_mul_f32_e32 v8, v8, v147
	v_cvt_pk_fp8_f32 v146, v0, v1
	v_med3_f32 v0, v82, s70, v178
	v_med3_f32 v1, v83, s70, v178
	v_mov_b32_e32 v147, v153
	v_cvt_pk_fp8_f32 v147, v0, v1
	v_mul_f32_e32 v5, v96, v5
	v_mul_f32_e32 v5, v5, v182
	v_med3_f32 v0, v80, s70, v178
	v_med3_f32 v1, v81, s70, v178
	v_lshlrev_b32_e32 v182, 4, v180
	v_cvt_pk_fp8_f32 v147, v0, v1 op_sel:[0,0,1]
	v_add_u32_e32 v0, s80, v182
	v_ashrrev_i32_e32 v1, 31, v0
	v_med3_f32 v2, v92, s70, v178
	v_med3_f32 v3, v93, s70, v178
	v_add_u32_sdwa v1, v0, v1 dst_sel:DWORD dst_unused:UNUSED_PAD src0_sel:DWORD src1_sel:BYTE_3
	v_cvt_pk_fp8_f32 v144, v2, v3 op_sel:[0,0,1]
	v_med3_f32 v2, v84, s70, v178
	v_med3_f32 v3, v85, s70, v178
	v_ashrrev_i32_e32 v1, 8, v1
	v_cvt_pk_fp8_f32 v146, v2, v3 op_sel:[0,0,1]
	v_mul_i32_i24_e32 v2, 0x100, v1
	v_sub_u32_e32 v2, v0, v2
	v_ashrrev_i32_e32 v2, 4, v2
	v_bitop3_b32 v2, v2, v1, 15 bitop3:0x78
	v_lshlrev_b32_e32 v3, 4, v2
	v_cmp_gt_i32_e32 vcc, 12, v2
	v_mul_f32_e32 v11, v96, v11
	v_mul_f32_e32 v11, v11, v152
	v_cndmask_b32_e32 v2, 0, v3, vcc
	v_mad_i32_i24 v152, v1, s88, v2
	v_add_u32_e32 v1, 0x2000, v0
	v_ashrrev_i32_e32 v2, 31, v1
	v_add_u32_sdwa v2, v1, v2 dst_sel:DWORD dst_unused:UNUSED_PAD src0_sel:DWORD src1_sel:BYTE_3
	s_mul_i32 s5, s6, 0x6c0000
	v_ashrrev_i32_e32 v2, 8, v2
	s_mul_hi_i32 s4, s6, 0x6c0000
	s_add_u32 s5, s68, s5
	v_mul_i32_i24_e32 v3, 0x100, v2
	s_addc_u32 s4, s69, s4
	v_mul_f32_e32 v4, v96, v4
	v_sub_u32_e32 v3, v1, v3
	s_add_u32 s64, s5, s7
	v_mul_f32_e32 v22, v96, v22
	v_mul_f32_e32 v4, v4, v184
	v_ashrrev_i32_e32 v3, 4, v3
	s_addc_u32 s65, s4, 0
	s_mul_i32 s5, s6, 0x1200000
	v_mul_f32_e32 v22, v22, v142
	v_med3_f32 v4, v4, s70, v178
	v_med3_f32 v5, v5, s70, v178
	v_mov_b32_e32 v142, v153
	v_bitop3_b32 v3, v3, v2, 15 bitop3:0x78
	s_mul_hi_i32 s4, s6, 0x1200000
	s_add_u32 s5, s12, s5
	v_cvt_pk_fp8_f32 v142, v4, v5
	v_lshlrev_b32_e32 v4, 4, v3
	v_cmp_gt_i32_e32 vcc, 12, v3
	s_addc_u32 s6, s13, s4
	s_lshl_b32 s4, s59, 9
	v_cndmask_b32_e32 v3, 0, v4, vcc
	s_add_u32 s4, s5, s4
	v_mul_f32_e32 v48, v48, v96
	v_mul_f32_e32 v49, v49, v96
	v_mad_i32_i24 v154, v2, s88, v3
	v_bfe_u32 v2, v180, 2, 2
	v_lshrrev_b32_e32 v4, 1, v180
	s_addc_u32 s5, s6, 0
	v_mul_f32_e32 v48, v48, v108
	v_mul_f32_e32 v49, v49, v107
	v_mul_f32_e32 v25, v96, v25
	v_and_b32_e32 v3, 48, v182
	v_and_or_b32 v2, v4, 8, v2
	v_ashrrev_i32_e32 v4, 8, v0
	v_lshrrev_b32_e32 v0, 3, v0
	s_movk_i32 s6, 0xc0
	v_mul_f32_e32 v25, v25, v131
	v_med3_f32 v48, v48, s70, v178
	v_med3_f32 v49, v49, s70, v178
	v_mov_b32_e32 v131, v153
	v_and_or_b32 v0, v0, s6, v3
	v_and_b32_e32 v3, 0x7fff0, v4
	v_lshrrev_b32_e32 v4, 1, v4
	s_add_u32 s66, s4, 0x58200100
	v_mul_f32_e32 v23, v96, v23
	v_cvt_pk_fp8_f32 v131, v48, v49
	v_and_b32_e32 v4, 4, v4
	s_addc_u32 s67, s5, 0
	v_mul_f32_e32 v50, v50, v96
	v_mul_f32_e32 v51, v51, v96
	v_mul_f32_e32 v23, v23, v141
	v_med3_f32 v8, v8, s70, v178
	v_med3_f32 v9, v9, s70, v178
	v_mov_b32_e32 v141, v153
	v_or3_b32 v3, v3, v4, v2
	v_ashrrev_i32_e32 v1, 8, v1
	s_add_i32 s56, s80, 0
	v_mul_f32_e32 v50, v50, v106
	v_mul_f32_e32 v51, v51, v105
	v_cvt_pk_fp8_f32 v141, v8, v9
	v_lshl_or_b32 v156, v3, 13, v0
	v_and_b32_e32 v3, 0x7fff0, v1
	v_lshrrev_b32_e32 v1, 1, v1
	s_add_i32 s57, s56, 0x8000
	s_add_i32 s86, s56, 0xa000
	v_ashrrev_i32_e32 v183, 5, v180
	v_med3_f32 v48, v50, s70, v178
	v_med3_f32 v49, v51, s70, v178
	v_and_b32_e32 v1, 4, v1
	s_mov_b32 m0, s57
	s_cmp_lg_u32 0, -1
	v_mul_f32_e32 v7, v96, v7
	v_cvt_pk_fp8_f32 v131, v48, v49 op_sel:[0,0,1]
	v_or3_b32 v1, v3, v1, v2
	global_load_lds_dwordx4 v152, s[64:65]
	s_mov_b32 m0, s86
	s_cselect_b32 s6, 0, 0
	s_add_i32 s91, s56, 0x2000
	v_lshlrev_b32_e32 v48, 1, v183
	v_mul_f32_e32 v7, v7, v158
	v_med3_f32 v8, v10, s70, v178
	v_med3_f32 v9, v11, s70, v178
	v_lshl_or_b32 v158, v1, 13, v0
	global_load_lds_dwordx4 v154, s[64:65]
	s_mov_b32 m0, s56
	s_add_u32 s38, s64, 0x30000
	v_bitop3_b32 v0, v48, v180, 15 bitop3:0x78
	v_cvt_pk_fp8_f32 v141, v8, v9 op_sel:[0,0,1]
	global_load_lds_dwordx4 v156, s[66:67]
	s_mov_b32 m0, s91
	s_addc_u32 s39, s65, 0
	s_add_i32 s95, s56, 0xc000
	v_lshlrev_b32_e32 v49, 8, v181
	v_lshlrev_b32_e32 v8, 4, v0
	v_mul_f32_e32 v6, v96, v6
	global_load_lds_dwordx4 v158, s[66:67]
	s_mov_b32 m0, s95
	s_add_i32 s18, s56, 0xe000
	v_add_u32_e32 v4, v8, v49
	v_mul_f32_e32 v60, v60, v96
	v_mul_f32_e32 v61, v61, v96
	v_mul_f32_e32 v56, v56, v96
	v_mul_f32_e32 v57, v57, v96
	v_mul_f32_e32 v52, v52, v96
	v_mul_f32_e32 v53, v53, v96
	v_mul_f32_e32 v44, v96, v44
	v_mul_f32_e32 v45, v96, v45
	v_mul_f32_e32 v40, v96, v40
	v_mul_f32_e32 v41, v96, v41
	v_mul_f32_e32 v36, v96, v36
	v_mul_f32_e32 v37, v96, v37
	v_mul_f32_e32 v32, v96, v32
	v_mul_f32_e32 v33, v96, v33
	v_mul_f32_e32 v6, v6, v159
	global_load_lds_dwordx4 v152, s[38:39]
	s_mov_b32 m0, s18
	v_add_u32_e32 v184, 0, v4
	v_xor_b32_e32 v4, 16, v4
	v_mul_f32_e32 v60, v60, v104
	v_mul_f32_e32 v61, v61, v103
	v_mul_f32_e32 v56, v56, v100
	v_mul_f32_e32 v57, v57, v99
	v_mul_f32_e32 v52, v52, v112
	v_mul_f32_e32 v53, v53, v111
	v_mul_f32_e32 v44, v44, v120
	v_mul_f32_e32 v45, v45, v119
	v_mul_f32_e32 v40, v40, v116
	v_mul_f32_e32 v41, v41, v115
	v_mul_f32_e32 v36, v36, v128
	v_mul_f32_e32 v37, v37, v127
	v_mul_f32_e32 v32, v32, v124
	v_mul_f32_e32 v33, v33, v123
	v_mul_f32_e32 v29, v96, v29
	v_mul_f32_e32 v30, v96, v30
	v_mul_f32_e32 v31, v96, v31
	v_mul_f32_e32 v24, v96, v24
	v_mul_f32_e32 v26, v96, v26
	v_mul_f32_e32 v27, v96, v27
	v_med3_f32 v6, v6, s70, v178
	v_med3_f32 v7, v7, s70, v178
	global_load_lds_dwordx4 v154, s[38:39]
	v_add_u32_e32 v185, 0, v4
	v_mul_f32_e32 v29, v29, v135
	v_mul_f32_e32 v30, v30, v134
	v_mul_f32_e32 v31, v31, v133
	v_mul_f32_e32 v24, v24, v132
	v_mul_f32_e32 v26, v26, v130
	v_mul_f32_e32 v27, v27, v129
	v_med3_f32 v60, v60, s70, v178
	v_med3_f32 v61, v61, s70, v178
	v_mov_b32_e32 v128, v153
	v_med3_f32 v56, v56, s70, v178
	v_med3_f32 v57, v57, s70, v178
	v_mov_b32_e32 v129, v153
	v_med3_f32 v52, v52, s70, v178
	v_med3_f32 v53, v53, s70, v178
	v_mov_b32_e32 v130, v153
	v_med3_f32 v44, v44, s70, v178
	v_med3_f32 v45, v45, s70, v178
	v_mov_b32_e32 v132, v153
	v_med3_f32 v40, v40, s70, v178
	v_med3_f32 v41, v41, s70, v178
	v_mov_b32_e32 v133, v153
	v_med3_f32 v36, v36, s70, v178
	v_med3_f32 v37, v37, s70, v178
	v_mov_b32_e32 v134, v153
	v_med3_f32 v32, v32, s70, v178
	v_med3_f32 v33, v33, s70, v178
	v_mov_b32_e32 v135, v153
	v_cvt_pk_fp8_f32 v142, v6, v7 op_sel:[0,0,1]
	s_waitcnt vmcnt(0)
	s_waitcnt vmcnt(0) lgkmcnt(0)
	s_barrier
	ds_read_b128 v[0:3], v184 offset:32768
	ds_read_b128 v[4:7], v185 offset:32768
	v_mul_f32_e32 v12, v96, v12
	v_mul_f32_e32 v13, v96, v13
	v_cvt_pk_fp8_f32 v128, v60, v61
	v_cvt_pk_fp8_f32 v129, v56, v57
	v_cvt_pk_fp8_f32 v130, v52, v53
	v_cvt_pk_fp8_f32 v132, v44, v45
	v_cvt_pk_fp8_f32 v133, v40, v41
	v_cvt_pk_fp8_f32 v134, v36, v37
	v_cvt_pk_fp8_f32 v135, v32, v33
	v_mul_f32_e32 v62, v62, v96
	v_mul_f32_e32 v63, v63, v96
	v_mul_f32_e32 v58, v58, v96
	v_mul_f32_e32 v59, v59, v96
	v_mul_f32_e32 v54, v54, v96
	v_mul_f32_e32 v55, v55, v96
	v_mul_f32_e32 v46, v96, v46
	v_mul_f32_e32 v47, v96, v47
	v_mul_f32_e32 v42, v96, v42
	v_mul_f32_e32 v43, v96, v43
	v_mul_f32_e32 v38, v96, v38
	v_mul_f32_e32 v39, v96, v39
	v_mul_f32_e32 v34, v96, v34
	v_mul_f32_e32 v35, v96, v35
	v_mul_f32_e32 v16, v96, v16
	v_mul_f32_e32 v12, v12, v151
	v_mul_f32_e32 v13, v13, v150
	v_mul_f32_e32 v62, v62, v102
	v_mul_f32_e32 v63, v63, v101
	v_mul_f32_e32 v58, v58, v98
	v_mul_f32_e32 v59, v59, v97
	v_mul_f32_e32 v54, v54, v110
	v_mul_f32_e32 v55, v55, v109
	v_mul_f32_e32 v46, v46, v118
	v_mul_f32_e32 v47, v47, v117
	v_mul_f32_e32 v42, v42, v114
	v_mul_f32_e32 v43, v43, v113
	v_mul_f32_e32 v38, v38, v126
	v_mul_f32_e32 v39, v39, v125
	v_mul_f32_e32 v34, v34, v122
	v_mul_f32_e32 v35, v35, v121
	v_mul_f32_e32 v16, v16, v140
	v_med3_f32 v12, v12, s70, v178
	v_med3_f32 v13, v13, s70, v178
	v_mov_b32_e32 v140, v153
	v_med3_f32 v62, v62, s70, v178
	v_med3_f32 v63, v63, s70, v178
	v_med3_f32 v56, v58, s70, v178
	v_med3_f32 v57, v59, s70, v178
	v_med3_f32 v54, v54, s70, v178
	v_med3_f32 v55, v55, s70, v178
	v_med3_f32 v46, v46, s70, v178
	v_med3_f32 v47, v47, s70, v178
	v_med3_f32 v40, v42, s70, v178
	v_med3_f32 v41, v43, s70, v178
	v_med3_f32 v38, v38, s70, v178
	v_med3_f32 v39, v39, s70, v178
	v_med3_f32 v32, v34, s70, v178
	v_med3_f32 v33, v35, s70, v178
	v_cvt_pk_fp8_f32 v140, v12, v13
	v_or_b32_e32 v50, 0x2000, v49
	v_mul_f32_e32 v17, v96, v17
	v_mul_f32_e32 v14, v96, v14
	v_mul_f32_e32 v15, v96, v15
	v_cvt_pk_fp8_f32 v128, v62, v63 op_sel:[0,0,1]
	v_cvt_pk_fp8_f32 v129, v56, v57 op_sel:[0,0,1]
	v_cvt_pk_fp8_f32 v130, v54, v55 op_sel:[0,0,1]
	v_cvt_pk_fp8_f32 v132, v46, v47 op_sel:[0,0,1]
	v_cvt_pk_fp8_f32 v133, v40, v41 op_sel:[0,0,1]
	v_cvt_pk_fp8_f32 v134, v38, v39 op_sel:[0,0,1]
	v_cvt_pk_fp8_f32 v135, v32, v33 op_sel:[0,0,1]
	v_add_u32_e32 v12, v8, v50
	v_mul_f32_e32 v17, v17, v139
	v_mul_f32_e32 v14, v14, v149
	v_mul_f32_e32 v15, v15, v148
	v_xor_b32_e32 v12, 16, v12
	v_med3_f32 v16, v16, s70, v178
	v_med3_f32 v17, v17, s70, v178
	v_mov_b32_e32 v139, v153
	v_med3_f32 v14, v14, s70, v178
	v_med3_f32 v15, v15, s70, v178
	v_add_u32_e32 v186, 0, v12
	v_cvt_pk_fp8_f32 v139, v16, v17
	v_cvt_pk_fp8_f32 v140, v14, v15 op_sel:[0,0,1]
	ds_read_b128 v[8:11], v184 offset:40960
	ds_read_b128 v[12:15], v186 offset:32768
	v_mul_f32_e32 v18, v96, v18
	v_mul_f32_e32 v19, v96, v19
	s_waitcnt lgkmcnt(2)
	v_mfma_f32_32x32x64_f8f6f4 v[32:47], v[0:7], v[128:135], 0
	v_med3_f32 v0, v74, s70, v178
	v_med3_f32 v1, v75, s70, v178
	v_mov_b32_e32 v149, v153
	v_mul_f32_e32 v28, v96, v28
	v_mul_f32_e32 v18, v18, v138
	v_mul_f32_e32 v19, v19, v137
	v_cvt_pk_fp8_f32 v149, v0, v1
	v_mul_f32_e32 v28, v28, v136
	v_med3_f32 v16, v18, s70, v178
	v_med3_f32 v17, v19, s70, v178
	v_med3_f32 v28, v28, s70, v178
	v_med3_f32 v29, v29, s70, v178
	v_mov_b32_e32 v136, v153
	v_med3_f32 v24, v24, s70, v178
	v_med3_f32 v25, v25, s70, v178
	v_mov_b32_e32 v137, v153
	v_med3_f32 v20, v20, s70, v178
	v_med3_f32 v21, v21, s70, v178
	v_mov_b32_e32 v138, v153
	v_cvt_pk_fp8_f32 v139, v16, v17 op_sel:[0,0,1]
	v_med3_f32 v16, v78, s70, v178
	v_med3_f32 v17, v79, s70, v178
	v_mov_b32_e32 v148, v153
	v_cvt_pk_fp8_f32 v136, v28, v29
	v_cvt_pk_fp8_f32 v137, v24, v25
	v_cvt_pk_fp8_f32 v138, v20, v21
	v_cvt_pk_fp8_f32 v148, v16, v17
	v_med3_f32 v0, v70, s70, v178
	v_med3_f32 v1, v71, s70, v178
	v_cvt_pk_fp8_f32 v149, v0, v1 op_sel:[0,0,1]
	v_med3_f32 v0, v68, s70, v178
	v_med3_f32 v1, v69, s70, v178
	v_mov_b32_e32 v150, v153
	v_cvt_pk_fp8_f32 v150, v0, v1
	v_add_u32_e32 v0, 4, v48
	v_med3_f32 v30, v30, s70, v178
	v_med3_f32 v31, v31, s70, v178
	v_med3_f32 v24, v26, s70, v178
	v_med3_f32 v25, v27, s70, v178
	v_med3_f32 v22, v22, s70, v178
	v_med3_f32 v23, v23, s70, v178
	v_med3_f32 v18, v76, s70, v178
	v_med3_f32 v19, v77, s70, v178
	v_bitop3_b32 v0, v0, v180, 15 bitop3:0x78
	v_cvt_pk_fp8_f32 v136, v30, v31 op_sel:[0,0,1]
	v_cvt_pk_fp8_f32 v137, v24, v25 op_sel:[0,0,1]
	v_cvt_pk_fp8_f32 v138, v22, v23 op_sel:[0,0,1]
	v_cvt_pk_fp8_f32 v148, v18, v19 op_sel:[0,0,1]
	s_waitcnt lgkmcnt(0)
	v_mfma_f32_32x32x64_f8f6f4 v[16:31], v[8:15], v[128:135], 0
	v_lshlrev_b32_e32 v8, 4, v0
	v_add_u32_e32 v4, v8, v49
	v_add_u32_e32 v187, 0, v4
	v_xor_b32_e32 v4, 16, v4
	v_add_u32_e32 v188, 0, v4
	ds_read_b128 v[0:3], v187 offset:32768
	ds_read_b128 v[4:7], v188 offset:32768
	v_add_u32_e32 v12, v8, v50
	v_xor_b32_e32 v12, 16, v12
	v_add_u32_e32 v189, 0, v12
	v_med3_f32 v53, v66, s70, v178
	v_med3_f32 v54, v67, s70, v178
	v_mov_b32_e32 v151, v153
	ds_read_b128 v[8:11], v187 offset:40960
	ds_read_b128 v[12:15], v189 offset:32768
	v_cvt_pk_fp8_f32 v151, v53, v54
	s_waitcnt lgkmcnt(2)
	v_mfma_f32_32x32x64_f8f6f4 v[32:47], v[0:7], v[136:143], v[32:47]
	v_med3_f32 v0, v64, s70, v178
	v_med3_f32 v1, v65, s70, v178
	v_cvt_pk_fp8_f32 v151, v0, v1 op_sel:[0,0,1]
	v_lshlrev_b32_e32 v0, 3, v180
	v_and_b32_e32 v1, 0xc0, v182
	v_lshlrev_b32_e32 v2, 1, v180
	v_and_or_b32 v1, v0, 24, v1
	v_and_b32_e32 v2, 32, v2
	v_and_b32_e32 v0, 0x100, v0
	v_or3_b32 v56, v1, v2, v0
	v_add_u32_e32 v0, 8, v48
	v_bitop3_b32 v0, v0, v180, 15 bitop3:0x78
	v_med3_f32 v51, v72, s70, v178
	v_med3_f32 v52, v73, s70, v178
	v_cvt_pk_fp8_f32 v150, v51, v52 op_sel:[0,0,1]
	s_waitcnt lgkmcnt(0)
	v_mfma_f32_32x32x64_f8f6f4 v[16:31], v[8:15], v[136:143], v[16:31]
	v_lshlrev_b32_e32 v8, 4, v0
	v_add_u32_e32 v4, v8, v49
	v_add_u32_e32 v191, 0, v4
	v_xor_b32_e32 v4, 16, v4
	v_add_u32_e32 v192, 0, v4
	ds_read_b128 v[0:3], v191 offset:32768
	ds_read_b128 v[4:7], v192 offset:32768
	v_add_u32_e32 v8, v8, v50
	v_xor_b32_e32 v8, 16, v8
	s_mov_b32 s36, s37
	v_add_u32_e32 v193, 0, v8
	ds_read_b128 v[48:51], v191 offset:40960
	ds_read_b128 v[52:55], v193 offset:32768
	s_mov_b32 s38, s37
	s_mov_b32 s39, s37
	s_waitcnt lgkmcnt(2)
	v_mfma_f32_32x32x64_f8f6f4 v[32:47], v[0:7], v[144:151], v[32:47]
	s_mov_b32 s40, s37
	s_mov_b32 s41, s37
	s_mov_b32 s42, s37
	s_mov_b32 s43, s37
	s_mov_b32 s44, s37
	s_mov_b32 s45, s37
	s_mov_b32 s46, s37
	s_mov_b32 s47, s37
	s_mov_b32 s48, s37
	s_mov_b32 s49, s37
	s_mov_b32 s50, s37
	s_mov_b32 s51, s37
	v_mov_b64_e32 v[0:1], s[36:37]
	v_mov_b64_e32 v[2:3], s[38:39]
	v_mov_b64_e32 v[4:5], s[40:41]
	v_mov_b64_e32 v[6:7], s[42:43]
	v_mov_b64_e32 v[8:9], s[44:45]
	v_mov_b64_e32 v[10:11], s[46:47]
	v_mov_b64_e32 v[12:13], s[48:49]
	v_mov_b64_e32 v[14:15], s[50:51]
	s_add_u32 s38, s64, 0x60000
	s_addc_u32 s39, s65, 0
	s_mov_b32 m0, s57
	s_add_u32 s4, s4, 0x58280100
	s_waitcnt lgkmcnt(0)
	s_barrier
	global_load_lds_dwordx4 v152, s[38:39]
	s_mov_b32 m0, s86
	s_addc_u32 s5, s5, 0
	s_add_i32 s40, s56, 0x4000
	global_load_lds_dwordx4 v154, s[38:39]
	s_mov_b32 m0, s40
	s_add_i32 s41, s56, 0x6000
	global_load_lds_dwordx4 v156, s[4:5]
	s_mov_b32 m0, s41
	v_mfma_f32_32x32x64_f8f6f4 v[16:31], v[48:55], v[144:151], v[16:31]
	global_load_lds_dwordx4 v158, s[4:5]
	v_max_f32_e32 v48, v33, v33
	v_max_f32_e32 v49, v32, v32
	v_max_f32_e32 v48, v49, v48
	v_max3_f32 v48, v48, v34, v35
	v_max3_f32 v48, v48, v36, v37
	v_max3_f32 v48, v48, v38, v39
	v_max3_f32 v48, v48, v40, v41
	v_max3_f32 v48, v48, v42, v43
	v_max3_f32 v48, v48, v44, v45
	v_max3_f32 v48, v48, v46, v47
	s_add_i32 s42, s33, -1
	v_add_u32_e32 v190, s6, v56
	s_mov_b32 s19, 4
	s_nop 5
	v_max3_f32 v48, v48, v16, v17
	v_max3_f32 v48, v48, v18, v19
	v_max3_f32 v48, v48, v20, v21
	v_max3_f32 v48, v48, v22, v23
	v_max3_f32 v48, v48, v24, v25
	v_max3_f32 v48, v48, v26, v27
	v_max3_f32 v48, v48, v28, v29
	v_max3_f32 v48, v48, v30, v31
	v_mov_b32_e32 v49, v48
	s_nop 1
	v_permlane32_swap_b32_e32 v48, v49
	v_max_f32_e32 v49, v49, v49
	v_max_f32_e32 v48, v48, v48
	v_max_f32_e32 v48, v48, v49
	v_add_f32_e32 v49, 0x7149f2ca, v48
	v_cmp_ge_f32_e32 vcc, s93, v49
	s_cmp_eq_u64 vcc, exec
	v_max_f32_e32 v49, 0xf149f2ca, v48
	s_cselect_b64 vcc, -1, 0
	v_cndmask_b32_e32 v195, v49, v179, vcc
	v_mul_f32_e32 v48, 0xbdd53b94, v195
	v_fmamk_f32 v32, v32, 0x3dd53b94, v48
	v_exp_f32_e32 v64, v32
	v_fmamk_f32 v32, v33, 0x3dd53b94, v48
	v_exp_f32_e32 v65, v32
	v_fmamk_f32 v32, v34, 0x3dd53b94, v48
	v_exp_f32_e32 v66, v32
	v_fmamk_f32 v32, v35, 0x3dd53b94, v48
	v_exp_f32_e32 v67, v32
	v_fmamk_f32 v32, v36, 0x3dd53b94, v48
	v_exp_f32_e32 v68, v32
	v_fmamk_f32 v32, v37, 0x3dd53b94, v48
	v_exp_f32_e32 v69, v32
	v_fmamk_f32 v32, v38, 0x3dd53b94, v48
	v_exp_f32_e32 v70, v32
	v_fmamk_f32 v32, v39, 0x3dd53b94, v48
	v_exp_f32_e32 v71, v32
	v_fmamk_f32 v32, v40, 0x3dd53b94, v48
	v_exp_f32_e32 v72, v32
	v_fmamk_f32 v32, v41, 0x3dd53b94, v48
	v_exp_f32_e32 v73, v32
	v_fmamk_f32 v32, v42, 0x3dd53b94, v48
	v_exp_f32_e32 v74, v32
	v_fmamk_f32 v32, v43, 0x3dd53b94, v48
	v_exp_f32_e32 v75, v32
	v_fmamk_f32 v32, v44, 0x3dd53b94, v48
	v_pk_fma_f32 v[86:87], v[22:23], s[54:55], v[48:49] op_sel_hi:[1,0,0]
	v_sub_f32_e32 v22, 0xf149f2ca, v49
	v_exp_f32_e32 v76, v32
	v_fmamk_f32 v32, v45, 0x3dd53b94, v48
	v_mul_f32_e32 v22, 0x3dd53b94, v22
	v_exp_f32_e32 v77, v32
	v_fmamk_f32 v32, v46, 0x3dd53b94, v48
	v_exp_f32_e32 v22, v22
	v_exp_f32_e32 v78, v32
	v_fmamk_f32 v32, v47, 0x3dd53b94, v48
	v_exp_f32_e32 v79, v32
	s_addk_i32 s6, 0x4000
	v_pk_fma_f32 v[94:95], v[30:31], s[54:55], v[48:49] op_sel_hi:[1,0,0]
	v_pk_fma_f32 v[92:93], v[28:29], s[54:55], v[48:49] op_sel_hi:[1,0,0]
	v_pk_fma_f32 v[90:91], v[26:27], s[54:55], v[48:49] op_sel_hi:[1,0,0]
	v_pk_fma_f32 v[88:89], v[24:25], s[54:55], v[48:49] op_sel_hi:[1,0,0]
	v_pk_fma_f32 v[84:85], v[20:21], s[54:55], v[48:49] op_sel_hi:[1,0,0]
	v_pk_fma_f32 v[82:83], v[18:19], s[54:55], v[48:49] op_sel_hi:[1,0,0]
	v_pk_fma_f32 v[80:81], v[16:17], s[54:55], v[48:49] op_sel_hi:[1,0,0]
	v_cndmask_b32_e64 v201, v22, 1.0, vcc
	v_add_u32_e32 v199, s6, v56
	v_mov_b64_e32 v[62:63], v[14:15]
	v_mov_b64_e32 v[46:47], v[14:15]
	v_mov_b64_e32 v[30:31], v[14:15]
	v_mov_b32_e32 v155, v153
	v_mov_b32_e32 v157, v153
	v_mov_b32_e32 v159, v153
	v_cmp_gt_u32_e64 s[4:5], 32, v180
	v_lshl_add_u32 v197, v181, 2, s77
	v_lshlrev_b32_e32 v196, 4, v183
	v_mov_b32_e32 v198, 0
	v_mov_b64_e32 v[60:61], v[12:13]
	v_mov_b64_e32 v[58:59], v[10:11]
	v_mov_b64_e32 v[56:57], v[8:9]
	v_mov_b64_e32 v[54:55], v[6:7]
	v_mov_b64_e32 v[52:53], v[4:5]
	v_mov_b64_e32 v[50:51], v[2:3]
	v_mov_b64_e32 v[48:49], v[0:1]
	v_mov_b64_e32 v[44:45], v[12:13]
	v_mov_b64_e32 v[42:43], v[10:11]
	v_mov_b64_e32 v[40:41], v[8:9]
	v_mov_b64_e32 v[38:39], v[6:7]
	v_mov_b64_e32 v[36:37], v[4:5]
	v_mov_b64_e32 v[34:35], v[2:3]
	v_mov_b64_e32 v[32:33], v[0:1]
	v_mov_b64_e32 v[28:29], v[12:13]
	v_mov_b64_e32 v[26:27], v[10:11]
	v_mov_b64_e32 v[24:25], v[8:9]
	v_mov_b64_e32 v[22:23], v[6:7]
	v_mov_b64_e32 v[20:21], v[4:5]
	v_mov_b64_e32 v[18:19], v[2:3]
	v_mov_b64_e32 v[16:17], v[0:1]
	s_mov_b32 vcc_lo, 0

.LBB0_595:
	s_add_u32 s40, s8, s38
	s_addc_u32 s41, s9, s39
	s_add_u32 s42, s40, 0x6ea00100
	ds_read_b128 v[176:179], v188
	ds_read_b128 v[196:199], v188 offset:2048
	ds_read_b128 v[180:183], v189
	ds_read_b128 v[200:203], v189 offset:2048
	s_addc_u32 s43, s41, 0
	s_add_u32 s68, s1, s38
	s_addc_u32 s69, s56, s39
	s_cmpk_eq_i32 s38, 0x700
	s_cselect_b64 vcc, -1, 0
	s_and_b64 s[40:41], vcc, exec
	ds_read_b128 v[204:207], v186
	ds_read_b128 v[212:215], v186 offset:2048
	ds_read_b128 v[208:211], v187
	ds_read_b128 v[216:219], v187 offset:2048
	ds_read_b128 v[220:223], v186 offset:4096
	ds_read_b128 v[228:231], v186 offset:6144
	ds_read_b128 v[224:227], v187 offset:4096
	ds_read_b128 v[232:235], v187 offset:6144
	s_waitcnt vmcnt(6)
	s_waitcnt lgkmcnt(8)
	s_barrier
	s_waitcnt lgkmcnt(0)
	v_cndmask_b32_e32 v184, v166, v139, vcc
	s_setprio 1
	s_waitcnt lgkmcnt(0)
	v_mfma_f32_16x16x128_f8f6f4 v[124:127], v[176:183], v[204:211], v[124:127]
	v_mfma_f32_16x16x128_f8f6f4 v[120:123], v[196:203], v[204:211], v[120:123]
	v_mfma_f32_16x16x128_f8f6f4 v[116:119], v[176:183], v[212:219], v[116:119]
	v_mfma_f32_16x16x128_f8f6f4 v[112:115], v[196:203], v[212:219], v[112:115]
	v_mfma_f32_16x16x128_f8f6f4 v[92:95], v[176:183], v[220:227], v[92:95]
	v_mfma_f32_16x16x128_f8f6f4 v[88:91], v[196:203], v[220:227], v[88:91]
	v_mfma_f32_16x16x128_f8f6f4 v[84:87], v[176:183], v[228:235], v[84:87]
	v_mfma_f32_16x16x128_f8f6f4 v[80:83], v[196:203], v[228:235], v[80:83]
	s_setprio 0
	s_barrier
	ds_read_b128 v[176:179], v188 offset:16384
	ds_read_b128 v[196:199], v188 offset:18432
	ds_read_b128 v[180:183], v189 offset:16384
	ds_read_b128 v[200:203], v189 offset:18432
	v_cndmask_b32_e32 v132, v151, v135, vcc
	s_cselect_b32 s43, s13, s43
	s_cselect_b32 s42, s12, s42
	s_cselect_b32 s41, s37, s69
	s_cselect_b32 s40, s36, s68
	v_cndmask_b32_e32 v155, v168, v143, vcc
	s_mov_b32 m0, s63
	v_lshl_add_u64 v[252:253], v[174:175], 0, s[38:39]
	global_load_lds_dwordx4 v[252:253], off
	v_lshl_add_u64 v[252:253], v[172:173], 0, s[38:39]
	s_mov_b32 m0, s64
	s_nop 0
	global_load_lds_dwordx4 v[252:253], off
	s_barrier
	s_waitcnt lgkmcnt(0)
	s_setprio 1
	v_mfma_f32_16x16x128_f8f6f4 v[108:111], v[176:183], v[204:211], v[108:111]
	v_mfma_f32_16x16x128_f8f6f4 v[104:107], v[196:203], v[204:211], v[104:107]
	v_mfma_f32_16x16x128_f8f6f4 v[100:103], v[176:183], v[212:219], v[100:103]
	v_mfma_f32_16x16x128_f8f6f4 v[96:99], v[196:203], v[212:219], v[96:99]
	v_mfma_f32_16x16x128_f8f6f4 v[76:79], v[176:183], v[220:227], v[76:79]
	v_mfma_f32_16x16x128_f8f6f4 v[72:75], v[196:203], v[220:227], v[72:75]
	v_mfma_f32_16x16x128_f8f6f4 v[68:71], v[176:183], v[228:235], v[68:71]
	v_mfma_f32_16x16x128_f8f6f4 v[64:67], v[196:203], v[228:235], v[64:67]
	s_setprio 0
	s_barrier
	ds_read_b128 v[196:199], v188
	ds_read_b128 v[204:207], v188 offset:2048
	ds_read_b128 v[200:203], v189
	ds_read_b128 v[208:211], v189 offset:2048
	s_mov_b32 m0, s33
	ds_read_b128 v[212:215], v186 offset:16384
	ds_read_b128 v[220:223], v186 offset:18432
	ds_read_b128 v[216:219], v187 offset:16384
	ds_read_b128 v[224:227], v187 offset:18432
	ds_read_b128 v[228:231], v186 offset:20480
	ds_read_b128 v[236:239], v186 offset:22528
	ds_read_b128 v[232:235], v187 offset:20480
	ds_read_b128 v[240:243], v187 offset:22528
	global_load_lds_dwordx4 v132, s[42:43]
	s_mov_b32 m0, s46
	v_mov_b32_e32 v185, v133
	global_load_lds_dwordx4 v184, s[42:43]
	s_waitcnt lgkmcnt(8)
	s_barrier
	s_waitcnt lgkmcnt(0)
	v_lshl_add_u64 v[182:183], s[42:43], 0, v[132:133]
	v_lshl_add_u64 v[180:181], s[42:43], 0, v[184:185]
	s_setprio 1
	s_waitcnt lgkmcnt(0)
	v_mfma_f32_16x16x128_f8f6f4 v[60:63], v[196:203], v[212:219], v[60:63]
	v_mfma_f32_16x16x128_f8f6f4 v[56:59], v[204:211], v[212:219], v[56:59]
	v_mfma_f32_16x16x128_f8f6f4 v[52:55], v[196:203], v[220:227], v[52:55]
	v_mfma_f32_16x16x128_f8f6f4 v[48:51], v[204:211], v[220:227], v[48:51]
	v_mfma_f32_16x16x128_f8f6f4 v[28:31], v[196:203], v[228:235], v[28:31]
	v_mfma_f32_16x16x128_f8f6f4 v[24:27], v[204:211], v[228:235], v[24:27]
	v_mfma_f32_16x16x128_f8f6f4 v[20:23], v[196:203], v[236:243], v[20:23]
	v_mfma_f32_16x16x128_f8f6f4 v[16:19], v[204:211], v[236:243], v[16:19]
	s_setprio 0
	s_barrier
	s_mov_b32 m0, s44
	v_lshl_add_u64 v[176:177], s[40:41], 0, v[130:131]
	ds_read_b128 v[196:199], v188 offset:16384
	ds_read_b128 v[204:207], v188 offset:18432
	ds_read_b128 v[200:203], v189 offset:16384
	ds_read_b128 v[208:211], v189 offset:18432
	global_load_lds_dwordx4 v[176:177], off
	v_lshl_add_u64 v[178:179], s[40:41], 0, v[128:129]
	s_mov_b32 m0, s45
	s_nop 0
	global_load_lds_dwordx4 v[178:179], off
	s_waitcnt vmcnt(8)
	s_waitcnt lgkmcnt(0)
	s_barrier
	s_setprio 1
	s_waitcnt lgkmcnt(0)
	v_mfma_f32_16x16x128_f8f6f4 v[44:47], v[196:203], v[212:219], v[44:47]
	v_mfma_f32_16x16x128_f8f6f4 v[40:43], v[204:211], v[212:219], v[40:43]
	v_mfma_f32_16x16x128_f8f6f4 v[36:39], v[196:203], v[220:227], v[36:39]
	v_mfma_f32_16x16x128_f8f6f4 v[32:35], v[204:211], v[220:227], v[32:35]
	v_mfma_f32_16x16x128_f8f6f4 v[12:15], v[196:203], v[228:235], v[12:15]
	v_mfma_f32_16x16x128_f8f6f4 v[8:11], v[204:211], v[228:235], v[8:11]
	v_mfma_f32_16x16x128_f8f6f4 v[4:7], v[196:203], v[236:243], v[4:7]
	v_mfma_f32_16x16x128_f8f6f4 v[0:3], v[204:211], v[236:243], v[0:3]
	s_setprio 0
	s_barrier
	ds_read_b128 v[196:199], v188 offset:32768
	ds_read_b128 v[204:207], v188 offset:34816
	ds_read_b128 v[200:203], v189 offset:32768
	ds_read_b128 v[208:211], v189 offset:34816
	s_mov_b32 m0, s49
	ds_read_b128 v[212:215], v186 offset:32768
	ds_read_b128 v[220:223], v186 offset:34816
	ds_read_b128 v[216:219], v187 offset:32768
	ds_read_b128 v[224:227], v187 offset:34816
	ds_read_b128 v[228:231], v186 offset:36864
	ds_read_b128 v[236:239], v186 offset:38912
	ds_read_b128 v[232:235], v187 offset:36864
	ds_read_b128 v[240:243], v187 offset:38912
	v_cndmask_b32_e32 v132, v170, v147, vcc
	global_load_lds_dwordx4 v155, s[42:43]
	s_mov_b32 m0, s50
	s_nop 0
	global_load_lds_dwordx4 v132, s[42:43]
	s_waitcnt vmcnt(8)
	s_waitcnt lgkmcnt(8)
	s_barrier
	s_waitcnt lgkmcnt(0)
	s_setprio 1
	v_mfma_f32_16x16x128_f8f6f4 v[124:127], v[196:203], v[212:219], v[124:127]
	v_mfma_f32_16x16x128_f8f6f4 v[120:123], v[204:211], v[212:219], v[120:123]
	v_mfma_f32_16x16x128_f8f6f4 v[116:119], v[196:203], v[220:227], v[116:119]
	v_mfma_f32_16x16x128_f8f6f4 v[112:115], v[204:211], v[220:227], v[112:115]
	v_mfma_f32_16x16x128_f8f6f4 v[92:95], v[196:203], v[228:235], v[92:95]
	v_mfma_f32_16x16x128_f8f6f4 v[88:91], v[204:211], v[228:235], v[88:91]
	v_mfma_f32_16x16x128_f8f6f4 v[84:87], v[196:203], v[236:243], v[84:87]
	v_mfma_f32_16x16x128_f8f6f4 v[80:83], v[204:211], v[236:243], v[80:83]
	s_setprio 0
	s_barrier
	ds_read_b128 v[196:199], v188 offset:49152
	ds_read_b128 v[204:207], v188 offset:51200
	ds_read_b128 v[200:203], v189 offset:49152
	ds_read_b128 v[208:211], v189 offset:51200
	s_add_u32 s42, s40, 0x40000
	s_addc_u32 s43, s41, 0
	v_lshl_add_u64 v[184:185], s[42:43], 0, v[130:131]
	s_mov_b32 m0, s47
	s_nop 0
	global_load_lds_dwordx4 v[184:185], off
	v_lshl_add_u64 v[184:185], s[42:43], 0, v[128:129]
	s_mov_b32 m0, s48
	s_nop 0
	global_load_lds_dwordx4 v[184:185], off
	s_waitcnt vmcnt(8)
	s_barrier
	s_waitcnt lgkmcnt(0)
	s_setprio 1
	v_mfma_f32_16x16x128_f8f6f4 v[108:111], v[196:203], v[212:219], v[108:111]
	v_mfma_f32_16x16x128_f8f6f4 v[104:107], v[204:211], v[212:219], v[104:107]
	v_mfma_f32_16x16x128_f8f6f4 v[100:103], v[196:203], v[220:227], v[100:103]
	v_mfma_f32_16x16x128_f8f6f4 v[96:99], v[204:211], v[220:227], v[96:99]
	v_mfma_f32_16x16x128_f8f6f4 v[76:79], v[196:203], v[228:235], v[76:79]
	v_mfma_f32_16x16x128_f8f6f4 v[72:75], v[204:211], v[228:235], v[72:75]
	v_mfma_f32_16x16x128_f8f6f4 v[68:71], v[196:203], v[236:243], v[68:71]
	v_mfma_f32_16x16x128_f8f6f4 v[64:67], v[204:211], v[236:243], v[64:67]
	s_setprio 0
	s_barrier
	ds_read_b128 v[196:199], v188 offset:32768
	ds_read_b128 v[204:207], v188 offset:34816
	ds_read_b128 v[200:203], v189 offset:32768
	ds_read_b128 v[208:211], v189 offset:34816
	s_mov_b32 m0, s55
	v_lshl_add_u64 v[182:183], v[182:183], 0, s[20:21]
	ds_read_b128 v[212:215], v186 offset:49152
	ds_read_b128 v[220:223], v186 offset:51200
	ds_read_b128 v[216:219], v187 offset:49152
	ds_read_b128 v[224:227], v187 offset:51200
	ds_read_b128 v[228:231], v186 offset:53248
	ds_read_b128 v[236:239], v186 offset:55296
	ds_read_b128 v[232:235], v187 offset:53248
	ds_read_b128 v[240:243], v187 offset:55296
	global_load_lds_dwordx4 v[182:183], off
	v_lshl_add_u64 v[180:181], v[180:181], 0, s[20:21]
	s_mov_b32 m0, s58
	s_nop 0
	global_load_lds_dwordx4 v[180:181], off
	s_waitcnt lgkmcnt(8)
	s_barrier
	s_waitcnt lgkmcnt(0)
	s_setprio 1
	v_mfma_f32_16x16x128_f8f6f4 v[60:63], v[196:203], v[212:219], v[60:63]
	v_mfma_f32_16x16x128_f8f6f4 v[56:59], v[204:211], v[212:219], v[56:59]
	v_mfma_f32_16x16x128_f8f6f4 v[52:55], v[196:203], v[220:227], v[52:55]
	v_mfma_f32_16x16x128_f8f6f4 v[48:51], v[204:211], v[220:227], v[48:51]
	v_mfma_f32_16x16x128_f8f6f4 v[28:31], v[196:203], v[228:235], v[28:31]
	v_mfma_f32_16x16x128_f8f6f4 v[24:27], v[204:211], v[228:235], v[24:27]
	v_mfma_f32_16x16x128_f8f6f4 v[20:23], v[196:203], v[236:243], v[20:23]
	v_mfma_f32_16x16x128_f8f6f4 v[16:19], v[204:211], v[236:243], v[16:19]
	s_setprio 0
	s_barrier
	s_mov_b32 m0, s53
	v_lshl_add_u64 v[176:177], v[176:177], 0, s[20:21]
	ds_read_b128 v[196:199], v188 offset:49152
	ds_read_b128 v[204:207], v188 offset:51200
	ds_read_b128 v[200:203], v189 offset:49152
	ds_read_b128 v[208:211], v189 offset:51200
	global_load_lds_dwordx4 v[176:177], off
	v_lshl_add_u64 v[176:177], v[178:179], 0, s[20:21]
	s_mov_b32 m0, s54
	s_nop 0
	global_load_lds_dwordx4 v[176:177], off
	s_waitcnt vmcnt(8)
	s_waitcnt lgkmcnt(0)
	s_barrier
	s_setprio 1
	s_waitcnt lgkmcnt(0)
	v_mfma_f32_16x16x128_f8f6f4 v[44:47], v[196:203], v[212:219], v[44:47]
	v_mfma_f32_16x16x128_f8f6f4 v[40:43], v[204:211], v[212:219], v[40:43]
	v_mfma_f32_16x16x128_f8f6f4 v[36:39], v[196:203], v[220:227], v[36:39]
	v_mfma_f32_16x16x128_f8f6f4 v[32:35], v[204:211], v[220:227], v[32:35]
	v_mfma_f32_16x16x128_f8f6f4 v[12:15], v[196:203], v[228:235], v[12:15]
	v_mfma_f32_16x16x128_f8f6f4 v[8:11], v[204:211], v[228:235], v[8:11]
	v_mfma_f32_16x16x128_f8f6f4 v[4:7], v[196:203], v[236:243], v[4:7]
	v_mfma_f32_16x16x128_f8f6f4 v[0:3], v[204:211], v[236:243], v[0:3]
	s_setprio 0
	s_barrier
	s_add_u32 s40, s40, 0x40080
	s_addc_u32 s41, s41, 0
	s_mov_b32 m0, s59
	v_lshl_add_u64 v[176:177], s[40:41], 0, v[130:131]
	global_load_lds_dwordx4 v[176:177], off
	v_lshl_add_u64 v[176:177], s[40:41], 0, v[128:129]
	s_mov_b32 m0, s60
	s_add_i32 s57, s57, 2
	global_load_lds_dwordx4 v[176:177], off
	s_add_u32 s38, s38, 0x100
	s_addc_u32 s39, s39, 0
	s_cmp_gt_u32 s57, 13
	s_cbranch_scc0 .LBB0_595
	s_and_b64 vcc, exec, s[26:27]
	s_cbranch_vccz .LBB0_598
	s_barrier

.LBB0_736:
	s_add_u32 s46, s8, s44
	s_addc_u32 s47, s9, s45
	s_add_u32 s48, s46, 0x49800100
	ds_read_b128 v[160:163], v148
	ds_read_b128 v[164:167], v148 offset:1024
	ds_read_b128 v[168:171], v148 offset:2048
	ds_read_b128 v[172:175], v148 offset:3072
	s_addc_u32 s49, s47, 0
	s_add_u32 s83, s80, s44
	s_addc_u32 s84, s81, s45
	s_cmpk_eq_i32 s44, 0x300
	s_cselect_b64 vcc, -1, 0
	s_and_b64 s[46:47], vcc, exec
	v_cndmask_b32_e32 v132, v158, v154, vcc
	s_cselect_b32 s49, s11, s49
	s_cselect_b32 s48, s10, s48
	s_cselect_b32 s47, s43, s84
	s_cselect_b32 s46, s42, s83
	v_cndmask_b32_e32 v139, v138, v156, vcc
	s_mov_b32 m0, s71
	v_lshl_add_u64 v[192:193], v[144:145], 0, s[44:45]
	ds_read_b128 v[176:179], v147
	ds_read_b128 v[180:183], v147 offset:1024
	ds_read_b128 v[184:187], v147 offset:2048
	ds_read_b128 v[188:191], v147 offset:3072
	ds_read_b128 v[196:199], v147 offset:4096
	ds_read_b128 v[200:203], v147 offset:5120
	ds_read_b128 v[204:207], v147 offset:6144
	ds_read_b128 v[208:211], v147 offset:7168
	global_load_lds_dwordx4 v[192:193], off
	v_lshl_add_u64 v[192:193], v[142:143], 0, s[44:45]
	s_mov_b32 m0, s72
	s_nop 0
	global_load_lds_dwordx4 v[192:193], off
	s_waitcnt lgkmcnt(8)
	s_barrier
	s_waitcnt lgkmcnt(0)
	v_cndmask_b32_e32 v192, v136, v155, vcc
	s_setprio 1
	s_waitcnt lgkmcnt(0)
	v_mfma_f32_16x16x32_bf16 v[124:127], v[160:163], v[176:179], v[124:127]
	v_mfma_f32_16x16x32_bf16 v[120:123], v[168:171], v[176:179], v[120:123]
	v_mfma_f32_16x16x32_bf16 v[116:119], v[160:163], v[184:187], v[116:119]
	v_mfma_f32_16x16x32_bf16 v[104:107], v[168:171], v[184:187], v[104:107]
	v_mfma_f32_16x16x32_bf16 v[96:99], v[160:163], v[196:199], v[96:99]
	v_mfma_f32_16x16x32_bf16 v[92:95], v[168:171], v[196:199], v[92:95]
	v_mfma_f32_16x16x32_bf16 v[84:87], v[160:163], v[204:207], v[84:87]
	v_mfma_f32_16x16x32_bf16 v[72:75], v[168:171], v[204:207], v[72:75]
	v_mfma_f32_16x16x32_bf16 v[124:127], v[164:167], v[180:183], v[124:127]
	v_mfma_f32_16x16x32_bf16 v[120:123], v[172:175], v[180:183], v[120:123]
	v_mfma_f32_16x16x32_bf16 v[116:119], v[164:167], v[188:191], v[116:119]
	v_mfma_f32_16x16x32_bf16 v[104:107], v[172:175], v[188:191], v[104:107]
	v_mfma_f32_16x16x32_bf16 v[96:99], v[164:167], v[200:203], v[96:99]
	v_mfma_f32_16x16x32_bf16 v[92:95], v[172:175], v[200:203], v[92:95]
	v_mfma_f32_16x16x32_bf16 v[84:87], v[164:167], v[208:211], v[84:87]
	v_mfma_f32_16x16x32_bf16 v[72:75], v[172:175], v[208:211], v[72:75]
	s_setprio 0
	s_barrier
	s_mov_b32 m0, s55
	v_lshl_add_u64 v[228:229], s[46:47], 0, v[130:131]
	ds_read_b128 v[212:215], v148 offset:16384
	ds_read_b128 v[216:219], v148 offset:17408
	ds_read_b128 v[220:223], v148 offset:18432
	ds_read_b128 v[224:227], v148 offset:19456
	global_load_lds_dwordx4 v[228:229], off
	v_lshl_add_u64 v[230:231], s[46:47], 0, v[128:129]
	s_mov_b32 m0, s56
	s_nop 0
	global_load_lds_dwordx4 v[230:231], off
	s_barrier
	s_waitcnt lgkmcnt(0)
	s_setprio 1
	v_mfma_f32_16x16x32_bf16 v[112:115], v[212:215], v[176:179], v[112:115]
	v_mfma_f32_16x16x32_bf16 v[108:111], v[220:223], v[176:179], v[108:111]
	v_mfma_f32_16x16x32_bf16 v[100:103], v[212:215], v[184:187], v[100:103]
	v_mfma_f32_16x16x32_bf16 v[88:91], v[220:223], v[184:187], v[88:91]
	v_mfma_f32_16x16x32_bf16 v[80:83], v[212:215], v[196:199], v[80:83]
	v_mfma_f32_16x16x32_bf16 v[76:79], v[220:223], v[196:199], v[76:79]
	v_mfma_f32_16x16x32_bf16 v[68:71], v[212:215], v[204:207], v[68:71]
	v_mfma_f32_16x16x32_bf16 v[64:67], v[220:223], v[204:207], v[64:67]
	v_mfma_f32_16x16x32_bf16 v[112:115], v[216:219], v[180:183], v[112:115]
	v_mfma_f32_16x16x32_bf16 v[108:111], v[224:227], v[180:183], v[108:111]
	v_mfma_f32_16x16x32_bf16 v[100:103], v[216:219], v[188:191], v[100:103]
	v_mfma_f32_16x16x32_bf16 v[88:91], v[224:227], v[188:191], v[88:91]
	v_mfma_f32_16x16x32_bf16 v[80:83], v[216:219], v[200:203], v[80:83]
	v_mfma_f32_16x16x32_bf16 v[76:79], v[224:227], v[200:203], v[76:79]
	v_mfma_f32_16x16x32_bf16 v[68:71], v[216:219], v[208:211], v[68:71]
	v_mfma_f32_16x16x32_bf16 v[64:67], v[224:227], v[208:211], v[64:67]
	s_setprio 0
	s_mov_b32 m0, s54
	s_barrier
	ds_read_b128 v[176:179], v147 offset:16384
	ds_read_b128 v[180:183], v147 offset:17408
	ds_read_b128 v[184:187], v147 offset:18432
	ds_read_b128 v[188:191], v147 offset:19456
	ds_read_b128 v[196:199], v147 offset:20480
	ds_read_b128 v[200:203], v147 offset:21504
	ds_read_b128 v[204:207], v147 offset:22528
	ds_read_b128 v[208:211], v147 offset:23552
	global_load_lds_dwordx4 v132, s[48:49]
	s_mov_b32 m0, s57
	v_mov_b32_e32 v193, v133
	global_load_lds_dwordx4 v192, s[48:49]
	s_barrier
	s_waitcnt lgkmcnt(0)
	v_lshl_add_u64 v[232:233], s[48:49], 0, v[132:133]
	v_lshl_add_u64 v[192:193], s[48:49], 0, v[192:193]
	s_setprio 1
	s_waitcnt lgkmcnt(0)
	v_mfma_f32_16x16x32_bf16 v[60:63], v[160:163], v[176:179], v[60:63]
	v_mfma_f32_16x16x32_bf16 v[56:59], v[168:171], v[176:179], v[56:59]
	v_mfma_f32_16x16x32_bf16 v[48:51], v[160:163], v[184:187], v[48:51]
	v_mfma_f32_16x16x32_bf16 v[44:47], v[168:171], v[184:187], v[44:47]
	v_mfma_f32_16x16x32_bf16 v[36:39], v[160:163], v[196:199], v[36:39]
	v_mfma_f32_16x16x32_bf16 v[24:27], v[168:171], v[196:199], v[24:27]
	v_mfma_f32_16x16x32_bf16 v[16:19], v[160:163], v[204:207], v[16:19]
	v_mfma_f32_16x16x32_bf16 v[8:11], v[168:171], v[204:207], v[8:11]
	v_mfma_f32_16x16x32_bf16 v[60:63], v[164:167], v[180:183], v[60:63]
	v_mfma_f32_16x16x32_bf16 v[56:59], v[172:175], v[180:183], v[56:59]
	v_mfma_f32_16x16x32_bf16 v[48:51], v[164:167], v[188:191], v[48:51]
	v_mfma_f32_16x16x32_bf16 v[44:47], v[172:175], v[188:191], v[44:47]
	v_mfma_f32_16x16x32_bf16 v[36:39], v[164:167], v[200:203], v[36:39]
	v_mfma_f32_16x16x32_bf16 v[24:27], v[172:175], v[200:203], v[24:27]
	v_mfma_f32_16x16x32_bf16 v[16:19], v[164:167], v[208:211], v[16:19]
	v_mfma_f32_16x16x32_bf16 v[8:11], v[172:175], v[208:211], v[8:11]
	s_setprio 0
	s_barrier
	s_add_u32 s84, s46, 0x80000
	s_addc_u32 s85, s47, 0
	s_mov_b32 m0, s58
	v_lshl_add_u64 v[160:161], s[84:85], 0, v[130:131]
	global_load_lds_dwordx4 v[160:161], off
	v_lshl_add_u64 v[160:161], s[84:85], 0, v[128:129]
	s_mov_b32 m0, s59
	s_nop 0
	global_load_lds_dwordx4 v[160:161], off
	s_waitcnt vmcnt(6)
	s_barrier
	s_setprio 1
	v_mfma_f32_16x16x32_bf16 v[52:55], v[212:215], v[176:179], v[52:55]
	v_mfma_f32_16x16x32_bf16 v[40:43], v[220:223], v[176:179], v[40:43]
	v_mfma_f32_16x16x32_bf16 v[32:35], v[212:215], v[184:187], v[32:35]
	v_mfma_f32_16x16x32_bf16 v[28:31], v[220:223], v[184:187], v[28:31]
	v_mfma_f32_16x16x32_bf16 v[20:23], v[212:215], v[196:199], v[20:23]
	v_mfma_f32_16x16x32_bf16 v[12:15], v[220:223], v[196:199], v[12:15]
	v_mfma_f32_16x16x32_bf16 v[4:7], v[212:215], v[204:207], v[4:7]
	v_mfma_f32_16x16x32_bf16 v[0:3], v[220:223], v[204:207], v[0:3]
	v_mfma_f32_16x16x32_bf16 v[52:55], v[216:219], v[180:183], v[52:55]
	v_mfma_f32_16x16x32_bf16 v[40:43], v[224:227], v[180:183], v[40:43]
	v_mfma_f32_16x16x32_bf16 v[32:35], v[216:219], v[188:191], v[32:35]
	v_mfma_f32_16x16x32_bf16 v[28:31], v[224:227], v[188:191], v[28:31]
	v_mfma_f32_16x16x32_bf16 v[20:23], v[216:219], v[200:203], v[20:23]
	v_mfma_f32_16x16x32_bf16 v[12:15], v[224:227], v[200:203], v[12:15]
	v_mfma_f32_16x16x32_bf16 v[4:7], v[216:219], v[208:211], v[4:7]
	v_mfma_f32_16x16x32_bf16 v[0:3], v[224:227], v[208:211], v[0:3]
	s_setprio 0
	s_barrier
	ds_read_b128 v[160:163], v148 offset:32768
	ds_read_b128 v[164:167], v148 offset:33792
	ds_read_b128 v[168:171], v148 offset:34816
	ds_read_b128 v[172:175], v148 offset:35840
	s_mov_b32 m0, s60
	ds_read_b128 v[176:179], v147 offset:32768
	ds_read_b128 v[180:183], v147 offset:33792
	ds_read_b128 v[184:187], v147 offset:34816
	ds_read_b128 v[188:191], v147 offset:35840
	ds_read_b128 v[196:199], v147 offset:36864
	ds_read_b128 v[200:203], v147 offset:37888
	ds_read_b128 v[204:207], v147 offset:38912
	ds_read_b128 v[208:211], v147 offset:39936
	v_cndmask_b32_e32 v132, v140, v157, vcc
	global_load_lds_dwordx4 v139, s[48:49]
	s_mov_b32 m0, s61
	s_nop 0
	global_load_lds_dwordx4 v132, s[48:49]
	s_waitcnt lgkmcnt(8)
	s_barrier
	s_waitcnt lgkmcnt(0)
	s_setprio 1
	v_mfma_f32_16x16x32_bf16 v[124:127], v[160:163], v[176:179], v[124:127]
	v_mfma_f32_16x16x32_bf16 v[120:123], v[168:171], v[176:179], v[120:123]
	v_mfma_f32_16x16x32_bf16 v[116:119], v[160:163], v[184:187], v[116:119]
	v_mfma_f32_16x16x32_bf16 v[104:107], v[168:171], v[184:187], v[104:107]
	v_mfma_f32_16x16x32_bf16 v[96:99], v[160:163], v[196:199], v[96:99]
	v_mfma_f32_16x16x32_bf16 v[92:95], v[168:171], v[196:199], v[92:95]
	v_mfma_f32_16x16x32_bf16 v[84:87], v[160:163], v[204:207], v[84:87]
	v_mfma_f32_16x16x32_bf16 v[72:75], v[168:171], v[204:207], v[72:75]
	v_mfma_f32_16x16x32_bf16 v[124:127], v[164:167], v[180:183], v[124:127]
	v_mfma_f32_16x16x32_bf16 v[120:123], v[172:175], v[180:183], v[120:123]
	v_mfma_f32_16x16x32_bf16 v[116:119], v[164:167], v[188:191], v[116:119]
	v_mfma_f32_16x16x32_bf16 v[104:107], v[172:175], v[188:191], v[104:107]
	v_mfma_f32_16x16x32_bf16 v[96:99], v[164:167], v[200:203], v[96:99]
	v_mfma_f32_16x16x32_bf16 v[92:95], v[172:175], v[200:203], v[92:95]
	v_mfma_f32_16x16x32_bf16 v[84:87], v[164:167], v[208:211], v[84:87]
	v_mfma_f32_16x16x32_bf16 v[72:75], v[172:175], v[208:211], v[72:75]
	s_setprio 0
	s_barrier
	s_mov_b32 m0, s64
	v_lshl_add_u64 v[228:229], v[228:229], 0, s[14:15]
	ds_read_b128 v[212:215], v148 offset:49152
	ds_read_b128 v[216:219], v148 offset:50176
	ds_read_b128 v[220:223], v148 offset:51200
	ds_read_b128 v[224:227], v148 offset:52224
	global_load_lds_dwordx4 v[228:229], off
	v_lshl_add_u64 v[228:229], v[230:231], 0, s[14:15]
	s_mov_b32 m0, s65
	s_nop 0
	global_load_lds_dwordx4 v[228:229], off
	s_barrier
	s_waitcnt lgkmcnt(0)
	s_setprio 1
	v_mfma_f32_16x16x32_bf16 v[112:115], v[212:215], v[176:179], v[112:115]
	v_mfma_f32_16x16x32_bf16 v[108:111], v[220:223], v[176:179], v[108:111]
	v_mfma_f32_16x16x32_bf16 v[100:103], v[212:215], v[184:187], v[100:103]
	v_mfma_f32_16x16x32_bf16 v[88:91], v[220:223], v[184:187], v[88:91]
	v_mfma_f32_16x16x32_bf16 v[80:83], v[212:215], v[196:199], v[80:83]
	v_mfma_f32_16x16x32_bf16 v[76:79], v[220:223], v[196:199], v[76:79]
	v_mfma_f32_16x16x32_bf16 v[68:71], v[212:215], v[204:207], v[68:71]
	v_mfma_f32_16x16x32_bf16 v[64:67], v[220:223], v[204:207], v[64:67]
	v_mfma_f32_16x16x32_bf16 v[112:115], v[216:219], v[180:183], v[112:115]
	v_mfma_f32_16x16x32_bf16 v[108:111], v[224:227], v[180:183], v[108:111]
	v_mfma_f32_16x16x32_bf16 v[100:103], v[216:219], v[188:191], v[100:103]
	v_mfma_f32_16x16x32_bf16 v[88:91], v[224:227], v[188:191], v[88:91]
	v_mfma_f32_16x16x32_bf16 v[80:83], v[216:219], v[200:203], v[80:83]
	v_mfma_f32_16x16x32_bf16 v[76:79], v[224:227], v[200:203], v[76:79]
	v_mfma_f32_16x16x32_bf16 v[68:71], v[216:219], v[208:211], v[68:71]
	v_mfma_f32_16x16x32_bf16 v[64:67], v[224:227], v[208:211], v[64:67]
	s_setprio 0
	s_mov_b32 m0, s66
	v_lshl_add_u64 v[228:229], v[232:233], 0, s[14:15]
	s_barrier
	ds_read_b128 v[176:179], v147 offset:49152
	ds_read_b128 v[180:183], v147 offset:50176
	ds_read_b128 v[184:187], v147 offset:51200
	ds_read_b128 v[188:191], v147 offset:52224
	ds_read_b128 v[196:199], v147 offset:53248
	ds_read_b128 v[200:203], v147 offset:54272
	ds_read_b128 v[204:207], v147 offset:55296
	ds_read_b128 v[208:211], v147 offset:56320
	global_load_lds_dwordx4 v[228:229], off
	v_lshl_add_u64 v[192:193], v[192:193], 0, s[14:15]
	s_mov_b32 m0, s67
	s_nop 0
	global_load_lds_dwordx4 v[192:193], off
	s_barrier
	s_waitcnt lgkmcnt(0)
	s_setprio 1
	v_mfma_f32_16x16x32_bf16 v[60:63], v[160:163], v[176:179], v[60:63]
	v_mfma_f32_16x16x32_bf16 v[56:59], v[168:171], v[176:179], v[56:59]
	v_mfma_f32_16x16x32_bf16 v[48:51], v[160:163], v[184:187], v[48:51]
	v_mfma_f32_16x16x32_bf16 v[44:47], v[168:171], v[184:187], v[44:47]
	v_mfma_f32_16x16x32_bf16 v[36:39], v[160:163], v[196:199], v[36:39]
	v_mfma_f32_16x16x32_bf16 v[24:27], v[168:171], v[196:199], v[24:27]
	v_mfma_f32_16x16x32_bf16 v[16:19], v[160:163], v[204:207], v[16:19]
	v_mfma_f32_16x16x32_bf16 v[8:11], v[168:171], v[204:207], v[8:11]
	v_mfma_f32_16x16x32_bf16 v[60:63], v[164:167], v[180:183], v[60:63]
	v_mfma_f32_16x16x32_bf16 v[56:59], v[172:175], v[180:183], v[56:59]
	v_mfma_f32_16x16x32_bf16 v[48:51], v[164:167], v[188:191], v[48:51]
	v_mfma_f32_16x16x32_bf16 v[44:47], v[172:175], v[188:191], v[44:47]
	v_mfma_f32_16x16x32_bf16 v[36:39], v[164:167], v[200:203], v[36:39]
	v_mfma_f32_16x16x32_bf16 v[24:27], v[172:175], v[200:203], v[24:27]
	v_mfma_f32_16x16x32_bf16 v[16:19], v[164:167], v[208:211], v[16:19]
	v_mfma_f32_16x16x32_bf16 v[8:11], v[172:175], v[208:211], v[8:11]
	s_setprio 0
	s_barrier
	s_add_u32 s46, s46, 0x80080
	s_addc_u32 s47, s47, 0
	s_mov_b32 m0, s68
	v_lshl_add_u64 v[160:161], s[46:47], 0, v[130:131]
	global_load_lds_dwordx4 v[160:161], off
	v_lshl_add_u64 v[160:161], s[46:47], 0, v[128:129]
	s_mov_b32 m0, s69
	s_nop 0
	global_load_lds_dwordx4 v[160:161], off
	s_waitcnt vmcnt(6)
	s_barrier
	s_setprio 1
	v_mfma_f32_16x16x32_bf16 v[52:55], v[212:215], v[176:179], v[52:55]
	v_mfma_f32_16x16x32_bf16 v[40:43], v[220:223], v[176:179], v[40:43]
	v_mfma_f32_16x16x32_bf16 v[32:35], v[212:215], v[184:187], v[32:35]
	v_mfma_f32_16x16x32_bf16 v[28:31], v[220:223], v[184:187], v[28:31]
	v_mfma_f32_16x16x32_bf16 v[20:23], v[212:215], v[196:199], v[20:23]
	v_mfma_f32_16x16x32_bf16 v[12:15], v[220:223], v[196:199], v[12:15]
	v_mfma_f32_16x16x32_bf16 v[4:7], v[212:215], v[204:207], v[4:7]
	v_mfma_f32_16x16x32_bf16 v[0:3], v[220:223], v[204:207], v[0:3]
	v_mfma_f32_16x16x32_bf16 v[52:55], v[216:219], v[180:183], v[52:55]
	v_mfma_f32_16x16x32_bf16 v[40:43], v[224:227], v[180:183], v[40:43]
	v_mfma_f32_16x16x32_bf16 v[32:35], v[216:219], v[188:191], v[32:35]
	v_mfma_f32_16x16x32_bf16 v[28:31], v[224:227], v[188:191], v[28:31]
	v_mfma_f32_16x16x32_bf16 v[20:23], v[216:219], v[200:203], v[20:23]
	v_mfma_f32_16x16x32_bf16 v[12:15], v[224:227], v[200:203], v[12:15]
	v_mfma_f32_16x16x32_bf16 v[4:7], v[216:219], v[208:211], v[4:7]
	v_mfma_f32_16x16x32_bf16 v[0:3], v[224:227], v[208:211], v[0:3]
	s_setprio 0
	s_add_i32 s82, s82, 2
	s_add_u32 s44, s44, 0x100
	s_addc_u32 s45, s45, 0
	s_cmp_gt_u32 s82, 5
	s_barrier
	s_cbranch_scc0 .LBB0_736
	s_and_b64 vcc, exec, s[18:19]
	s_cbranch_vccz .LBB0_740
	s_barrier
	s_andn2_b64 vcc, exec, s[20:21]
	s_cbranch_vccz .LBB0_741

.LBB0_756:
	s_add_u32 s38, s8, s36
	s_addc_u32 s39, s9, s37
	s_add_u32 s40, s38, 0x14000100
	ds_read_b128 v[144:147], v154
	ds_read_b128 v[168:171], v154 offset:2048
	ds_read_b128 v[148:151], v155
	ds_read_b128 v[172:175], v155 offset:2048
	s_addc_u32 s41, s39, 0
	s_add_u32 s68, s0, s36
	s_addc_u32 s69, s1, s37
	s_cmpk_eq_i32 s36, 0x700
	s_cselect_b64 vcc, -1, 0
	s_and_b64 s[38:39], vcc, exec
	ds_read_b128 v[176:179], v152
	ds_read_b128 v[184:187], v152 offset:2048
	ds_read_b128 v[180:183], v153
	ds_read_b128 v[188:191], v153 offset:2048
	ds_read_b128 v[196:199], v152 offset:4096
	ds_read_b128 v[204:207], v152 offset:6144
	ds_read_b128 v[200:203], v153 offset:4096
	ds_read_b128 v[208:211], v153 offset:6144
	s_waitcnt vmcnt(6)
	s_waitcnt lgkmcnt(8)
	s_barrier
	s_waitcnt lgkmcnt(0)
	v_cndmask_b32_e32 v192, v134, v163, vcc
	s_setprio 1
	s_waitcnt lgkmcnt(0)
	v_mfma_f32_16x16x128_f8f6f4 v[124:127], v[144:151], v[176:183], v[124:127]
	v_mfma_f32_16x16x128_f8f6f4 v[120:123], v[168:175], v[176:183], v[120:123]
	v_mfma_f32_16x16x128_f8f6f4 v[108:111], v[144:151], v[184:191], v[108:111]
	v_mfma_f32_16x16x128_f8f6f4 v[104:107], v[168:175], v[184:191], v[104:107]
	v_mfma_f32_16x16x128_f8f6f4 v[92:95], v[144:151], v[196:203], v[92:95]
	v_mfma_f32_16x16x128_f8f6f4 v[88:91], v[168:175], v[196:203], v[88:91]
	v_mfma_f32_16x16x128_f8f6f4 v[76:79], v[144:151], v[204:211], v[76:79]
	v_mfma_f32_16x16x128_f8f6f4 v[72:75], v[168:175], v[204:211], v[72:75]
	s_setprio 0
	s_barrier
	ds_read_b128 v[234:237], v154 offset:16384
	ds_read_b128 v[242:245], v154 offset:18432
	ds_read_b128 v[238:241], v155 offset:16384
	ds_read_b128 v[246:249], v155 offset:18432
	v_cndmask_b32_e32 v132, v166, v162, vcc
	s_cselect_b32 s41, s11, s41
	s_cselect_b32 s40, s10, s40
	s_cselect_b32 s39, s31, s69
	s_cselect_b32 s38, s30, s68
	v_cndmask_b32_e32 v137, v136, v164, vcc
	s_mov_b32 m0, s66
	v_lshl_add_u64 v[220:221], v[142:143], 0, s[36:37]
	global_load_lds_dwordx4 v[220:221], off
	v_lshl_add_u64 v[220:221], v[140:141], 0, s[36:37]
	s_mov_b32 m0, s67
	s_nop 0
	global_load_lds_dwordx4 v[220:221], off
	s_barrier
	s_waitcnt lgkmcnt(0)
	s_setprio 1
	v_mfma_f32_16x16x128_f8f6f4 v[116:119], v[234:241], v[176:183], v[116:119]
	v_mfma_f32_16x16x128_f8f6f4 v[112:115], v[242:249], v[176:183], v[112:115]
	v_mfma_f32_16x16x128_f8f6f4 v[100:103], v[234:241], v[184:191], v[100:103]
	v_mfma_f32_16x16x128_f8f6f4 v[96:99], v[242:249], v[184:191], v[96:99]
	v_mfma_f32_16x16x128_f8f6f4 v[84:87], v[234:241], v[196:203], v[84:87]
	v_mfma_f32_16x16x128_f8f6f4 v[80:83], v[242:249], v[196:203], v[80:83]
	v_mfma_f32_16x16x128_f8f6f4 v[68:71], v[234:241], v[204:211], v[68:71]
	v_mfma_f32_16x16x128_f8f6f4 v[64:67], v[242:249], v[204:211], v[64:67]
	s_setprio 0
	s_barrier
	s_mov_b32 m0, s35
	ds_read_b128 v[184:187], v152 offset:16384
	ds_read_b128 v[196:199], v152 offset:18432
	ds_read_b128 v[188:191], v153 offset:16384
	ds_read_b128 v[200:203], v153 offset:18432
	ds_read_b128 v[204:207], v152 offset:20480
	ds_read_b128 v[212:215], v152 offset:22528
	ds_read_b128 v[208:211], v153 offset:20480
	ds_read_b128 v[216:219], v153 offset:22528
	global_load_lds_dwordx4 v132, s[40:41]
	s_mov_b32 m0, s45
	v_mov_b32_e32 v193, v133
	global_load_lds_dwordx4 v192, s[40:41]
	s_waitcnt lgkmcnt(8)
	s_barrier
	s_waitcnt lgkmcnt(0)
	v_lshl_add_u64 v[252:253], s[40:41], 0, v[132:133]
	v_lshl_add_u64 v[250:251], s[40:41], 0, v[192:193]
	s_setprio 1
	s_waitcnt lgkmcnt(0)
	v_mfma_f32_16x16x128_f8f6f4 v[60:63], v[144:151], v[184:191], v[60:63]
	v_mfma_f32_16x16x128_f8f6f4 v[56:59], v[168:175], v[184:191], v[56:59]
	v_mfma_f32_16x16x128_f8f6f4 v[44:47], v[144:151], v[196:203], v[44:47]
	v_mfma_f32_16x16x128_f8f6f4 v[40:43], v[168:175], v[196:203], v[40:43]
	v_mfma_f32_16x16x128_f8f6f4 v[28:31], v[144:151], v[204:211], v[28:31]
	v_mfma_f32_16x16x128_f8f6f4 v[24:27], v[168:175], v[204:211], v[24:27]
	v_mfma_f32_16x16x128_f8f6f4 v[12:15], v[144:151], v[212:219], v[12:15]
	v_mfma_f32_16x16x128_f8f6f4 v[8:11], v[168:175], v[212:219], v[8:11]
	s_setprio 0
	s_barrier
	s_mov_b32 m0, s43
	v_lshl_add_u64 v[144:145], s[38:39], 0, v[130:131]
	global_load_lds_dwordx4 v[144:145], off
	v_lshl_add_u64 v[146:147], s[38:39], 0, v[128:129]
	s_mov_b32 m0, s44
	s_nop 0
	global_load_lds_dwordx4 v[146:147], off
	s_waitcnt vmcnt(8)
	s_waitcnt lgkmcnt(0)
	s_barrier
	s_setprio 1
	s_waitcnt lgkmcnt(0)
	v_mfma_f32_16x16x128_f8f6f4 v[52:55], v[234:241], v[184:191], v[52:55]
	v_mfma_f32_16x16x128_f8f6f4 v[48:51], v[242:249], v[184:191], v[48:51]
	v_mfma_f32_16x16x128_f8f6f4 v[36:39], v[234:241], v[196:203], v[36:39]
	v_mfma_f32_16x16x128_f8f6f4 v[32:35], v[242:249], v[196:203], v[32:35]
	v_mfma_f32_16x16x128_f8f6f4 v[20:23], v[234:241], v[204:211], v[20:23]
	v_mfma_f32_16x16x128_f8f6f4 v[16:19], v[242:249], v[204:211], v[16:19]
	v_mfma_f32_16x16x128_f8f6f4 v[4:7], v[234:241], v[212:219], v[4:7]
	v_mfma_f32_16x16x128_f8f6f4 v[0:3], v[242:249], v[212:219], v[0:3]
	s_setprio 0
	s_barrier
	ds_read_b128 v[168:171], v154 offset:32768
	ds_read_b128 v[176:179], v154 offset:34816
	ds_read_b128 v[172:175], v155 offset:32768
	ds_read_b128 v[180:183], v155 offset:34816
	s_mov_b32 m0, s48
	ds_read_b128 v[184:187], v152 offset:32768
	ds_read_b128 v[196:199], v152 offset:34816
	ds_read_b128 v[188:191], v153 offset:32768
	ds_read_b128 v[200:203], v153 offset:34816
	ds_read_b128 v[204:207], v152 offset:36864
	ds_read_b128 v[212:215], v152 offset:38912
	ds_read_b128 v[208:211], v153 offset:36864
	ds_read_b128 v[216:219], v153 offset:38912
	v_cndmask_b32_e32 v132, v138, v165, vcc
	global_load_lds_dwordx4 v137, s[40:41]
	s_mov_b32 m0, s49
	s_nop 0
	global_load_lds_dwordx4 v132, s[40:41]
	s_waitcnt vmcnt(8)
	s_waitcnt lgkmcnt(8)
	s_barrier
	s_waitcnt lgkmcnt(0)
	s_setprio 1
	v_mfma_f32_16x16x128_f8f6f4 v[124:127], v[168:175], v[184:191], v[124:127]
	v_mfma_f32_16x16x128_f8f6f4 v[120:123], v[176:183], v[184:191], v[120:123]
	v_mfma_f32_16x16x128_f8f6f4 v[108:111], v[168:175], v[196:203], v[108:111]
	v_mfma_f32_16x16x128_f8f6f4 v[104:107], v[176:183], v[196:203], v[104:107]
	v_mfma_f32_16x16x128_f8f6f4 v[92:95], v[168:175], v[204:211], v[92:95]
	v_mfma_f32_16x16x128_f8f6f4 v[88:91], v[176:183], v[204:211], v[88:91]
	v_mfma_f32_16x16x128_f8f6f4 v[76:79], v[168:175], v[212:219], v[76:79]
	v_mfma_f32_16x16x128_f8f6f4 v[72:75], v[176:183], v[212:219], v[72:75]
	s_setprio 0
	s_barrier
	ds_read_b128 v[234:237], v154 offset:49152
	ds_read_b128 v[242:245], v154 offset:51200
	ds_read_b128 v[238:241], v155 offset:49152
	ds_read_b128 v[246:249], v155 offset:51200
	s_add_u32 s40, s38, 0x4000
	s_addc_u32 s41, s39, 0
	v_lshl_add_u64 v[192:193], s[40:41], 0, v[130:131]
	s_mov_b32 m0, s46
	s_nop 0
	global_load_lds_dwordx4 v[192:193], off
	v_lshl_add_u64 v[192:193], s[40:41], 0, v[128:129]
	s_mov_b32 m0, s47
	s_nop 0
	global_load_lds_dwordx4 v[192:193], off
	s_waitcnt vmcnt(8)
	s_barrier
	s_waitcnt lgkmcnt(0)
	s_setprio 1
	v_mfma_f32_16x16x128_f8f6f4 v[116:119], v[234:241], v[184:191], v[116:119]
	v_mfma_f32_16x16x128_f8f6f4 v[112:115], v[242:249], v[184:191], v[112:115]
	v_mfma_f32_16x16x128_f8f6f4 v[100:103], v[234:241], v[196:203], v[100:103]
	v_mfma_f32_16x16x128_f8f6f4 v[96:99], v[242:249], v[196:203], v[96:99]
	v_mfma_f32_16x16x128_f8f6f4 v[84:87], v[234:241], v[204:211], v[84:87]
	v_mfma_f32_16x16x128_f8f6f4 v[80:83], v[242:249], v[204:211], v[80:83]
	v_mfma_f32_16x16x128_f8f6f4 v[68:71], v[234:241], v[212:219], v[68:71]
	v_mfma_f32_16x16x128_f8f6f4 v[64:67], v[242:249], v[212:219], v[64:67]
	s_setprio 0
	s_barrier
	s_mov_b32 m0, s60
	v_lshl_add_u64 v[252:253], v[252:253], 0, s[16:17]
	ds_read_b128 v[184:187], v152 offset:49152
	ds_read_b128 v[196:199], v152 offset:51200
	ds_read_b128 v[188:191], v153 offset:49152
	ds_read_b128 v[200:203], v153 offset:51200
	ds_read_b128 v[204:207], v152 offset:53248
	ds_read_b128 v[212:215], v152 offset:55296
	ds_read_b128 v[208:211], v153 offset:53248
	ds_read_b128 v[216:219], v153 offset:55296
	global_load_lds_dwordx4 v[252:253], off
	v_lshl_add_u64 v[250:251], v[250:251], 0, s[16:17]
	s_mov_b32 m0, s61
	s_nop 0
	global_load_lds_dwordx4 v[250:251], off
	s_waitcnt lgkmcnt(8)
	s_barrier
	s_waitcnt lgkmcnt(0)
	s_setprio 1
	v_mfma_f32_16x16x128_f8f6f4 v[60:63], v[168:175], v[184:191], v[60:63]
	v_mfma_f32_16x16x128_f8f6f4 v[56:59], v[176:183], v[184:191], v[56:59]
	v_mfma_f32_16x16x128_f8f6f4 v[44:47], v[168:175], v[196:203], v[44:47]
	v_mfma_f32_16x16x128_f8f6f4 v[40:43], v[176:183], v[196:203], v[40:43]
	v_mfma_f32_16x16x128_f8f6f4 v[28:31], v[168:175], v[204:211], v[28:31]
	v_mfma_f32_16x16x128_f8f6f4 v[24:27], v[176:183], v[204:211], v[24:27]
	v_mfma_f32_16x16x128_f8f6f4 v[12:15], v[168:175], v[212:219], v[12:15]
	v_mfma_f32_16x16x128_f8f6f4 v[8:11], v[176:183], v[212:219], v[8:11]
	s_setprio 0
	s_barrier
	s_mov_b32 m0, s58
	v_lshl_add_u64 v[144:145], v[144:145], 0, s[16:17]
	global_load_lds_dwordx4 v[144:145], off
	v_lshl_add_u64 v[144:145], v[146:147], 0, s[16:17]
	s_mov_b32 m0, s59
	s_nop 0
	global_load_lds_dwordx4 v[144:145], off
	s_waitcnt vmcnt(8)
	s_waitcnt lgkmcnt(0)
	s_barrier
	s_setprio 1
	s_waitcnt lgkmcnt(0)
	v_mfma_f32_16x16x128_f8f6f4 v[52:55], v[234:241], v[184:191], v[52:55]
	v_mfma_f32_16x16x128_f8f6f4 v[48:51], v[242:249], v[184:191], v[48:51]
	v_mfma_f32_16x16x128_f8f6f4 v[36:39], v[234:241], v[196:203], v[36:39]
	v_mfma_f32_16x16x128_f8f6f4 v[32:35], v[242:249], v[196:203], v[32:35]
	v_mfma_f32_16x16x128_f8f6f4 v[20:23], v[234:241], v[204:211], v[20:23]
	v_mfma_f32_16x16x128_f8f6f4 v[16:19], v[242:249], v[204:211], v[16:19]
	v_mfma_f32_16x16x128_f8f6f4 v[4:7], v[234:241], v[212:219], v[4:7]
	v_mfma_f32_16x16x128_f8f6f4 v[0:3], v[242:249], v[212:219], v[0:3]
	s_setprio 0
	s_barrier
	s_add_u32 s38, s38, 0x4080
	s_addc_u32 s39, s39, 0
	s_mov_b32 m0, s62
	v_lshl_add_u64 v[144:145], s[38:39], 0, v[130:131]
	global_load_lds_dwordx4 v[144:145], off
	v_lshl_add_u64 v[144:145], s[38:39], 0, v[128:129]
	s_mov_b32 m0, s63
	s_add_i32 s57, s57, 2
	global_load_lds_dwordx4 v[144:145], off
	s_add_u32 s36, s36, 0x100
	s_addc_u32 s37, s37, 0
	s_cmp_gt_u32 s57, 13
	s_cbranch_scc0 .LBB0_756
	s_and_b64 vcc, exec, s[20:21]
	s_cbranch_vccz .LBB0_759
	s_barrier

.LBB0_845:
	s_waitcnt lgkmcnt(0)
	s_barrier
	s_and_saveexec_b64 s[24:25], s[4:5]
	s_cbranch_execz .LBB0_849
	ds_read_b32 v30, v8
	v_mov_b32_e32 v29, 0
	s_waitcnt lgkmcnt(0)
	v_cmp_ne_u32_e32 vcc, 0, v30
	s_and_saveexec_b64 s[26:27], vcc
	s_cbranch_execz .LBB0_848
	global_atomic_add v29, v[4:5], v30, off sc0

.LBB0_926:
	s_or_b64 exec, exec, s[4:5]
	s_add_i32 s0, 0, 0x22140
	v_mov_b32_e32 v1, s0
	s_waitcnt lgkmcnt(0)
	s_barrier
	ds_read_b32 v1, v1
	s_waitcnt lgkmcnt(0)
	v_cmp_lt_i32_e32 vcc, v0, v1
	s_and_saveexec_b64 s[4:5], vcc
	s_cbranch_execz .LBB0_931
	s_mov_b64 s[6:7], 0

.LBB0_931:
	s_or_b64 exec, exec, s[4:5]
	s_add_u32 s54, s20, 0x4000000
	s_waitcnt lgkmcnt(0)
	s_barrier
	s_addc_u32 s55, s21, 0
	s_add_u32 s58, s20, 0x2c80000
	v_ashrrev_i32_e32 v6, 4, v4
	v_and_b32_e32 v7, 15, v4
	v_lshlrev_b32_e32 v0, 5, v6
	v_lshlrev_b32_e32 v3, 2, v4
	s_addc_u32 s59, s21, 0
	s_lshr_b32 s1, s95, 8
	v_lshlrev_b32_e32 v2, 6, v7
	v_and_b32_e32 v0, 32, v0
	v_and_b32_e32 v3, 32, v3
	v_ashrrev_i32_e32 v1, 5, v4
	v_bitop3_b32 v0, v0, v3, v2 bitop3:0x36
	v_lshrrev_b32_e32 v2, 2, v4
	v_lshrrev_b32_e32 v3, 3, v4
	s_lshl_b32 s0, s1, 13
	v_xor_b32_e32 v2, v2, v3
	v_lshl_add_u32 v3, v1, 10, s0
	s_lshl_b32 s0, s3, 5
	s_and_b32 s12, s0, 0x60
	v_lshlrev_b32_e32 v2, 4, v2
	s_lshr_b32 s0, s12, 3
	v_and_b32_e32 v2, 16, v2
	v_add_lshl_u32 v1, v1, s0, 10
	v_or3_b32 v3, v2, v3, v0
	v_or3_b32 v0, v2, v1, v0
	s_add_i32 s0, 0, 0x10000
	v_add_u32_e32 v197, s0, v0
	v_xad_u32 v198, v0, 16, s0
	s_add_i32 s0, 0, 0x22140
	v_add_u32_e32 v195, 0, v3
	v_xad_u32 v196, v3, 16, 0
	v_mov_b32_e32 v0, s0
	ds_read_b32 v0, v0
	s_waitcnt lgkmcnt(0)
	v_readfirstlane_b32 s0, v0
	s_lshl_b32 s0, s0, 2
	s_add_i32 s0, s0, 32
	s_cmp_lt_i32 s23, s0
	s_cselect_b64 s[4:5], -1, 0
	s_cmp_ge_i32 s23, s0
	s_cbranch_scc1 .LBB0_935
	s_ashr_i32 s0, s23, 31
	s_lshr_b32 s0, s0, 30
	s_add_i32 s6, s23, s0
	s_ashr_i32 s0, s6, 2
	s_and_b32 s6, s6, -4
	v_cmp_ge_i32_e32 vcc, s0, v0
	s_sub_i32 s44, s23, s6
	s_cbranch_vccz .LBB0_936
	s_ashr_i32 s45, s44, 31
	v_sub_u32_e32 v0, s0, v0
	s_lshl_b64 s[6:7], s[44:45], 19
	s_add_u32 s16, s58, s6
	v_lshlrev_b32_e32 v0, 8, v0
	s_addc_u32 s17, s59, s7
	v_add_u32_e32 v174, 0xf41e0000, v0
	s_cbranch_execz .LBB0_937
	v_mov_b32_e32 v171, -1
	v_mov_b32_e32 v5, 0x100
	s_lshl_b32 s0, s0, 8
	s_andn2_b64 vcc, exec, s[4:5]
	s_cbranch_vccnz .LBB0_978
	s_branch .LBB0_938

.LBB0_962:
	s_add_u32 s50, s20, s48
	s_addc_u32 s51, s21, s49
	ds_read_b128 v[186:189], v197
	ds_read_b128 v[202:205], v197 offset:2048
	ds_read_b128 v[190:193], v198
	ds_read_b128 v[206:209], v198 offset:2048
	s_add_u32 s52, s50, 0x14000100
	s_addc_u32 s53, s51, 0
	s_and_b64 s[50:51], s[16:17], exec
	s_cselect_b32 s53, s27, s53
	s_cselect_b32 s52, s26, s52
	s_add_u32 s77, s56, s48
	s_addc_u32 s78, s57, s49
	s_and_b64 s[50:51], s[16:17], exec
	s_cselect_b32 s51, s43, s78
	s_cselect_b32 s50, s42, s77
	ds_read_b128 v[210:213], v195
	ds_read_b128 v[218:221], v195 offset:2048
	ds_read_b128 v[214:217], v196
	ds_read_b128 v[222:225], v196 offset:2048
	ds_read_b128 v[226:229], v195 offset:4096
	ds_read_b128 v[234:237], v195 offset:6144
	ds_read_b128 v[230:233], v196 offset:4096
	ds_read_b128 v[238:241], v196 offset:6144
	s_waitcnt vmcnt(6)
	s_waitcnt lgkmcnt(8)
	s_barrier
	s_waitcnt lgkmcnt(0)
	s_setprio 1
	v_mfma_f32_16x16x128_f8f6f4 v[124:127], v[186:193], v[210:217], v[124:127]
	v_mfma_f32_16x16x128_f8f6f4 v[120:123], v[202:209], v[210:217], v[120:123]
	v_mfma_f32_16x16x128_f8f6f4 v[108:111], v[186:193], v[218:225], v[108:111]
	v_mfma_f32_16x16x128_f8f6f4 v[104:107], v[202:209], v[218:225], v[104:107]
	v_mfma_f32_16x16x128_f8f6f4 v[92:95], v[186:193], v[226:233], v[92:95]
	v_mfma_f32_16x16x128_f8f6f4 v[88:91], v[202:209], v[226:233], v[88:91]
	v_mfma_f32_16x16x128_f8f6f4 v[76:79], v[186:193], v[234:241], v[76:79]
	v_mfma_f32_16x16x128_f8f6f4 v[72:75], v[202:209], v[234:241], v[72:75]
	s_setprio 0
	s_barrier
	ds_read_b128 v[186:189], v197 offset:16384
	ds_read_b128 v[202:205], v197 offset:18432
	ds_read_b128 v[190:193], v198 offset:16384
	ds_read_b128 v[206:209], v198 offset:18432
	v_cndmask_b32_e64 v136, v175, v181, s[16:17]
	v_cndmask_b32_e64 v177, v176, v173, s[16:17]
	v_lshl_add_u64 v[242:243], v[184:185], 0, s[48:49]
	s_add_i32 m0, s45, 0xc000
	s_nop 0
	global_load_lds_dwordx4 v[242:243], off
	v_lshl_add_u64 v[242:243], v[182:183], 0, s[48:49]
	s_add_i32 m0, s45, 0xe000
	v_cndmask_b32_e64 v250, v178, v179, s[16:17]
	global_load_lds_dwordx4 v[242:243], off
	s_barrier
	s_waitcnt lgkmcnt(0)
	s_setprio 1
	v_mfma_f32_16x16x128_f8f6f4 v[116:119], v[186:193], v[210:217], v[116:119]
	v_mfma_f32_16x16x128_f8f6f4 v[112:115], v[202:209], v[210:217], v[112:115]
	v_mfma_f32_16x16x128_f8f6f4 v[100:103], v[186:193], v[218:225], v[100:103]
	v_mfma_f32_16x16x128_f8f6f4 v[96:99], v[202:209], v[218:225], v[96:99]
	v_mfma_f32_16x16x128_f8f6f4 v[84:87], v[186:193], v[226:233], v[84:87]
	v_mfma_f32_16x16x128_f8f6f4 v[80:83], v[202:209], v[226:233], v[80:83]
	v_mfma_f32_16x16x128_f8f6f4 v[68:71], v[186:193], v[234:241], v[68:71]
	v_mfma_f32_16x16x128_f8f6f4 v[64:67], v[202:209], v[234:241], v[64:67]
	s_setprio 0
	s_barrier
	ds_read_b128 v[202:205], v197
	ds_read_b128 v[210:213], v197 offset:2048
	ds_read_b128 v[206:209], v198
	ds_read_b128 v[214:217], v198 offset:2048
	s_mov_b32 m0, s45
	ds_read_b128 v[218:221], v195 offset:16384
	ds_read_b128 v[226:229], v195 offset:18432
	ds_read_b128 v[222:225], v196 offset:16384
	ds_read_b128 v[230:233], v196 offset:18432
	ds_read_b128 v[234:237], v195 offset:20480
	ds_read_b128 v[242:245], v195 offset:22528
	ds_read_b128 v[238:241], v196 offset:20480
	ds_read_b128 v[246:249], v196 offset:22528
	global_load_lds_dwordx4 v136, s[52:53]
	s_mov_b32 m0, s62
	v_mov_b32_e32 v251, v137
	global_load_lds_dwordx4 v250, s[52:53]
	s_waitcnt lgkmcnt(8)
	s_barrier
	s_waitcnt lgkmcnt(0)
	v_lshl_add_u64 v[192:193], s[52:53], 0, v[136:137]
	v_lshl_add_u64 v[190:191], s[52:53], 0, v[250:251]
	s_setprio 1
	s_waitcnt lgkmcnt(0)
	v_mfma_f32_16x16x128_f8f6f4 v[60:63], v[202:209], v[218:225], v[60:63]
	v_mfma_f32_16x16x128_f8f6f4 v[56:59], v[210:217], v[218:225], v[56:59]
	v_mfma_f32_16x16x128_f8f6f4 v[44:47], v[202:209], v[226:233], v[44:47]
	v_mfma_f32_16x16x128_f8f6f4 v[40:43], v[210:217], v[226:233], v[40:43]
	v_mfma_f32_16x16x128_f8f6f4 v[28:31], v[202:209], v[234:241], v[28:31]
	v_mfma_f32_16x16x128_f8f6f4 v[24:27], v[210:217], v[234:241], v[24:27]
	v_mfma_f32_16x16x128_f8f6f4 v[12:15], v[202:209], v[242:249], v[12:15]
	v_mfma_f32_16x16x128_f8f6f4 v[8:11], v[210:217], v[242:249], v[8:11]
	s_setprio 0
	s_barrier
	s_mov_b32 m0, s60
	v_lshl_add_u64 v[186:187], s[50:51], 0, v[138:139]
	ds_read_b128 v[202:205], v197 offset:16384
	ds_read_b128 v[210:213], v197 offset:18432
	ds_read_b128 v[206:209], v198 offset:16384
	ds_read_b128 v[214:217], v198 offset:18432
	global_load_lds_dwordx4 v[186:187], off
	v_lshl_add_u64 v[188:189], s[50:51], 0, v[140:141]
	s_mov_b32 m0, s61
	s_nop 0
	global_load_lds_dwordx4 v[188:189], off
	s_waitcnt vmcnt(8)
	s_waitcnt lgkmcnt(0)
	s_barrier
	s_setprio 1
	s_waitcnt lgkmcnt(0)
	v_mfma_f32_16x16x128_f8f6f4 v[52:55], v[202:209], v[218:225], v[52:55]
	v_mfma_f32_16x16x128_f8f6f4 v[48:51], v[210:217], v[218:225], v[48:51]
	v_mfma_f32_16x16x128_f8f6f4 v[36:39], v[202:209], v[226:233], v[36:39]
	v_mfma_f32_16x16x128_f8f6f4 v[32:35], v[210:217], v[226:233], v[32:35]
	v_mfma_f32_16x16x128_f8f6f4 v[20:23], v[202:209], v[234:241], v[20:23]
	v_mfma_f32_16x16x128_f8f6f4 v[16:19], v[210:217], v[234:241], v[16:19]
	v_mfma_f32_16x16x128_f8f6f4 v[4:7], v[202:209], v[242:249], v[4:7]
	v_mfma_f32_16x16x128_f8f6f4 v[0:3], v[210:217], v[242:249], v[0:3]
	s_setprio 0
	s_barrier
	ds_read_b128 v[202:205], v197 offset:32768
	ds_read_b128 v[210:213], v197 offset:34816
	ds_read_b128 v[206:209], v198 offset:32768
	ds_read_b128 v[214:217], v198 offset:34816
	s_mov_b32 m0, s65
	v_cndmask_b32_e64 v136, v180, v199, s[16:17]
	s_add_u32 s16, s50, 0x4000
	ds_read_b128 v[218:221], v195 offset:32768
	ds_read_b128 v[226:229], v195 offset:34816
	ds_read_b128 v[222:225], v196 offset:32768
	ds_read_b128 v[230:233], v196 offset:34816
	ds_read_b128 v[234:237], v195 offset:36864
	ds_read_b128 v[242:245], v195 offset:38912
	ds_read_b128 v[238:241], v196 offset:36864
	ds_read_b128 v[246:249], v196 offset:38912
	global_load_lds_dwordx4 v177, s[52:53]
	s_mov_b32 m0, s66
	s_addc_u32 s17, s51, 0
	global_load_lds_dwordx4 v136, s[52:53]
	s_waitcnt vmcnt(8)
	s_waitcnt lgkmcnt(8)
	s_barrier
	s_waitcnt lgkmcnt(0)
	s_setprio 1
	v_mfma_f32_16x16x128_f8f6f4 v[124:127], v[202:209], v[218:225], v[124:127]
	v_mfma_f32_16x16x128_f8f6f4 v[120:123], v[210:217], v[218:225], v[120:123]
	v_mfma_f32_16x16x128_f8f6f4 v[108:111], v[202:209], v[226:233], v[108:111]
	v_mfma_f32_16x16x128_f8f6f4 v[104:107], v[210:217], v[226:233], v[104:107]
	v_mfma_f32_16x16x128_f8f6f4 v[92:95], v[202:209], v[234:241], v[92:95]
	v_mfma_f32_16x16x128_f8f6f4 v[88:91], v[210:217], v[234:241], v[88:91]
	v_mfma_f32_16x16x128_f8f6f4 v[76:79], v[202:209], v[242:249], v[76:79]
	v_mfma_f32_16x16x128_f8f6f4 v[72:75], v[210:217], v[242:249], v[72:75]
	s_setprio 0
	s_barrier
	ds_read_b128 v[202:205], v197 offset:49152
	ds_read_b128 v[210:213], v197 offset:51200
	ds_read_b128 v[206:209], v198 offset:49152
	ds_read_b128 v[214:217], v198 offset:51200
	v_lshl_add_u64 v[250:251], s[16:17], 0, v[138:139]
	s_mov_b32 m0, s63
	s_nop 0
	global_load_lds_dwordx4 v[250:251], off
	v_lshl_add_u64 v[250:251], s[16:17], 0, v[140:141]
	s_mov_b32 m0, s64
	s_nop 0
	global_load_lds_dwordx4 v[250:251], off
	s_waitcnt vmcnt(8)
	s_barrier
	s_waitcnt lgkmcnt(0)
	s_setprio 1
	v_mfma_f32_16x16x128_f8f6f4 v[116:119], v[202:209], v[218:225], v[116:119]
	v_mfma_f32_16x16x128_f8f6f4 v[112:115], v[210:217], v[218:225], v[112:115]
	v_mfma_f32_16x16x128_f8f6f4 v[100:103], v[202:209], v[226:233], v[100:103]
	v_mfma_f32_16x16x128_f8f6f4 v[96:99], v[210:217], v[226:233], v[96:99]
	v_mfma_f32_16x16x128_f8f6f4 v[84:87], v[202:209], v[234:241], v[84:87]
	v_mfma_f32_16x16x128_f8f6f4 v[80:83], v[210:217], v[234:241], v[80:83]
	v_mfma_f32_16x16x128_f8f6f4 v[68:71], v[202:209], v[242:249], v[68:71]
	v_mfma_f32_16x16x128_f8f6f4 v[64:67], v[210:217], v[242:249], v[64:67]
	s_setprio 0
	s_barrier
	ds_read_b128 v[202:205], v197 offset:32768
	ds_read_b128 v[210:213], v197 offset:34816
	ds_read_b128 v[206:209], v198 offset:32768
	ds_read_b128 v[214:217], v198 offset:34816
	s_mov_b32 m0, s69
	v_lshl_add_u64 v[192:193], v[192:193], 0, s[34:35]
	ds_read_b128 v[218:221], v195 offset:49152
	ds_read_b128 v[226:229], v195 offset:51200
	ds_read_b128 v[222:225], v196 offset:49152
	ds_read_b128 v[230:233], v196 offset:51200
	ds_read_b128 v[234:237], v195 offset:53248
	ds_read_b128 v[242:245], v195 offset:55296
	ds_read_b128 v[238:241], v196 offset:53248
	ds_read_b128 v[246:249], v196 offset:55296
	global_load_lds_dwordx4 v[192:193], off
	v_lshl_add_u64 v[190:191], v[190:191], 0, s[34:35]
	s_mov_b32 m0, s70
	s_nop 0
	global_load_lds_dwordx4 v[190:191], off
	s_waitcnt lgkmcnt(8)
	s_barrier
	s_waitcnt lgkmcnt(0)
	s_setprio 1
	v_mfma_f32_16x16x128_f8f6f4 v[60:63], v[202:209], v[218:225], v[60:63]
	v_mfma_f32_16x16x128_f8f6f4 v[56:59], v[210:217], v[218:225], v[56:59]
	v_mfma_f32_16x16x128_f8f6f4 v[44:47], v[202:209], v[226:233], v[44:47]
	v_mfma_f32_16x16x128_f8f6f4 v[40:43], v[210:217], v[226:233], v[40:43]
	v_mfma_f32_16x16x128_f8f6f4 v[28:31], v[202:209], v[234:241], v[28:31]
	v_mfma_f32_16x16x128_f8f6f4 v[24:27], v[210:217], v[234:241], v[24:27]
	v_mfma_f32_16x16x128_f8f6f4 v[12:15], v[202:209], v[242:249], v[12:15]
	v_mfma_f32_16x16x128_f8f6f4 v[8:11], v[210:217], v[242:249], v[8:11]
	s_setprio 0
	s_barrier
	s_mov_b32 m0, s67
	v_lshl_add_u64 v[186:187], v[186:187], 0, s[34:35]
	ds_read_b128 v[202:205], v197 offset:49152
	ds_read_b128 v[210:213], v197 offset:51200
	ds_read_b128 v[206:209], v198 offset:49152
	ds_read_b128 v[214:217], v198 offset:51200
	global_load_lds_dwordx4 v[186:187], off
	v_lshl_add_u64 v[186:187], v[188:189], 0, s[34:35]
	s_mov_b32 m0, s68
	s_nop 0
	global_load_lds_dwordx4 v[186:187], off
	s_waitcnt vmcnt(8)
	s_waitcnt lgkmcnt(0)
	s_barrier
	s_setprio 1
	s_waitcnt lgkmcnt(0)
	v_mfma_f32_16x16x128_f8f6f4 v[52:55], v[202:209], v[218:225], v[52:55]
	v_mfma_f32_16x16x128_f8f6f4 v[48:51], v[210:217], v[218:225], v[48:51]
	v_mfma_f32_16x16x128_f8f6f4 v[36:39], v[202:209], v[226:233], v[36:39]
	v_mfma_f32_16x16x128_f8f6f4 v[32:35], v[210:217], v[226:233], v[32:35]
	v_mfma_f32_16x16x128_f8f6f4 v[20:23], v[202:209], v[234:241], v[20:23]
	v_mfma_f32_16x16x128_f8f6f4 v[16:19], v[210:217], v[234:241], v[16:19]
	v_mfma_f32_16x16x128_f8f6f4 v[4:7], v[202:209], v[242:249], v[4:7]
	v_mfma_f32_16x16x128_f8f6f4 v[0:3], v[210:217], v[242:249], v[0:3]
	s_setprio 0
	s_barrier
	s_add_u32 s16, s50, 0x4080
	s_addc_u32 s17, s51, 0
	s_mov_b32 m0, s71
	v_lshl_add_u64 v[186:187], s[16:17], 0, v[138:139]
	global_load_lds_dwordx4 v[186:187], off
	v_lshl_add_u64 v[186:187], s[16:17], 0, v[140:141]
	s_mov_b32 m0, s72
	s_add_i32 s76, s76, 2
	global_load_lds_dwordx4 v[186:187], off
	s_add_u32 s48, s48, 0x100
	s_addc_u32 s49, s49, 0
	s_cmp_gt_u32 s76, 13
	s_cbranch_scc1 .LBB0_972

.LBB0_1040:
	s_or_b64 exec, exec, s[4:5]
	s_add_i32 s0, 0, 0x22140
	v_mov_b32_e32 v1, s0
	s_waitcnt lgkmcnt(0)
	s_barrier
	ds_read_b32 v1, v1
	s_waitcnt lgkmcnt(0)
	v_cmp_lt_i32_e32 vcc, v0, v1
	s_and_saveexec_b64 s[4:5], vcc
	s_cbranch_execz .LBB0_1045
	s_mov_b64 s[10:11], 0

.LBB0_1045:
	s_or_b64 exec, exec, s[4:5]
	v_mov_b32_e32 v4, v144
	s_waitcnt lgkmcnt(0)
	s_barrier
	s_bfe_u32 s23, s95, 0x20006
	v_and_b32_e32 v5, 15, v4
	v_lshlrev_b32_e32 v0, 1, v4
	v_lshlrev_b32_e32 v2, 2, v4
	v_lshlrev_b32_e32 v1, 6, v5
	v_and_b32_e32 v0, 32, v0
	v_and_b32_e32 v2, 32, v2
	v_bitop3_b32 v0, v1, v2, v0 bitop3:0x36
	v_lshrrev_b32_e32 v1, 2, v4
	v_lshrrev_b32_e32 v2, 3, v4
	s_lshr_b32 s54, s95, 8
	v_xor_b32_e32 v1, v1, v2
	v_lshlrev_b32_e32 v2, 5, v4
	v_lshlrev_b32_e32 v1, 4, v1
	s_lshl_b32 s60, s54, 13
	v_and_b32_e32 v2, 0xfffffc00, v2
	s_lshl_b32 s58, s23, 12
	v_and_b32_e32 v1, 16, v1
	v_add_u32_e32 v3, s60, v2
	v_add_u32_e32 v2, s58, v2
	v_or3_b32 v3, v1, v3, v0
	v_or3_b32 v0, v1, v2, v0
	s_add_i32 s59, 0, 0x10000
	s_add_i32 s0, 0, 0x22140
	v_add_u32_e32 v145, 0, v3
	v_xad_u32 v146, v3, 16, 0
	v_add_u32_e32 v147, s59, v0
	v_xad_u32 v148, v0, 16, s59
	v_mov_b32_e32 v0, s0
	ds_read_b32 v0, v0
	s_lshl_b32 s55, s3, 10
	s_lshl_b32 s33, s54, 6
	s_lshl_b32 s61, s23, 5
	s_waitcnt lgkmcnt(0)
	v_lshlrev_b32_e32 v1, 3, v0
	v_cmp_ge_i32_e32 vcc, s27, v1
	s_cbranch_vccnz .LBB0_1068
	s_add_u32 s10, s8, 0x24000000
	s_addc_u32 s11, s9, 0
	s_ashr_i32 s0, s27, 31
	s_lshr_b32 s0, s0, 29
	s_add_i32 s0, s27, s0
	s_ashr_i32 s0, s0, 3
	v_cmp_ge_i32_e32 vcc, s0, v0
	s_mov_b64 s[4:5], s[10:11]
	s_cbranch_vccnz .LBB0_1048
	s_lshl_b32 s1, s0, 1
	s_add_i32 s1, s1, 0
	s_add_i32 s1, s1, 0x22240
	v_mov_b32_e32 v0, s1
	ds_read_u16 v0, v0
	s_mov_b32 s5, 0
	s_waitcnt lgkmcnt(0)
	v_readfirstlane_b32 s1, v0
	s_and_b32 s4, s1, 0xffff
	s_lshl_b64 s[4:5], s[4:5], 20
	s_add_u32 s4, s10, s4
	s_addc_u32 s5, s11, s5

.LBB0_1060:
	v_mov_b32_e32 v137, v133
	v_mov_b32_e32 v139, v133
	s_mov_b64 s[44:45], 0
	s_mov_b64 s[40:41], -1
	s_mov_b64 s[42:43], 0
	s_add_u32 s52, s12, s44
	s_addc_u32 s53, s13, s45
	s_add_u32 s29, s52, 0x100
	s_addc_u32 s48, s53, 0
	s_and_b64 s[46:47], s[42:43], exec
	s_cselect_b32 s46, s12, s29
	s_cselect_b32 s47, s13, s48
	s_add_u32 s29, s38, s44
	s_addc_u32 s44, s39, s45
	s_add_u32 s29, s29, 0x100
	s_addc_u32 s48, s44, 0
	ds_read_b128 v[162:165], v147
	ds_read_b128 v[170:173], v147 offset:2048
	ds_read_b128 v[166:169], v148
	ds_read_b128 v[174:177], v148 offset:2048
	s_and_b64 s[44:45], s[42:43], exec
	s_cselect_b32 s51, s35, s48
	s_cselect_b32 s50, s34, s29
	ds_read_b128 v[178:181], v145
	ds_read_b128 v[186:189], v145 offset:2048
	ds_read_b128 v[182:185], v146
	ds_read_b128 v[190:193], v146 offset:2048
	ds_read_b128 v[196:199], v145 offset:4096
	ds_read_b128 v[204:207], v145 offset:6144
	ds_read_b128 v[200:203], v146 offset:4096
	ds_read_b128 v[208:211], v146 offset:6144
	s_waitcnt vmcnt(6)
	s_waitcnt lgkmcnt(8)
	s_barrier
	s_waitcnt lgkmcnt(0)
	v_cndmask_b32_e64 v140, v134, v158, s[42:43]
	s_setprio 1
	s_waitcnt lgkmcnt(0)
	v_mfma_f32_16x16x128_f8f6f4 v[124:127], v[162:169], v[178:185], 0
	v_mfma_f32_16x16x128_f8f6f4 v[120:123], v[170:177], v[178:185], 0
	v_mfma_f32_16x16x128_f8f6f4 v[108:111], v[162:169], v[186:193], 0
	v_mfma_f32_16x16x128_f8f6f4 v[104:107], v[170:177], v[186:193], 0
	v_mfma_f32_16x16x128_f8f6f4 v[92:95], v[162:169], v[196:203], 0
	v_mfma_f32_16x16x128_f8f6f4 v[88:91], v[170:177], v[196:203], 0
	v_mfma_f32_16x16x128_f8f6f4 v[76:79], v[162:169], v[204:211], 0
	v_mfma_f32_16x16x128_f8f6f4 v[72:75], v[170:177], v[204:211], 0
	s_setprio 0
	s_barrier
	ds_read_b128 v[218:221], v147 offset:16384
	ds_read_b128 v[226:229], v147 offset:18432
	ds_read_b128 v[222:225], v148 offset:16384
	ds_read_b128 v[230:233], v148 offset:18432
	s_add_i32 m0, s0, 0xc000
	s_add_i32 s29, s0, 0xe000
	s_add_u32 s48, s50, 0x1000
	s_addc_u32 s49, s51, 0
	s_add_u32 s44, s50, 0x1080
	s_addc_u32 s45, s51, 0
	v_cndmask_b32_e64 v132, v135, v157, s[42:43]
	v_cndmask_b32_e64 v161, v136, v159, s[42:43]
	v_lshl_add_u64 v[252:253], s[52:53], 0, v[136:137]
	v_lshl_add_u64 v[252:253], v[252:253], 0, s[20:21]
	global_load_lds_dwordx4 v[252:253], off
	v_lshl_add_u64 v[252:253], s[52:53], 0, v[138:139]
	v_lshl_add_u64 v[252:253], v[252:253], 0, s[20:21]
	s_mov_b32 m0, s29
	s_nop 0
	global_load_lds_dwordx4 v[252:253], off
	s_barrier
	s_waitcnt lgkmcnt(0)
	s_setprio 1
	v_mfma_f32_16x16x128_f8f6f4 v[116:119], v[218:225], v[178:185], 0
	v_mfma_f32_16x16x128_f8f6f4 v[112:115], v[226:233], v[178:185], 0
	v_mfma_f32_16x16x128_f8f6f4 v[100:103], v[218:225], v[186:193], 0
	v_mfma_f32_16x16x128_f8f6f4 v[96:99], v[226:233], v[186:193], 0
	v_mfma_f32_16x16x128_f8f6f4 v[84:87], v[218:225], v[196:203], 0
	v_mfma_f32_16x16x128_f8f6f4 v[80:83], v[226:233], v[196:203], 0
	v_mfma_f32_16x16x128_f8f6f4 v[68:71], v[218:225], v[204:211], 0
	v_mfma_f32_16x16x128_f8f6f4 v[64:67], v[226:233], v[204:211], 0
	s_setprio 0
	s_barrier
	s_mov_b32 m0, s0
	ds_read_b128 v[178:181], v145 offset:16384
	ds_read_b128 v[186:189], v145 offset:18432
	ds_read_b128 v[182:185], v146 offset:16384
	ds_read_b128 v[190:193], v146 offset:18432
	ds_read_b128 v[196:199], v145 offset:20480
	ds_read_b128 v[204:207], v145 offset:22528
	ds_read_b128 v[200:203], v146 offset:20480
	ds_read_b128 v[208:211], v146 offset:22528
	global_load_lds_dwordx4 v132, s[46:47]
	s_mov_b32 m0, s56
	v_mov_b32_e32 v141, v133
	global_load_lds_dwordx4 v140, s[46:47]
	s_waitcnt lgkmcnt(8)
	s_barrier
	s_waitcnt lgkmcnt(0)
	v_lshl_add_u64 v[212:213], s[46:47], 0, v[132:133]
	v_lshl_add_u64 v[214:215], s[46:47], 0, v[140:141]
	s_setprio 1
	s_waitcnt lgkmcnt(0)
	v_mfma_f32_16x16x128_f8f6f4 v[60:63], v[162:169], v[178:185], 0
	v_mfma_f32_16x16x128_f8f6f4 v[56:59], v[170:177], v[178:185], 0
	v_mfma_f32_16x16x128_f8f6f4 v[44:47], v[162:169], v[186:193], 0
	v_mfma_f32_16x16x128_f8f6f4 v[40:43], v[170:177], v[186:193], 0
	v_mfma_f32_16x16x128_f8f6f4 v[28:31], v[162:169], v[196:203], 0
	v_mfma_f32_16x16x128_f8f6f4 v[24:27], v[170:177], v[196:203], 0
	v_mfma_f32_16x16x128_f8f6f4 v[12:15], v[162:169], v[204:211], 0
	v_mfma_f32_16x16x128_f8f6f4 v[8:11], v[170:177], v[204:211], 0
	s_setprio 0
	s_barrier
	s_mov_b32 m0, s1
	v_lshl_add_u64 v[140:141], s[50:51], 0, v[128:129]
	global_load_lds_dwordx4 v[140:141], off
	v_lshl_add_u64 v[142:143], s[50:51], 0, v[130:131]
	s_mov_b32 m0, s37
	s_nop 0
	global_load_lds_dwordx4 v[142:143], off
	s_waitcnt vmcnt(8)
	s_waitcnt lgkmcnt(0)
	s_barrier
	s_setprio 1
	s_waitcnt lgkmcnt(0)
	v_mfma_f32_16x16x128_f8f6f4 v[52:55], v[218:225], v[178:185], 0
	v_mfma_f32_16x16x128_f8f6f4 v[48:51], v[226:233], v[178:185], 0
	v_mfma_f32_16x16x128_f8f6f4 v[36:39], v[218:225], v[186:193], 0
	v_mfma_f32_16x16x128_f8f6f4 v[32:35], v[226:233], v[186:193], 0
	v_mfma_f32_16x16x128_f8f6f4 v[20:23], v[218:225], v[196:203], 0
	v_mfma_f32_16x16x128_f8f6f4 v[16:19], v[226:233], v[196:203], 0
	v_mfma_f32_16x16x128_f8f6f4 v[4:7], v[218:225], v[204:211], 0
	v_mfma_f32_16x16x128_f8f6f4 v[0:3], v[226:233], v[204:211], 0
	s_setprio 0
	s_barrier
	ds_read_b128 v[162:165], v147 offset:32768
	ds_read_b128 v[170:173], v147 offset:34816
	ds_read_b128 v[166:169], v148 offset:32768
	ds_read_b128 v[174:177], v148 offset:34816
	s_mov_b32 m0, s63
	ds_read_b128 v[178:181], v145 offset:32768
	ds_read_b128 v[186:189], v145 offset:34816
	ds_read_b128 v[182:185], v146 offset:32768
	ds_read_b128 v[190:193], v146 offset:34816
	ds_read_b128 v[196:199], v145 offset:36864
	ds_read_b128 v[204:207], v145 offset:38912
	ds_read_b128 v[200:203], v146 offset:36864
	ds_read_b128 v[208:211], v146 offset:38912
	v_cndmask_b32_e64 v132, v138, v160, s[42:43]
	global_load_lds_dwordx4 v161, s[46:47]
	s_mov_b32 m0, s64
	s_nop 0
	global_load_lds_dwordx4 v132, s[46:47]
	s_waitcnt vmcnt(8)
	s_waitcnt lgkmcnt(8)
	s_barrier
	s_waitcnt lgkmcnt(0)
	s_setprio 1
	v_mfma_f32_16x16x128_f8f6f4 v[124:127], v[162:169], v[178:185], v[124:127]
	v_mfma_f32_16x16x128_f8f6f4 v[120:123], v[170:177], v[178:185], v[120:123]
	v_mfma_f32_16x16x128_f8f6f4 v[108:111], v[162:169], v[186:193], v[108:111]
	v_mfma_f32_16x16x128_f8f6f4 v[104:107], v[170:177], v[186:193], v[104:107]
	v_mfma_f32_16x16x128_f8f6f4 v[92:95], v[162:169], v[196:203], v[92:95]
	v_mfma_f32_16x16x128_f8f6f4 v[88:91], v[170:177], v[196:203], v[88:91]
	v_mfma_f32_16x16x128_f8f6f4 v[76:79], v[162:169], v[204:211], v[76:79]
	v_mfma_f32_16x16x128_f8f6f4 v[72:75], v[170:177], v[204:211], v[72:75]
	s_setprio 0
	s_barrier
	ds_read_b128 v[218:221], v147 offset:49152
	ds_read_b128 v[226:229], v147 offset:51200
	ds_read_b128 v[222:225], v148 offset:49152
	ds_read_b128 v[230:233], v148 offset:51200
	v_lshl_add_u64 v[216:217], s[48:49], 0, v[128:129]
	s_mov_b32 m0, s57
	s_nop 0
	global_load_lds_dwordx4 v[216:217], off
	v_lshl_add_u64 v[216:217], s[48:49], 0, v[130:131]
	s_mov_b32 m0, s62
	s_nop 0
	global_load_lds_dwordx4 v[216:217], off
	s_waitcnt vmcnt(8)
	s_barrier
	s_waitcnt lgkmcnt(0)
	s_setprio 1
	v_mfma_f32_16x16x128_f8f6f4 v[116:119], v[218:225], v[178:185], v[116:119]
	v_mfma_f32_16x16x128_f8f6f4 v[112:115], v[226:233], v[178:185], v[112:115]
	v_mfma_f32_16x16x128_f8f6f4 v[100:103], v[218:225], v[186:193], v[100:103]
	v_mfma_f32_16x16x128_f8f6f4 v[96:99], v[226:233], v[186:193], v[96:99]
	v_mfma_f32_16x16x128_f8f6f4 v[84:87], v[218:225], v[196:203], v[84:87]
	v_mfma_f32_16x16x128_f8f6f4 v[80:83], v[226:233], v[196:203], v[80:83]
	v_mfma_f32_16x16x128_f8f6f4 v[68:71], v[218:225], v[204:211], v[68:71]
	v_mfma_f32_16x16x128_f8f6f4 v[64:67], v[226:233], v[204:211], v[64:67]
	s_setprio 0
	s_barrier
	s_mov_b32 m0, s67
	v_lshl_add_u64 v[212:213], v[212:213], 0, s[20:21]
	ds_read_b128 v[178:181], v145 offset:49152
	ds_read_b128 v[186:189], v145 offset:51200
	ds_read_b128 v[182:185], v146 offset:49152
	ds_read_b128 v[190:193], v146 offset:51200
	ds_read_b128 v[196:199], v145 offset:53248
	ds_read_b128 v[204:207], v145 offset:55296
	ds_read_b128 v[200:203], v146 offset:53248
	ds_read_b128 v[208:211], v146 offset:55296
	global_load_lds_dwordx4 v[212:213], off
	v_lshl_add_u64 v[212:213], v[214:215], 0, s[20:21]
	s_mov_b32 m0, s68
	s_nop 0
	global_load_lds_dwordx4 v[212:213], off
	s_waitcnt lgkmcnt(8)
	s_barrier
	s_waitcnt lgkmcnt(0)
	s_setprio 1
	v_mfma_f32_16x16x128_f8f6f4 v[60:63], v[162:169], v[178:185], v[60:63]
	v_mfma_f32_16x16x128_f8f6f4 v[56:59], v[170:177], v[178:185], v[56:59]
	v_mfma_f32_16x16x128_f8f6f4 v[44:47], v[162:169], v[186:193], v[44:47]
	v_mfma_f32_16x16x128_f8f6f4 v[40:43], v[170:177], v[186:193], v[40:43]
	v_mfma_f32_16x16x128_f8f6f4 v[28:31], v[162:169], v[196:203], v[28:31]
	v_mfma_f32_16x16x128_f8f6f4 v[24:27], v[170:177], v[196:203], v[24:27]
	v_mfma_f32_16x16x128_f8f6f4 v[12:15], v[162:169], v[204:211], v[12:15]
	v_mfma_f32_16x16x128_f8f6f4 v[8:11], v[170:177], v[204:211], v[8:11]
	s_setprio 0
	s_barrier
	s_mov_b32 m0, s65
	v_lshl_add_u64 v[140:141], v[140:141], 0, s[20:21]
	global_load_lds_dwordx4 v[140:141], off
	v_lshl_add_u64 v[140:141], v[142:143], 0, s[20:21]
	s_mov_b32 m0, s66
	s_nop 0
	global_load_lds_dwordx4 v[140:141], off
	s_waitcnt vmcnt(8)
	s_waitcnt lgkmcnt(0)
	s_barrier
	s_setprio 1
	s_waitcnt lgkmcnt(0)
	v_mfma_f32_16x16x128_f8f6f4 v[52:55], v[218:225], v[178:185], v[52:55]
	v_mfma_f32_16x16x128_f8f6f4 v[48:51], v[226:233], v[178:185], v[48:51]
	v_mfma_f32_16x16x128_f8f6f4 v[36:39], v[218:225], v[186:193], v[36:39]
	v_mfma_f32_16x16x128_f8f6f4 v[32:35], v[226:233], v[186:193], v[32:35]
	v_mfma_f32_16x16x128_f8f6f4 v[20:23], v[218:225], v[196:203], v[20:23]
	v_mfma_f32_16x16x128_f8f6f4 v[16:19], v[226:233], v[196:203], v[16:19]
	v_mfma_f32_16x16x128_f8f6f4 v[4:7], v[218:225], v[204:211], v[4:7]
	v_mfma_f32_16x16x128_f8f6f4 v[0:3], v[226:233], v[204:211], v[0:3]
	s_setprio 0
	s_barrier
	s_mov_b32 m0, s69
	v_lshl_add_u64 v[140:141], s[44:45], 0, v[128:129]
	global_load_lds_dwordx4 v[140:141], off
	v_lshl_add_u64 v[140:141], s[44:45], 0, v[130:131]
	s_mov_b32 m0, s70
	s_andn2_b64 vcc, exec, s[40:41]
	global_load_lds_dwordx4 v[140:141], off
	s_mov_b64 s[42:43], -1
	s_mov_b64 s[40:41], 0
	s_mov_b64 s[44:45], 0x100
	s_cbranch_vccz .LBB0_1061
	s_branch .Lpeel_after_1061
.LBB0_1061:
	s_add_u32 s52, s12, s44
	s_addc_u32 s53, s13, s45
	s_add_u32 s29, s52, 0x100
	s_addc_u32 s48, s53, 0
	s_and_b64 s[46:47], s[42:43], exec
	s_cselect_b32 s46, s12, s29
	s_cselect_b32 s47, s13, s48
	s_add_u32 s29, s38, s44
	s_addc_u32 s44, s39, s45
	s_add_u32 s29, s29, 0x100
	s_addc_u32 s48, s44, 0
	ds_read_b128 v[162:165], v147
	ds_read_b128 v[170:173], v147 offset:2048
	ds_read_b128 v[166:169], v148
	ds_read_b128 v[174:177], v148 offset:2048
	s_and_b64 s[44:45], s[42:43], exec
	s_cselect_b32 s51, s35, s48
	s_cselect_b32 s50, s34, s29
	ds_read_b128 v[178:181], v145
	ds_read_b128 v[186:189], v145 offset:2048
	ds_read_b128 v[182:185], v146
	ds_read_b128 v[190:193], v146 offset:2048
	ds_read_b128 v[196:199], v145 offset:4096
	ds_read_b128 v[204:207], v145 offset:6144
	ds_read_b128 v[200:203], v146 offset:4096
	ds_read_b128 v[208:211], v146 offset:6144
	s_waitcnt vmcnt(6)
	s_waitcnt lgkmcnt(8)
	s_barrier
	s_waitcnt lgkmcnt(0)
	v_cndmask_b32_e64 v140, v134, v158, s[42:43]
	s_setprio 1
	s_waitcnt lgkmcnt(0)
	v_mfma_f32_16x16x128_f8f6f4 v[124:127], v[162:169], v[178:185], v[124:127]
	v_mfma_f32_16x16x128_f8f6f4 v[120:123], v[170:177], v[178:185], v[120:123]
	v_mfma_f32_16x16x128_f8f6f4 v[108:111], v[162:169], v[186:193], v[108:111]
	v_mfma_f32_16x16x128_f8f6f4 v[104:107], v[170:177], v[186:193], v[104:107]
	v_mfma_f32_16x16x128_f8f6f4 v[92:95], v[162:169], v[196:203], v[92:95]
	v_mfma_f32_16x16x128_f8f6f4 v[88:91], v[170:177], v[196:203], v[88:91]
	v_mfma_f32_16x16x128_f8f6f4 v[76:79], v[162:169], v[204:211], v[76:79]
	v_mfma_f32_16x16x128_f8f6f4 v[72:75], v[170:177], v[204:211], v[72:75]
	s_setprio 0
	s_barrier
	ds_read_b128 v[218:221], v147 offset:16384
	ds_read_b128 v[226:229], v147 offset:18432
	ds_read_b128 v[222:225], v148 offset:16384
	ds_read_b128 v[230:233], v148 offset:18432
	s_add_i32 m0, s0, 0xc000
	s_add_i32 s29, s0, 0xe000
	s_add_u32 s48, s50, 0x1000
	s_addc_u32 s49, s51, 0
	s_add_u32 s44, s50, 0x1080
	s_addc_u32 s45, s51, 0
	v_cndmask_b32_e64 v132, v135, v157, s[42:43]
	v_cndmask_b32_e64 v161, v136, v159, s[42:43]
	v_lshl_add_u64 v[252:253], s[52:53], 0, v[136:137]
	v_lshl_add_u64 v[252:253], v[252:253], 0, s[20:21]
	global_load_lds_dwordx4 v[252:253], off
	v_lshl_add_u64 v[252:253], s[52:53], 0, v[138:139]
	v_lshl_add_u64 v[252:253], v[252:253], 0, s[20:21]
	s_mov_b32 m0, s29
	s_nop 0
	global_load_lds_dwordx4 v[252:253], off
	s_barrier
	s_waitcnt lgkmcnt(0)
	s_setprio 1
	v_mfma_f32_16x16x128_f8f6f4 v[116:119], v[218:225], v[178:185], v[116:119]
	v_mfma_f32_16x16x128_f8f6f4 v[112:115], v[226:233], v[178:185], v[112:115]
	v_mfma_f32_16x16x128_f8f6f4 v[100:103], v[218:225], v[186:193], v[100:103]
	v_mfma_f32_16x16x128_f8f6f4 v[96:99], v[226:233], v[186:193], v[96:99]
	v_mfma_f32_16x16x128_f8f6f4 v[84:87], v[218:225], v[196:203], v[84:87]
	v_mfma_f32_16x16x128_f8f6f4 v[80:83], v[226:233], v[196:203], v[80:83]
	v_mfma_f32_16x16x128_f8f6f4 v[68:71], v[218:225], v[204:211], v[68:71]
	v_mfma_f32_16x16x128_f8f6f4 v[64:67], v[226:233], v[204:211], v[64:67]
	s_setprio 0
	s_barrier
	s_mov_b32 m0, s0
	ds_read_b128 v[178:181], v145 offset:16384
	ds_read_b128 v[186:189], v145 offset:18432
	ds_read_b128 v[182:185], v146 offset:16384
	ds_read_b128 v[190:193], v146 offset:18432
	ds_read_b128 v[196:199], v145 offset:20480
	ds_read_b128 v[204:207], v145 offset:22528
	ds_read_b128 v[200:203], v146 offset:20480
	ds_read_b128 v[208:211], v146 offset:22528
	global_load_lds_dwordx4 v132, s[46:47]
	s_mov_b32 m0, s56
	v_mov_b32_e32 v141, v133
	global_load_lds_dwordx4 v140, s[46:47]
	s_waitcnt lgkmcnt(8)
	s_barrier
	s_waitcnt lgkmcnt(0)
	v_lshl_add_u64 v[212:213], s[46:47], 0, v[132:133]
	v_lshl_add_u64 v[214:215], s[46:47], 0, v[140:141]
	s_setprio 1
	s_waitcnt lgkmcnt(0)
	v_mfma_f32_16x16x128_f8f6f4 v[60:63], v[162:169], v[178:185], v[60:63]
	v_mfma_f32_16x16x128_f8f6f4 v[56:59], v[170:177], v[178:185], v[56:59]
	v_mfma_f32_16x16x128_f8f6f4 v[44:47], v[162:169], v[186:193], v[44:47]
	v_mfma_f32_16x16x128_f8f6f4 v[40:43], v[170:177], v[186:193], v[40:43]
	v_mfma_f32_16x16x128_f8f6f4 v[28:31], v[162:169], v[196:203], v[28:31]
	v_mfma_f32_16x16x128_f8f6f4 v[24:27], v[170:177], v[196:203], v[24:27]
	v_mfma_f32_16x16x128_f8f6f4 v[12:15], v[162:169], v[204:211], v[12:15]
	v_mfma_f32_16x16x128_f8f6f4 v[8:11], v[170:177], v[204:211], v[8:11]
	s_setprio 0
	s_barrier
	s_mov_b32 m0, s1
	v_lshl_add_u64 v[140:141], s[50:51], 0, v[128:129]
	global_load_lds_dwordx4 v[140:141], off
	v_lshl_add_u64 v[142:143], s[50:51], 0, v[130:131]
	s_mov_b32 m0, s37
	s_nop 0
	global_load_lds_dwordx4 v[142:143], off
	s_waitcnt vmcnt(8)
	s_waitcnt lgkmcnt(0)
	s_barrier
	s_setprio 1
	s_waitcnt lgkmcnt(0)
	v_mfma_f32_16x16x128_f8f6f4 v[52:55], v[218:225], v[178:185], v[52:55]
	v_mfma_f32_16x16x128_f8f6f4 v[48:51], v[226:233], v[178:185], v[48:51]
	v_mfma_f32_16x16x128_f8f6f4 v[36:39], v[218:225], v[186:193], v[36:39]
	v_mfma_f32_16x16x128_f8f6f4 v[32:35], v[226:233], v[186:193], v[32:35]
	v_mfma_f32_16x16x128_f8f6f4 v[20:23], v[218:225], v[196:203], v[20:23]
	v_mfma_f32_16x16x128_f8f6f4 v[16:19], v[226:233], v[196:203], v[16:19]
	v_mfma_f32_16x16x128_f8f6f4 v[4:7], v[218:225], v[204:211], v[4:7]
	v_mfma_f32_16x16x128_f8f6f4 v[0:3], v[226:233], v[204:211], v[0:3]
	s_setprio 0
	s_barrier
	ds_read_b128 v[162:165], v147 offset:32768
	ds_read_b128 v[170:173], v147 offset:34816
	ds_read_b128 v[166:169], v148 offset:32768
	ds_read_b128 v[174:177], v148 offset:34816
	s_mov_b32 m0, s63
	ds_read_b128 v[178:181], v145 offset:32768
	ds_read_b128 v[186:189], v145 offset:34816
	ds_read_b128 v[182:185], v146 offset:32768
	ds_read_b128 v[190:193], v146 offset:34816
	ds_read_b128 v[196:199], v145 offset:36864
	ds_read_b128 v[204:207], v145 offset:38912
	ds_read_b128 v[200:203], v146 offset:36864
	ds_read_b128 v[208:211], v146 offset:38912
	v_cndmask_b32_e64 v132, v138, v160, s[42:43]
	global_load_lds_dwordx4 v161, s[46:47]
	s_mov_b32 m0, s64
	s_nop 0
	global_load_lds_dwordx4 v132, s[46:47]
	s_waitcnt vmcnt(8)
	s_waitcnt lgkmcnt(8)
	s_barrier
	s_waitcnt lgkmcnt(0)
	s_setprio 1
	v_mfma_f32_16x16x128_f8f6f4 v[124:127], v[162:169], v[178:185], v[124:127]
	v_mfma_f32_16x16x128_f8f6f4 v[120:123], v[170:177], v[178:185], v[120:123]
	v_mfma_f32_16x16x128_f8f6f4 v[108:111], v[162:169], v[186:193], v[108:111]
	v_mfma_f32_16x16x128_f8f6f4 v[104:107], v[170:177], v[186:193], v[104:107]
	v_mfma_f32_16x16x128_f8f6f4 v[92:95], v[162:169], v[196:203], v[92:95]
	v_mfma_f32_16x16x128_f8f6f4 v[88:91], v[170:177], v[196:203], v[88:91]
	v_mfma_f32_16x16x128_f8f6f4 v[76:79], v[162:169], v[204:211], v[76:79]
	v_mfma_f32_16x16x128_f8f6f4 v[72:75], v[170:177], v[204:211], v[72:75]
	s_setprio 0
	s_barrier
	ds_read_b128 v[218:221], v147 offset:49152
	ds_read_b128 v[226:229], v147 offset:51200
	ds_read_b128 v[222:225], v148 offset:49152
	ds_read_b128 v[230:233], v148 offset:51200
	v_lshl_add_u64 v[216:217], s[48:49], 0, v[128:129]
	s_mov_b32 m0, s57
	s_nop 0
	global_load_lds_dwordx4 v[216:217], off
	v_lshl_add_u64 v[216:217], s[48:49], 0, v[130:131]
	s_mov_b32 m0, s62
	s_nop 0
	global_load_lds_dwordx4 v[216:217], off
	s_waitcnt vmcnt(8)
	s_barrier
	s_waitcnt lgkmcnt(0)
	s_setprio 1
	v_mfma_f32_16x16x128_f8f6f4 v[116:119], v[218:225], v[178:185], v[116:119]
	v_mfma_f32_16x16x128_f8f6f4 v[112:115], v[226:233], v[178:185], v[112:115]
	v_mfma_f32_16x16x128_f8f6f4 v[100:103], v[218:225], v[186:193], v[100:103]
	v_mfma_f32_16x16x128_f8f6f4 v[96:99], v[226:233], v[186:193], v[96:99]
	v_mfma_f32_16x16x128_f8f6f4 v[84:87], v[218:225], v[196:203], v[84:87]
	v_mfma_f32_16x16x128_f8f6f4 v[80:83], v[226:233], v[196:203], v[80:83]
	v_mfma_f32_16x16x128_f8f6f4 v[68:71], v[218:225], v[204:211], v[68:71]
	v_mfma_f32_16x16x128_f8f6f4 v[64:67], v[226:233], v[204:211], v[64:67]
	s_setprio 0
	s_barrier
	s_mov_b32 m0, s67
	v_lshl_add_u64 v[212:213], v[212:213], 0, s[20:21]
	ds_read_b128 v[178:181], v145 offset:49152
	ds_read_b128 v[186:189], v145 offset:51200
	ds_read_b128 v[182:185], v146 offset:49152
	ds_read_b128 v[190:193], v146 offset:51200
	ds_read_b128 v[196:199], v145 offset:53248
	ds_read_b128 v[204:207], v145 offset:55296
	ds_read_b128 v[200:203], v146 offset:53248
	ds_read_b128 v[208:211], v146 offset:55296
	global_load_lds_dwordx4 v[212:213], off
	v_lshl_add_u64 v[212:213], v[214:215], 0, s[20:21]
	s_mov_b32 m0, s68
	s_nop 0
	global_load_lds_dwordx4 v[212:213], off
	s_waitcnt lgkmcnt(8)
	s_barrier
	s_waitcnt lgkmcnt(0)
	s_setprio 1
	v_mfma_f32_16x16x128_f8f6f4 v[60:63], v[162:169], v[178:185], v[60:63]
	v_mfma_f32_16x16x128_f8f6f4 v[56:59], v[170:177], v[178:185], v[56:59]
	v_mfma_f32_16x16x128_f8f6f4 v[44:47], v[162:169], v[186:193], v[44:47]
	v_mfma_f32_16x16x128_f8f6f4 v[40:43], v[170:177], v[186:193], v[40:43]
	v_mfma_f32_16x16x128_f8f6f4 v[28:31], v[162:169], v[196:203], v[28:31]
	v_mfma_f32_16x16x128_f8f6f4 v[24:27], v[170:177], v[196:203], v[24:27]
	v_mfma_f32_16x16x128_f8f6f4 v[12:15], v[162:169], v[204:211], v[12:15]
	v_mfma_f32_16x16x128_f8f6f4 v[8:11], v[170:177], v[204:211], v[8:11]
	s_setprio 0
	s_barrier
	s_mov_b32 m0, s65
	v_lshl_add_u64 v[140:141], v[140:141], 0, s[20:21]
	global_load_lds_dwordx4 v[140:141], off
	v_lshl_add_u64 v[140:141], v[142:143], 0, s[20:21]
	s_mov_b32 m0, s66
	s_nop 0
	global_load_lds_dwordx4 v[140:141], off
	s_waitcnt vmcnt(8)
	s_waitcnt lgkmcnt(0)
	s_barrier
	s_setprio 1
	s_waitcnt lgkmcnt(0)
	v_mfma_f32_16x16x128_f8f6f4 v[52:55], v[218:225], v[178:185], v[52:55]
	v_mfma_f32_16x16x128_f8f6f4 v[48:51], v[226:233], v[178:185], v[48:51]
	v_mfma_f32_16x16x128_f8f6f4 v[36:39], v[218:225], v[186:193], v[36:39]
	v_mfma_f32_16x16x128_f8f6f4 v[32:35], v[226:233], v[186:193], v[32:35]
	v_mfma_f32_16x16x128_f8f6f4 v[20:23], v[218:225], v[196:203], v[20:23]
	v_mfma_f32_16x16x128_f8f6f4 v[16:19], v[226:233], v[196:203], v[16:19]
	v_mfma_f32_16x16x128_f8f6f4 v[4:7], v[218:225], v[204:211], v[4:7]
	v_mfma_f32_16x16x128_f8f6f4 v[0:3], v[226:233], v[204:211], v[0:3]
	s_setprio 0
	s_barrier
	s_mov_b32 m0, s69
	v_lshl_add_u64 v[140:141], s[44:45], 0, v[128:129]
	global_load_lds_dwordx4 v[140:141], off
	v_lshl_add_u64 v[140:141], s[44:45], 0, v[130:131]
	s_mov_b32 m0, s70
	s_andn2_b64 vcc, exec, s[40:41]
	global_load_lds_dwordx4 v[140:141], off
	s_mov_b64 s[42:43], -1
	s_mov_b64 s[40:41], 0
	s_mov_b64 s[44:45], 0x100
	s_cbranch_vccz .LBB0_1061

.LBB0_1080:
	v_mov_b32_e32 v137, v133
	v_mov_b32_e32 v139, v133
	s_mov_b64 s[34:35], 0
	s_mov_b64 s[28:29], -1
	s_mov_b64 s[30:31], 0
	s_add_u32 s42, s10, s34
	s_addc_u32 s43, s11, s35
	s_add_u32 s38, s42, 0x100
	s_addc_u32 s39, s43, 0
	s_and_b64 s[36:37], s[30:31], exec
	s_cselect_b32 s36, s10, s38
	s_cselect_b32 s37, s11, s39
	s_add_u32 s34, s26, s34
	s_addc_u32 s35, s27, s35
	s_add_u32 s38, s34, 0x100
	s_addc_u32 s39, s35, 0
	ds_read_b128 v[160:163], v147
	ds_read_b128 v[168:171], v147 offset:2048
	ds_read_b128 v[164:167], v148
	ds_read_b128 v[172:175], v148 offset:2048
	s_and_b64 s[34:35], s[30:31], exec
	s_cselect_b32 s41, s25, s39
	s_cselect_b32 s40, s24, s38
	ds_read_b128 v[176:179], v145
	ds_read_b128 v[184:187], v145 offset:2048
	ds_read_b128 v[180:183], v146
	ds_read_b128 v[188:191], v146 offset:2048
	ds_read_b128 v[196:199], v145 offset:4096
	ds_read_b128 v[204:207], v145 offset:6144
	ds_read_b128 v[200:203], v146 offset:4096
	ds_read_b128 v[208:211], v146 offset:6144
	s_waitcnt vmcnt(6)
	s_waitcnt lgkmcnt(8)
	s_barrier
	s_waitcnt lgkmcnt(0)
	v_cndmask_b32_e64 v140, v134, v156, s[30:31]
	s_setprio 1
	s_waitcnt lgkmcnt(0)
	v_mfma_f32_16x16x128_f8f6f4 v[124:127], v[160:167], v[176:183], 0
	v_mfma_f32_16x16x128_f8f6f4 v[120:123], v[168:175], v[176:183], 0
	v_mfma_f32_16x16x128_f8f6f4 v[108:111], v[160:167], v[184:191], 0
	v_mfma_f32_16x16x128_f8f6f4 v[104:107], v[168:175], v[184:191], 0
	v_mfma_f32_16x16x128_f8f6f4 v[92:95], v[160:167], v[196:203], 0
	v_mfma_f32_16x16x128_f8f6f4 v[88:91], v[168:175], v[196:203], 0
	v_mfma_f32_16x16x128_f8f6f4 v[76:79], v[160:167], v[204:211], 0
	v_mfma_f32_16x16x128_f8f6f4 v[72:75], v[168:175], v[204:211], 0
	s_setprio 0
	s_barrier
	ds_read_b128 v[218:221], v147 offset:16384
	ds_read_b128 v[226:229], v147 offset:18432
	ds_read_b128 v[222:225], v148 offset:16384
	ds_read_b128 v[230:233], v148 offset:18432
	s_add_i32 m0, s1, 0xc000
	s_add_i32 s64, s1, 0xe000
	s_add_u32 s38, s40, 0x1000
	s_addc_u32 s39, s41, 0
	s_add_u32 s34, s40, 0x1080
	s_addc_u32 s35, s41, 0
	v_cndmask_b32_e64 v132, v135, v155, s[30:31]
	v_cndmask_b32_e64 v159, v136, v157, s[30:31]
	v_lshl_add_u64 v[252:253], s[42:43], 0, v[136:137]
	v_lshl_add_u64 v[252:253], v[252:253], 0, s[16:17]
	global_load_lds_dwordx4 v[252:253], off
	v_lshl_add_u64 v[252:253], s[42:43], 0, v[138:139]
	v_lshl_add_u64 v[252:253], v[252:253], 0, s[16:17]
	s_mov_b32 m0, s64
	s_nop 0
	global_load_lds_dwordx4 v[252:253], off
	s_barrier
	s_waitcnt lgkmcnt(0)
	s_setprio 1
	v_mfma_f32_16x16x128_f8f6f4 v[116:119], v[218:225], v[176:183], 0
	v_mfma_f32_16x16x128_f8f6f4 v[112:115], v[226:233], v[176:183], 0
	v_mfma_f32_16x16x128_f8f6f4 v[100:103], v[218:225], v[184:191], 0
	v_mfma_f32_16x16x128_f8f6f4 v[96:99], v[226:233], v[184:191], 0
	v_mfma_f32_16x16x128_f8f6f4 v[84:87], v[218:225], v[196:203], 0
	v_mfma_f32_16x16x128_f8f6f4 v[80:83], v[226:233], v[196:203], 0
	v_mfma_f32_16x16x128_f8f6f4 v[68:71], v[218:225], v[204:211], 0
	v_mfma_f32_16x16x128_f8f6f4 v[64:67], v[226:233], v[204:211], 0
	s_setprio 0
	s_barrier
	s_mov_b32 m0, s1
	ds_read_b128 v[176:179], v145 offset:16384
	ds_read_b128 v[184:187], v145 offset:18432
	ds_read_b128 v[180:183], v146 offset:16384
	ds_read_b128 v[188:191], v146 offset:18432
	ds_read_b128 v[196:199], v145 offset:20480
	ds_read_b128 v[204:207], v145 offset:22528
	ds_read_b128 v[200:203], v146 offset:20480
	ds_read_b128 v[208:211], v146 offset:22528
	global_load_lds_dwordx4 v132, s[36:37]
	s_mov_b32 m0, s48
	v_mov_b32_e32 v141, v133
	global_load_lds_dwordx4 v140, s[36:37]
	s_waitcnt lgkmcnt(8)
	s_barrier
	s_waitcnt lgkmcnt(0)
	v_lshl_add_u64 v[192:193], s[36:37], 0, v[132:133]
	v_lshl_add_u64 v[212:213], s[36:37], 0, v[140:141]
	s_setprio 1
	s_waitcnt lgkmcnt(0)
	v_mfma_f32_16x16x128_f8f6f4 v[60:63], v[160:167], v[176:183], 0
	v_mfma_f32_16x16x128_f8f6f4 v[56:59], v[168:175], v[176:183], 0
	v_mfma_f32_16x16x128_f8f6f4 v[44:47], v[160:167], v[184:191], 0
	v_mfma_f32_16x16x128_f8f6f4 v[40:43], v[168:175], v[184:191], 0
	v_mfma_f32_16x16x128_f8f6f4 v[28:31], v[160:167], v[196:203], 0
	v_mfma_f32_16x16x128_f8f6f4 v[24:27], v[168:175], v[196:203], 0
	v_mfma_f32_16x16x128_f8f6f4 v[12:15], v[160:167], v[204:211], 0
	v_mfma_f32_16x16x128_f8f6f4 v[8:11], v[168:175], v[204:211], 0
	s_setprio 0
	s_barrier
	s_mov_b32 m0, s46
	v_lshl_add_u64 v[140:141], s[40:41], 0, v[130:131]
	global_load_lds_dwordx4 v[140:141], off
	v_lshl_add_u64 v[142:143], s[40:41], 0, v[128:129]
	s_mov_b32 m0, s47
	s_nop 0
	global_load_lds_dwordx4 v[142:143], off
	s_waitcnt vmcnt(8)
	s_waitcnt lgkmcnt(0)
	s_barrier
	s_setprio 1
	s_waitcnt lgkmcnt(0)
	v_mfma_f32_16x16x128_f8f6f4 v[52:55], v[218:225], v[176:183], 0
	v_mfma_f32_16x16x128_f8f6f4 v[48:51], v[226:233], v[176:183], 0
	v_mfma_f32_16x16x128_f8f6f4 v[36:39], v[218:225], v[184:191], 0
	v_mfma_f32_16x16x128_f8f6f4 v[32:35], v[226:233], v[184:191], 0
	v_mfma_f32_16x16x128_f8f6f4 v[20:23], v[218:225], v[196:203], 0
	v_mfma_f32_16x16x128_f8f6f4 v[16:19], v[226:233], v[196:203], 0
	v_mfma_f32_16x16x128_f8f6f4 v[4:7], v[218:225], v[204:211], 0
	v_mfma_f32_16x16x128_f8f6f4 v[0:3], v[226:233], v[204:211], 0
	s_setprio 0
	s_barrier
	ds_read_b128 v[160:163], v147 offset:32768
	ds_read_b128 v[168:171], v147 offset:34816
	ds_read_b128 v[164:167], v148 offset:32768
	ds_read_b128 v[172:175], v148 offset:34816
	s_mov_b32 m0, s51
	ds_read_b128 v[176:179], v145 offset:32768
	ds_read_b128 v[184:187], v145 offset:34816
	ds_read_b128 v[180:183], v146 offset:32768
	ds_read_b128 v[188:191], v146 offset:34816
	ds_read_b128 v[196:199], v145 offset:36864
	ds_read_b128 v[204:207], v145 offset:38912
	ds_read_b128 v[200:203], v146 offset:36864
	ds_read_b128 v[208:211], v146 offset:38912
	v_cndmask_b32_e64 v132, v138, v158, s[30:31]
	global_load_lds_dwordx4 v159, s[36:37]
	s_mov_b32 m0, s52
	s_nop 0
	global_load_lds_dwordx4 v132, s[36:37]
	s_waitcnt vmcnt(8)
	s_waitcnt lgkmcnt(8)
	s_barrier
	s_waitcnt lgkmcnt(0)
	s_setprio 1
	v_mfma_f32_16x16x128_f8f6f4 v[124:127], v[160:167], v[176:183], v[124:127]
	v_mfma_f32_16x16x128_f8f6f4 v[120:123], v[168:175], v[176:183], v[120:123]
	v_mfma_f32_16x16x128_f8f6f4 v[108:111], v[160:167], v[184:191], v[108:111]
	v_mfma_f32_16x16x128_f8f6f4 v[104:107], v[168:175], v[184:191], v[104:107]
	v_mfma_f32_16x16x128_f8f6f4 v[92:95], v[160:167], v[196:203], v[92:95]
	v_mfma_f32_16x16x128_f8f6f4 v[88:91], v[168:175], v[196:203], v[88:91]
	v_mfma_f32_16x16x128_f8f6f4 v[76:79], v[160:167], v[204:211], v[76:79]
	v_mfma_f32_16x16x128_f8f6f4 v[72:75], v[168:175], v[204:211], v[72:75]
	s_setprio 0
	s_barrier
	ds_read_b128 v[218:221], v147 offset:49152
	ds_read_b128 v[226:229], v147 offset:51200
	ds_read_b128 v[222:225], v148 offset:49152
	ds_read_b128 v[230:233], v148 offset:51200
	v_lshl_add_u64 v[214:215], s[38:39], 0, v[130:131]
	s_mov_b32 m0, s49
	s_nop 0
	global_load_lds_dwordx4 v[214:215], off
	v_lshl_add_u64 v[214:215], s[38:39], 0, v[128:129]
	s_mov_b32 m0, s50
	s_nop 0
	global_load_lds_dwordx4 v[214:215], off
	s_waitcnt vmcnt(8)
	s_barrier
	s_waitcnt lgkmcnt(0)
	s_setprio 1
	v_mfma_f32_16x16x128_f8f6f4 v[116:119], v[218:225], v[176:183], v[116:119]
	v_mfma_f32_16x16x128_f8f6f4 v[112:115], v[226:233], v[176:183], v[112:115]
	v_mfma_f32_16x16x128_f8f6f4 v[100:103], v[218:225], v[184:191], v[100:103]
	v_mfma_f32_16x16x128_f8f6f4 v[96:99], v[226:233], v[184:191], v[96:99]
	v_mfma_f32_16x16x128_f8f6f4 v[84:87], v[218:225], v[196:203], v[84:87]
	v_mfma_f32_16x16x128_f8f6f4 v[80:83], v[226:233], v[196:203], v[80:83]
	v_mfma_f32_16x16x128_f8f6f4 v[68:71], v[218:225], v[204:211], v[68:71]
	v_mfma_f32_16x16x128_f8f6f4 v[64:67], v[226:233], v[204:211], v[64:67]
	s_setprio 0
	s_barrier
	s_mov_b32 m0, s56
	v_lshl_add_u64 v[192:193], v[192:193], 0, s[16:17]
	ds_read_b128 v[176:179], v145 offset:49152
	ds_read_b128 v[184:187], v145 offset:51200
	ds_read_b128 v[180:183], v146 offset:49152
	ds_read_b128 v[188:191], v146 offset:51200
	ds_read_b128 v[196:199], v145 offset:53248
	ds_read_b128 v[204:207], v145 offset:55296
	ds_read_b128 v[200:203], v146 offset:53248
	ds_read_b128 v[208:211], v146 offset:55296
	global_load_lds_dwordx4 v[192:193], off
	v_lshl_add_u64 v[192:193], v[212:213], 0, s[16:17]
	s_mov_b32 m0, s57
	s_nop 0
	global_load_lds_dwordx4 v[192:193], off
	s_waitcnt lgkmcnt(8)
	s_barrier
	s_waitcnt lgkmcnt(0)
	s_setprio 1
	v_mfma_f32_16x16x128_f8f6f4 v[60:63], v[160:167], v[176:183], v[60:63]
	v_mfma_f32_16x16x128_f8f6f4 v[56:59], v[168:175], v[176:183], v[56:59]
	v_mfma_f32_16x16x128_f8f6f4 v[44:47], v[160:167], v[184:191], v[44:47]
	v_mfma_f32_16x16x128_f8f6f4 v[40:43], v[168:175], v[184:191], v[40:43]
	v_mfma_f32_16x16x128_f8f6f4 v[28:31], v[160:167], v[196:203], v[28:31]
	v_mfma_f32_16x16x128_f8f6f4 v[24:27], v[168:175], v[196:203], v[24:27]
	v_mfma_f32_16x16x128_f8f6f4 v[12:15], v[160:167], v[204:211], v[12:15]
	v_mfma_f32_16x16x128_f8f6f4 v[8:11], v[168:175], v[204:211], v[8:11]
	s_setprio 0
	s_barrier
	s_mov_b32 m0, s54
	v_lshl_add_u64 v[140:141], v[140:141], 0, s[16:17]
	global_load_lds_dwordx4 v[140:141], off
	v_lshl_add_u64 v[140:141], v[142:143], 0, s[16:17]
	s_mov_b32 m0, s55
	s_nop 0
	global_load_lds_dwordx4 v[140:141], off
	s_waitcnt vmcnt(8)
	s_waitcnt lgkmcnt(0)
	s_barrier
	s_setprio 1
	s_waitcnt lgkmcnt(0)
	v_mfma_f32_16x16x128_f8f6f4 v[52:55], v[218:225], v[176:183], v[52:55]
	v_mfma_f32_16x16x128_f8f6f4 v[48:51], v[226:233], v[176:183], v[48:51]
	v_mfma_f32_16x16x128_f8f6f4 v[36:39], v[218:225], v[184:191], v[36:39]
	v_mfma_f32_16x16x128_f8f6f4 v[32:35], v[226:233], v[184:191], v[32:35]
	v_mfma_f32_16x16x128_f8f6f4 v[20:23], v[218:225], v[196:203], v[20:23]
	v_mfma_f32_16x16x128_f8f6f4 v[16:19], v[226:233], v[196:203], v[16:19]
	v_mfma_f32_16x16x128_f8f6f4 v[4:7], v[218:225], v[204:211], v[4:7]
	v_mfma_f32_16x16x128_f8f6f4 v[0:3], v[226:233], v[204:211], v[0:3]
	s_setprio 0
	s_barrier
	s_mov_b32 m0, s58
	v_lshl_add_u64 v[140:141], s[34:35], 0, v[130:131]
	global_load_lds_dwordx4 v[140:141], off
	v_lshl_add_u64 v[140:141], s[34:35], 0, v[128:129]
	s_mov_b32 m0, s59
	s_andn2_b64 vcc, exec, s[28:29]
	global_load_lds_dwordx4 v[140:141], off
	s_mov_b64 s[30:31], -1
	s_mov_b64 s[28:29], 0
	s_mov_b64 s[34:35], 0x100
	s_cbranch_vccz .LBB0_1081
	s_branch .Lpeel_after_1081
.LBB0_1081:
	s_add_u32 s42, s10, s34
	s_addc_u32 s43, s11, s35
	s_add_u32 s38, s42, 0x100
	s_addc_u32 s39, s43, 0
	s_and_b64 s[36:37], s[30:31], exec
	s_cselect_b32 s36, s10, s38
	s_cselect_b32 s37, s11, s39
	s_add_u32 s34, s26, s34
	s_addc_u32 s35, s27, s35
	s_add_u32 s38, s34, 0x100
	s_addc_u32 s39, s35, 0
	ds_read_b128 v[160:163], v147
	ds_read_b128 v[168:171], v147 offset:2048
	ds_read_b128 v[164:167], v148
	ds_read_b128 v[172:175], v148 offset:2048
	s_and_b64 s[34:35], s[30:31], exec
	s_cselect_b32 s41, s25, s39
	s_cselect_b32 s40, s24, s38
	ds_read_b128 v[176:179], v145
	ds_read_b128 v[184:187], v145 offset:2048
	ds_read_b128 v[180:183], v146
	ds_read_b128 v[188:191], v146 offset:2048
	ds_read_b128 v[196:199], v145 offset:4096
	ds_read_b128 v[204:207], v145 offset:6144
	ds_read_b128 v[200:203], v146 offset:4096
	ds_read_b128 v[208:211], v146 offset:6144
	s_waitcnt vmcnt(6)
	s_waitcnt lgkmcnt(8)
	s_barrier
	s_waitcnt lgkmcnt(0)
	v_cndmask_b32_e64 v140, v134, v156, s[30:31]
	s_setprio 1
	s_waitcnt lgkmcnt(0)
	v_mfma_f32_16x16x128_f8f6f4 v[124:127], v[160:167], v[176:183], v[124:127]
	v_mfma_f32_16x16x128_f8f6f4 v[120:123], v[168:175], v[176:183], v[120:123]
	v_mfma_f32_16x16x128_f8f6f4 v[108:111], v[160:167], v[184:191], v[108:111]
	v_mfma_f32_16x16x128_f8f6f4 v[104:107], v[168:175], v[184:191], v[104:107]
	v_mfma_f32_16x16x128_f8f6f4 v[92:95], v[160:167], v[196:203], v[92:95]
	v_mfma_f32_16x16x128_f8f6f4 v[88:91], v[168:175], v[196:203], v[88:91]
	v_mfma_f32_16x16x128_f8f6f4 v[76:79], v[160:167], v[204:211], v[76:79]
	v_mfma_f32_16x16x128_f8f6f4 v[72:75], v[168:175], v[204:211], v[72:75]
	s_setprio 0
	s_barrier
	ds_read_b128 v[218:221], v147 offset:16384
	ds_read_b128 v[226:229], v147 offset:18432
	ds_read_b128 v[222:225], v148 offset:16384
	ds_read_b128 v[230:233], v148 offset:18432
	s_add_i32 m0, s1, 0xc000
	s_add_i32 s64, s1, 0xe000
	s_add_u32 s38, s40, 0x1000
	s_addc_u32 s39, s41, 0
	s_add_u32 s34, s40, 0x1080
	s_addc_u32 s35, s41, 0
	v_cndmask_b32_e64 v132, v135, v155, s[30:31]
	v_cndmask_b32_e64 v159, v136, v157, s[30:31]
	v_lshl_add_u64 v[252:253], s[42:43], 0, v[136:137]
	v_lshl_add_u64 v[252:253], v[252:253], 0, s[16:17]
	global_load_lds_dwordx4 v[252:253], off
	v_lshl_add_u64 v[252:253], s[42:43], 0, v[138:139]
	v_lshl_add_u64 v[252:253], v[252:253], 0, s[16:17]
	s_mov_b32 m0, s64
	s_nop 0
	global_load_lds_dwordx4 v[252:253], off
	s_barrier
	s_waitcnt lgkmcnt(0)
	s_setprio 1
	v_mfma_f32_16x16x128_f8f6f4 v[116:119], v[218:225], v[176:183], v[116:119]
	v_mfma_f32_16x16x128_f8f6f4 v[112:115], v[226:233], v[176:183], v[112:115]
	v_mfma_f32_16x16x128_f8f6f4 v[100:103], v[218:225], v[184:191], v[100:103]
	v_mfma_f32_16x16x128_f8f6f4 v[96:99], v[226:233], v[184:191], v[96:99]
	v_mfma_f32_16x16x128_f8f6f4 v[84:87], v[218:225], v[196:203], v[84:87]
	v_mfma_f32_16x16x128_f8f6f4 v[80:83], v[226:233], v[196:203], v[80:83]
	v_mfma_f32_16x16x128_f8f6f4 v[68:71], v[218:225], v[204:211], v[68:71]
	v_mfma_f32_16x16x128_f8f6f4 v[64:67], v[226:233], v[204:211], v[64:67]
	s_setprio 0
	s_barrier
	s_mov_b32 m0, s1
	ds_read_b128 v[176:179], v145 offset:16384
	ds_read_b128 v[184:187], v145 offset:18432
	ds_read_b128 v[180:183], v146 offset:16384
	ds_read_b128 v[188:191], v146 offset:18432
	ds_read_b128 v[196:199], v145 offset:20480
	ds_read_b128 v[204:207], v145 offset:22528
	ds_read_b128 v[200:203], v146 offset:20480
	ds_read_b128 v[208:211], v146 offset:22528
	global_load_lds_dwordx4 v132, s[36:37]
	s_mov_b32 m0, s48
	v_mov_b32_e32 v141, v133
	global_load_lds_dwordx4 v140, s[36:37]
	s_waitcnt lgkmcnt(8)
	s_barrier
	s_waitcnt lgkmcnt(0)
	v_lshl_add_u64 v[192:193], s[36:37], 0, v[132:133]
	v_lshl_add_u64 v[212:213], s[36:37], 0, v[140:141]
	s_setprio 1
	s_waitcnt lgkmcnt(0)
	v_mfma_f32_16x16x128_f8f6f4 v[60:63], v[160:167], v[176:183], v[60:63]
	v_mfma_f32_16x16x128_f8f6f4 v[56:59], v[168:175], v[176:183], v[56:59]
	v_mfma_f32_16x16x128_f8f6f4 v[44:47], v[160:167], v[184:191], v[44:47]
	v_mfma_f32_16x16x128_f8f6f4 v[40:43], v[168:175], v[184:191], v[40:43]
	v_mfma_f32_16x16x128_f8f6f4 v[28:31], v[160:167], v[196:203], v[28:31]
	v_mfma_f32_16x16x128_f8f6f4 v[24:27], v[168:175], v[196:203], v[24:27]
	v_mfma_f32_16x16x128_f8f6f4 v[12:15], v[160:167], v[204:211], v[12:15]
	v_mfma_f32_16x16x128_f8f6f4 v[8:11], v[168:175], v[204:211], v[8:11]
	s_setprio 0
	s_barrier
	s_mov_b32 m0, s46
	v_lshl_add_u64 v[140:141], s[40:41], 0, v[130:131]
	global_load_lds_dwordx4 v[140:141], off
	v_lshl_add_u64 v[142:143], s[40:41], 0, v[128:129]
	s_mov_b32 m0, s47
	s_nop 0
	global_load_lds_dwordx4 v[142:143], off
	s_waitcnt vmcnt(8)
	s_waitcnt lgkmcnt(0)
	s_barrier
	s_setprio 1
	s_waitcnt lgkmcnt(0)
	v_mfma_f32_16x16x128_f8f6f4 v[52:55], v[218:225], v[176:183], v[52:55]
	v_mfma_f32_16x16x128_f8f6f4 v[48:51], v[226:233], v[176:183], v[48:51]
	v_mfma_f32_16x16x128_f8f6f4 v[36:39], v[218:225], v[184:191], v[36:39]
	v_mfma_f32_16x16x128_f8f6f4 v[32:35], v[226:233], v[184:191], v[32:35]
	v_mfma_f32_16x16x128_f8f6f4 v[20:23], v[218:225], v[196:203], v[20:23]
	v_mfma_f32_16x16x128_f8f6f4 v[16:19], v[226:233], v[196:203], v[16:19]
	v_mfma_f32_16x16x128_f8f6f4 v[4:7], v[218:225], v[204:211], v[4:7]
	v_mfma_f32_16x16x128_f8f6f4 v[0:3], v[226:233], v[204:211], v[0:3]
	s_setprio 0
	s_barrier
	ds_read_b128 v[160:163], v147 offset:32768
	ds_read_b128 v[168:171], v147 offset:34816
	ds_read_b128 v[164:167], v148 offset:32768
	ds_read_b128 v[172:175], v148 offset:34816
	s_mov_b32 m0, s51
	ds_read_b128 v[176:179], v145 offset:32768
	ds_read_b128 v[184:187], v145 offset:34816
	ds_read_b128 v[180:183], v146 offset:32768
	ds_read_b128 v[188:191], v146 offset:34816
	ds_read_b128 v[196:199], v145 offset:36864
	ds_read_b128 v[204:207], v145 offset:38912
	ds_read_b128 v[200:203], v146 offset:36864
	ds_read_b128 v[208:211], v146 offset:38912
	v_cndmask_b32_e64 v132, v138, v158, s[30:31]
	global_load_lds_dwordx4 v159, s[36:37]
	s_mov_b32 m0, s52
	s_nop 0
	global_load_lds_dwordx4 v132, s[36:37]
	s_waitcnt vmcnt(8)
	s_waitcnt lgkmcnt(8)
	s_barrier
	s_waitcnt lgkmcnt(0)
	s_setprio 1
	v_mfma_f32_16x16x128_f8f6f4 v[124:127], v[160:167], v[176:183], v[124:127]
	v_mfma_f32_16x16x128_f8f6f4 v[120:123], v[168:175], v[176:183], v[120:123]
	v_mfma_f32_16x16x128_f8f6f4 v[108:111], v[160:167], v[184:191], v[108:111]
	v_mfma_f32_16x16x128_f8f6f4 v[104:107], v[168:175], v[184:191], v[104:107]
	v_mfma_f32_16x16x128_f8f6f4 v[92:95], v[160:167], v[196:203], v[92:95]
	v_mfma_f32_16x16x128_f8f6f4 v[88:91], v[168:175], v[196:203], v[88:91]
	v_mfma_f32_16x16x128_f8f6f4 v[76:79], v[160:167], v[204:211], v[76:79]
	v_mfma_f32_16x16x128_f8f6f4 v[72:75], v[168:175], v[204:211], v[72:75]
	s_setprio 0
	s_barrier
	ds_read_b128 v[218:221], v147 offset:49152
	ds_read_b128 v[226:229], v147 offset:51200
	ds_read_b128 v[222:225], v148 offset:49152
	ds_read_b128 v[230:233], v148 offset:51200
	v_lshl_add_u64 v[214:215], s[38:39], 0, v[130:131]
	s_mov_b32 m0, s49
	s_nop 0
	global_load_lds_dwordx4 v[214:215], off
	v_lshl_add_u64 v[214:215], s[38:39], 0, v[128:129]
	s_mov_b32 m0, s50
	s_nop 0
	global_load_lds_dwordx4 v[214:215], off
	s_waitcnt vmcnt(8)
	s_barrier
	s_waitcnt lgkmcnt(0)
	s_setprio 1
	v_mfma_f32_16x16x128_f8f6f4 v[116:119], v[218:225], v[176:183], v[116:119]
	v_mfma_f32_16x16x128_f8f6f4 v[112:115], v[226:233], v[176:183], v[112:115]
	v_mfma_f32_16x16x128_f8f6f4 v[100:103], v[218:225], v[184:191], v[100:103]
	v_mfma_f32_16x16x128_f8f6f4 v[96:99], v[226:233], v[184:191], v[96:99]
	v_mfma_f32_16x16x128_f8f6f4 v[84:87], v[218:225], v[196:203], v[84:87]
	v_mfma_f32_16x16x128_f8f6f4 v[80:83], v[226:233], v[196:203], v[80:83]
	v_mfma_f32_16x16x128_f8f6f4 v[68:71], v[218:225], v[204:211], v[68:71]
	v_mfma_f32_16x16x128_f8f6f4 v[64:67], v[226:233], v[204:211], v[64:67]
	s_setprio 0
	s_barrier
	s_mov_b32 m0, s56
	v_lshl_add_u64 v[192:193], v[192:193], 0, s[16:17]
	ds_read_b128 v[176:179], v145 offset:49152
	ds_read_b128 v[184:187], v145 offset:51200
	ds_read_b128 v[180:183], v146 offset:49152
	ds_read_b128 v[188:191], v146 offset:51200
	ds_read_b128 v[196:199], v145 offset:53248
	ds_read_b128 v[204:207], v145 offset:55296
	ds_read_b128 v[200:203], v146 offset:53248
	ds_read_b128 v[208:211], v146 offset:55296
	global_load_lds_dwordx4 v[192:193], off
	v_lshl_add_u64 v[192:193], v[212:213], 0, s[16:17]
	s_mov_b32 m0, s57
	s_nop 0
	global_load_lds_dwordx4 v[192:193], off
	s_waitcnt lgkmcnt(8)
	s_barrier
	s_waitcnt lgkmcnt(0)
	s_setprio 1
	v_mfma_f32_16x16x128_f8f6f4 v[60:63], v[160:167], v[176:183], v[60:63]
	v_mfma_f32_16x16x128_f8f6f4 v[56:59], v[168:175], v[176:183], v[56:59]
	v_mfma_f32_16x16x128_f8f6f4 v[44:47], v[160:167], v[184:191], v[44:47]
	v_mfma_f32_16x16x128_f8f6f4 v[40:43], v[168:175], v[184:191], v[40:43]
	v_mfma_f32_16x16x128_f8f6f4 v[28:31], v[160:167], v[196:203], v[28:31]
	v_mfma_f32_16x16x128_f8f6f4 v[24:27], v[168:175], v[196:203], v[24:27]
	v_mfma_f32_16x16x128_f8f6f4 v[12:15], v[160:167], v[204:211], v[12:15]
	v_mfma_f32_16x16x128_f8f6f4 v[8:11], v[168:175], v[204:211], v[8:11]
	s_setprio 0
	s_barrier
	s_mov_b32 m0, s54
	v_lshl_add_u64 v[140:141], v[140:141], 0, s[16:17]
	global_load_lds_dwordx4 v[140:141], off
	v_lshl_add_u64 v[140:141], v[142:143], 0, s[16:17]
	s_mov_b32 m0, s55
	s_nop 0
	global_load_lds_dwordx4 v[140:141], off
	s_waitcnt vmcnt(8)
	s_waitcnt lgkmcnt(0)
	s_barrier
	s_setprio 1
	s_waitcnt lgkmcnt(0)
	v_mfma_f32_16x16x128_f8f6f4 v[52:55], v[218:225], v[176:183], v[52:55]
	v_mfma_f32_16x16x128_f8f6f4 v[48:51], v[226:233], v[176:183], v[48:51]
	v_mfma_f32_16x16x128_f8f6f4 v[36:39], v[218:225], v[184:191], v[36:39]
	v_mfma_f32_16x16x128_f8f6f4 v[32:35], v[226:233], v[184:191], v[32:35]
	v_mfma_f32_16x16x128_f8f6f4 v[20:23], v[218:225], v[196:203], v[20:23]
	v_mfma_f32_16x16x128_f8f6f4 v[16:19], v[226:233], v[196:203], v[16:19]
	v_mfma_f32_16x16x128_f8f6f4 v[4:7], v[218:225], v[204:211], v[4:7]
	v_mfma_f32_16x16x128_f8f6f4 v[0:3], v[226:233], v[204:211], v[0:3]
	s_setprio 0
	s_barrier
	s_mov_b32 m0, s58
	v_lshl_add_u64 v[140:141], s[34:35], 0, v[130:131]
	global_load_lds_dwordx4 v[140:141], off
	v_lshl_add_u64 v[140:141], s[34:35], 0, v[128:129]
	s_mov_b32 m0, s59
	s_andn2_b64 vcc, exec, s[28:29]
	global_load_lds_dwordx4 v[140:141], off
	s_mov_b64 s[30:31], -1
	s_mov_b64 s[28:29], 0
	s_mov_b64 s[34:35], 0x100
	s_cbranch_vccz .LBB0_1081

.LBB0_1150:
	s_or_b64 exec, exec, s[10:11]
	s_add_i32 s10, 0, 0x22140
	v_mov_b32_e32 v4, s10
	s_waitcnt lgkmcnt(0)
	s_barrier
	ds_read_b32 v4, v4
	s_waitcnt lgkmcnt(0)
	v_cmp_lt_i32_e32 vcc, v3, v4
	s_and_saveexec_b64 s[10:11], vcc
	s_cbranch_execz .LBB0_1155
	s_mov_b64 s[12:13], 0

.LBB0_1155:
	s_or_b64 exec, exec, s[10:11]
	s_lshl_b32 s0, s0, 3
	s_abs_i32 s10, s0
	v_cvt_f32_u32_e32 v3, s10
	s_sub_i32 s12, 0, s10
	s_add_i32 s11, s0, 0x47ff
	s_xor_b32 s0, s11, s0
	v_rcp_iflag_f32_e32 v3, v3
	s_abs_i32 s11, s11
	s_lshl_b32 s1, s1, 3
	s_add_i32 s1, s1, s3
	v_mul_f32_e32 v3, 0x4f7ffffe, v3
	v_cvt_u32_f32_e32 v3, v3
	s_ashr_i32 s0, s0, 31
	s_waitcnt lgkmcnt(0)
	v_readfirstlane_b32 s13, v3
	s_mul_i32 s12, s12, s13
	s_mul_hi_u32 s12, s13, s12
	s_add_i32 s13, s13, s12
	s_mul_hi_u32 s12, s11, s13
	s_mul_i32 s13, s12, s10
	s_sub_i32 s11, s11, s13
	s_add_i32 s13, s12, 1
	s_sub_i32 s14, s11, s10
	s_cmp_ge_u32 s11, s10
	s_cselect_b32 s12, s13, s12
	s_cselect_b32 s11, s14, s11
	s_add_i32 s13, s12, 1
	s_cmp_ge_u32 s11, s10
	s_cselect_b32 s10, s13, s12
	s_xor_b32 s10, s10, s0
	s_sub_i32 s0, s10, s0
	s_add_i32 s10, s1, 1
	s_mul_i32 s10, s0, s10
	s_min_i32 s22, s10, 0x4800
	s_mul_i32 s10, s0, s1
	s_cmp_ge_i32 s10, s22
	s_mov_b32 s13, 0
	s_barrier
	s_cbranch_scc1 .LBB0_1162
	v_lshlrev_b32_e32 v64, 3, v1
	v_and_b32_e32 v1, 7, v1
	v_lshlrev_b32_e32 v74, 2, v1
	v_add_u32_e32 v1, 64, v2
	v_xor_b32_e32 v2, 1, v0
	v_cmp_lt_i32_e32 vcc, v2, v1
	v_mov_b32_e32 v75, 0
	v_ashrrev_i32_e32 v65, 31, v64
	v_cndmask_b32_e32 v2, v0, v2, vcc
	v_lshlrev_b32_e32 v140, 2, v2
	v_xor_b32_e32 v2, 2, v0
	v_cmp_lt_i32_e32 vcc, v2, v1
	v_lshl_add_u64 v[4:5], s[8:9], 0, v[74:75]
	s_mov_b64 s[0:1], 0x49180000
	v_cndmask_b32_e32 v2, v0, v2, vcc
	v_lshlrev_b32_e32 v141, 2, v2
	v_xor_b32_e32 v2, 4, v0
	v_cmp_lt_i32_e32 vcc, v2, v1
	s_add_u32 s23, s8, 0x7c000
	v_lshl_add_u64 v[66:67], v[4:5], 0, s[0:1]
	v_cndmask_b32_e32 v2, v0, v2, vcc
	v_lshlrev_b32_e32 v142, 2, v2
	v_xor_b32_e32 v2, 8, v0
	v_cmp_lt_i32_e32 vcc, v2, v1
	v_lshl_add_u64 v[4:5], s[8:9], 0, v[64:65]
	s_mov_b64 s[0:1], 0x62800000
	v_cndmask_b32_e32 v2, v0, v2, vcc
	v_lshlrev_b32_e32 v143, 2, v2
	v_xor_b32_e32 v2, 16, v0
	v_cmp_lt_i32_e32 vcc, v2, v1
	s_addc_u32 s33, s9, 0
	v_lshl_add_u64 v[68:69], v[4:5], 0, s[0:1]
	v_cndmask_b32_e32 v2, v0, v2, vcc
	v_lshlrev_b32_e32 v144, 2, v2
	v_xor_b32_e32 v2, 32, v0
	v_cmp_lt_i32_e32 vcc, v2, v1
	s_mov_b64 s[0:1], 0x34000000
	s_add_u32 s14, s8, 0x49800000
	v_cndmask_b32_e32 v0, v0, v2, vcc
	v_lshlrev_b32_e32 v145, 2, v0
	v_lshl_add_u64 v[0:1], v[64:65], 1, s[8:9]
	v_lshl_add_u64 v[70:71], v[0:1], 0, s[0:1]
	s_mov_b64 s[0:1], 0x3d000000
	s_addc_u32 s15, s9, 0
	v_lshl_add_u64 v[72:73], v[4:5], 0, s[0:1]
	v_mov_b32_e32 v74, v75
	v_mov_b32_e32 v76, v75
	v_mov_b32_e32 v77, v75
	v_mov_b32_e32 v88, v75
	v_mov_b32_e32 v89, v75
	v_mov_b32_e32 v82, v75
	v_mov_b32_e32 v83, v75
	v_mov_b32_e32 v92, v75
	v_mov_b32_e32 v93, v75
	v_mov_b32_e32 v84, v75
	v_mov_b32_e32 v85, v75
	v_mov_b32_e32 v94, v75
	v_mov_b32_e32 v95, v75
	v_mov_b32_e32 v86, v75
	v_mov_b32_e32 v87, v75
	v_mov_b32_e32 v96, v75
	v_mov_b32_e32 v97, v75
	v_mov_b32_e32 v78, v75
	v_mov_b32_e32 v79, v75
	v_mov_b32_e32 v100, v75
	v_mov_b32_e32 v101, v75
	v_mov_b32_e32 v90, v75
	v_mov_b32_e32 v91, v75
	v_mov_b32_e32 v102, v75
	v_mov_b32_e32 v103, v75
	v_mov_b32_e32 v80, v75
	v_mov_b32_e32 v81, v75
	v_mov_b32_e32 v104, v75
	v_mov_b32_e32 v105, v75
	v_mov_b32_e32 v98, v75
	v_mov_b32_e32 v99, v75
	s_mov_b32 s43, -1
	s_mov_b64 s[16:17], 0x1a000
	s_mov_b64 s[18:19], 0x1b000
	s_mov_b32 s38, 0x1b000
	s_mov_b64 s[20:21], 0x1b800
	s_mov_b64 s[24:25], 0x2000
	s_mov_b64 s[26:27], 0x3000
	s_mov_b64 s[28:29], 0x1000
	s_movk_i32 s39, 0x3000
	s_movk_i32 s40, 0x1000
	s_mov_b64 s[30:31], 0x3800
	s_mov_b64 s[34:35], 0x1800
	s_add_i32 s41, 0, 0x22040
	v_mov_b32_e32 v146, 0x358637bd
	s_mov_b32 s42, 0xc3dc0000
	v_mov_b32_e32 v147, 0x43dc0000
	v_mov_b32_e32 v4, v75
	v_mov_b32_e32 v5, v75
	v_mov_b32_e32 v6, v75
	v_mov_b32_e32 v7, v75
	v_mov_b32_e32 v0, v75
	v_mov_b32_e32 v1, v75
	v_mov_b32_e32 v2, v75
	v_mov_b32_e32 v3, v75
	v_mov_b32_e32 v8, v75
	v_mov_b32_e32 v9, v75
	v_mov_b32_e32 v10, v75
	v_mov_b32_e32 v11, v75
	v_mov_b32_e32 v12, v75
	v_mov_b32_e32 v13, v75
	v_mov_b32_e32 v14, v75
	v_mov_b32_e32 v15, v75
	v_mov_b32_e32 v16, v75
	v_mov_b32_e32 v17, v75
	v_mov_b32_e32 v18, v75
	v_mov_b32_e32 v19, v75
	v_mov_b32_e32 v20, v75
	v_mov_b32_e32 v21, v75
	v_mov_b32_e32 v22, v75
	v_mov_b32_e32 v23, v75
	v_mov_b32_e32 v24, v75
	v_mov_b32_e32 v25, v75
	v_mov_b32_e32 v26, v75
	v_mov_b32_e32 v27, v75
	v_mov_b32_e32 v28, v75
	v_mov_b32_e32 v29, v75
	v_mov_b32_e32 v30, v75
	v_mov_b32_e32 v31, v75

.LBB0_1248:
	s_add_u32 s33, s16, s46
	s_addc_u32 s48, s17, s47
	s_add_u32 s33, s33, 0x3d000100
	ds_read_b128 v[148:151], v164
	ds_read_b128 v[204:207], v164 offset:2048
	ds_read_b128 v[152:155], v165
	ds_read_b128 v[208:211], v165 offset:2048
	s_addc_u32 s50, s48, 0
	s_add_u32 s56, s0, s46
	s_addc_u32 s57, s1, s47
	s_cmpk_eq_i32 s46, 0x700
	s_cselect_b64 vcc, -1, 0
	s_and_b64 s[48:49], vcc, exec
	ds_read_b128 v[212:215], v162
	ds_read_b128 v[220:223], v162 offset:2048
	ds_read_b128 v[216:219], v163
	ds_read_b128 v[224:227], v163 offset:2048
	ds_read_b128 v[228:231], v162 offset:4096
	ds_read_b128 v[236:239], v162 offset:6144
	ds_read_b128 v[232:235], v163 offset:4096
	ds_read_b128 v[240:243], v163 offset:6144
	s_waitcnt vmcnt(6)
	s_waitcnt lgkmcnt(8)
	s_barrier
	s_waitcnt lgkmcnt(0)
	v_cndmask_b32_e32 v156, v138, v201, vcc
	s_setprio 1
	s_waitcnt lgkmcnt(0)
	v_mfma_f32_16x16x128_f8f6f4 v[124:127], v[148:155], v[212:219], v[124:127]
	v_mfma_f32_16x16x128_f8f6f4 v[120:123], v[204:211], v[212:219], v[120:123]
	v_mfma_f32_16x16x128_f8f6f4 v[108:111], v[148:155], v[220:227], v[108:111]
	v_mfma_f32_16x16x128_f8f6f4 v[104:107], v[204:211], v[220:227], v[104:107]
	v_mfma_f32_16x16x128_f8f6f4 v[92:95], v[148:155], v[228:235], v[92:95]
	v_mfma_f32_16x16x128_f8f6f4 v[88:91], v[204:211], v[228:235], v[88:91]
	v_mfma_f32_16x16x128_f8f6f4 v[76:79], v[148:155], v[236:243], v[76:79]
	v_mfma_f32_16x16x128_f8f6f4 v[72:75], v[204:211], v[236:243], v[72:75]
	s_setprio 0
	s_barrier
	ds_read_b128 v[148:151], v164 offset:16384
	ds_read_b128 v[204:207], v164 offset:18432
	ds_read_b128 v[152:155], v165 offset:16384
	ds_read_b128 v[208:211], v165 offset:18432
	v_cndmask_b32_e32 v132, v139, v200, vcc
	s_cselect_b32 s51, s19, s50
	s_cselect_b32 s50, s18, s33
	s_cselect_b32 s49, s45, s57
	s_cselect_b32 s48, s44, s56
	v_cndmask_b32_e32 v141, v140, v202, vcc
	v_lshl_add_u64 v[252:253], v[146:147], 0, s[46:47]
	s_add_i32 m0, s39, 0xc000
	s_nop 0
	global_load_lds_dwordx4 v[252:253], off
	v_lshl_add_u64 v[252:253], v[144:145], 0, s[46:47]
	s_add_i32 m0, s39, 0xe000
	s_nop 0
	global_load_lds_dwordx4 v[252:253], off
	s_barrier
	s_waitcnt lgkmcnt(0)
	s_setprio 1
	v_mfma_f32_16x16x128_f8f6f4 v[116:119], v[148:155], v[212:219], v[116:119]
	v_mfma_f32_16x16x128_f8f6f4 v[112:115], v[204:211], v[212:219], v[112:115]
	v_mfma_f32_16x16x128_f8f6f4 v[100:103], v[148:155], v[220:227], v[100:103]
	v_mfma_f32_16x16x128_f8f6f4 v[96:99], v[204:211], v[220:227], v[96:99]
	v_mfma_f32_16x16x128_f8f6f4 v[84:87], v[148:155], v[228:235], v[84:87]
	v_mfma_f32_16x16x128_f8f6f4 v[80:83], v[204:211], v[228:235], v[80:83]
	v_mfma_f32_16x16x128_f8f6f4 v[68:71], v[148:155], v[236:243], v[68:71]
	v_mfma_f32_16x16x128_f8f6f4 v[64:67], v[204:211], v[236:243], v[64:67]
	s_setprio 0
	s_barrier
	ds_read_b128 v[204:207], v164
	ds_read_b128 v[212:215], v164 offset:2048
	ds_read_b128 v[208:211], v165
	ds_read_b128 v[216:219], v165 offset:2048
	s_mov_b32 m0, s39
	ds_read_b128 v[220:223], v162 offset:16384
	ds_read_b128 v[228:231], v162 offset:18432
	ds_read_b128 v[224:227], v163 offset:16384
	ds_read_b128 v[232:235], v163 offset:18432
	ds_read_b128 v[236:239], v162 offset:20480
	ds_read_b128 v[244:247], v162 offset:22528
	ds_read_b128 v[240:243], v163 offset:20480
	ds_read_b128 v[248:251], v163 offset:22528
	global_load_lds_dwordx4 v132, s[50:51]
	s_mov_b32 m0, s54
	v_mov_b32_e32 v157, v133
	global_load_lds_dwordx4 v156, s[50:51]
	s_waitcnt lgkmcnt(8)
	s_barrier
	s_waitcnt lgkmcnt(0)
	v_lshl_add_u64 v[154:155], s[50:51], 0, v[132:133]
	v_lshl_add_u64 v[152:153], s[50:51], 0, v[156:157]
	s_setprio 1
	s_waitcnt lgkmcnt(0)
	v_mfma_f32_16x16x128_f8f6f4 v[60:63], v[204:211], v[220:227], v[60:63]
	v_mfma_f32_16x16x128_f8f6f4 v[56:59], v[212:219], v[220:227], v[56:59]
	v_mfma_f32_16x16x128_f8f6f4 v[44:47], v[204:211], v[228:235], v[44:47]
	v_mfma_f32_16x16x128_f8f6f4 v[40:43], v[212:219], v[228:235], v[40:43]
	v_mfma_f32_16x16x128_f8f6f4 v[28:31], v[204:211], v[236:243], v[28:31]
	v_mfma_f32_16x16x128_f8f6f4 v[24:27], v[212:219], v[236:243], v[24:27]
	v_mfma_f32_16x16x128_f8f6f4 v[12:15], v[204:211], v[244:251], v[12:15]
	v_mfma_f32_16x16x128_f8f6f4 v[8:11], v[212:219], v[244:251], v[8:11]
	s_setprio 0
	s_barrier
	s_mov_b32 m0, s52
	v_lshl_add_u64 v[148:149], s[48:49], 0, v[128:129]
	ds_read_b128 v[204:207], v164 offset:16384
	ds_read_b128 v[212:215], v164 offset:18432
	ds_read_b128 v[208:211], v165 offset:16384
	ds_read_b128 v[216:219], v165 offset:18432
	global_load_lds_dwordx4 v[148:149], off
	v_lshl_add_u64 v[150:151], s[48:49], 0, v[130:131]
	s_mov_b32 m0, s53
	s_nop 0
	global_load_lds_dwordx4 v[150:151], off
	s_waitcnt vmcnt(8)
	s_waitcnt lgkmcnt(0)
	s_barrier
	s_setprio 1
	s_waitcnt lgkmcnt(0)
	v_mfma_f32_16x16x128_f8f6f4 v[52:55], v[204:211], v[220:227], v[52:55]
	v_mfma_f32_16x16x128_f8f6f4 v[48:51], v[212:219], v[220:227], v[48:51]
	v_mfma_f32_16x16x128_f8f6f4 v[36:39], v[204:211], v[228:235], v[36:39]
	v_mfma_f32_16x16x128_f8f6f4 v[32:35], v[212:219], v[228:235], v[32:35]
	v_mfma_f32_16x16x128_f8f6f4 v[20:23], v[204:211], v[236:243], v[20:23]
	v_mfma_f32_16x16x128_f8f6f4 v[16:19], v[212:219], v[236:243], v[16:19]
	v_mfma_f32_16x16x128_f8f6f4 v[4:7], v[204:211], v[244:251], v[4:7]
	v_mfma_f32_16x16x128_f8f6f4 v[0:3], v[212:219], v[244:251], v[0:3]
	s_setprio 0
	s_barrier
	ds_read_b128 v[204:207], v164 offset:32768
	ds_read_b128 v[212:215], v164 offset:34816
	ds_read_b128 v[208:211], v165 offset:32768
	ds_read_b128 v[216:219], v165 offset:34816
	s_mov_b32 m0, s59
	ds_read_b128 v[220:223], v162 offset:32768
	ds_read_b128 v[228:231], v162 offset:34816
	ds_read_b128 v[224:227], v163 offset:32768
	ds_read_b128 v[232:235], v163 offset:34816
	ds_read_b128 v[236:239], v162 offset:36864
	ds_read_b128 v[244:247], v162 offset:38912
	ds_read_b128 v[240:243], v163 offset:36864
	ds_read_b128 v[248:251], v163 offset:38912
	v_cndmask_b32_e32 v132, v142, v203, vcc
	global_load_lds_dwordx4 v141, s[50:51]
	s_mov_b32 m0, s60
	s_nop 0
	global_load_lds_dwordx4 v132, s[50:51]
	s_waitcnt vmcnt(8)
	s_waitcnt lgkmcnt(8)
	s_barrier
	s_waitcnt lgkmcnt(0)
	s_setprio 1
	v_mfma_f32_16x16x128_f8f6f4 v[124:127], v[204:211], v[220:227], v[124:127]
	v_mfma_f32_16x16x128_f8f6f4 v[120:123], v[212:219], v[220:227], v[120:123]
	v_mfma_f32_16x16x128_f8f6f4 v[108:111], v[204:211], v[228:235], v[108:111]
	v_mfma_f32_16x16x128_f8f6f4 v[104:107], v[212:219], v[228:235], v[104:107]
	v_mfma_f32_16x16x128_f8f6f4 v[92:95], v[204:211], v[236:243], v[92:95]
	v_mfma_f32_16x16x128_f8f6f4 v[88:91], v[212:219], v[236:243], v[88:91]
	v_mfma_f32_16x16x128_f8f6f4 v[76:79], v[204:211], v[244:251], v[76:79]
	v_mfma_f32_16x16x128_f8f6f4 v[72:75], v[212:219], v[244:251], v[72:75]
	s_setprio 0
	s_barrier
	ds_read_b128 v[204:207], v164 offset:49152
	ds_read_b128 v[212:215], v164 offset:51200
	ds_read_b128 v[208:211], v165 offset:49152
	ds_read_b128 v[216:219], v165 offset:51200
	s_add_u32 s50, s48, 0x4000
	s_addc_u32 s51, s49, 0
	v_lshl_add_u64 v[156:157], s[50:51], 0, v[128:129]
	s_mov_b32 m0, s55
	s_nop 0
	global_load_lds_dwordx4 v[156:157], off
	v_lshl_add_u64 v[156:157], s[50:51], 0, v[130:131]
	s_mov_b32 m0, s58
	s_nop 0
	global_load_lds_dwordx4 v[156:157], off
	s_waitcnt vmcnt(8)
	s_barrier
	s_waitcnt lgkmcnt(0)
	s_setprio 1
	v_mfma_f32_16x16x128_f8f6f4 v[116:119], v[204:211], v[220:227], v[116:119]
	v_mfma_f32_16x16x128_f8f6f4 v[112:115], v[212:219], v[220:227], v[112:115]
	v_mfma_f32_16x16x128_f8f6f4 v[100:103], v[204:211], v[228:235], v[100:103]
	v_mfma_f32_16x16x128_f8f6f4 v[96:99], v[212:219], v[228:235], v[96:99]
	v_mfma_f32_16x16x128_f8f6f4 v[84:87], v[204:211], v[236:243], v[84:87]
	v_mfma_f32_16x16x128_f8f6f4 v[80:83], v[212:219], v[236:243], v[80:83]
	v_mfma_f32_16x16x128_f8f6f4 v[68:71], v[204:211], v[244:251], v[68:71]
	v_mfma_f32_16x16x128_f8f6f4 v[64:67], v[212:219], v[244:251], v[64:67]
	s_setprio 0
	s_barrier
	ds_read_b128 v[204:207], v164 offset:32768
	ds_read_b128 v[212:215], v164 offset:34816
	ds_read_b128 v[208:211], v165 offset:32768
	ds_read_b128 v[216:219], v165 offset:34816
	s_mov_b32 m0, s64
	v_lshl_add_u64 v[154:155], v[154:155], 0, s[30:31]
	ds_read_b128 v[220:223], v162 offset:49152
	ds_read_b128 v[228:231], v162 offset:51200
	ds_read_b128 v[224:227], v163 offset:49152
	ds_read_b128 v[232:235], v163 offset:51200
	ds_read_b128 v[236:239], v162 offset:53248
	ds_read_b128 v[244:247], v162 offset:55296
	ds_read_b128 v[240:243], v163 offset:53248
	ds_read_b128 v[248:251], v163 offset:55296
	global_load_lds_dwordx4 v[154:155], off
	v_lshl_add_u64 v[152:153], v[152:153], 0, s[30:31]
	s_mov_b32 m0, s65
	s_nop 0
	global_load_lds_dwordx4 v[152:153], off
	s_waitcnt lgkmcnt(8)
	s_barrier
	s_waitcnt lgkmcnt(0)
	s_setprio 1
	v_mfma_f32_16x16x128_f8f6f4 v[60:63], v[204:211], v[220:227], v[60:63]
	v_mfma_f32_16x16x128_f8f6f4 v[56:59], v[212:219], v[220:227], v[56:59]
	v_mfma_f32_16x16x128_f8f6f4 v[44:47], v[204:211], v[228:235], v[44:47]
	v_mfma_f32_16x16x128_f8f6f4 v[40:43], v[212:219], v[228:235], v[40:43]
	v_mfma_f32_16x16x128_f8f6f4 v[28:31], v[204:211], v[236:243], v[28:31]
	v_mfma_f32_16x16x128_f8f6f4 v[24:27], v[212:219], v[236:243], v[24:27]
	v_mfma_f32_16x16x128_f8f6f4 v[12:15], v[204:211], v[244:251], v[12:15]
	v_mfma_f32_16x16x128_f8f6f4 v[8:11], v[212:219], v[244:251], v[8:11]
	s_setprio 0
	s_barrier
	s_mov_b32 m0, s62
	v_lshl_add_u64 v[148:149], v[148:149], 0, s[30:31]
	ds_read_b128 v[152:155], v164 offset:49152
	ds_read_b128 v[204:207], v164 offset:51200
	ds_read_b128 v[156:159], v165 offset:49152
	ds_read_b128 v[208:211], v165 offset:51200
	global_load_lds_dwordx4 v[148:149], off
	v_lshl_add_u64 v[148:149], v[150:151], 0, s[30:31]
	s_mov_b32 m0, s63
	s_nop 0
	global_load_lds_dwordx4 v[148:149], off
	s_waitcnt vmcnt(8)
	s_waitcnt lgkmcnt(0)
	s_barrier
	s_setprio 1
	s_waitcnt lgkmcnt(0)
	v_mfma_f32_16x16x128_f8f6f4 v[52:55], v[152:159], v[220:227], v[52:55]
	v_mfma_f32_16x16x128_f8f6f4 v[48:51], v[204:211], v[220:227], v[48:51]
	v_mfma_f32_16x16x128_f8f6f4 v[36:39], v[152:159], v[228:235], v[36:39]
	v_mfma_f32_16x16x128_f8f6f4 v[32:35], v[204:211], v[228:235], v[32:35]
	v_mfma_f32_16x16x128_f8f6f4 v[20:23], v[152:159], v[236:243], v[20:23]
	v_mfma_f32_16x16x128_f8f6f4 v[16:19], v[204:211], v[236:243], v[16:19]
	v_mfma_f32_16x16x128_f8f6f4 v[4:7], v[152:159], v[244:251], v[4:7]
	v_mfma_f32_16x16x128_f8f6f4 v[0:3], v[204:211], v[244:251], v[0:3]
	s_setprio 0
	s_barrier
	s_add_u32 s48, s48, 0x4080
	s_addc_u32 s49, s49, 0
	s_mov_b32 m0, s66
	v_lshl_add_u64 v[148:149], s[48:49], 0, v[128:129]
	global_load_lds_dwordx4 v[148:149], off
	v_lshl_add_u64 v[148:149], s[48:49], 0, v[130:131]
	s_mov_b32 m0, s67
	s_add_i32 s20, s20, 2
	global_load_lds_dwordx4 v[148:149], off
	s_add_u32 s46, s46, 0x100
	s_addc_u32 s47, s47, 0
	s_cmp_gt_u32 s20, 13
	s_cbranch_scc0 .LBB0_1248
	s_and_b64 vcc, exec, s[36:37]
	s_cbranch_vccz .LBB0_1251
	s_barrier

.LBB0_1373:
	s_and_b32 s12, s12, 63
	s_lshl_b32 s12, s12, s37
	s_and_b32 s33, s12, s33
	v_add_u32_e32 v64, s33, v98
	s_lshl_b32 s12, s19, 2
	s_lshl_b32 s18, s18, 9
	v_add_u32_e32 v66, s33, v99
	v_mad_i64_i32 v[64:65], s[42:43], s40, v64, 0
	s_and_b32 s12, s18, s12
	v_mad_i64_i32 v[66:67], s[18:19], s40, v66, 0
	v_lshl_add_u64 v[64:65], v[64:65], 2, s[38:39]
	v_lshl_add_u64 v[66:67], v[66:67], 2, s[38:39]
	v_lshl_add_u64 v[64:65], v[64:65], 0, s[12:13]
	v_lshl_add_u64 v[66:67], v[66:67], 0, s[12:13]
	v_lshl_add_u64 v[64:65], v[64:65], 0, v[144:145]
	v_lshl_add_u64 v[66:67], v[66:67], 0, v[144:145]
	global_load_dwordx4 v[92:95], v[64:65], off nt
	global_load_dwordx4 v[88:91], v[66:67], off nt
	v_add_u32_e32 v64, s33, v100
	v_add_u32_e32 v66, s33, v101
	v_mad_i64_i32 v[64:65], s[18:19], s40, v64, 0
	v_mad_i64_i32 v[66:67], s[18:19], s40, v66, 0
	v_lshl_add_u64 v[64:65], v[64:65], 2, s[38:39]
	v_lshl_add_u64 v[66:67], v[66:67], 2, s[38:39]
	v_lshl_add_u64 v[64:65], v[64:65], 0, s[12:13]
	v_lshl_add_u64 v[66:67], v[66:67], 0, s[12:13]
	v_lshl_add_u64 v[64:65], v[64:65], 0, v[144:145]
	v_lshl_add_u64 v[66:67], v[66:67], 0, v[144:145]
	global_load_dwordx4 v[84:87], v[64:65], off nt
	global_load_dwordx4 v[80:83], v[66:67], off nt
	v_add_u32_e32 v64, s33, v102
	v_add_u32_e32 v66, s33, v103
	v_mad_i64_i32 v[64:65], s[18:19], s40, v64, 0
	v_mad_i64_i32 v[66:67], s[18:19], s40, v66, 0
	v_lshl_add_u64 v[64:65], v[64:65], 2, s[38:39]
	v_lshl_add_u64 v[66:67], v[66:67], 2, s[38:39]
	v_lshl_add_u64 v[64:65], v[64:65], 0, s[12:13]
	v_lshl_add_u64 v[66:67], v[66:67], 0, s[12:13]
	v_lshl_add_u64 v[64:65], v[64:65], 0, v[144:145]
	v_lshl_add_u64 v[66:67], v[66:67], 0, v[144:145]
	global_load_dwordx4 v[76:79], v[64:65], off nt
	global_load_dwordx4 v[72:75], v[66:67], off nt
	v_add_u32_e32 v64, s33, v104
	v_add_u32_e32 v66, s33, v105
	v_mad_i64_i32 v[64:65], s[18:19], s40, v64, 0
	v_mad_i64_i32 v[66:67], s[18:19], s40, v66, 0
	v_lshl_add_u64 v[64:65], v[64:65], 2, s[38:39]
	v_lshl_add_u64 v[66:67], v[66:67], 2, s[38:39]
	v_lshl_add_u64 v[64:65], v[64:65], 0, s[12:13]
	v_lshl_add_u64 v[66:67], v[66:67], 0, s[12:13]
	v_lshl_add_u64 v[64:65], v[64:65], 0, v[144:145]
	v_lshl_add_u64 v[66:67], v[66:67], 0, v[144:145]
	global_load_dwordx4 v[68:71], v[64:65], off nt
	s_nop 0
	global_load_dwordx4 v[64:67], v[66:67], off nt
	s_waitcnt lgkmcnt(0)
	s_barrier
	ds_read2st64_b32 v[196:197], v204 offset1:2
	ds_read2st64_b32 v[198:199], v204 offset0:4 offset1:6
	ds_read2st64_b32 v[200:201], v204 offset0:8 offset1:10
	ds_read2st64_b32 v[202:203], v204 offset0:12 offset1:14
	ds_read2st64_b32 v[222:223], v204 offset0:16 offset1:18
	ds_read2st64_b32 v[224:225], v204 offset0:20 offset1:22
	ds_read2st64_b32 v[226:227], v204 offset0:24 offset1:26
	ds_read2st64_b32 v[228:229], v204 offset0:28 offset1:30
	ds_read_b32 v204, v205
	ds_read_b32 v205, v206
	ds_read_b32 v206, v207
	ds_read_b32 v207, v208
	ds_read_b32 v208, v209
	ds_read_b32 v209, v210
	ds_read_b32 v210, v211
	ds_read_b32 v211, v212
	ds_read_b32 v212, v213
	ds_read_b32 v213, v214
	ds_read_b32 v214, v215
	ds_read_b32 v215, v216
	ds_read_b32 v216, v217
	ds_read_b32 v217, v218
	ds_read_b32 v218, v219
	ds_read_b32 v219, v220
	s_waitcnt lgkmcnt(14)
	v_med3_f32 v220, v196, s97, v185
	v_med3_f32 v197, v197, s97, v185
	v_mov_b32_e32 v196, v145
	v_cvt_pk_fp8_f32 v196, v220, v197
	v_med3_f32 v200, v200, s97, v185
	v_med3_f32 v201, v201, s97, v185
	v_mov_b32_e32 v197, v145
	v_cvt_pk_fp8_f32 v197, v200, v201
	v_med3_f32 v198, v198, s97, v185
	v_med3_f32 v199, v199, s97, v185
	v_cvt_pk_fp8_f32 v196, v198, v199 op_sel:[0,0,1]
	v_med3_f32 v198, v202, s97, v185
	v_med3_f32 v199, v203, s97, v185
	v_cvt_pk_fp8_f32 v197, v198, v199 op_sel:[0,0,1]
	v_med3_f32 v199, v222, s97, v185
	v_med3_f32 v200, v223, s97, v185
	v_mov_b32_e32 v198, v145
	v_cvt_pk_fp8_f32 v198, v199, v200
	v_med3_f32 v200, v226, s97, v185
	v_med3_f32 v203, v227, s97, v185
	v_mov_b32_e32 v199, v145
	v_cvt_pk_fp8_f32 v199, v200, v203
	v_med3_f32 v201, v224, s97, v185
	v_med3_f32 v202, v225, s97, v185
	v_cvt_pk_fp8_f32 v198, v201, v202 op_sel:[0,0,1]
	v_med3_f32 v200, v228, s97, v185
	v_med3_f32 v201, v229, s97, v185
	v_cvt_pk_fp8_f32 v199, v200, v201 op_sel:[0,0,1]
	v_med3_f32 v201, v204, s97, v185
	v_med3_f32 v202, v205, s97, v185
	v_mov_b32_e32 v200, v145
	v_cvt_pk_fp8_f32 v200, v201, v202
	s_waitcnt lgkmcnt(11)
	v_med3_f32 v202, v208, s97, v185
	s_waitcnt lgkmcnt(10)
	v_med3_f32 v205, v209, s97, v185
	v_mov_b32_e32 v201, v145
	v_cvt_pk_fp8_f32 v201, v202, v205
	v_med3_f32 v203, v206, s97, v185
	v_med3_f32 v204, v207, s97, v185
	v_cvt_pk_fp8_f32 v200, v203, v204 op_sel:[0,0,1]
	s_waitcnt lgkmcnt(9)
	v_med3_f32 v202, v210, s97, v185
	s_waitcnt lgkmcnt(8)
	v_med3_f32 v203, v211, s97, v185
	v_cvt_pk_fp8_f32 v201, v202, v203 op_sel:[0,0,1]
	s_waitcnt lgkmcnt(7)
	v_med3_f32 v203, v212, s97, v185
	s_waitcnt lgkmcnt(6)
	v_med3_f32 v204, v213, s97, v185
	v_mov_b32_e32 v202, v145
	v_cvt_pk_fp8_f32 v202, v203, v204
	s_waitcnt lgkmcnt(3)
	v_med3_f32 v204, v216, s97, v185
	s_waitcnt lgkmcnt(2)
	v_med3_f32 v207, v217, s97, v185
	v_mov_b32_e32 v203, v145
	v_cvt_pk_fp8_f32 v203, v204, v207
	v_med3_f32 v205, v214, s97, v185
	v_med3_f32 v206, v215, s97, v185
	v_cvt_pk_fp8_f32 v202, v205, v206 op_sel:[0,0,1]
	s_waitcnt lgkmcnt(1)
	v_med3_f32 v204, v218, s97, v185
	s_waitcnt lgkmcnt(0)
	v_med3_f32 v205, v219, s97, v185
	s_cmp_lt_i32 s5, 0
	v_cvt_pk_fp8_f32 v203, v204, v205 op_sel:[0,0,1]
	v_add_u32_e32 v204, s5, v107
	s_cselect_b64 vcc, -1, 0
	v_cndmask_b32_e32 v206, v204, v106, vcc
	v_mov_b64_e32 v[204:205], s[6:7]
	v_mad_i64_i32 v[204:205], s[6:7], s36, v206, v[204:205]
	s_mov_b32 s5, s13
	v_lshl_add_u64 v[204:205], v[204:205], 0, s[4:5]
	s_add_i32 s1, s1, 3
	v_lshl_add_u64 v[204:205], v[204:205], 0, v[96:97]
	s_cmp_ge_i32 s1, s88
	global_store_dwordx4 v[204:205], v[196:199], off nt
	global_store_dwordx4 v[204:205], v[200:203], off offset:16 nt
	s_cbranch_scc1 .LBB0_1403

.LBB0_1384:
	s_and_b32 s12, s12, 63
	s_lshl_b32 s12, s12, s41
	s_and_b32 s37, s12, s37
	v_add_u32_e32 v0, s37, v98
	v_add_u32_e32 v2, s37, v99
	v_add_u32_e32 v8, s37, v100
	v_add_u32_e32 v10, s37, v101
	v_add_u32_e32 v16, s37, v102
	v_add_u32_e32 v18, s37, v103
	v_add_u32_e32 v24, s37, v104
	v_add_u32_e32 v26, s37, v105
	v_mad_i64_i32 v[0:1], s[42:43], s40, v0, 0
	s_lshl_b32 s12, s33, 2
	s_lshl_b32 s19, s19, 9
	v_mad_i64_i32 v[2:3], s[42:43], s40, v2, 0
	v_mad_i64_i32 v[8:9], s[42:43], s40, v8, 0
	v_mad_i64_i32 v[10:11], s[42:43], s40, v10, 0
	v_mad_i64_i32 v[16:17], s[42:43], s40, v16, 0
	v_mad_i64_i32 v[18:19], s[42:43], s40, v18, 0
	v_mad_i64_i32 v[24:25], s[42:43], s40, v24, 0
	v_mad_i64_i32 v[26:27], s[40:41], s40, v26, 0
	v_lshl_add_u64 v[0:1], v[0:1], 2, s[38:39]
	s_and_b32 s12, s19, s12
	v_lshl_add_u64 v[2:3], v[2:3], 2, s[38:39]
	v_lshl_add_u64 v[8:9], v[8:9], 2, s[38:39]
	v_lshl_add_u64 v[10:11], v[10:11], 2, s[38:39]
	v_lshl_add_u64 v[16:17], v[16:17], 2, s[38:39]
	v_lshl_add_u64 v[18:19], v[18:19], 2, s[38:39]
	v_lshl_add_u64 v[24:25], v[24:25], 2, s[38:39]
	v_lshl_add_u64 v[26:27], v[26:27], 2, s[38:39]
	v_lshl_add_u64 v[0:1], v[0:1], 0, s[12:13]
	v_lshl_add_u64 v[2:3], v[2:3], 0, s[12:13]
	v_lshl_add_u64 v[8:9], v[8:9], 0, s[12:13]
	v_lshl_add_u64 v[10:11], v[10:11], 0, s[12:13]
	v_lshl_add_u64 v[16:17], v[16:17], 0, s[12:13]
	v_lshl_add_u64 v[18:19], v[18:19], 0, s[12:13]
	v_lshl_add_u64 v[24:25], v[24:25], 0, s[12:13]
	v_lshl_add_u64 v[26:27], v[26:27], 0, s[12:13]
	v_lshl_add_u64 v[0:1], v[0:1], 0, v[144:145]
	v_lshl_add_u64 v[2:3], v[2:3], 0, v[144:145]
	v_lshl_add_u64 v[8:9], v[8:9], 0, v[144:145]
	v_lshl_add_u64 v[10:11], v[10:11], 0, v[144:145]
	v_lshl_add_u64 v[16:17], v[16:17], 0, v[144:145]
	v_lshl_add_u64 v[18:19], v[18:19], 0, v[144:145]
	v_lshl_add_u64 v[24:25], v[24:25], 0, v[144:145]
	v_lshl_add_u64 v[26:27], v[26:27], 0, v[144:145]
	global_load_dwordx4 v[4:7], v[0:1], off nt
	s_nop 0
	global_load_dwordx4 v[0:3], v[2:3], off nt
	s_nop 0
	global_load_dwordx4 v[12:15], v[8:9], off nt
	s_nop 0
	global_load_dwordx4 v[8:11], v[10:11], off nt
	s_nop 0
	global_load_dwordx4 v[20:23], v[16:17], off nt
	s_nop 0
	global_load_dwordx4 v[16:19], v[18:19], off nt
	s_nop 0
	global_load_dwordx4 v[28:31], v[24:25], off nt
	s_nop 0
	global_load_dwordx4 v[24:27], v[26:27], off nt
	v_add3_u32 v204, s18, v108, v141
	s_waitcnt lgkmcnt(0)
	s_barrier
	ds_read2st64_b32 v[222:223], v204 offset1:2
	ds_read2st64_b32 v[224:225], v204 offset0:4 offset1:6
	ds_read2st64_b32 v[226:227], v204 offset0:8 offset1:10
	ds_read2st64_b32 v[228:229], v204 offset0:12 offset1:14
	ds_read2st64_b32 v[230:231], v204 offset0:16 offset1:18
	ds_read2st64_b32 v[232:233], v204 offset0:20 offset1:22
	ds_read2st64_b32 v[234:235], v204 offset0:24 offset1:26
	ds_read2st64_b32 v[236:237], v204 offset0:28 offset1:30
	s_waitcnt lgkmcnt(7)
	v_med3_f32 v253, v222, s97, v185
	v_med3_f32 v223, v223, s97, v185
	v_mov_b32_e32 v222, v145
	v_cvt_pk_fp8_f32 v222, v253, v223
	s_waitcnt lgkmcnt(5)
	v_med3_f32 v226, v226, s97, v185
	v_med3_f32 v227, v227, s97, v185
	v_mov_b32_e32 v223, v145
	v_cvt_pk_fp8_f32 v223, v226, v227
	v_med3_f32 v224, v224, s97, v185
	v_med3_f32 v225, v225, s97, v185
	v_cvt_pk_fp8_f32 v222, v224, v225 op_sel:[0,0,1]
	s_waitcnt lgkmcnt(4)
	v_med3_f32 v224, v228, s97, v185
	v_med3_f32 v225, v229, s97, v185
	v_cvt_pk_fp8_f32 v223, v224, v225 op_sel:[0,0,1]
	s_waitcnt lgkmcnt(3)
	v_med3_f32 v225, v230, s97, v185
	v_med3_f32 v226, v231, s97, v185
	v_mov_b32_e32 v224, v145
	v_cvt_pk_fp8_f32 v224, v225, v226
	s_waitcnt lgkmcnt(1)
	v_med3_f32 v226, v234, s97, v185
	v_med3_f32 v229, v235, s97, v185
	v_mov_b32_e32 v225, v145
	v_cvt_pk_fp8_f32 v225, v226, v229
	v_add3_u32 v205, s18, v117, v142
	v_add3_u32 v206, s18, v118, v143
	v_add3_u32 v207, s18, v119, v146
	v_add3_u32 v208, s18, v120, v147
	v_add3_u32 v209, s18, v121, v148
	v_add3_u32 v210, s18, v122, v149
	v_add3_u32 v211, s18, v123, v150
	v_add3_u32 v212, s18, v124, v151
	ds_read_b32 v221, v205
	ds_read_b32 v238, v206
	ds_read_b32 v239, v207
	ds_read_b32 v240, v208
	ds_read_b32 v241, v209
	ds_read_b32 v242, v210
	ds_read_b32 v243, v211
	ds_read_b32 v244, v212
	v_med3_f32 v227, v232, s97, v185
	v_med3_f32 v228, v233, s97, v185
	v_cvt_pk_fp8_f32 v224, v227, v228 op_sel:[0,0,1]
	s_waitcnt lgkmcnt(8)
	v_med3_f32 v226, v236, s97, v185
	v_med3_f32 v227, v237, s97, v185
	v_cvt_pk_fp8_f32 v225, v226, v227 op_sel:[0,0,1]
	s_waitcnt lgkmcnt(7)
	v_med3_f32 v221, v221, s97, v185
	s_waitcnt lgkmcnt(6)
	v_med3_f32 v227, v238, s97, v185
	v_mov_b32_e32 v226, v145
	v_cvt_pk_fp8_f32 v226, v221, v227
	s_waitcnt lgkmcnt(3)
	v_med3_f32 v221, v241, s97, v185
	s_waitcnt lgkmcnt(2)
	v_med3_f32 v230, v242, s97, v185
	v_mov_b32_e32 v227, v145
	v_cvt_pk_fp8_f32 v227, v221, v230
	v_add3_u32 v213, s18, v125, v187
	v_add3_u32 v214, s18, v126, v188
	v_add3_u32 v215, s18, v127, v189
	v_add3_u32 v216, s18, v128, v190
	v_add3_u32 v217, s18, v129, v191
	v_add3_u32 v218, s18, v130, v192
	v_add3_u32 v219, s18, v131, v193
	v_add3_u32 v220, s18, v132, v195
	ds_read_b32 v245, v213
	ds_read_b32 v246, v214
	ds_read_b32 v247, v215
	ds_read_b32 v248, v216
	ds_read_b32 v249, v217
	ds_read_b32 v250, v218
	ds_read_b32 v251, v219
	ds_read_b32 v252, v220
	v_med3_f32 v228, v239, s97, v185
	v_med3_f32 v229, v240, s97, v185
	v_cvt_pk_fp8_f32 v226, v228, v229 op_sel:[0,0,1]
	s_waitcnt lgkmcnt(9)
	v_med3_f32 v221, v243, s97, v185
	s_waitcnt lgkmcnt(8)
	v_med3_f32 v228, v244, s97, v185
	v_cvt_pk_fp8_f32 v227, v221, v228 op_sel:[0,0,1]
	s_waitcnt lgkmcnt(7)
	v_med3_f32 v221, v245, s97, v185
	s_waitcnt lgkmcnt(6)
	v_med3_f32 v229, v246, s97, v185
	v_mov_b32_e32 v228, v145
	v_cvt_pk_fp8_f32 v228, v221, v229
	s_waitcnt lgkmcnt(3)
	v_med3_f32 v221, v249, s97, v185
	s_waitcnt lgkmcnt(2)
	v_med3_f32 v232, v250, s97, v185
	v_mov_b32_e32 v229, v145
	v_cvt_pk_fp8_f32 v229, v221, v232
	v_med3_f32 v230, v247, s97, v185
	v_med3_f32 v231, v248, s97, v185
	v_cvt_pk_fp8_f32 v228, v230, v231 op_sel:[0,0,1]
	s_waitcnt lgkmcnt(1)
	v_med3_f32 v221, v251, s97, v185
	s_waitcnt lgkmcnt(0)
	v_med3_f32 v230, v252, s97, v185
	s_cmp_lt_i32 s5, 0
	v_cvt_pk_fp8_f32 v229, v221, v230 op_sel:[0,0,1]
	v_add_u32_e32 v221, s5, v107
	s_cselect_b64 vcc, -1, 0
	v_cndmask_b32_e32 v221, v221, v106, vcc
	v_mov_b64_e32 v[230:231], s[6:7]
	v_mad_i64_i32 v[230:231], s[6:7], s36, v221, v[230:231]
	s_mov_b32 s5, s13
	v_lshl_add_u64 v[230:231], v[230:231], 0, s[4:5]
	s_add_i32 s4, s1, 1
	s_min_i32 s19, s4, s89
	s_lshl_b32 s4, s19, 1
	s_and_b32 s4, s4, 0xffffe000
	s_and_b32 s18, s19, 0xfff
	s_or_b32 s4, s18, s4
	s_bfe_i32 s5, s19, 0x1001e
	s_bitset1_b32 s4, 12
	s_lshr_b32 s5, s5, 19
	s_add_i32 s5, s4, s5
	s_and_b32 s6, s5, 0xffffe000
	s_sub_i32 s6, s4, s6
	s_ashr_i32 s36, s6, 6
	s_and_b32 s12, s19, 63
	s_ashr_i32 s37, s36, 31
	v_lshl_add_u64 v[230:231], v[230:231], 0, v[96:97]
	s_cmpk_lt_i32 s4, 0x4000
	s_mov_b64 s[38:39], -1
	global_store_dwordx4 v[230:231], v[222:225], off nt
	global_store_dwordx4 v[230:231], v[226:229], off offset:16 nt
	s_cbranch_scc1 .LBB0_1386
	s_lshl_b32 s4, s12, 3
	s_lshl_b32 s6, s18, 16
	s_and_b32 s4, s4, 0x180
	s_and_b32 s18, s6, 0xf0000
	s_lshl_b64 s[6:7], s[36:37], 20
	s_add_u32 s6, s77, s6
	s_addc_u32 s7, s78, s7
	s_add_u32 s6, s6, s18
	s_addc_u32 s7, s7, 0
	s_mov_b64 s[38:39], 0

.LBB0_1394:
	s_and_b32 s12, s12, 63
	s_lshl_b32 s12, s12, s41
	s_and_b32 s37, s12, s37
	v_add_u32_e32 v32, s37, v98
	v_add_u32_e32 v34, s37, v99
	v_add_u32_e32 v40, s37, v100
	v_add_u32_e32 v42, s37, v101
	v_add_u32_e32 v48, s37, v102
	v_add_u32_e32 v50, s37, v103
	v_add_u32_e32 v56, s37, v104
	v_add_u32_e32 v58, s37, v105
	v_mad_i64_i32 v[32:33], s[42:43], s40, v32, 0
	s_lshl_b32 s12, s33, 2
	s_lshl_b32 s19, s19, 9
	v_mad_i64_i32 v[34:35], s[42:43], s40, v34, 0
	v_mad_i64_i32 v[40:41], s[42:43], s40, v40, 0
	v_mad_i64_i32 v[42:43], s[42:43], s40, v42, 0
	v_mad_i64_i32 v[48:49], s[42:43], s40, v48, 0
	v_mad_i64_i32 v[50:51], s[42:43], s40, v50, 0
	v_mad_i64_i32 v[56:57], s[42:43], s40, v56, 0
	v_mad_i64_i32 v[58:59], s[40:41], s40, v58, 0
	v_lshl_add_u64 v[32:33], v[32:33], 2, s[38:39]
	s_and_b32 s12, s19, s12
	v_lshl_add_u64 v[34:35], v[34:35], 2, s[38:39]
	v_lshl_add_u64 v[40:41], v[40:41], 2, s[38:39]
	v_lshl_add_u64 v[42:43], v[42:43], 2, s[38:39]
	v_lshl_add_u64 v[48:49], v[48:49], 2, s[38:39]
	v_lshl_add_u64 v[50:51], v[50:51], 2, s[38:39]
	v_lshl_add_u64 v[56:57], v[56:57], 2, s[38:39]
	v_lshl_add_u64 v[58:59], v[58:59], 2, s[38:39]
	v_lshl_add_u64 v[32:33], v[32:33], 0, s[12:13]
	v_lshl_add_u64 v[34:35], v[34:35], 0, s[12:13]
	v_lshl_add_u64 v[40:41], v[40:41], 0, s[12:13]
	v_lshl_add_u64 v[42:43], v[42:43], 0, s[12:13]
	v_lshl_add_u64 v[48:49], v[48:49], 0, s[12:13]
	v_lshl_add_u64 v[50:51], v[50:51], 0, s[12:13]
	v_lshl_add_u64 v[56:57], v[56:57], 0, s[12:13]
	v_lshl_add_u64 v[58:59], v[58:59], 0, s[12:13]
	v_lshl_add_u64 v[32:33], v[32:33], 0, v[144:145]
	v_lshl_add_u64 v[34:35], v[34:35], 0, v[144:145]
	v_lshl_add_u64 v[40:41], v[40:41], 0, v[144:145]
	v_lshl_add_u64 v[42:43], v[42:43], 0, v[144:145]
	v_lshl_add_u64 v[48:49], v[48:49], 0, v[144:145]
	v_lshl_add_u64 v[50:51], v[50:51], 0, v[144:145]
	v_lshl_add_u64 v[56:57], v[56:57], 0, v[144:145]
	v_lshl_add_u64 v[58:59], v[58:59], 0, v[144:145]
	global_load_dwordx4 v[36:39], v[32:33], off nt
	s_nop 0
	global_load_dwordx4 v[32:35], v[34:35], off nt
	s_nop 0
	global_load_dwordx4 v[44:47], v[40:41], off nt
	s_nop 0
	global_load_dwordx4 v[40:43], v[42:43], off nt
	s_nop 0
	global_load_dwordx4 v[52:55], v[48:49], off nt
	s_nop 0
	global_load_dwordx4 v[48:51], v[50:51], off nt
	s_nop 0
	global_load_dwordx4 v[60:63], v[56:57], off nt
	s_nop 0
	global_load_dwordx4 v[56:59], v[58:59], off nt
	v_add3_u32 v221, s18, v108, v141
	s_waitcnt lgkmcnt(0)
	s_barrier
	ds_read2st64_b32 v[222:223], v221 offset1:2
	ds_read2st64_b32 v[224:225], v221 offset0:4 offset1:6
	ds_read2st64_b32 v[226:227], v221 offset0:8 offset1:10
	ds_read2st64_b32 v[228:229], v221 offset0:12 offset1:14
	ds_read2st64_b32 v[230:231], v221 offset0:16 offset1:18
	ds_read2st64_b32 v[232:233], v221 offset0:20 offset1:22
	ds_read2st64_b32 v[234:235], v221 offset0:24 offset1:26
	ds_read2st64_b32 v[236:237], v221 offset0:28 offset1:30
	s_waitcnt lgkmcnt(7)
	v_med3_f32 v253, v222, s97, v185
	v_med3_f32 v223, v223, s97, v185
	v_mov_b32_e32 v222, v145
	v_cvt_pk_fp8_f32 v222, v253, v223
	s_waitcnt lgkmcnt(5)
	v_med3_f32 v226, v226, s97, v185
	v_med3_f32 v227, v227, s97, v185
	v_mov_b32_e32 v223, v145
	v_cvt_pk_fp8_f32 v223, v226, v227
	v_med3_f32 v224, v224, s97, v185
	v_med3_f32 v225, v225, s97, v185
	v_cvt_pk_fp8_f32 v222, v224, v225 op_sel:[0,0,1]
	s_waitcnt lgkmcnt(4)
	v_med3_f32 v224, v228, s97, v185
	v_med3_f32 v225, v229, s97, v185
	v_cvt_pk_fp8_f32 v223, v224, v225 op_sel:[0,0,1]
	s_waitcnt lgkmcnt(3)
	v_med3_f32 v225, v230, s97, v185
	v_med3_f32 v226, v231, s97, v185
	v_mov_b32_e32 v224, v145
	v_cvt_pk_fp8_f32 v224, v225, v226
	s_waitcnt lgkmcnt(1)
	v_med3_f32 v226, v234, s97, v185
	v_med3_f32 v229, v235, s97, v185
	v_mov_b32_e32 v225, v145
	v_cvt_pk_fp8_f32 v225, v226, v229
	v_add3_u32 v221, s18, v117, v142
	v_add3_u32 v238, s18, v118, v143
	v_add3_u32 v239, s18, v119, v146
	v_add3_u32 v240, s18, v120, v147
	v_add3_u32 v241, s18, v121, v148
	v_add3_u32 v242, s18, v122, v149
	v_add3_u32 v243, s18, v123, v150
	v_add3_u32 v244, s18, v124, v151
	ds_read_b32 v221, v221
	ds_read_b32 v238, v238
	ds_read_b32 v239, v239
	ds_read_b32 v240, v240
	ds_read_b32 v241, v241
	ds_read_b32 v242, v242
	ds_read_b32 v243, v243
	ds_read_b32 v244, v244
	v_med3_f32 v227, v232, s97, v185
	v_med3_f32 v228, v233, s97, v185
	v_cvt_pk_fp8_f32 v224, v227, v228 op_sel:[0,0,1]
	s_waitcnt lgkmcnt(8)
	v_med3_f32 v226, v236, s97, v185
	v_med3_f32 v227, v237, s97, v185
	v_cvt_pk_fp8_f32 v225, v226, v227 op_sel:[0,0,1]
	s_waitcnt lgkmcnt(7)
	v_med3_f32 v221, v221, s97, v185
	s_waitcnt lgkmcnt(6)
	v_med3_f32 v227, v238, s97, v185
	v_mov_b32_e32 v226, v145
	v_cvt_pk_fp8_f32 v226, v221, v227
	s_waitcnt lgkmcnt(3)
	v_med3_f32 v221, v241, s97, v185
	s_waitcnt lgkmcnt(2)
	v_med3_f32 v230, v242, s97, v185
	v_mov_b32_e32 v227, v145
	v_cvt_pk_fp8_f32 v227, v221, v230
	v_add3_u32 v245, s18, v125, v187
	v_add3_u32 v246, s18, v126, v188
	v_add3_u32 v247, s18, v127, v189
	v_add3_u32 v248, s18, v128, v190
	v_add3_u32 v249, s18, v129, v191
	v_add3_u32 v250, s18, v130, v192
	v_add3_u32 v251, s18, v131, v193
	v_add3_u32 v252, s18, v132, v195
	ds_read_b32 v245, v245
	ds_read_b32 v246, v246
	ds_read_b32 v247, v247
	ds_read_b32 v248, v248
	ds_read_b32 v249, v249
	ds_read_b32 v250, v250
	ds_read_b32 v251, v251
	ds_read_b32 v252, v252
	v_med3_f32 v228, v239, s97, v185
	v_med3_f32 v229, v240, s97, v185
	v_cvt_pk_fp8_f32 v226, v228, v229 op_sel:[0,0,1]
	s_waitcnt lgkmcnt(9)
	v_med3_f32 v221, v243, s97, v185
	s_waitcnt lgkmcnt(8)
	v_med3_f32 v228, v244, s97, v185
	v_cvt_pk_fp8_f32 v227, v221, v228 op_sel:[0,0,1]
	s_waitcnt lgkmcnt(7)
	v_med3_f32 v221, v245, s97, v185
	s_waitcnt lgkmcnt(6)
	v_med3_f32 v229, v246, s97, v185
	v_mov_b32_e32 v228, v145
	v_cvt_pk_fp8_f32 v228, v221, v229
	s_waitcnt lgkmcnt(3)
	v_med3_f32 v221, v249, s97, v185
	s_waitcnt lgkmcnt(2)
	v_med3_f32 v232, v250, s97, v185
	v_mov_b32_e32 v229, v145
	v_cvt_pk_fp8_f32 v229, v221, v232
	v_med3_f32 v230, v247, s97, v185
	v_med3_f32 v231, v248, s97, v185
	v_cvt_pk_fp8_f32 v228, v230, v231 op_sel:[0,0,1]
	s_waitcnt lgkmcnt(1)
	v_med3_f32 v221, v251, s97, v185
	s_waitcnt lgkmcnt(0)
	v_med3_f32 v230, v252, s97, v185
	s_cmp_lt_i32 s5, 0
	v_cvt_pk_fp8_f32 v229, v221, v230 op_sel:[0,0,1]
	v_add_u32_e32 v221, s5, v107
	s_cselect_b64 vcc, -1, 0
	v_cndmask_b32_e32 v221, v221, v106, vcc
	v_mov_b64_e32 v[230:231], s[6:7]
	v_mad_i64_i32 v[230:231], s[6:7], s36, v221, v[230:231]
	s_mov_b32 s5, s13
	v_lshl_add_u64 v[230:231], v[230:231], 0, s[4:5]
	s_add_i32 s4, s1, 2
	s_min_i32 s18, s4, s89
	s_lshl_b32 s4, s18, 1
	s_and_b32 s4, s4, 0xffffe000
	s_and_b32 s19, s18, 0xfff
	s_or_b32 s4, s19, s4
	s_bfe_i32 s5, s18, 0x1001e
	s_bitset1_b32 s4, 12
	s_lshr_b32 s5, s5, 19
	s_add_i32 s5, s4, s5
	s_and_b32 s6, s5, 0xffffe000
	s_sub_i32 s6, s4, s6
	s_ashr_i32 s36, s6, 6
	s_and_b32 s12, s18, 63
	s_ashr_i32 s37, s36, 31
	v_lshl_add_u64 v[230:231], v[230:231], 0, v[96:97]
	s_cmpk_lt_i32 s4, 0x4000
	s_mov_b64 s[38:39], -1
	global_store_dwordx4 v[230:231], v[222:225], off nt
	global_store_dwordx4 v[230:231], v[226:229], off offset:16 nt
	s_cbranch_scc1 .LBB0_1396
	s_lshl_b32 s4, s12, 3
	s_lshl_b32 s6, s19, 16
	s_and_b32 s4, s4, 0x180
	s_and_b32 s19, s6, 0xf0000
	s_lshl_b64 s[6:7], s[36:37], 20
	s_add_u32 s6, s77, s6
	s_addc_u32 s7, s78, s7
	s_add_u32 s6, s6, s19
	s_addc_u32 s7, s7, 0
	s_mov_b64 s[38:39], 0

.LBB0_1405:
	s_cmpk_gt_i32 s68, 0x3ff
	s_cbranch_scc1 .LBB0_1353
	s_lshl_b32 s4, s68, 8
	s_ashr_i32 s0, s68, 7
	s_and_b32 s33, s4, 0x700
	s_bfe_u32 s1, s68, 0x40003
	s_add_i32 s4, s33, 0x100
	s_mul_i32 s6, s0, 0x900
	s_mul_hi_i32 s5, s0, 0x900
	s_add_u32 s62, s6, s4
	s_addc_u32 s63, s5, 0
	s_mul_i32 s4, s63, 0x1800
	s_mul_hi_u32 s5, s62, 0x1800
	s_add_i32 s5, s5, s4
	s_mul_i32 s4, s62, 0x1800
	s_add_u32 s4, s73, s4
	s_addc_u32 s5, s74, s5
	s_lshl_b32 s95, s1, 7
	s_lshl_b32 s1, s1, 8
	s_add_u32 s6, s4, s1
	s_addc_u32 s7, s5, 0
	s_mul_i32 s4, s0, 0x120000
	s_mul_hi_i32 s1, s0, 0x120000
	s_add_u32 s4, s71, s4
	s_addc_u32 s1, s72, s1
	s_lshl_b32 s5, s68, 2
	s_and_b32 s5, s5, 0x180
	s_add_u32 s64, s4, s5
	s_addc_u32 s65, s1, 0
	s_mul_hi_i32 s1, s0, 0xd80000
	s_mul_i32 s0, s0, 0xd80000
	s_add_u32 s0, s73, s0
	s_addc_u32 s1, s74, s1
	s_lshl_b32 s4, s5, 1
	v_mov_b32_e32 v187, v152
	s_add_u32 s12, s0, s4
	s_load_dwordx2 s[4:5], s[10:11], 0x88
	s_movk_i32 s0, 0xc00
	v_and_b32_e32 v188, 31, v187
	s_waitcnt vmcnt(28)
	v_or_b32_e32 v0, s82, v188
	v_mul_lo_u32 v144, v0, s0
	v_and_b32_e32 v0, 0xffffffe0, v187
	v_lshl_add_u64 v[2:3], v[144:145], 1, s[6:7]
	v_ashrrev_i32_e32 v1, 31, v0
	v_lshl_add_u64 v[6:7], v[0:1], 1, v[2:3]
	global_load_dwordx4 v[12:15], v[6:7], off offset:48
	global_load_dwordx4 v[16:19], v[6:7], off offset:32
	global_load_dwordx4 v[20:23], v[6:7], off offset:16
	global_load_dwordx4 v[2:5], v[6:7], off
	global_load_dwordx4 v[68:71], v[6:7], off offset:176
	global_load_dwordx4 v[72:75], v[6:7], off offset:160
	global_load_dwordx4 v[24:27], v[6:7], off offset:144
	global_load_dwordx4 v[28:31], v[6:7], off offset:128
	s_addc_u32 s58, s1, 0
	s_add_u32 s66, s12, 0x1400
	s_addc_u32 s67, s58, 0
	s_add_i32 s33, s33, s82
	s_lshr_b32 s0, s33, 6
	v_mov_b32_e32 v128, v145
	v_mov_b32_e32 v129, v145
	v_mov_b32_e32 v130, v145
	v_mov_b32_e32 v131, v145
	v_mov_b32_e32 v132, v145
	v_mov_b32_e32 v133, v145
	v_mov_b32_e32 v134, v145
	v_mov_b32_e32 v135, v145
	v_mov_b32_e32 v136, v145
	v_mov_b32_e32 v137, v145
	v_mov_b32_e32 v138, v145
	v_mov_b32_e32 v139, v145
	v_mov_b32_e32 v140, v145
	v_mov_b32_e32 v141, v145
	v_mov_b32_e32 v142, v145
	v_mov_b32_e32 v143, v145
	v_lshlrev_b32_e32 v190, 4, v187
	s_add_i32 s33, s84, 0
	s_add_i32 s59, s33, 0x8000
	s_mov_b32 m0, s59
	s_add_i32 s70, s33, 0x2000
	v_ashrrev_i32_e32 v189, 5, v187
	s_add_i32 s18, s33, 0xa000
	s_mov_b32 s36, 0
	s_mov_b32 s37, s36
	s_mov_b32 s38, s36
	s_mov_b32 s39, s36
	s_mov_b32 s40, s36
	s_mov_b32 s41, s36
	s_mov_b32 s42, s36
	s_mov_b32 s43, s36
	s_mov_b32 s44, s36
	s_mov_b32 s45, s36
	s_mov_b32 s46, s36
	s_mov_b32 s47, s36
	s_mov_b32 s48, s36
	s_mov_b32 s49, s36
	s_mov_b32 s50, s36
	s_mov_b32 s51, s36
	s_mov_b32 s61, 0x120000
	v_mov_b32_e32 v147, v145
	v_mov_b32_e32 v149, v145
	v_lshl_add_u32 v202, v188, 2, s81
	v_lshlrev_b32_e32 v201, 4, v189
	v_mov_b32_e32 v203, 0
	s_mov_b32 s19, 0x20000
	s_waitcnt vmcnt(7)
	v_lshlrev_b32_e32 v65, 16, v12
	s_waitcnt vmcnt(6)
	v_lshlrev_b32_e32 v64, 16, v16
	s_waitcnt vmcnt(5)
	v_lshlrev_b32_e32 v54, 16, v20
	s_waitcnt vmcnt(4)
	v_and_b32_e32 v45, 0xffff0000, v2
	v_lshlrev_b32_e32 v51, 16, v2
	v_mul_f32_e32 v36, v45, v45
	v_lshlrev_b32_e32 v40, 16, v3
	v_fmac_f32_e32 v36, v51, v51
	v_and_b32_e32 v10, 0xffff0000, v3
	v_fmac_f32_e32 v36, v40, v40
	v_lshlrev_b32_e32 v8, 16, v4
	v_fmac_f32_e32 v36, v10, v10
	v_and_b32_e32 v6, 0xffff0000, v4
	v_fmac_f32_e32 v36, v8, v8
	v_lshlrev_b32_e32 v4, 16, v5
	v_fmac_f32_e32 v36, v6, v6
	v_and_b32_e32 v2, 0xffff0000, v5
	v_fmac_f32_e32 v36, v4, v4
	v_fmac_f32_e32 v36, v2, v2
	v_and_b32_e32 v48, 0xffff0000, v20
	v_fmac_f32_e32 v36, v54, v54
	v_lshlrev_b32_e32 v42, 16, v21
	v_fmac_f32_e32 v36, v48, v48
	v_and_b32_e32 v11, 0xffff0000, v21
	v_fmac_f32_e32 v36, v42, v42
	v_lshlrev_b32_e32 v9, 16, v22
	v_fmac_f32_e32 v36, v11, v11
	v_and_b32_e32 v7, 0xffff0000, v22
	v_fmac_f32_e32 v36, v9, v9
	v_lshlrev_b32_e32 v5, 16, v23
	v_fmac_f32_e32 v36, v7, v7
	v_and_b32_e32 v3, 0xffff0000, v23
	v_fmac_f32_e32 v36, v5, v5
	v_fmac_f32_e32 v36, v3, v3
	v_and_b32_e32 v61, 0xffff0000, v16
	v_fmac_f32_e32 v36, v64, v64
	v_lshlrev_b32_e32 v58, 16, v17
	v_fmac_f32_e32 v36, v61, v61
	v_and_b32_e32 v55, 0xffff0000, v17
	v_fmac_f32_e32 v36, v58, v58
	v_lshlrev_b32_e32 v52, 16, v18
	v_fmac_f32_e32 v36, v55, v55
	v_and_b32_e32 v49, 0xffff0000, v18
	v_fmac_f32_e32 v36, v52, v52
	v_lshlrev_b32_e32 v46, 16, v19
	v_fmac_f32_e32 v36, v49, v49
	v_and_b32_e32 v43, 0xffff0000, v19
	v_fmac_f32_e32 v36, v46, v46
	v_fmac_f32_e32 v36, v43, v43
	v_and_b32_e32 v62, 0xffff0000, v12
	v_fmac_f32_e32 v36, v65, v65
	v_lshlrev_b32_e32 v59, 16, v13
	v_fmac_f32_e32 v36, v62, v62
	v_and_b32_e32 v56, 0xffff0000, v13
	v_fmac_f32_e32 v36, v59, v59
	v_lshlrev_b32_e32 v53, 16, v14
	v_fmac_f32_e32 v36, v56, v56
	v_and_b32_e32 v50, 0xffff0000, v14
	v_fmac_f32_e32 v36, v53, v53
	v_lshlrev_b32_e32 v47, 16, v15
	v_fmac_f32_e32 v36, v50, v50
	v_and_b32_e32 v44, 0xffff0000, v15
	v_fmac_f32_e32 v36, v47, v47
	v_fmac_f32_e32 v36, v44, v44
	s_waitcnt vmcnt(0)
	v_lshlrev_b32_e32 v41, 16, v28
	v_and_b32_e32 v39, 0xffff0000, v28
	v_fmac_f32_e32 v36, v41, v41
	v_lshlrev_b32_e32 v38, 16, v29
	v_fmac_f32_e32 v36, v39, v39
	v_and_b32_e32 v37, 0xffff0000, v29
	v_fmac_f32_e32 v36, v38, v38
	v_lshlrev_b32_e32 v19, 16, v30
	v_fmac_f32_e32 v36, v37, v37
	v_and_b32_e32 v18, 0xffff0000, v30
	v_fmac_f32_e32 v36, v19, v19
	v_lshlrev_b32_e32 v16, 16, v31
	v_fmac_f32_e32 v36, v18, v18
	v_and_b32_e32 v14, 0xffff0000, v31
	v_fmac_f32_e32 v36, v16, v16
	v_fmac_f32_e32 v36, v14, v14
	v_lshlrev_b32_e32 v82, 16, v24
	v_and_b32_e32 v81, 0xffff0000, v24
	v_fmac_f32_e32 v36, v82, v82
	v_lshlrev_b32_e32 v80, 16, v25
	v_fmac_f32_e32 v36, v81, v81
	v_and_b32_e32 v79, 0xffff0000, v25
	v_fmac_f32_e32 v36, v80, v80
	v_lshlrev_b32_e32 v78, 16, v26
	v_fmac_f32_e32 v36, v79, v79
	v_and_b32_e32 v67, 0xffff0000, v26
	v_fmac_f32_e32 v36, v78, v78
	v_lshlrev_b32_e32 v17, 16, v27
	v_fmac_f32_e32 v36, v67, v67
	v_and_b32_e32 v15, 0xffff0000, v27
	v_fmac_f32_e32 v36, v17, v17
	v_fmac_f32_e32 v36, v15, v15
	v_lshlrev_b32_e32 v34, 16, v72
	v_and_b32_e32 v32, 0xffff0000, v72
	v_fmac_f32_e32 v36, v34, v34
	v_lshlrev_b32_e32 v30, 16, v73
	v_fmac_f32_e32 v36, v32, v32
	v_and_b32_e32 v28, 0xffff0000, v73
	v_fmac_f32_e32 v36, v30, v30
	v_lshlrev_b32_e32 v26, 16, v74
	v_fmac_f32_e32 v36, v28, v28
	v_and_b32_e32 v24, 0xffff0000, v74
	v_fmac_f32_e32 v36, v26, v26
	v_lshlrev_b32_e32 v22, 16, v75
	v_fmac_f32_e32 v36, v24, v24
	v_and_b32_e32 v20, 0xffff0000, v75
	v_fmac_f32_e32 v36, v22, v22
	v_fmac_f32_e32 v36, v20, v20
	v_lshlrev_b32_e32 v35, 16, v68
	v_and_b32_e32 v33, 0xffff0000, v68
	v_fmac_f32_e32 v36, v35, v35
	v_lshlrev_b32_e32 v31, 16, v69
	v_fmac_f32_e32 v36, v33, v33
	v_and_b32_e32 v29, 0xffff0000, v69
	v_fmac_f32_e32 v36, v31, v31
	v_lshlrev_b32_e32 v27, 16, v70
	v_fmac_f32_e32 v36, v29, v29
	v_and_b32_e32 v25, 0xffff0000, v70
	v_fmac_f32_e32 v36, v27, v27
	v_lshlrev_b32_e32 v23, 16, v71
	v_fmac_f32_e32 v36, v25, v25
	v_and_b32_e32 v21, 0xffff0000, v71
	v_fmac_f32_e32 v36, v23, v23
	v_fmac_f32_e32 v36, v21, v21
	v_mov_b32_e32 v12, v36
	s_nop 1
	v_permlane32_swap_b32_e32 v36, v12
	v_add_f32_e32 v12, v36, v12
	v_mov_b32_e32 v13, 0x358637bd
	v_fmamk_f32 v12, v12, 0x3c000000, v13
	v_rsq_f32_e32 v36, v12
	s_waitcnt lgkmcnt(0)
	v_lshl_add_u64 v[12:13], v[0:1], 2, s[4:5]
	global_load_dwordx4 v[86:89], v[12:13], off offset:48
	global_load_dwordx4 v[90:93], v[12:13], off offset:32
	global_load_dwordx4 v[94:97], v[12:13], off offset:16
	global_load_dwordx4 v[68:71], v[12:13], off
	v_cmp_gt_u32_e64 s[4:5], 32, v187
	s_waitcnt vmcnt(0)
	v_mul_f32_e32 v0, v68, v36
	v_mul_f32_e32 v84, v0, v51
	v_mul_f32_e32 v0, v69, v36
	v_mul_f32_e32 v77, v0, v45
	v_mul_f32_e32 v0, v70, v36
	v_mul_f32_e32 v75, v0, v40
	v_mul_f32_e32 v0, v71, v36
	v_mul_f32_e32 v73, v0, v10
	v_mul_f32_e32 v0, v94, v36
	v_mul_f32_e32 v71, v0, v8
	v_mul_f32_e32 v0, v95, v36
	v_mul_f32_e32 v69, v0, v6
	v_mul_f32_e32 v0, v96, v36
	v_mul_f32_e32 v66, v0, v4
	v_mul_f32_e32 v0, v97, v36
	v_mul_f32_e32 v63, v0, v2
	v_mul_f32_e32 v0, v90, v36
	v_mul_f32_e32 v60, v0, v54
	v_mul_f32_e32 v0, v91, v36
	v_mul_f32_e32 v57, v0, v48
	v_mul_f32_e32 v0, v92, v36
	v_mul_f32_e32 v54, v0, v42
	v_mul_f32_e32 v0, v93, v36
	v_mul_f32_e32 v51, v0, v11
	v_mul_f32_e32 v0, v86, v36
	v_mul_f32_e32 v48, v0, v9
	v_mul_f32_e32 v0, v87, v36
	v_mul_f32_e32 v45, v0, v7
	v_mul_f32_e32 v0, v88, v36
	v_mul_f32_e32 v42, v0, v5
	v_mul_f32_e32 v0, v89, v36
	v_mul_f32_e32 v40, v0, v3
	global_load_dwordx4 v[0:3], v[12:13], off offset:112
	global_load_dwordx4 v[4:7], v[12:13], off offset:96
	global_load_dwordx4 v[8:11], v[12:13], off offset:80
	global_load_dwordx4 v[86:89], v[12:13], off offset:64
	s_waitcnt vmcnt(3)
	v_mul_f32_e32 v0, v36, v0
	s_waitcnt vmcnt(2)
	v_mul_f32_e32 v4, v36, v4
	s_waitcnt vmcnt(1)
	v_mul_f32_e32 v8, v36, v8
	s_waitcnt vmcnt(0)
	v_mul_f32_e32 v68, v36, v86
	v_mul_f32_e32 v74, v8, v52
	v_mul_f32_e32 v8, v36, v9
	v_mul_f32_e32 v65, v4, v65
	v_mul_f32_e32 v4, v36, v5
	v_mul_f32_e32 v53, v0, v53
	v_mul_f32_e32 v0, v36, v1
	v_mul_f32_e32 v86, v68, v64
	v_mul_f32_e32 v64, v36, v87
	v_mul_f32_e32 v72, v8, v49
	v_mul_f32_e32 v8, v36, v10
	v_mul_f32_e32 v62, v4, v62
	v_mul_f32_e32 v4, v36, v6
	v_mul_f32_e32 v50, v0, v50
	v_mul_f32_e32 v0, v36, v2
	v_mul_f32_e32 v85, v64, v61
	v_mul_f32_e32 v61, v36, v88
	v_mul_f32_e32 v70, v8, v46
	v_mul_f32_e32 v8, v36, v11
	v_mul_f32_e32 v59, v4, v59
	v_mul_f32_e32 v4, v36, v7
	v_mul_f32_e32 v47, v0, v47
	v_mul_f32_e32 v0, v36, v3
	v_mul_f32_e32 v83, v61, v58
	v_mul_f32_e32 v58, v36, v89
	v_mul_f32_e32 v68, v8, v43
	v_mul_f32_e32 v56, v4, v56
	v_mul_f32_e32 v44, v0, v44
	global_load_dwordx4 v[0:3], v[12:13], off offset:304
	global_load_dwordx4 v[4:7], v[12:13], off offset:288
	global_load_dwordx4 v[8:11], v[12:13], off offset:272
	global_load_dwordx4 v[88:91], v[12:13], off offset:256
	v_mul_f32_e32 v76, v58, v55
	s_waitcnt vmcnt(3)
	v_mul_f32_e32 v0, v36, v0
	s_waitcnt vmcnt(2)
	v_mul_f32_e32 v4, v36, v4
	s_waitcnt vmcnt(1)
	v_mul_f32_e32 v8, v36, v8
	s_waitcnt vmcnt(0)
	v_mul_f32_e32 v43, v36, v88
	v_mul_f32_e32 v64, v43, v41
	v_mul_f32_e32 v41, v36, v89
	v_mul_f32_e32 v61, v41, v39
	v_mul_f32_e32 v39, v36, v90
	v_mul_f32_e32 v52, v8, v19
	v_mul_f32_e32 v8, v36, v9
	v_mul_f32_e32 v41, v4, v82
	v_mul_f32_e32 v4, v36, v5
	v_mul_f32_e32 v19, v0, v78
	v_mul_f32_e32 v0, v36, v1
	v_mul_f32_e32 v58, v39, v38
	v_mul_f32_e32 v38, v36, v91
	v_mul_f32_e32 v49, v8, v18
	v_mul_f32_e32 v8, v36, v10
	v_mul_f32_e32 v39, v4, v81
	v_mul_f32_e32 v4, v36, v6
	v_mul_f32_e32 v18, v0, v67
	v_mul_f32_e32 v0, v36, v2
	v_mul_f32_e32 v55, v38, v37
	v_mul_f32_e32 v46, v8, v16
	v_mul_f32_e32 v8, v36, v11
	v_mul_f32_e32 v38, v4, v80
	v_mul_f32_e32 v4, v36, v7
	v_mul_f32_e32 v17, v0, v17
	v_mul_f32_e32 v0, v36, v3
	v_mul_f32_e32 v43, v8, v14
	v_mul_f32_e32 v37, v4, v79
	v_mul_f32_e32 v16, v0, v15
	global_load_dwordx4 v[0:3], v[12:13], off offset:368
	global_load_dwordx4 v[4:7], v[12:13], off offset:352
	global_load_dwordx4 v[8:11], v[12:13], off offset:336
	s_nop 0
	global_load_dwordx4 v[12:15], v[12:13], off offset:320
	v_cvt_f32_u32_e32 v78, s0
	s_movk_i32 s0, 0x60
	s_waitcnt vmcnt(3)
	v_mul_f32_e32 v0, v36, v0
	s_waitcnt vmcnt(2)
	v_mul_f32_e32 v4, v36, v4
	s_waitcnt vmcnt(1)
	v_mul_f32_e32 v8, v36, v8
	s_waitcnt vmcnt(0)
	v_add_u32_e32 v206, s84, v190
	v_ashrrev_i32_e32 v207, 31, v206
	v_lshrrev_b32_e32 v207, 25, v207
	v_add_u32_e32 v207, v206, v207
	v_ashrrev_i32_e32 v208, 7, v207
	v_and_b32_e32 v207, 0xffffff80, v207
	v_sub_u32_e32 v207, v206, v207
	v_ashrrev_i32_e32 v207, 4, v207
	v_lshrrev_b32_e32 v209, 1, v208
	v_ashrrev_i32_e32 v210, 8, v206
	v_bitop3_b32 v207, v209, v207, 7 bitop3:0x6c
	v_bfe_u32 v209, v187, 2, 2
	v_lshrrev_b32_e32 v215, 1, v187
	v_and_b32_e32 v214, 0xfffff0, v210
	v_lshrrev_b32_e32 v210, 1, v210
	v_and_or_b32 v209, v215, 8, v209
	v_lshlrev_b32_e32 v212, 3, v187
	v_and_b32_e32 v210, 4, v210
	v_lshrrev_b32_e32 v211, 4, v206
	v_and_b32_e32 v213, 24, v212
	v_or3_b32 v210, v214, v210, v209
	v_and_b32_e32 v211, 0x60, v211
	v_or_b32_e32 v211, v211, v213
	v_mul_i32_i24_e32 v210, 0xc00, v210
	v_add_u32_e32 v206, 0x2000, v206
	v_or_b32_e32 v210, v210, v211
	v_ashrrev_i32_e32 v206, 8, v206
	v_lshlrev_b32_e32 v146, 1, v210
	v_and_b32_e32 v210, 0xfffff0, v206
	v_lshrrev_b32_e32 v206, 1, v206
	v_cmp_gt_i32_e32 vcc, 8, v207
	v_lshlrev_b32_e32 v207, 4, v207
	v_and_b32_e32 v206, 4, v206
	v_cndmask_b32_e32 v207, 0, v207, vcc
	v_or3_b32 v206, v210, v206, v209
	v_mul_i32_i24_e32 v206, 0xc00, v206
	v_lshl_add_u32 v144, v208, 9, v207
	v_or_b32_e32 v206, v206, v211
	global_load_lds_dwordx4 v144, s[64:65]
	s_mov_b32 m0, s33
	v_lshlrev_b32_e32 v148, 1, v206
	v_lshl_add_u64 v[150:151], s[64:65], 0, v[144:145]
	global_load_lds_dwordx4 v146, s[66:67]
	s_mov_b32 m0, s70
	s_nop 0
	global_load_lds_dwordx4 v148, s[66:67]
	v_add_co_u32_e32 v206, vcc, 0x8000, v150
	v_addc_co_u32_e32 v207, vcc, 0, v151, vcc
	s_mov_b32 m0, s18
	s_nop 0
	global_load_lds_dwordx4 v[206:207], off
	v_mul_f32_e32 v12, v36, v12
	v_mul_f32_e32 v67, v12, v34
	v_mul_f32_e32 v12, v36, v13
	v_mul_f32_e32 v34, v12, v32
	v_mul_f32_e32 v12, v36, v14
	v_mul_f32_e32 v32, v12, v30
	v_mul_f32_e32 v12, v36, v15
	v_mul_f32_e32 v30, v12, v28
	v_mul_f32_e32 v28, v8, v26
	v_mul_f32_e32 v8, v36, v9
	v_mul_f32_e32 v15, v4, v35
	v_mul_f32_e32 v4, v36, v5
	v_mul_f32_e32 v26, v8, v24
	v_mul_f32_e32 v8, v36, v10
	v_mul_f32_e32 v13, v4, v33
	v_mul_f32_e32 v4, v36, v6
	v_mul_f32_e32 v24, v8, v22
	v_mul_f32_e32 v8, v36, v11
	v_mul_f32_e32 v11, v4, v31
	v_mul_f32_e32 v4, v36, v7
	v_mul_f32_e32 v6, v0, v27
	v_mul_f32_e32 v0, v36, v1
	v_mul_f32_e32 v22, v8, v20
	v_mul_f32_e32 v8, v4, v29
	v_mul_f32_e32 v4, v0, v25
	v_mul_f32_e32 v0, v36, v2
	v_mul_f32_e32 v2, v0, v23
	v_mul_f32_e32 v0, v36, v3
	v_mov_b32_e32 v3, v84
	v_mov_b32_e32 v5, v84
	s_nop 1
	v_permlane32_swap_b32_e32 v3, v5
	v_cndmask_b32_e64 v3, v3, v5, s[4:5]
	v_mul_f32_e32 v5, 0.15915494, v78
	v_cos_f32_e32 v7, v5
	v_sin_f32_e32 v5, v5
	v_mul_f32_e32 v0, v0, v21
	v_or_b32_e32 v1, s83, v188
	v_cvt_f32_ubyte0_e32 v1, v1
	v_mul_f32_e32 v3, v5, v3
	v_cndmask_b32_e64 v3, v3, -v3, s[4:5]
	v_fmac_f32_e32 v3, v7, v84
	v_mov_b32_e32 v5, v77
	v_mov_b32_e32 v7, v77
	s_nop 1
	v_permlane32_swap_b32_e32 v5, v7
	v_cndmask_b32_e64 v5, v5, v7, s[4:5]
	v_mul_f32_e32 v7, v154, v78
	v_mul_f32_e32 v7, 0.15915494, v7
	v_cos_f32_e32 v9, v7
	v_sin_f32_e32 v7, v7
	s_nop 0
	v_mul_f32_e32 v5, v7, v5
	v_cndmask_b32_e64 v5, v5, -v5, s[4:5]
	v_fmac_f32_e32 v5, v9, v77
	v_mov_b32_e32 v7, v75
	v_mov_b32_e32 v9, v75
	s_nop 1
	v_permlane32_swap_b32_e32 v7, v9
	v_cndmask_b32_e64 v7, v7, v9, s[4:5]
	v_mul_f32_e32 v9, v155, v78
	v_mul_f32_e32 v9, 0.15915494, v9
	v_cos_f32_e32 v10, v9
	v_sin_f32_e32 v9, v9
	s_nop 0
	v_mul_f32_e32 v7, v9, v7
	v_cndmask_b32_e64 v7, v7, -v7, s[4:5]
	v_fmac_f32_e32 v7, v10, v75
	v_mov_b32_e32 v9, v73
	v_mov_b32_e32 v10, v73
	s_nop 1
	v_permlane32_swap_b32_e32 v9, v10
	v_cndmask_b32_e64 v9, v9, v10, s[4:5]
	v_mul_f32_e32 v10, v156, v78
	v_mul_f32_e32 v10, 0.15915494, v10
	v_cos_f32_e32 v12, v10
	v_sin_f32_e32 v10, v10
	s_nop 0
	v_mul_f32_e32 v9, v10, v9
	v_cndmask_b32_e64 v9, v9, -v9, s[4:5]
	v_fmac_f32_e32 v9, v12, v73
	v_mov_b32_e32 v10, v71
	v_mov_b32_e32 v12, v71
	s_nop 1
	v_permlane32_swap_b32_e32 v10, v12
	v_cndmask_b32_e64 v10, v10, v12, s[4:5]
	v_mul_f32_e32 v12, v157, v78
	v_mul_f32_e32 v12, 0.15915494, v12
	v_cos_f32_e32 v14, v12
	v_sin_f32_e32 v12, v12
	s_nop 0
	v_mul_f32_e32 v10, v12, v10
	v_cndmask_b32_e64 v10, v10, -v10, s[4:5]
	v_fmac_f32_e32 v10, v14, v71
	v_mov_b32_e32 v12, v69
	v_mov_b32_e32 v14, v69
	s_nop 1
	v_permlane32_swap_b32_e32 v12, v14
	v_cndmask_b32_e64 v12, v12, v14, s[4:5]
	v_mul_f32_e32 v14, v158, v78
	v_mul_f32_e32 v14, 0.15915494, v14
	v_cos_f32_e32 v20, v14
	v_sin_f32_e32 v14, v14
	s_nop 0
	v_mul_f32_e32 v12, v14, v12
	v_cndmask_b32_e64 v12, v12, -v12, s[4:5]
	v_fmac_f32_e32 v12, v20, v69
	v_mov_b32_e32 v14, v66
	v_mov_b32_e32 v20, v66
	s_nop 1
	v_permlane32_swap_b32_e32 v14, v20
	v_cndmask_b32_e64 v14, v14, v20, s[4:5]
	v_mul_f32_e32 v20, v159, v78
	v_mul_f32_e32 v20, 0.15915494, v20
	v_cos_f32_e32 v21, v20
	v_sin_f32_e32 v20, v20
	s_nop 0
	v_mul_f32_e32 v14, v20, v14
	v_cndmask_b32_e64 v14, v14, -v14, s[4:5]
	v_fmac_f32_e32 v14, v21, v66
	v_mov_b32_e32 v20, v63
	v_mov_b32_e32 v21, v63
	s_nop 1
	v_permlane32_swap_b32_e32 v20, v21
	v_cndmask_b32_e64 v20, v20, v21, s[4:5]
	v_mul_f32_e32 v21, v160, v78
	v_mul_f32_e32 v21, 0.15915494, v21
	v_cos_f32_e32 v23, v21
	v_sin_f32_e32 v21, v21
	s_nop 0
	v_mul_f32_e32 v20, v21, v20
	v_cndmask_b32_e64 v20, v20, -v20, s[4:5]
	v_fmac_f32_e32 v20, v23, v63
	v_mov_b32_e32 v21, v60
	v_mov_b32_e32 v23, v60
	s_nop 1
	v_permlane32_swap_b32_e32 v21, v23
	v_cndmask_b32_e64 v21, v21, v23, s[4:5]
	v_mul_f32_e32 v23, v161, v78
	v_mul_f32_e32 v23, 0.15915494, v23
	v_cos_f32_e32 v25, v23
	v_sin_f32_e32 v23, v23
	s_nop 0
	v_mul_f32_e32 v21, v23, v21
	v_cndmask_b32_e64 v21, v21, -v21, s[4:5]
	v_fmac_f32_e32 v21, v25, v60
	v_mov_b32_e32 v23, v57
	v_mov_b32_e32 v25, v57
	s_nop 1
	v_permlane32_swap_b32_e32 v23, v25
	v_cndmask_b32_e64 v23, v23, v25, s[4:5]
	v_mul_f32_e32 v25, v162, v78
	v_mul_f32_e32 v25, 0.15915494, v25
	v_cos_f32_e32 v27, v25
	v_sin_f32_e32 v25, v25
	s_nop 0
	v_mul_f32_e32 v23, v25, v23
	v_cndmask_b32_e64 v23, v23, -v23, s[4:5]
	v_fmac_f32_e32 v23, v27, v57
	v_mov_b32_e32 v25, v54
	v_mov_b32_e32 v27, v54
	s_nop 1
	v_permlane32_swap_b32_e32 v25, v27
	v_cndmask_b32_e64 v25, v25, v27, s[4:5]
	v_mul_f32_e32 v27, v163, v78
	v_mul_f32_e32 v27, 0.15915494, v27
	v_cos_f32_e32 v29, v27
	v_sin_f32_e32 v27, v27
	s_nop 0
	v_mul_f32_e32 v25, v27, v25
	v_cndmask_b32_e64 v25, v25, -v25, s[4:5]
	v_fmac_f32_e32 v25, v29, v54
	v_mov_b32_e32 v27, v51
	v_mov_b32_e32 v29, v51
	s_nop 1
	v_permlane32_swap_b32_e32 v27, v29
	v_cndmask_b32_e64 v27, v27, v29, s[4:5]
	v_mul_f32_e32 v29, v164, v78
	v_mul_f32_e32 v29, 0.15915494, v29
	v_cos_f32_e32 v31, v29
	v_sin_f32_e32 v29, v29
	s_nop 0
	v_mul_f32_e32 v27, v29, v27
	v_cndmask_b32_e64 v27, v27, -v27, s[4:5]
	v_fmac_f32_e32 v27, v31, v51
	v_mov_b32_e32 v29, v48
	v_mov_b32_e32 v31, v48
	s_nop 1
	v_permlane32_swap_b32_e32 v29, v31
	v_cndmask_b32_e64 v29, v29, v31, s[4:5]
	v_mul_f32_e32 v31, v165, v78
	v_mul_f32_e32 v31, 0.15915494, v31
	v_cos_f32_e32 v33, v31
	v_sin_f32_e32 v31, v31
	s_nop 0
	v_mul_f32_e32 v29, v31, v29
	v_cndmask_b32_e64 v29, v29, -v29, s[4:5]
	v_fmac_f32_e32 v29, v33, v48
	v_mov_b32_e32 v31, v45
	v_mov_b32_e32 v33, v45
	s_nop 1
	v_permlane32_swap_b32_e32 v31, v33
	v_cndmask_b32_e64 v31, v31, v33, s[4:5]
	v_mul_f32_e32 v33, v166, v78
	v_mul_f32_e32 v33, 0.15915494, v33
	v_cos_f32_e32 v35, v33
	v_sin_f32_e32 v33, v33
	s_nop 0
	v_mul_f32_e32 v31, v33, v31
	v_cndmask_b32_e64 v31, v31, -v31, s[4:5]
	v_fmac_f32_e32 v31, v35, v45
	v_mov_b32_e32 v33, v42
	v_mov_b32_e32 v35, v42
	s_nop 1
	v_permlane32_swap_b32_e32 v33, v35
	v_cndmask_b32_e64 v33, v33, v35, s[4:5]
	v_mul_f32_e32 v35, v167, v78
	v_mul_f32_e32 v35, 0.15915494, v35
	v_cos_f32_e32 v36, v35
	v_sin_f32_e32 v35, v35
	s_nop 0
	v_mul_f32_e32 v33, v35, v33
	v_cndmask_b32_e64 v33, v33, -v33, s[4:5]
	v_fmac_f32_e32 v33, v36, v42
	v_mov_b32_e32 v35, v40
	v_mov_b32_e32 v36, v40
	s_nop 1
	v_permlane32_swap_b32_e32 v35, v36
	v_cndmask_b32_e64 v35, v35, v36, s[4:5]
	v_mul_f32_e32 v36, v168, v78
	v_mul_f32_e32 v36, 0.15915494, v36
	v_cos_f32_e32 v42, v36
	v_sin_f32_e32 v36, v36
	s_nop 0
	v_mul_f32_e32 v35, v36, v35
	v_cndmask_b32_e64 v35, v35, -v35, s[4:5]
	v_fmac_f32_e32 v35, v42, v40
	v_mov_b32_e32 v36, v86
	v_mov_b32_e32 v40, v86
	s_nop 1
	v_permlane32_swap_b32_e32 v36, v40
	v_cndmask_b32_e64 v36, v36, v40, s[4:5]
	v_mul_f32_e32 v40, v169, v78
	v_mul_f32_e32 v40, 0.15915494, v40
	v_cos_f32_e32 v42, v40
	v_sin_f32_e32 v40, v40
	s_nop 0
	v_mul_f32_e32 v36, v40, v36
	v_cndmask_b32_e64 v36, v36, -v36, s[4:5]
	v_fmac_f32_e32 v36, v42, v86
	v_mov_b32_e32 v40, v85
	v_mov_b32_e32 v42, v85
	s_nop 1
	v_permlane32_swap_b32_e32 v40, v42
	v_cndmask_b32_e64 v40, v40, v42, s[4:5]
	v_mul_f32_e32 v42, v170, v78
	v_mul_f32_e32 v42, 0.15915494, v42
	v_cos_f32_e32 v45, v42
	v_sin_f32_e32 v42, v42
	s_nop 0
	v_mul_f32_e32 v40, v42, v40
	v_cndmask_b32_e64 v40, v40, -v40, s[4:5]
	v_fmac_f32_e32 v40, v45, v85
	v_mov_b32_e32 v42, v83
	v_mov_b32_e32 v45, v83
	s_nop 1
	v_permlane32_swap_b32_e32 v42, v45
	v_cndmask_b32_e64 v42, v42, v45, s[4:5]
	v_mul_f32_e32 v45, v171, v78
	v_mul_f32_e32 v45, 0.15915494, v45
	v_cos_f32_e32 v48, v45
	v_sin_f32_e32 v45, v45
	s_nop 0
	v_mul_f32_e32 v42, v45, v42
	v_cndmask_b32_e64 v42, v42, -v42, s[4:5]
	v_fmac_f32_e32 v42, v48, v83
	v_mov_b32_e32 v45, v76
	v_mov_b32_e32 v48, v76
	s_nop 1
	v_permlane32_swap_b32_e32 v45, v48
	v_cndmask_b32_e64 v45, v45, v48, s[4:5]
	v_mul_f32_e32 v48, v172, v78
	v_mul_f32_e32 v48, 0.15915494, v48
	v_cos_f32_e32 v51, v48
	v_sin_f32_e32 v48, v48
	s_nop 0
	v_mul_f32_e32 v45, v48, v45
	v_cndmask_b32_e64 v45, v45, -v45, s[4:5]
	v_fmac_f32_e32 v45, v51, v76
	v_mov_b32_e32 v48, v74
	v_mov_b32_e32 v51, v74
	s_nop 1
	v_permlane32_swap_b32_e32 v48, v51
	v_cndmask_b32_e64 v48, v48, v51, s[4:5]
	v_mul_f32_e32 v51, v173, v78
	v_mul_f32_e32 v51, 0.15915494, v51
	v_cos_f32_e32 v54, v51
	v_sin_f32_e32 v51, v51
	s_nop 0
	v_mul_f32_e32 v48, v51, v48
	v_cndmask_b32_e64 v48, v48, -v48, s[4:5]
	v_fmac_f32_e32 v48, v54, v74
	v_mov_b32_e32 v51, v72
	v_mov_b32_e32 v54, v72
	s_nop 1
	v_permlane32_swap_b32_e32 v51, v54
	v_cndmask_b32_e64 v51, v51, v54, s[4:5]
	v_mul_f32_e32 v54, v174, v78
	v_mul_f32_e32 v54, 0.15915494, v54
	v_cos_f32_e32 v57, v54
	v_sin_f32_e32 v54, v54
	s_nop 0
	v_mul_f32_e32 v51, v54, v51
	v_cndmask_b32_e64 v51, v51, -v51, s[4:5]
	v_fmac_f32_e32 v51, v57, v72
	v_mov_b32_e32 v54, v70
	v_mov_b32_e32 v57, v70
	s_nop 1
	v_permlane32_swap_b32_e32 v54, v57
	v_cndmask_b32_e64 v54, v54, v57, s[4:5]
	v_mul_f32_e32 v57, v175, v78
	v_mul_f32_e32 v57, 0.15915494, v57
	v_cos_f32_e32 v60, v57
	v_sin_f32_e32 v57, v57
	s_nop 0
	v_mul_f32_e32 v54, v57, v54
	v_cndmask_b32_e64 v54, v54, -v54, s[4:5]
	v_fmac_f32_e32 v54, v60, v70
	v_mov_b32_e32 v57, v68
	v_mov_b32_e32 v60, v68
	s_nop 1
	v_permlane32_swap_b32_e32 v57, v60
	v_cndmask_b32_e64 v57, v57, v60, s[4:5]
	v_mul_f32_e32 v60, v176, v78
	v_mul_f32_e32 v60, 0.15915494, v60
	v_cos_f32_e32 v63, v60
	v_sin_f32_e32 v60, v60
	s_nop 0
	v_mul_f32_e32 v57, v60, v57
	v_cndmask_b32_e64 v57, v57, -v57, s[4:5]
	v_fmac_f32_e32 v57, v63, v68
	v_mov_b32_e32 v60, v65
	v_mov_b32_e32 v63, v65
	s_nop 1
	v_permlane32_swap_b32_e32 v60, v63
	v_cndmask_b32_e64 v60, v60, v63, s[4:5]
	v_mul_f32_e32 v63, v177, v78
	v_mul_f32_e32 v63, 0.15915494, v63
	v_cos_f32_e32 v66, v63
	v_sin_f32_e32 v63, v63
	s_nop 0
	v_mul_f32_e32 v60, v63, v60
	v_cndmask_b32_e64 v60, v60, -v60, s[4:5]
	v_fmac_f32_e32 v60, v66, v65
	v_mov_b32_e32 v63, v62
	v_mov_b32_e32 v65, v62
	s_nop 1
	v_permlane32_swap_b32_e32 v63, v65
	v_cndmask_b32_e64 v63, v63, v65, s[4:5]
	v_mul_f32_e32 v65, v178, v78
	v_mul_f32_e32 v65, 0.15915494, v65
	v_cos_f32_e32 v66, v65
	v_sin_f32_e32 v65, v65
	s_nop 0
	v_mul_f32_e32 v63, v65, v63
	v_cndmask_b32_e64 v63, v63, -v63, s[4:5]
	v_fmac_f32_e32 v63, v66, v62
	v_mov_b32_e32 v62, v59
	v_mov_b32_e32 v65, v59
	s_nop 1
	v_permlane32_swap_b32_e32 v62, v65
	v_cndmask_b32_e64 v62, v62, v65, s[4:5]
	v_mul_f32_e32 v65, v179, v78
	v_mul_f32_e32 v65, 0.15915494, v65
	v_cos_f32_e32 v66, v65
	v_sin_f32_e32 v65, v65
	s_nop 0
	v_mul_f32_e32 v62, v65, v62
	v_cndmask_b32_e64 v62, v62, -v62, s[4:5]
	v_fmac_f32_e32 v62, v66, v59
	v_mov_b32_e32 v59, v56
	v_mov_b32_e32 v65, v56
	s_nop 1
	v_permlane32_swap_b32_e32 v59, v65
	v_cndmask_b32_e64 v59, v59, v65, s[4:5]
	v_mul_f32_e32 v65, v180, v78
	v_mul_f32_e32 v65, 0.15915494, v65
	v_cos_f32_e32 v66, v65
	v_sin_f32_e32 v65, v65
	s_nop 0
	v_mul_f32_e32 v59, v65, v59
	v_cndmask_b32_e64 v59, v59, -v59, s[4:5]
	v_fmac_f32_e32 v59, v66, v56
	v_mov_b32_e32 v56, v53
	v_mov_b32_e32 v65, v53
	s_nop 1
	v_permlane32_swap_b32_e32 v56, v65
	v_cndmask_b32_e64 v56, v56, v65, s[4:5]
	v_mul_f32_e32 v65, v181, v78
	v_mul_f32_e32 v65, 0.15915494, v65
	v_cos_f32_e32 v66, v65
	v_sin_f32_e32 v65, v65
	s_nop 0
	v_mul_f32_e32 v56, v65, v56
	v_cndmask_b32_e64 v56, v56, -v56, s[4:5]
	v_fmac_f32_e32 v56, v66, v53
	v_mov_b32_e32 v53, v50
	v_mov_b32_e32 v65, v50
	s_nop 1
	v_permlane32_swap_b32_e32 v53, v65
	v_cndmask_b32_e64 v53, v53, v65, s[4:5]
	v_mul_f32_e32 v65, v182, v78
	v_mul_f32_e32 v65, 0.15915494, v65
	v_cos_f32_e32 v66, v65
	v_sin_f32_e32 v65, v65
	s_nop 0
	v_mul_f32_e32 v53, v65, v53
	v_cndmask_b32_e64 v53, v53, -v53, s[4:5]
	v_fmac_f32_e32 v53, v66, v50
	v_mov_b32_e32 v50, v47
	v_mov_b32_e32 v65, v47
	s_nop 1
	v_permlane32_swap_b32_e32 v50, v65
	v_cndmask_b32_e64 v50, v50, v65, s[4:5]
	v_mul_f32_e32 v65, v183, v78
	v_mul_f32_e32 v65, 0.15915494, v65
	v_cos_f32_e32 v66, v65
	v_sin_f32_e32 v65, v65
	s_nop 0
	v_mul_f32_e32 v50, v65, v50
	v_cndmask_b32_e64 v50, v50, -v50, s[4:5]
	v_fmac_f32_e32 v50, v66, v47
	v_mov_b32_e32 v47, v44
	v_mov_b32_e32 v65, v44
	s_nop 1
	v_permlane32_swap_b32_e32 v47, v65
	v_cndmask_b32_e64 v47, v47, v65, s[4:5]
	v_mul_f32_e32 v65, v184, v78
	v_mul_f32_e32 v65, 0.15915494, v65
	v_cos_f32_e32 v66, v65
	v_sin_f32_e32 v65, v65
	s_nop 0
	v_mul_f32_e32 v47, v65, v47
	v_cndmask_b32_e64 v47, v47, -v47, s[4:5]
	v_fmac_f32_e32 v47, v66, v44
	v_mov_b32_e32 v44, v64
	v_mov_b32_e32 v65, v64
	s_nop 1
	v_permlane32_swap_b32_e32 v44, v65
	v_cndmask_b32_e64 v44, v44, v65, s[4:5]
	v_mul_f32_e32 v65, 0.15915494, v1
	v_cos_f32_e32 v66, v65
	v_sin_f32_e32 v65, v65
	s_nop 0
	v_mul_f32_e32 v44, v65, v44
	v_cndmask_b32_e64 v44, v44, -v44, s[4:5]
	v_fmac_f32_e32 v44, v66, v64
	v_mov_b32_e32 v64, v61
	v_mov_b32_e32 v65, v61
	s_nop 1
	v_permlane32_swap_b32_e32 v64, v65
	v_cndmask_b32_e64 v64, v64, v65, s[4:5]
	v_mul_f32_e32 v65, v154, v1
	v_mul_f32_e32 v65, 0.15915494, v65
	v_cos_f32_e32 v66, v65
	v_sin_f32_e32 v65, v65
	s_nop 0
	v_mul_f32_e32 v64, v65, v64
	v_cndmask_b32_e64 v64, v64, -v64, s[4:5]
	v_fmac_f32_e32 v64, v66, v61
	v_mov_b32_e32 v61, v58
	v_mov_b32_e32 v65, v58
	s_nop 1
	v_permlane32_swap_b32_e32 v61, v65
	v_cndmask_b32_e64 v61, v61, v65, s[4:5]
	v_mul_f32_e32 v65, v155, v1
	v_mul_f32_e32 v65, 0.15915494, v65
	v_cos_f32_e32 v66, v65
	v_sin_f32_e32 v65, v65
	s_nop 0
	v_mul_f32_e32 v61, v65, v61
	v_cndmask_b32_e64 v61, v61, -v61, s[4:5]
	v_fmac_f32_e32 v61, v66, v58
	v_mov_b32_e32 v58, v55
	v_mov_b32_e32 v65, v55
	s_nop 1
	v_permlane32_swap_b32_e32 v58, v65
	v_cndmask_b32_e64 v58, v58, v65, s[4:5]
	v_mul_f32_e32 v65, v156, v1
	v_mul_f32_e32 v65, 0.15915494, v65
	v_cos_f32_e32 v66, v65
	v_sin_f32_e32 v65, v65
	s_nop 0
	v_mul_f32_e32 v58, v65, v58
	v_cndmask_b32_e64 v58, v58, -v58, s[4:5]
	v_fmac_f32_e32 v58, v66, v55
	v_mov_b32_e32 v55, v52
	v_mov_b32_e32 v65, v52
	s_nop 1
	v_permlane32_swap_b32_e32 v55, v65
	v_cndmask_b32_e64 v55, v55, v65, s[4:5]
	v_mul_f32_e32 v65, v157, v1
	v_mul_f32_e32 v65, 0.15915494, v65
	v_cos_f32_e32 v66, v65
	v_sin_f32_e32 v65, v65
	s_nop 0
	v_mul_f32_e32 v55, v65, v55
	v_cndmask_b32_e64 v55, v55, -v55, s[4:5]
	v_fmac_f32_e32 v55, v66, v52
	v_mov_b32_e32 v52, v49
	v_mov_b32_e32 v65, v49
	s_nop 1
	v_permlane32_swap_b32_e32 v52, v65
	v_cndmask_b32_e64 v52, v52, v65, s[4:5]
	v_mul_f32_e32 v65, v158, v1
	v_mul_f32_e32 v65, 0.15915494, v65
	v_cos_f32_e32 v66, v65
	v_sin_f32_e32 v65, v65
	s_nop 0
	v_mul_f32_e32 v52, v65, v52
	v_cndmask_b32_e64 v52, v52, -v52, s[4:5]
	v_fmac_f32_e32 v52, v66, v49
	v_mov_b32_e32 v49, v46
	v_mov_b32_e32 v65, v46
	s_nop 1
	v_permlane32_swap_b32_e32 v49, v65
	v_cndmask_b32_e64 v49, v49, v65, s[4:5]
	v_mul_f32_e32 v65, v159, v1
	v_mul_f32_e32 v65, 0.15915494, v65
	v_cos_f32_e32 v66, v65
	v_sin_f32_e32 v65, v65
	s_nop 0
	v_mul_f32_e32 v49, v65, v49
	v_cndmask_b32_e64 v49, v49, -v49, s[4:5]
	v_fmac_f32_e32 v49, v66, v46
	v_mov_b32_e32 v46, v43
	v_mov_b32_e32 v65, v43
	s_nop 1
	v_permlane32_swap_b32_e32 v46, v65
	v_cndmask_b32_e64 v46, v46, v65, s[4:5]
	v_mul_f32_e32 v65, v160, v1
	v_mul_f32_e32 v65, 0.15915494, v65
	v_cos_f32_e32 v66, v65
	v_sin_f32_e32 v65, v65
	s_nop 0
	v_mul_f32_e32 v46, v65, v46
	v_cndmask_b32_e64 v46, v46, -v46, s[4:5]
	v_fmac_f32_e32 v46, v66, v43
	v_mov_b32_e32 v43, v41
	v_mov_b32_e32 v65, v41
	s_nop 1
	v_permlane32_swap_b32_e32 v43, v65
	v_cndmask_b32_e64 v43, v43, v65, s[4:5]
	v_mul_f32_e32 v65, v161, v1
	v_mul_f32_e32 v65, 0.15915494, v65
	v_cos_f32_e32 v66, v65
	v_sin_f32_e32 v65, v65
	s_nop 0
	v_mul_f32_e32 v43, v65, v43
	v_cndmask_b32_e64 v43, v43, -v43, s[4:5]
	v_fmac_f32_e32 v43, v66, v41
	v_mov_b32_e32 v41, v39
	v_mov_b32_e32 v65, v39
	s_nop 1
	v_permlane32_swap_b32_e32 v41, v65
	v_cndmask_b32_e64 v41, v41, v65, s[4:5]
	v_mul_f32_e32 v65, v162, v1
	v_mul_f32_e32 v65, 0.15915494, v65
	v_cos_f32_e32 v66, v65
	v_sin_f32_e32 v65, v65
	s_nop 0
	v_mul_f32_e32 v41, v65, v41
	v_cndmask_b32_e64 v41, v41, -v41, s[4:5]
	v_fmac_f32_e32 v41, v66, v39
	v_mov_b32_e32 v39, v38
	v_mov_b32_e32 v65, v38
	s_nop 1
	v_permlane32_swap_b32_e32 v39, v65
	v_cndmask_b32_e64 v39, v39, v65, s[4:5]
	v_mul_f32_e32 v65, v163, v1
	v_mul_f32_e32 v65, 0.15915494, v65
	v_cos_f32_e32 v66, v65
	v_sin_f32_e32 v65, v65
	s_nop 0
	v_mul_f32_e32 v39, v65, v39
	v_cndmask_b32_e64 v39, v39, -v39, s[4:5]
	v_fmac_f32_e32 v39, v66, v38
	v_mov_b32_e32 v38, v37
	v_mov_b32_e32 v65, v37
	s_nop 1
	v_permlane32_swap_b32_e32 v38, v65
	v_cndmask_b32_e64 v38, v38, v65, s[4:5]
	v_mul_f32_e32 v65, v164, v1
	v_mul_f32_e32 v65, 0.15915494, v65
	v_cos_f32_e32 v66, v65
	v_sin_f32_e32 v65, v65
	s_nop 0
	v_mul_f32_e32 v38, v65, v38
	v_cndmask_b32_e64 v38, v38, -v38, s[4:5]
	v_fmac_f32_e32 v38, v66, v37
	v_mov_b32_e32 v37, v19
	v_mov_b32_e32 v65, v19
	s_nop 1
	v_permlane32_swap_b32_e32 v37, v65
	v_cndmask_b32_e64 v37, v37, v65, s[4:5]
	v_mul_f32_e32 v65, v165, v1
	v_mul_f32_e32 v65, 0.15915494, v65
	v_cos_f32_e32 v66, v65
	v_sin_f32_e32 v65, v65
	s_nop 0
	v_mul_f32_e32 v37, v65, v37
	v_cndmask_b32_e64 v37, v37, -v37, s[4:5]
	v_fmac_f32_e32 v37, v66, v19
	v_mov_b32_e32 v19, v18
	v_mov_b32_e32 v65, v18
	s_nop 1
	v_permlane32_swap_b32_e32 v19, v65
	v_cndmask_b32_e64 v19, v19, v65, s[4:5]
	v_mul_f32_e32 v65, v166, v1
	v_mul_f32_e32 v65, 0.15915494, v65
	v_cos_f32_e32 v66, v65
	v_sin_f32_e32 v65, v65
	s_nop 0
	v_mul_f32_e32 v19, v65, v19
	v_cndmask_b32_e64 v19, v19, -v19, s[4:5]
	v_fmac_f32_e32 v19, v66, v18
	v_mov_b32_e32 v18, v17
	v_mov_b32_e32 v65, v17
	s_nop 1
	v_permlane32_swap_b32_e32 v18, v65
	v_cndmask_b32_e64 v18, v18, v65, s[4:5]
	v_mul_f32_e32 v65, v167, v1
	v_mul_f32_e32 v65, 0.15915494, v65
	v_cos_f32_e32 v66, v65
	v_sin_f32_e32 v65, v65
	s_nop 0
	v_mul_f32_e32 v18, v65, v18
	v_cndmask_b32_e64 v18, v18, -v18, s[4:5]
	v_fmac_f32_e32 v18, v66, v17
	v_mov_b32_e32 v17, v16
	v_mov_b32_e32 v65, v16
	s_nop 1
	v_permlane32_swap_b32_e32 v17, v65
	v_cndmask_b32_e64 v17, v17, v65, s[4:5]
	v_mul_f32_e32 v65, v168, v1
	v_mul_f32_e32 v65, 0.15915494, v65
	v_cos_f32_e32 v66, v65
	v_sin_f32_e32 v65, v65
	s_nop 0
	v_mul_f32_e32 v17, v65, v17
	v_cndmask_b32_e64 v17, v17, -v17, s[4:5]
	v_fmac_f32_e32 v17, v66, v16
	v_mov_b32_e32 v16, v67
	v_mov_b32_e32 v65, v67
	s_nop 1
	v_permlane32_swap_b32_e32 v16, v65
	v_cndmask_b32_e64 v16, v16, v65, s[4:5]
	v_mul_f32_e32 v65, v169, v1
	v_mul_f32_e32 v65, 0.15915494, v65
	v_cos_f32_e32 v66, v65
	v_sin_f32_e32 v65, v65
	s_nop 0
	v_mul_f32_e32 v16, v65, v16
	v_cndmask_b32_e64 v16, v16, -v16, s[4:5]
	v_fmac_f32_e32 v16, v66, v67
	v_mov_b32_e32 v65, v34
	v_mov_b32_e32 v66, v34
	s_nop 1
	v_permlane32_swap_b32_e32 v65, v66
	v_cndmask_b32_e64 v65, v65, v66, s[4:5]
	v_mul_f32_e32 v66, v170, v1
	v_mul_f32_e32 v66, 0.15915494, v66
	v_cos_f32_e32 v67, v66
	v_sin_f32_e32 v66, v66
	s_nop 0
	v_mul_f32_e32 v65, v66, v65
	v_cndmask_b32_e64 v65, v65, -v65, s[4:5]
	v_fmac_f32_e32 v65, v67, v34
	v_mov_b32_e32 v34, v32
	v_mov_b32_e32 v66, v32
	s_nop 1
	v_permlane32_swap_b32_e32 v34, v66
	v_cndmask_b32_e64 v34, v34, v66, s[4:5]
	v_mul_f32_e32 v66, v171, v1
	v_mul_f32_e32 v66, 0.15915494, v66
	v_cos_f32_e32 v67, v66
	v_sin_f32_e32 v66, v66
	s_nop 0
	v_mul_f32_e32 v34, v66, v34
	v_cndmask_b32_e64 v34, v34, -v34, s[4:5]
	v_fmac_f32_e32 v34, v67, v32
	v_mov_b32_e32 v32, v30
	v_mov_b32_e32 v66, v30
	s_nop 1
	v_permlane32_swap_b32_e32 v32, v66
	v_cndmask_b32_e64 v32, v32, v66, s[4:5]
	v_mul_f32_e32 v66, v172, v1
	v_mul_f32_e32 v66, 0.15915494, v66
	v_cos_f32_e32 v67, v66
	v_sin_f32_e32 v66, v66
	s_nop 0
	v_mul_f32_e32 v32, v66, v32
	v_cndmask_b32_e64 v32, v32, -v32, s[4:5]
	v_fmac_f32_e32 v32, v67, v30
	v_mov_b32_e32 v30, v28
	v_mov_b32_e32 v66, v28
	s_nop 1
	v_permlane32_swap_b32_e32 v30, v66
	v_cndmask_b32_e64 v30, v30, v66, s[4:5]
	v_mul_f32_e32 v66, v173, v1
	v_mul_f32_e32 v66, 0.15915494, v66
	v_cos_f32_e32 v67, v66
	v_sin_f32_e32 v66, v66
	s_nop 0
	v_mul_f32_e32 v30, v66, v30
	v_cndmask_b32_e64 v30, v30, -v30, s[4:5]
	v_fmac_f32_e32 v30, v67, v28
	v_mov_b32_e32 v28, v26
	v_mov_b32_e32 v66, v26
	s_nop 1
	v_permlane32_swap_b32_e32 v28, v66
	v_cndmask_b32_e64 v28, v28, v66, s[4:5]
	v_mul_f32_e32 v66, v174, v1
	v_mul_f32_e32 v66, 0.15915494, v66
	v_cos_f32_e32 v67, v66
	v_sin_f32_e32 v66, v66
	s_nop 0
	v_mul_f32_e32 v28, v66, v28
	v_cndmask_b32_e64 v28, v28, -v28, s[4:5]
	v_fmac_f32_e32 v28, v67, v26
	v_mov_b32_e32 v26, v24
	v_mov_b32_e32 v66, v24
	s_nop 1
	v_permlane32_swap_b32_e32 v26, v66
	v_cndmask_b32_e64 v26, v26, v66, s[4:5]
	v_mul_f32_e32 v66, v175, v1
	v_mul_f32_e32 v66, 0.15915494, v66
	v_cos_f32_e32 v67, v66
	v_sin_f32_e32 v66, v66
	s_nop 0
	v_mul_f32_e32 v26, v66, v26
	v_cndmask_b32_e64 v26, v26, -v26, s[4:5]
	v_fmac_f32_e32 v26, v67, v24
	v_mov_b32_e32 v24, v22
	v_mov_b32_e32 v66, v22
	s_nop 1
	v_permlane32_swap_b32_e32 v24, v66
	v_cndmask_b32_e64 v24, v24, v66, s[4:5]
	v_mul_f32_e32 v66, v176, v1
	v_mul_f32_e32 v66, 0.15915494, v66
	v_cos_f32_e32 v67, v66
	v_sin_f32_e32 v66, v66
	s_nop 0
	v_mul_f32_e32 v24, v66, v24
	v_cndmask_b32_e64 v24, v24, -v24, s[4:5]
	v_fmac_f32_e32 v24, v67, v22
	v_mov_b32_e32 v22, v15
	v_mov_b32_e32 v66, v15
	s_nop 1
	v_permlane32_swap_b32_e32 v22, v66
	v_cndmask_b32_e64 v22, v22, v66, s[4:5]
	v_mul_f32_e32 v66, v177, v1
	v_mul_f32_e32 v66, 0.15915494, v66
	v_cos_f32_e32 v67, v66
	v_sin_f32_e32 v66, v66
	s_nop 0
	v_mul_f32_e32 v22, v66, v22
	v_cndmask_b32_e64 v22, v22, -v22, s[4:5]
	v_fmac_f32_e32 v22, v67, v15
	v_mov_b32_e32 v15, v13
	v_mov_b32_e32 v66, v13
	s_nop 1
	v_permlane32_swap_b32_e32 v15, v66
	v_cndmask_b32_e64 v15, v15, v66, s[4:5]
	v_mul_f32_e32 v66, v178, v1
	v_mul_f32_e32 v66, 0.15915494, v66
	v_cos_f32_e32 v67, v66
	v_sin_f32_e32 v66, v66
	s_nop 0
	v_mul_f32_e32 v15, v66, v15
	v_cndmask_b32_e64 v15, v15, -v15, s[4:5]
	v_fmac_f32_e32 v15, v67, v13
	v_mov_b32_e32 v13, v11
	v_mov_b32_e32 v66, v11
	s_nop 1
	v_permlane32_swap_b32_e32 v13, v66
	v_cndmask_b32_e64 v13, v13, v66, s[4:5]
	v_mul_f32_e32 v66, v179, v1
	v_mul_f32_e32 v66, 0.15915494, v66
	v_cos_f32_e32 v67, v66
	v_sin_f32_e32 v66, v66
	s_nop 0
	v_mul_f32_e32 v13, v66, v13
	v_cndmask_b32_e64 v13, v13, -v13, s[4:5]
	v_fmac_f32_e32 v13, v67, v11
	v_mov_b32_e32 v11, v8
	v_mov_b32_e32 v66, v8
	s_nop 1
	v_permlane32_swap_b32_e32 v11, v66
	v_cndmask_b32_e64 v11, v11, v66, s[4:5]
	v_mul_f32_e32 v66, v180, v1
	v_mul_f32_e32 v66, 0.15915494, v66
	v_cos_f32_e32 v67, v66
	v_sin_f32_e32 v66, v66
	s_nop 0
	v_mul_f32_e32 v11, v66, v11
	v_cndmask_b32_e64 v11, v11, -v11, s[4:5]
	v_fmac_f32_e32 v11, v67, v8
	v_mov_b32_e32 v8, v6
	v_mov_b32_e32 v66, v6
	s_nop 1
	v_permlane32_swap_b32_e32 v8, v66
	v_cndmask_b32_e64 v8, v8, v66, s[4:5]
	v_mul_f32_e32 v66, v181, v1
	v_mul_f32_e32 v66, 0.15915494, v66
	v_cos_f32_e32 v67, v66
	v_sin_f32_e32 v66, v66
	s_nop 0
	v_mul_f32_e32 v8, v66, v8
	v_cndmask_b32_e64 v8, v8, -v8, s[4:5]
	v_fmac_f32_e32 v8, v67, v6
	v_mov_b32_e32 v6, v4
	v_mov_b32_e32 v66, v4
	s_nop 1
	v_permlane32_swap_b32_e32 v6, v66
	v_cndmask_b32_e64 v6, v6, v66, s[4:5]
	v_mul_f32_e32 v66, v182, v1
	v_mul_f32_e32 v66, 0.15915494, v66
	v_cos_f32_e32 v67, v66
	v_sin_f32_e32 v66, v66
	s_nop 0
	v_mul_f32_e32 v6, v66, v6
	v_cndmask_b32_e64 v6, v6, -v6, s[4:5]
	v_fmac_f32_e32 v6, v67, v4
	v_mov_b32_e32 v4, v2
	v_mov_b32_e32 v66, v2
	s_nop 1
	v_permlane32_swap_b32_e32 v4, v66
	v_cndmask_b32_e64 v4, v4, v66, s[4:5]
	v_mul_f32_e32 v66, v183, v1
	v_mul_f32_e32 v66, 0.15915494, v66
	v_cos_f32_e32 v67, v66
	v_sin_f32_e32 v66, v66
	v_mul_f32_e32 v1, v184, v1
	v_mul_f32_e32 v1, 0.15915494, v1
	v_mul_f32_e32 v4, v66, v4
	v_cndmask_b32_e64 v4, v4, -v4, s[4:5]
	v_fmac_f32_e32 v4, v67, v2
	v_mov_b32_e32 v2, v0
	v_mov_b32_e32 v66, v0
	s_nop 1
	v_permlane32_swap_b32_e32 v2, v66
	v_cndmask_b32_e64 v2, v2, v66, s[4:5]
	v_cos_f32_e32 v66, v1
	v_sin_f32_e32 v1, v1
	s_nop 0
	v_mul_f32_e32 v1, v1, v2
	v_cndmask_b32_e64 v1, v1, -v1, s[4:5]
	v_fmac_f32_e32 v1, v66, v0
	v_med3_f32 v0, v3, s97, v185
	v_med3_f32 v2, v5, s97, v185
	v_cvt_pk_fp8_f32 v128, v0, v2
	v_med3_f32 v0, v10, s97, v185
	v_med3_f32 v2, v12, s97, v185
	v_cvt_pk_fp8_f32 v129, v0, v2
	v_med3_f32 v0, v21, s97, v185
	v_med3_f32 v2, v23, s97, v185
	v_cvt_pk_fp8_f32 v130, v0, v2
	v_med3_f32 v0, v29, s97, v185
	v_med3_f32 v2, v31, s97, v185
	v_med3_f32 v3, v7, s97, v185
	v_med3_f32 v5, v9, s97, v185
	v_cvt_pk_fp8_f32 v131, v0, v2
	v_med3_f32 v0, v36, s97, v185
	v_med3_f32 v2, v40, s97, v185
	v_cvt_pk_fp8_f32 v128, v3, v5 op_sel:[0,0,1]
	v_med3_f32 v3, v14, s97, v185
	v_med3_f32 v5, v20, s97, v185
	v_cvt_pk_fp8_f32 v132, v0, v2
	v_med3_f32 v0, v48, s97, v185
	v_med3_f32 v2, v51, s97, v185
	v_cvt_pk_fp8_f32 v129, v3, v5 op_sel:[0,0,1]
	v_med3_f32 v3, v25, s97, v185
	v_med3_f32 v5, v27, s97, v185
	v_cvt_pk_fp8_f32 v133, v0, v2
	v_med3_f32 v0, v60, s97, v185
	v_med3_f32 v2, v63, s97, v185
	v_cvt_pk_fp8_f32 v130, v3, v5 op_sel:[0,0,1]
	v_med3_f32 v3, v33, s97, v185
	v_med3_f32 v5, v35, s97, v185
	v_cvt_pk_fp8_f32 v134, v0, v2
	v_med3_f32 v0, v56, s97, v185
	v_med3_f32 v2, v53, s97, v185
	v_cvt_pk_fp8_f32 v131, v3, v5 op_sel:[0,0,1]
	v_med3_f32 v3, v42, s97, v185
	v_med3_f32 v5, v45, s97, v185
	v_cvt_pk_fp8_f32 v135, v0, v2
	v_med3_f32 v0, v44, s97, v185
	v_med3_f32 v2, v64, s97, v185
	v_cvt_pk_fp8_f32 v132, v3, v5 op_sel:[0,0,1]
	v_med3_f32 v3, v54, s97, v185
	v_med3_f32 v5, v57, s97, v185
	v_cvt_pk_fp8_f32 v136, v0, v2
	v_med3_f32 v0, v55, s97, v185
	v_med3_f32 v2, v52, s97, v185
	v_cvt_pk_fp8_f32 v133, v3, v5 op_sel:[0,0,1]
	v_med3_f32 v3, v62, s97, v185
	v_med3_f32 v5, v59, s97, v185
	v_cvt_pk_fp8_f32 v137, v0, v2
	v_med3_f32 v0, v43, s97, v185
	v_med3_f32 v2, v41, s97, v185
	v_cvt_pk_fp8_f32 v134, v3, v5 op_sel:[0,0,1]
	v_med3_f32 v3, v50, s97, v185
	v_med3_f32 v5, v47, s97, v185
	v_cvt_pk_fp8_f32 v138, v0, v2
	v_med3_f32 v0, v37, s97, v185
	v_med3_f32 v2, v19, s97, v185
	v_cvt_pk_fp8_f32 v135, v3, v5 op_sel:[0,0,1]
	v_med3_f32 v3, v61, s97, v185
	v_med3_f32 v5, v58, s97, v185
	v_cvt_pk_fp8_f32 v139, v0, v2
	v_med3_f32 v0, v16, s97, v185
	v_med3_f32 v2, v65, s97, v185
	v_cvt_pk_fp8_f32 v136, v3, v5 op_sel:[0,0,1]
	v_med3_f32 v3, v49, s97, v185
	v_med3_f32 v5, v46, s97, v185
	v_cvt_pk_fp8_f32 v140, v0, v2
	v_med3_f32 v0, v30, s97, v185
	v_med3_f32 v2, v28, s97, v185
	v_cvt_pk_fp8_f32 v137, v3, v5 op_sel:[0,0,1]
	v_med3_f32 v3, v39, s97, v185
	v_med3_f32 v5, v38, s97, v185
	v_cvt_pk_fp8_f32 v141, v0, v2
	v_med3_f32 v0, v22, s97, v185
	v_med3_f32 v2, v15, s97, v185
	v_cvt_pk_fp8_f32 v138, v3, v5 op_sel:[0,0,1]
	v_med3_f32 v3, v18, s97, v185
	v_med3_f32 v5, v17, s97, v185
	v_cvt_pk_fp8_f32 v142, v0, v2
	v_med3_f32 v0, v8, s97, v185
	v_med3_f32 v2, v6, s97, v185
	v_cvt_pk_fp8_f32 v139, v3, v5 op_sel:[0,0,1]
	v_med3_f32 v3, v34, s97, v185
	v_med3_f32 v5, v32, s97, v185
	v_cvt_pk_fp8_f32 v143, v0, v2
	v_cvt_pk_fp8_f32 v140, v3, v5 op_sel:[0,0,1]
	v_med3_f32 v3, v26, s97, v185
	v_med3_f32 v5, v24, s97, v185
	v_cvt_pk_fp8_f32 v141, v3, v5 op_sel:[0,0,1]
	v_med3_f32 v3, v13, s97, v185
	v_med3_f32 v5, v11, s97, v185
	v_cvt_pk_fp8_f32 v142, v3, v5 op_sel:[0,0,1]
	v_med3_f32 v3, v4, s97, v185
	v_med3_f32 v1, v1, s97, v185
	v_add_u32_e32 v0, s84, v190
	v_cvt_pk_fp8_f32 v143, v3, v1 op_sel:[0,0,1]
	v_ashrrev_i32_e32 v1, 31, v0
	v_lshrrev_b32_e32 v1, 25, v1
	v_add_u32_e32 v1, v0, v1
	v_ashrrev_i32_e32 v2, 7, v1
	v_and_b32_e32 v1, 0xffffff80, v1
	v_sub_u32_e32 v1, v0, v1
	v_ashrrev_i32_e32 v1, 4, v1
	v_lshrrev_b32_e32 v3, 1, v2
	v_ashrrev_i32_e32 v4, 8, v0
	v_bitop3_b32 v1, v3, v1, 7 bitop3:0x6c
	v_bfe_u32 v3, v187, 2, 2
	v_lshrrev_b32_e32 v48, 1, v187
	v_and_b32_e32 v8, 0xfffff0, v4
	v_lshrrev_b32_e32 v4, 1, v4
	v_and_or_b32 v3, v48, 8, v3
	v_lshlrev_b32_e32 v6, 3, v187
	v_and_b32_e32 v4, 4, v4
	v_lshrrev_b32_e32 v5, 4, v0
	v_and_b32_e32 v7, 24, v6
	v_or3_b32 v4, v8, v4, v3
	v_and_or_b32 v5, v5, s0, v7
	v_mul_i32_i24_e32 v4, 0xc00, v4
	v_add_u32_e32 v0, 0x2000, v0
	v_or_b32_e32 v4, v4, v5
	v_ashrrev_i32_e32 v0, 8, v0
	v_lshlrev_b32_e32 v146, 1, v4
	v_and_b32_e32 v4, 0xfffff0, v0
	v_lshrrev_b32_e32 v0, 1, v0
	v_cmp_gt_i32_e32 vcc, 8, v1
	v_lshlrev_b32_e32 v1, 4, v1
	v_and_b32_e32 v0, 4, v0
	v_cndmask_b32_e32 v1, 0, v1, vcc
	v_or3_b32 v0, v4, v0, v3
	v_mul_i32_i24_e32 v0, 0xc00, v0
	v_lshl_add_u32 v144, v2, 9, v1
	v_or_b32_e32 v0, v0, v5
	s_movk_i32 s0, 0xc0
	v_lshlrev_b32_e32 v1, 1, v187
	v_lshlrev_b32_e32 v148, 1, v0
	v_and_or_b32 v0, v190, s0, v7
	v_and_b32_e32 v1, 32, v1
	v_and_b32_e32 v2, 0x100, v6
	v_lshl_add_u64 v[150:151], s[64:65], 0, v[144:145]
	s_mov_b64 s[0:1], 0x8000
	v_or3_b32 v49, v0, v1, v2
	v_lshl_add_u64 v[0:1], v[150:151], 0, s[0:1]
	v_lshlrev_b32_e32 v50, 1, v189
	v_bitop3_b32 v0, v50, v48, 7 bitop3:0x78
	v_lshlrev_b32_e32 v51, 7, v188
	v_lshlrev_b32_e32 v0, 4, v0
	v_add_u32_e32 v1, v0, v51
	v_add_u32_e32 v191, 0, v1
	s_waitcnt vmcnt(0)
	s_waitcnt vmcnt(0) lgkmcnt(0)
	s_barrier
	ds_read_b128 v[16:19], v191 offset:32768
	v_xor_b32_e32 v1, 16, v1
	v_add_u32_e32 v192, 0, v1
	v_or_b32_e32 v52, 0x1000, v51
	ds_read_b128 v[20:23], v192 offset:32768
	ds_read_b128 v[24:27], v191 offset:36864
	v_add_u32_e32 v0, v0, v52
	v_xor_b32_e32 v0, 16, v0
	v_add_u32_e32 v193, 0, v0
	ds_read_b128 v[28:31], v193 offset:32768
	s_waitcnt lgkmcnt(2)
	v_mfma_f32_32x32x64_f8f6f4 v[32:47], v[16:23], v[128:135], 0
	v_add_u32_e32 v50, 4, v50
	v_bitop3_b32 v48, v50, v48, 7 bitop3:0x78
	v_lshlrev_b32_e32 v48, 4, v48
	v_add_u32_e32 v54, v48, v51
	v_add_u32_e32 v195, 0, v54
	v_add_u32_e32 v48, v48, v52
	ds_read_b128 v[50:53], v195 offset:32768
	v_xor_b32_e32 v54, 16, v54
	v_add_u32_e32 v196, 0, v54
	ds_read_b128 v[54:57], v196 offset:32768
	ds_read_b128 v[58:61], v195 offset:36864
	v_xor_b32_e32 v48, 16, v48
	v_add_u32_e32 v197, 0, v48
	ds_read_b128 v[62:65], v197 offset:32768
	s_mov_b64 s[0:1], 0x10000
	s_mov_b32 m0, s59
	s_waitcnt lgkmcnt(4)
	v_mfma_f32_32x32x64_f8f6f4 v[16:31], v[24:31], v[128:135], 0
	s_waitcnt lgkmcnt(0)
	s_barrier
	v_mov_b64_e32 v[0:1], s[36:37]
	v_mov_b64_e32 v[14:15], s[50:51]
	v_mov_b64_e32 v[2:3], s[38:39]
	v_mov_b64_e32 v[4:5], s[40:41]
	v_mov_b64_e32 v[6:7], s[42:43]
	v_mov_b64_e32 v[8:9], s[44:45]
	v_mov_b64_e32 v[10:11], s[46:47]
	v_mov_b64_e32 v[12:13], s[48:49]
	v_mfma_f32_32x32x64_f8f6f4 v[32:47], v[50:57], v[136:143], v[32:47]
	v_mfma_f32_32x32x64_f8f6f4 v[16:31], v[58:65], v[136:143], v[16:31]
	s_nop 15
	s_nop 2
	v_max_f32_e32 v48, v33, v33
	v_max_f32_e32 v50, v32, v32
	v_max_f32_e32 v48, v50, v48
	v_max3_f32 v48, v48, v34, v35
	v_max3_f32 v48, v48, v36, v37
	v_max3_f32 v48, v48, v38, v39
	v_max3_f32 v48, v48, v40, v41
	v_max3_f32 v48, v48, v42, v43
	v_max3_f32 v48, v48, v44, v45
	v_max3_f32 v48, v48, v46, v47
	v_max3_f32 v48, v48, v16, v17
	v_max3_f32 v48, v48, v18, v19
	v_max3_f32 v48, v48, v20, v21
	v_max3_f32 v48, v48, v22, v23
	v_max3_f32 v48, v48, v24, v25
	v_max3_f32 v48, v48, v26, v27
	v_max3_f32 v48, v48, v28, v29
	v_max3_f32 v48, v48, v30, v31
	v_mov_b32_e32 v50, v48
	s_nop 1
	v_permlane32_swap_b32_e32 v48, v50
	v_max_f32_e32 v50, v50, v50
	v_max_f32_e32 v48, v48, v48
	v_max_f32_e32 v48, v48, v50
	v_add_f32_e32 v50, 0x7149f2ca, v48
	v_cmp_ge_f32_e32 vcc, s22, v50
	s_cmp_eq_u64 vcc, exec
	s_cselect_b64 vcc, -1, 0
	v_max_f32_e32 v48, 0xf149f2ca, v48
	v_cndmask_b32_e32 v198, v48, v186, vcc
	v_sub_f32_e32 v50, 0xf149f2ca, v48
	v_mul_f32_e32 v48, 0xbe0293ee, v198
	v_fmamk_f32 v32, v32, 0x3e0293ee, v48
	v_fmamk_f32 v33, v33, 0x3e0293ee, v48
	s_add_u32 s6, s12, 0x61400
	v_exp_f32_e32 v64, v32
	v_exp_f32_e32 v65, v33
	v_lshl_add_u64 v[32:33], v[150:151], 0, s[0:1]
	s_addc_u32 s7, s58, 0
	s_add_i32 s0, s33, 0x4000
	global_load_lds_dwordx4 v[32:33], off
	s_mov_b32 m0, s0
	s_add_i32 s1, s33, 0x6000
	global_load_lds_dwordx4 v146, s[6:7]
	s_mov_b32 m0, s1
	v_mul_f32_e32 v50, 0x3e0293ee, v50
	global_load_lds_dwordx4 v148, s[6:7]
	v_exp_f32_e32 v32, v50
	v_fmamk_f32 v34, v34, 0x3e0293ee, v48
	v_fmamk_f32 v35, v35, 0x3e0293ee, v48
	v_fmamk_f32 v36, v36, 0x3e0293ee, v48
	v_fmamk_f32 v37, v37, 0x3e0293ee, v48
	v_fmamk_f32 v38, v38, 0x3e0293ee, v48
	v_fmamk_f32 v39, v39, 0x3e0293ee, v48
	v_fmamk_f32 v40, v40, 0x3e0293ee, v48
	v_fmamk_f32 v41, v41, 0x3e0293ee, v48
	v_fmamk_f32 v42, v42, 0x3e0293ee, v48
	v_fmamk_f32 v43, v43, 0x3e0293ee, v48
	v_fmamk_f32 v44, v44, 0x3e0293ee, v48
	v_fmamk_f32 v45, v45, 0x3e0293ee, v48
	v_fmamk_f32 v46, v46, 0x3e0293ee, v48
	v_fmamk_f32 v47, v47, 0x3e0293ee, v48
	s_cmp_lg_u32 0, -1
	v_exp_f32_e32 v66, v34
	v_exp_f32_e32 v67, v35
	v_exp_f32_e32 v68, v36
	v_exp_f32_e32 v69, v37
	v_exp_f32_e32 v70, v38
	v_exp_f32_e32 v71, v39
	v_exp_f32_e32 v72, v40
	v_exp_f32_e32 v73, v41
	v_exp_f32_e32 v74, v42
	v_exp_f32_e32 v75, v43
	v_exp_f32_e32 v76, v44
	v_exp_f32_e32 v77, v45
	v_exp_f32_e32 v78, v46
	v_exp_f32_e32 v79, v47
	s_cselect_b32 s6, 0, 0
	v_add_u32_e32 v199, s6, v49
	s_addk_i32 s6, 0x4000
	v_cndmask_b32_e64 v200, v32, 1.0, vcc
	v_pk_fma_f32 v[94:95], v[30:31], s[54:55], v[48:49] op_sel_hi:[1,0,0]
	v_pk_fma_f32 v[92:93], v[28:29], s[54:55], v[48:49] op_sel_hi:[1,0,0]
	v_pk_fma_f32 v[90:91], v[26:27], s[54:55], v[48:49] op_sel_hi:[1,0,0]
	v_pk_fma_f32 v[88:89], v[24:25], s[54:55], v[48:49] op_sel_hi:[1,0,0]
	v_pk_fma_f32 v[86:87], v[22:23], s[54:55], v[48:49] op_sel_hi:[1,0,0]
	v_pk_fma_f32 v[84:85], v[20:21], s[54:55], v[48:49] op_sel_hi:[1,0,0]
	v_pk_fma_f32 v[82:83], v[18:19], s[54:55], v[48:49] op_sel_hi:[1,0,0]
	v_pk_fma_f32 v[80:81], v[16:17], s[54:55], v[48:49] op_sel_hi:[1,0,0]
	v_add_u32_e32 v204, s6, v49
	v_mov_b64_e32 v[62:63], v[14:15]
	v_mov_b64_e32 v[46:47], v[14:15]
	v_mov_b64_e32 v[30:31], v[14:15]
	v_mov_b64_e32 v[60:61], v[12:13]
	v_mov_b64_e32 v[58:59], v[10:11]
	v_mov_b64_e32 v[56:57], v[8:9]
	v_mov_b64_e32 v[54:55], v[6:7]
	v_mov_b64_e32 v[52:53], v[4:5]
	v_mov_b64_e32 v[50:51], v[2:3]
	v_mov_b64_e32 v[48:49], v[0:1]
	v_mov_b64_e32 v[44:45], v[12:13]
	v_mov_b64_e32 v[42:43], v[10:11]
	v_mov_b64_e32 v[40:41], v[8:9]
	v_mov_b64_e32 v[38:39], v[6:7]
	v_mov_b64_e32 v[36:37], v[4:5]
	v_mov_b64_e32 v[34:35], v[2:3]
	v_mov_b64_e32 v[32:33], v[0:1]
	v_mov_b64_e32 v[28:29], v[12:13]
	v_mov_b64_e32 v[26:27], v[10:11]
	v_mov_b64_e32 v[24:25], v[8:9]
	v_mov_b64_e32 v[22:23], v[6:7]
	v_mov_b64_e32 v[20:21], v[4:5]
	v_mov_b64_e32 v[18:19], v[2:3]
	v_mov_b64_e32 v[16:17], v[0:1]

.LBB0_1503:
	s_add_u32 s36, s8, s34
	s_addc_u32 s37, s9, s35
	s_add_u32 s38, s36, 0x6ea00100
	ds_read_b128 v[144:147], v168
	ds_read_b128 v[152:155], v168 offset:2048
	ds_read_b128 v[148:151], v169
	ds_read_b128 v[156:159], v169 offset:2048
	s_addc_u32 s39, s37, 0
	s_add_u32 s60, s56, s34
	s_addc_u32 s61, s57, s35
	s_cmpk_eq_i32 s34, 0x700
	s_cselect_b64 vcc, -1, 0
	s_and_b64 s[36:37], vcc, exec
	ds_read_b128 v[184:187], v166
	ds_read_b128 v[196:199], v166 offset:2048
	ds_read_b128 v[188:191], v167
	ds_read_b128 v[200:203], v167 offset:2048
	ds_read_b128 v[204:207], v166 offset:4096
	ds_read_b128 v[212:215], v166 offset:6144
	ds_read_b128 v[208:211], v167 offset:4096
	ds_read_b128 v[216:219], v167 offset:6144
	s_waitcnt vmcnt(6)
	s_waitcnt lgkmcnt(8)
	s_barrier
	s_waitcnt lgkmcnt(0)
	v_cndmask_b32_e32 v160, v134, v180, vcc
	s_setprio 1
	s_waitcnt lgkmcnt(0)
	v_mfma_f32_16x16x128_f8f6f4 v[124:127], v[144:151], v[184:191], v[124:127]
	v_mfma_f32_16x16x128_f8f6f4 v[120:123], v[152:159], v[184:191], v[120:123]
	v_mfma_f32_16x16x128_f8f6f4 v[112:115], v[144:151], v[196:203], v[112:115]
	v_mfma_f32_16x16x128_f8f6f4 v[104:107], v[152:159], v[196:203], v[104:107]
	v_mfma_f32_16x16x128_f8f6f4 v[96:99], v[144:151], v[204:211], v[96:99]
	v_mfma_f32_16x16x128_f8f6f4 v[88:91], v[152:159], v[204:211], v[88:91]
	v_mfma_f32_16x16x128_f8f6f4 v[80:83], v[144:151], v[212:219], v[80:83]
	v_mfma_f32_16x16x128_f8f6f4 v[72:75], v[152:159], v[212:219], v[72:75]
	s_setprio 0
	s_barrier
	ds_read_b128 v[228:231], v168 offset:16384
	ds_read_b128 v[236:239], v168 offset:18432
	ds_read_b128 v[232:235], v169 offset:16384
	ds_read_b128 v[240:243], v169 offset:18432
	v_cndmask_b32_e32 v132, v135, v179, vcc
	s_cselect_b32 s39, s11, s39
	s_cselect_b32 s38, s10, s38
	s_cselect_b32 s37, s31, s61
	s_cselect_b32 s36, s30, s60
	v_cndmask_b32_e32 v137, v136, v181, vcc
	v_lshl_add_u64 v[252:253], v[142:143], 0, s[34:35]
	s_add_i32 m0, s27, 0xc000
	s_nop 0
	global_load_lds_dwordx4 v[252:253], off
	v_lshl_add_u64 v[252:253], v[140:141], 0, s[34:35]
	s_add_i32 m0, s27, 0xe000
	s_nop 0
	global_load_lds_dwordx4 v[252:253], off
	s_barrier
	s_waitcnt lgkmcnt(0)
	s_setprio 1
	v_mfma_f32_16x16x128_f8f6f4 v[116:119], v[228:235], v[184:191], v[116:119]
	v_mfma_f32_16x16x128_f8f6f4 v[108:111], v[236:243], v[184:191], v[108:111]
	v_mfma_f32_16x16x128_f8f6f4 v[100:103], v[228:235], v[196:203], v[100:103]
	v_mfma_f32_16x16x128_f8f6f4 v[92:95], v[236:243], v[196:203], v[92:95]
	v_mfma_f32_16x16x128_f8f6f4 v[84:87], v[228:235], v[204:211], v[84:87]
	v_mfma_f32_16x16x128_f8f6f4 v[76:79], v[236:243], v[204:211], v[76:79]
	v_mfma_f32_16x16x128_f8f6f4 v[68:71], v[228:235], v[212:219], v[68:71]
	v_mfma_f32_16x16x128_f8f6f4 v[64:67], v[236:243], v[212:219], v[64:67]
	s_setprio 0
	s_barrier
	s_mov_b32 m0, s27
	ds_read_b128 v[196:199], v166 offset:16384
	ds_read_b128 v[204:207], v166 offset:18432
	ds_read_b128 v[200:203], v167 offset:16384
	ds_read_b128 v[208:211], v167 offset:18432
	ds_read_b128 v[212:215], v166 offset:20480
	ds_read_b128 v[220:223], v166 offset:22528
	ds_read_b128 v[216:219], v167 offset:20480
	ds_read_b128 v[224:227], v167 offset:22528
	global_load_lds_dwordx4 v132, s[38:39]
	s_mov_b32 m0, s41
	v_mov_b32_e32 v161, v133
	global_load_lds_dwordx4 v160, s[38:39]
	s_waitcnt lgkmcnt(8)
	s_barrier
	s_waitcnt lgkmcnt(0)
	v_lshl_add_u64 v[246:247], s[38:39], 0, v[132:133]
	v_lshl_add_u64 v[244:245], s[38:39], 0, v[160:161]
	s_setprio 1
	s_waitcnt lgkmcnt(0)
	v_mfma_f32_16x16x128_f8f6f4 v[60:63], v[144:151], v[196:203], v[60:63]
	v_mfma_f32_16x16x128_f8f6f4 v[56:59], v[152:159], v[196:203], v[56:59]
	v_mfma_f32_16x16x128_f8f6f4 v[48:51], v[144:151], v[204:211], v[48:51]
	v_mfma_f32_16x16x128_f8f6f4 v[40:43], v[152:159], v[204:211], v[40:43]
	v_mfma_f32_16x16x128_f8f6f4 v[32:35], v[144:151], v[212:219], v[32:35]
	v_mfma_f32_16x16x128_f8f6f4 v[24:27], v[152:159], v[212:219], v[24:27]
	v_mfma_f32_16x16x128_f8f6f4 v[16:19], v[144:151], v[220:227], v[16:19]
	v_mfma_f32_16x16x128_f8f6f4 v[8:11], v[152:159], v[220:227], v[8:11]
	s_setprio 0
	s_barrier
	s_mov_b32 m0, s33
	v_lshl_add_u64 v[144:145], s[36:37], 0, v[128:129]
	global_load_lds_dwordx4 v[144:145], off
	v_lshl_add_u64 v[146:147], s[36:37], 0, v[130:131]
	s_mov_b32 m0, s40
	s_nop 0
	global_load_lds_dwordx4 v[146:147], off
	s_waitcnt vmcnt(8)
	s_waitcnt lgkmcnt(0)
	s_barrier
	s_setprio 1
	s_waitcnt lgkmcnt(0)
	v_mfma_f32_16x16x128_f8f6f4 v[52:55], v[228:235], v[196:203], v[52:55]
	v_mfma_f32_16x16x128_f8f6f4 v[44:47], v[236:243], v[196:203], v[44:47]
	v_mfma_f32_16x16x128_f8f6f4 v[36:39], v[228:235], v[204:211], v[36:39]
	v_mfma_f32_16x16x128_f8f6f4 v[28:31], v[236:243], v[204:211], v[28:31]
	v_mfma_f32_16x16x128_f8f6f4 v[20:23], v[228:235], v[212:219], v[20:23]
	v_mfma_f32_16x16x128_f8f6f4 v[12:15], v[236:243], v[212:219], v[12:15]
	v_mfma_f32_16x16x128_f8f6f4 v[4:7], v[228:235], v[220:227], v[4:7]
	v_mfma_f32_16x16x128_f8f6f4 v[0:3], v[236:243], v[220:227], v[0:3]
	s_setprio 0
	s_barrier
	ds_read_b128 v[152:155], v168 offset:32768
	ds_read_b128 v[184:187], v168 offset:34816
	ds_read_b128 v[156:159], v169 offset:32768
	ds_read_b128 v[188:191], v169 offset:34816
	s_mov_b32 m0, s44
	ds_read_b128 v[196:199], v166 offset:32768
	ds_read_b128 v[204:207], v166 offset:34816
	ds_read_b128 v[200:203], v167 offset:32768
	ds_read_b128 v[208:211], v167 offset:34816
	ds_read_b128 v[212:215], v166 offset:36864
	ds_read_b128 v[220:223], v166 offset:38912
	ds_read_b128 v[216:219], v167 offset:36864
	ds_read_b128 v[224:227], v167 offset:38912
	v_cndmask_b32_e32 v132, v138, v182, vcc
	global_load_lds_dwordx4 v137, s[38:39]
	s_mov_b32 m0, s45
	s_nop 0
	global_load_lds_dwordx4 v132, s[38:39]
	s_waitcnt vmcnt(8)
	s_waitcnt lgkmcnt(8)
	s_barrier
	s_waitcnt lgkmcnt(0)
	s_setprio 1
	v_mfma_f32_16x16x128_f8f6f4 v[124:127], v[152:159], v[196:203], v[124:127]
	v_mfma_f32_16x16x128_f8f6f4 v[120:123], v[184:191], v[196:203], v[120:123]
	v_mfma_f32_16x16x128_f8f6f4 v[112:115], v[152:159], v[204:211], v[112:115]
	v_mfma_f32_16x16x128_f8f6f4 v[104:107], v[184:191], v[204:211], v[104:107]
	v_mfma_f32_16x16x128_f8f6f4 v[96:99], v[152:159], v[212:219], v[96:99]
	v_mfma_f32_16x16x128_f8f6f4 v[88:91], v[184:191], v[212:219], v[88:91]
	v_mfma_f32_16x16x128_f8f6f4 v[80:83], v[152:159], v[220:227], v[80:83]
	v_mfma_f32_16x16x128_f8f6f4 v[72:75], v[184:191], v[220:227], v[72:75]
	s_setprio 0
	s_barrier
	ds_read_b128 v[228:231], v168 offset:49152
	ds_read_b128 v[236:239], v168 offset:51200
	ds_read_b128 v[232:235], v169 offset:49152
	ds_read_b128 v[240:243], v169 offset:51200
	s_add_u32 s38, s36, 0x40000
	s_addc_u32 s39, s37, 0
	v_lshl_add_u64 v[160:161], s[38:39], 0, v[128:129]
	s_mov_b32 m0, s42
	s_nop 0
	global_load_lds_dwordx4 v[160:161], off
	v_lshl_add_u64 v[160:161], s[38:39], 0, v[130:131]
	s_mov_b32 m0, s43
	s_nop 0
	global_load_lds_dwordx4 v[160:161], off
	s_waitcnt vmcnt(8)
	s_barrier
	s_waitcnt lgkmcnt(0)
	s_setprio 1
	v_mfma_f32_16x16x128_f8f6f4 v[116:119], v[228:235], v[196:203], v[116:119]
	v_mfma_f32_16x16x128_f8f6f4 v[108:111], v[236:243], v[196:203], v[108:111]
	v_mfma_f32_16x16x128_f8f6f4 v[100:103], v[228:235], v[204:211], v[100:103]
	v_mfma_f32_16x16x128_f8f6f4 v[92:95], v[236:243], v[204:211], v[92:95]
	v_mfma_f32_16x16x128_f8f6f4 v[84:87], v[228:235], v[212:219], v[84:87]
	v_mfma_f32_16x16x128_f8f6f4 v[76:79], v[236:243], v[212:219], v[76:79]
	v_mfma_f32_16x16x128_f8f6f4 v[68:71], v[228:235], v[220:227], v[68:71]
	v_mfma_f32_16x16x128_f8f6f4 v[64:67], v[236:243], v[220:227], v[64:67]
	s_setprio 0
	s_barrier
	s_mov_b32 m0, s50
	v_lshl_add_u64 v[246:247], v[246:247], 0, s[16:17]
	ds_read_b128 v[196:199], v166 offset:49152
	ds_read_b128 v[204:207], v166 offset:51200
	ds_read_b128 v[200:203], v167 offset:49152
	ds_read_b128 v[208:211], v167 offset:51200
	ds_read_b128 v[212:215], v166 offset:53248
	ds_read_b128 v[220:223], v166 offset:55296
	ds_read_b128 v[216:219], v167 offset:53248
	ds_read_b128 v[224:227], v167 offset:55296
	global_load_lds_dwordx4 v[246:247], off
	v_lshl_add_u64 v[244:245], v[244:245], 0, s[16:17]
	s_mov_b32 m0, s51
	s_nop 0
	global_load_lds_dwordx4 v[244:245], off
	s_waitcnt lgkmcnt(8)
	s_barrier
	s_waitcnt lgkmcnt(0)
	s_setprio 1
	v_mfma_f32_16x16x128_f8f6f4 v[60:63], v[152:159], v[196:203], v[60:63]
	v_mfma_f32_16x16x128_f8f6f4 v[56:59], v[184:191], v[196:203], v[56:59]
	v_mfma_f32_16x16x128_f8f6f4 v[48:51], v[152:159], v[204:211], v[48:51]
	v_mfma_f32_16x16x128_f8f6f4 v[40:43], v[184:191], v[204:211], v[40:43]
	v_mfma_f32_16x16x128_f8f6f4 v[32:35], v[152:159], v[212:219], v[32:35]
	v_mfma_f32_16x16x128_f8f6f4 v[24:27], v[184:191], v[212:219], v[24:27]
	v_mfma_f32_16x16x128_f8f6f4 v[16:19], v[152:159], v[220:227], v[16:19]
	v_mfma_f32_16x16x128_f8f6f4 v[8:11], v[184:191], v[220:227], v[8:11]
	s_setprio 0
	s_barrier
	s_mov_b32 m0, s48
	v_lshl_add_u64 v[144:145], v[144:145], 0, s[16:17]
	global_load_lds_dwordx4 v[144:145], off
	v_lshl_add_u64 v[144:145], v[146:147], 0, s[16:17]
	s_mov_b32 m0, s49
	s_nop 0
	global_load_lds_dwordx4 v[144:145], off
	s_waitcnt vmcnt(8)
	s_waitcnt lgkmcnt(0)
	s_barrier
	s_setprio 1
	s_waitcnt lgkmcnt(0)
	v_mfma_f32_16x16x128_f8f6f4 v[52:55], v[228:235], v[196:203], v[52:55]
	v_mfma_f32_16x16x128_f8f6f4 v[44:47], v[236:243], v[196:203], v[44:47]
	v_mfma_f32_16x16x128_f8f6f4 v[36:39], v[228:235], v[204:211], v[36:39]
	v_mfma_f32_16x16x128_f8f6f4 v[28:31], v[236:243], v[204:211], v[28:31]
	v_mfma_f32_16x16x128_f8f6f4 v[20:23], v[228:235], v[212:219], v[20:23]
	v_mfma_f32_16x16x128_f8f6f4 v[12:15], v[236:243], v[212:219], v[12:15]
	v_mfma_f32_16x16x128_f8f6f4 v[4:7], v[228:235], v[220:227], v[4:7]
	v_mfma_f32_16x16x128_f8f6f4 v[0:3], v[236:243], v[220:227], v[0:3]
	s_setprio 0
	s_barrier
	s_add_u32 s36, s36, 0x40080
	s_addc_u32 s37, s37, 0
	s_mov_b32 m0, s52
	v_lshl_add_u64 v[144:145], s[36:37], 0, v[128:129]
	global_load_lds_dwordx4 v[144:145], off
	v_lshl_add_u64 v[144:145], s[36:37], 0, v[130:131]
	s_mov_b32 m0, s53
	s_add_i32 s59, s59, 2
	global_load_lds_dwordx4 v[144:145], off
	s_add_u32 s34, s34, 0x100
	s_addc_u32 s35, s35, 0
	s_cmp_gt_u32 s59, 13
	s_cbranch_scc0 .LBB0_1503
	s_and_b64 vcc, exec, s[20:21]
	s_cbranch_vccz .LBB0_1506
	s_barrier

.LBB0_1644:
	s_add_u32 s48, s8, s46
	s_addc_u32 s49, s9, s47
	s_add_u32 s50, s48, 0x49800100
	ds_read_b128 v[160:163], v148
	ds_read_b128 v[164:167], v148 offset:1024
	ds_read_b128 v[168:171], v148 offset:2048
	ds_read_b128 v[172:175], v148 offset:3072
	s_addc_u32 s51, s49, 0
	s_add_u32 s85, s82, s46
	s_addc_u32 s86, s83, s47
	s_cmpk_eq_i32 s46, 0x300
	s_cselect_b64 vcc, -1, 0
	s_and_b64 s[48:49], vcc, exec
	v_cndmask_b32_e32 v132, v158, v154, vcc
	s_cselect_b32 s51, s13, s51
	s_cselect_b32 s50, s12, s50
	s_cselect_b32 s49, s45, s86
	s_cselect_b32 s48, s44, s85
	v_cndmask_b32_e32 v139, v138, v156, vcc
	s_mov_b32 m0, s73
	v_lshl_add_u64 v[192:193], v[144:145], 0, s[46:47]
	ds_read_b128 v[176:179], v147
	ds_read_b128 v[180:183], v147 offset:1024
	ds_read_b128 v[184:187], v147 offset:2048
	ds_read_b128 v[188:191], v147 offset:3072
	ds_read_b128 v[196:199], v147 offset:4096
	ds_read_b128 v[200:203], v147 offset:5120
	ds_read_b128 v[204:207], v147 offset:6144
	ds_read_b128 v[208:211], v147 offset:7168
	global_load_lds_dwordx4 v[192:193], off
	v_lshl_add_u64 v[192:193], v[142:143], 0, s[46:47]
	s_mov_b32 m0, s74
	s_nop 0
	global_load_lds_dwordx4 v[192:193], off
	s_waitcnt lgkmcnt(8)
	s_barrier
	s_waitcnt lgkmcnt(0)
	v_cndmask_b32_e32 v192, v136, v155, vcc
	s_setprio 1
	s_waitcnt lgkmcnt(0)
	v_mfma_f32_16x16x32_bf16 v[124:127], v[160:163], v[176:179], v[124:127]
	v_mfma_f32_16x16x32_bf16 v[120:123], v[168:171], v[176:179], v[120:123]
	v_mfma_f32_16x16x32_bf16 v[116:119], v[160:163], v[184:187], v[116:119]
	v_mfma_f32_16x16x32_bf16 v[104:107], v[168:171], v[184:187], v[104:107]
	v_mfma_f32_16x16x32_bf16 v[96:99], v[160:163], v[196:199], v[96:99]
	v_mfma_f32_16x16x32_bf16 v[92:95], v[168:171], v[196:199], v[92:95]
	v_mfma_f32_16x16x32_bf16 v[84:87], v[160:163], v[204:207], v[84:87]
	v_mfma_f32_16x16x32_bf16 v[72:75], v[168:171], v[204:207], v[72:75]
	v_mfma_f32_16x16x32_bf16 v[124:127], v[164:167], v[180:183], v[124:127]
	v_mfma_f32_16x16x32_bf16 v[120:123], v[172:175], v[180:183], v[120:123]
	v_mfma_f32_16x16x32_bf16 v[116:119], v[164:167], v[188:191], v[116:119]
	v_mfma_f32_16x16x32_bf16 v[104:107], v[172:175], v[188:191], v[104:107]
	v_mfma_f32_16x16x32_bf16 v[96:99], v[164:167], v[200:203], v[96:99]
	v_mfma_f32_16x16x32_bf16 v[92:95], v[172:175], v[200:203], v[92:95]
	v_mfma_f32_16x16x32_bf16 v[84:87], v[164:167], v[208:211], v[84:87]
	v_mfma_f32_16x16x32_bf16 v[72:75], v[172:175], v[208:211], v[72:75]
	s_setprio 0
	s_barrier
	s_mov_b32 m0, s57
	v_lshl_add_u64 v[228:229], s[48:49], 0, v[130:131]
	ds_read_b128 v[212:215], v148 offset:16384
	ds_read_b128 v[216:219], v148 offset:17408
	ds_read_b128 v[220:223], v148 offset:18432
	ds_read_b128 v[224:227], v148 offset:19456
	global_load_lds_dwordx4 v[228:229], off
	v_lshl_add_u64 v[230:231], s[48:49], 0, v[128:129]
	s_mov_b32 m0, s58
	s_nop 0
	global_load_lds_dwordx4 v[230:231], off
	s_barrier
	s_waitcnt lgkmcnt(0)
	s_setprio 1
	v_mfma_f32_16x16x32_bf16 v[112:115], v[212:215], v[176:179], v[112:115]
	v_mfma_f32_16x16x32_bf16 v[108:111], v[220:223], v[176:179], v[108:111]
	v_mfma_f32_16x16x32_bf16 v[100:103], v[212:215], v[184:187], v[100:103]
	v_mfma_f32_16x16x32_bf16 v[88:91], v[220:223], v[184:187], v[88:91]
	v_mfma_f32_16x16x32_bf16 v[80:83], v[212:215], v[196:199], v[80:83]
	v_mfma_f32_16x16x32_bf16 v[76:79], v[220:223], v[196:199], v[76:79]
	v_mfma_f32_16x16x32_bf16 v[68:71], v[212:215], v[204:207], v[68:71]
	v_mfma_f32_16x16x32_bf16 v[64:67], v[220:223], v[204:207], v[64:67]
	v_mfma_f32_16x16x32_bf16 v[112:115], v[216:219], v[180:183], v[112:115]
	v_mfma_f32_16x16x32_bf16 v[108:111], v[224:227], v[180:183], v[108:111]
	v_mfma_f32_16x16x32_bf16 v[100:103], v[216:219], v[188:191], v[100:103]
	v_mfma_f32_16x16x32_bf16 v[88:91], v[224:227], v[188:191], v[88:91]
	v_mfma_f32_16x16x32_bf16 v[80:83], v[216:219], v[200:203], v[80:83]
	v_mfma_f32_16x16x32_bf16 v[76:79], v[224:227], v[200:203], v[76:79]
	v_mfma_f32_16x16x32_bf16 v[68:71], v[216:219], v[208:211], v[68:71]
	v_mfma_f32_16x16x32_bf16 v[64:67], v[224:227], v[208:211], v[64:67]
	s_setprio 0
	s_mov_b32 m0, s56
	s_barrier
	ds_read_b128 v[176:179], v147 offset:16384
	ds_read_b128 v[180:183], v147 offset:17408
	ds_read_b128 v[184:187], v147 offset:18432
	ds_read_b128 v[188:191], v147 offset:19456
	ds_read_b128 v[196:199], v147 offset:20480
	ds_read_b128 v[200:203], v147 offset:21504
	ds_read_b128 v[204:207], v147 offset:22528
	ds_read_b128 v[208:211], v147 offset:23552
	global_load_lds_dwordx4 v132, s[50:51]
	s_mov_b32 m0, s59
	v_mov_b32_e32 v193, v133
	global_load_lds_dwordx4 v192, s[50:51]
	s_barrier
	s_waitcnt lgkmcnt(0)
	v_lshl_add_u64 v[232:233], s[50:51], 0, v[132:133]
	v_lshl_add_u64 v[192:193], s[50:51], 0, v[192:193]
	s_setprio 1
	s_waitcnt lgkmcnt(0)
	v_mfma_f32_16x16x32_bf16 v[60:63], v[160:163], v[176:179], v[60:63]
	v_mfma_f32_16x16x32_bf16 v[56:59], v[168:171], v[176:179], v[56:59]
	v_mfma_f32_16x16x32_bf16 v[48:51], v[160:163], v[184:187], v[48:51]
	v_mfma_f32_16x16x32_bf16 v[44:47], v[168:171], v[184:187], v[44:47]
	v_mfma_f32_16x16x32_bf16 v[36:39], v[160:163], v[196:199], v[36:39]
	v_mfma_f32_16x16x32_bf16 v[24:27], v[168:171], v[196:199], v[24:27]
	v_mfma_f32_16x16x32_bf16 v[16:19], v[160:163], v[204:207], v[16:19]
	v_mfma_f32_16x16x32_bf16 v[8:11], v[168:171], v[204:207], v[8:11]
	v_mfma_f32_16x16x32_bf16 v[60:63], v[164:167], v[180:183], v[60:63]
	v_mfma_f32_16x16x32_bf16 v[56:59], v[172:175], v[180:183], v[56:59]
	v_mfma_f32_16x16x32_bf16 v[48:51], v[164:167], v[188:191], v[48:51]
	v_mfma_f32_16x16x32_bf16 v[44:47], v[172:175], v[188:191], v[44:47]
	v_mfma_f32_16x16x32_bf16 v[36:39], v[164:167], v[200:203], v[36:39]
	v_mfma_f32_16x16x32_bf16 v[24:27], v[172:175], v[200:203], v[24:27]
	v_mfma_f32_16x16x32_bf16 v[16:19], v[164:167], v[208:211], v[16:19]
	v_mfma_f32_16x16x32_bf16 v[8:11], v[172:175], v[208:211], v[8:11]
	s_setprio 0
	s_barrier
	s_add_u32 s86, s48, 0x80000
	s_addc_u32 s87, s49, 0
	s_mov_b32 m0, s60
	v_lshl_add_u64 v[160:161], s[86:87], 0, v[130:131]
	global_load_lds_dwordx4 v[160:161], off
	v_lshl_add_u64 v[160:161], s[86:87], 0, v[128:129]
	s_mov_b32 m0, s61
	s_nop 0
	global_load_lds_dwordx4 v[160:161], off
	s_waitcnt vmcnt(6)
	s_barrier
	s_setprio 1
	v_mfma_f32_16x16x32_bf16 v[52:55], v[212:215], v[176:179], v[52:55]
	v_mfma_f32_16x16x32_bf16 v[40:43], v[220:223], v[176:179], v[40:43]
	v_mfma_f32_16x16x32_bf16 v[32:35], v[212:215], v[184:187], v[32:35]
	v_mfma_f32_16x16x32_bf16 v[28:31], v[220:223], v[184:187], v[28:31]
	v_mfma_f32_16x16x32_bf16 v[20:23], v[212:215], v[196:199], v[20:23]
	v_mfma_f32_16x16x32_bf16 v[12:15], v[220:223], v[196:199], v[12:15]
	v_mfma_f32_16x16x32_bf16 v[4:7], v[212:215], v[204:207], v[4:7]
	v_mfma_f32_16x16x32_bf16 v[0:3], v[220:223], v[204:207], v[0:3]
	v_mfma_f32_16x16x32_bf16 v[52:55], v[216:219], v[180:183], v[52:55]
	v_mfma_f32_16x16x32_bf16 v[40:43], v[224:227], v[180:183], v[40:43]
	v_mfma_f32_16x16x32_bf16 v[32:35], v[216:219], v[188:191], v[32:35]
	v_mfma_f32_16x16x32_bf16 v[28:31], v[224:227], v[188:191], v[28:31]
	v_mfma_f32_16x16x32_bf16 v[20:23], v[216:219], v[200:203], v[20:23]
	v_mfma_f32_16x16x32_bf16 v[12:15], v[224:227], v[200:203], v[12:15]
	v_mfma_f32_16x16x32_bf16 v[4:7], v[216:219], v[208:211], v[4:7]
	v_mfma_f32_16x16x32_bf16 v[0:3], v[224:227], v[208:211], v[0:3]
	s_setprio 0
	s_barrier
	ds_read_b128 v[160:163], v148 offset:32768
	ds_read_b128 v[164:167], v148 offset:33792
	ds_read_b128 v[168:171], v148 offset:34816
	ds_read_b128 v[172:175], v148 offset:35840
	s_mov_b32 m0, s62
	ds_read_b128 v[176:179], v147 offset:32768
	ds_read_b128 v[180:183], v147 offset:33792
	ds_read_b128 v[184:187], v147 offset:34816
	ds_read_b128 v[188:191], v147 offset:35840
	ds_read_b128 v[196:199], v147 offset:36864
	ds_read_b128 v[200:203], v147 offset:37888
	ds_read_b128 v[204:207], v147 offset:38912
	ds_read_b128 v[208:211], v147 offset:39936
	v_cndmask_b32_e32 v132, v140, v157, vcc
	global_load_lds_dwordx4 v139, s[50:51]
	s_mov_b32 m0, s63
	s_nop 0
	global_load_lds_dwordx4 v132, s[50:51]
	s_waitcnt lgkmcnt(8)
	s_barrier
	s_waitcnt lgkmcnt(0)
	s_setprio 1
	v_mfma_f32_16x16x32_bf16 v[124:127], v[160:163], v[176:179], v[124:127]
	v_mfma_f32_16x16x32_bf16 v[120:123], v[168:171], v[176:179], v[120:123]
	v_mfma_f32_16x16x32_bf16 v[116:119], v[160:163], v[184:187], v[116:119]
	v_mfma_f32_16x16x32_bf16 v[104:107], v[168:171], v[184:187], v[104:107]
	v_mfma_f32_16x16x32_bf16 v[96:99], v[160:163], v[196:199], v[96:99]
	v_mfma_f32_16x16x32_bf16 v[92:95], v[168:171], v[196:199], v[92:95]
	v_mfma_f32_16x16x32_bf16 v[84:87], v[160:163], v[204:207], v[84:87]
	v_mfma_f32_16x16x32_bf16 v[72:75], v[168:171], v[204:207], v[72:75]
	v_mfma_f32_16x16x32_bf16 v[124:127], v[164:167], v[180:183], v[124:127]
	v_mfma_f32_16x16x32_bf16 v[120:123], v[172:175], v[180:183], v[120:123]
	v_mfma_f32_16x16x32_bf16 v[116:119], v[164:167], v[188:191], v[116:119]
	v_mfma_f32_16x16x32_bf16 v[104:107], v[172:175], v[188:191], v[104:107]
	v_mfma_f32_16x16x32_bf16 v[96:99], v[164:167], v[200:203], v[96:99]
	v_mfma_f32_16x16x32_bf16 v[92:95], v[172:175], v[200:203], v[92:95]
	v_mfma_f32_16x16x32_bf16 v[84:87], v[164:167], v[208:211], v[84:87]
	v_mfma_f32_16x16x32_bf16 v[72:75], v[172:175], v[208:211], v[72:75]
	s_setprio 0
	s_barrier
	s_mov_b32 m0, s66
	v_lshl_add_u64 v[228:229], v[228:229], 0, s[16:17]
	ds_read_b128 v[212:215], v148 offset:49152
	ds_read_b128 v[216:219], v148 offset:50176
	ds_read_b128 v[220:223], v148 offset:51200
	ds_read_b128 v[224:227], v148 offset:52224
	global_load_lds_dwordx4 v[228:229], off
	v_lshl_add_u64 v[228:229], v[230:231], 0, s[16:17]
	s_mov_b32 m0, s67
	s_nop 0
	global_load_lds_dwordx4 v[228:229], off
	s_barrier
	s_waitcnt lgkmcnt(0)
	s_setprio 1
	v_mfma_f32_16x16x32_bf16 v[112:115], v[212:215], v[176:179], v[112:115]
	v_mfma_f32_16x16x32_bf16 v[108:111], v[220:223], v[176:179], v[108:111]
	v_mfma_f32_16x16x32_bf16 v[100:103], v[212:215], v[184:187], v[100:103]
	v_mfma_f32_16x16x32_bf16 v[88:91], v[220:223], v[184:187], v[88:91]
	v_mfma_f32_16x16x32_bf16 v[80:83], v[212:215], v[196:199], v[80:83]
	v_mfma_f32_16x16x32_bf16 v[76:79], v[220:223], v[196:199], v[76:79]
	v_mfma_f32_16x16x32_bf16 v[68:71], v[212:215], v[204:207], v[68:71]
	v_mfma_f32_16x16x32_bf16 v[64:67], v[220:223], v[204:207], v[64:67]
	v_mfma_f32_16x16x32_bf16 v[112:115], v[216:219], v[180:183], v[112:115]
	v_mfma_f32_16x16x32_bf16 v[108:111], v[224:227], v[180:183], v[108:111]
	v_mfma_f32_16x16x32_bf16 v[100:103], v[216:219], v[188:191], v[100:103]
	v_mfma_f32_16x16x32_bf16 v[88:91], v[224:227], v[188:191], v[88:91]
	v_mfma_f32_16x16x32_bf16 v[80:83], v[216:219], v[200:203], v[80:83]
	v_mfma_f32_16x16x32_bf16 v[76:79], v[224:227], v[200:203], v[76:79]
	v_mfma_f32_16x16x32_bf16 v[68:71], v[216:219], v[208:211], v[68:71]
	v_mfma_f32_16x16x32_bf16 v[64:67], v[224:227], v[208:211], v[64:67]
	s_setprio 0
	s_mov_b32 m0, s68
	v_lshl_add_u64 v[228:229], v[232:233], 0, s[16:17]
	s_barrier
	ds_read_b128 v[176:179], v147 offset:49152
	ds_read_b128 v[180:183], v147 offset:50176
	ds_read_b128 v[184:187], v147 offset:51200
	ds_read_b128 v[188:191], v147 offset:52224
	ds_read_b128 v[196:199], v147 offset:53248
	ds_read_b128 v[200:203], v147 offset:54272
	ds_read_b128 v[204:207], v147 offset:55296
	ds_read_b128 v[208:211], v147 offset:56320
	global_load_lds_dwordx4 v[228:229], off
	v_lshl_add_u64 v[192:193], v[192:193], 0, s[16:17]
	s_mov_b32 m0, s69
	s_nop 0
	global_load_lds_dwordx4 v[192:193], off
	s_barrier
	s_waitcnt lgkmcnt(0)
	s_setprio 1
	v_mfma_f32_16x16x32_bf16 v[60:63], v[160:163], v[176:179], v[60:63]
	v_mfma_f32_16x16x32_bf16 v[56:59], v[168:171], v[176:179], v[56:59]
	v_mfma_f32_16x16x32_bf16 v[48:51], v[160:163], v[184:187], v[48:51]
	v_mfma_f32_16x16x32_bf16 v[44:47], v[168:171], v[184:187], v[44:47]
	v_mfma_f32_16x16x32_bf16 v[36:39], v[160:163], v[196:199], v[36:39]
	v_mfma_f32_16x16x32_bf16 v[24:27], v[168:171], v[196:199], v[24:27]
	v_mfma_f32_16x16x32_bf16 v[16:19], v[160:163], v[204:207], v[16:19]
	v_mfma_f32_16x16x32_bf16 v[8:11], v[168:171], v[204:207], v[8:11]
	v_mfma_f32_16x16x32_bf16 v[60:63], v[164:167], v[180:183], v[60:63]
	v_mfma_f32_16x16x32_bf16 v[56:59], v[172:175], v[180:183], v[56:59]
	v_mfma_f32_16x16x32_bf16 v[48:51], v[164:167], v[188:191], v[48:51]
	v_mfma_f32_16x16x32_bf16 v[44:47], v[172:175], v[188:191], v[44:47]
	v_mfma_f32_16x16x32_bf16 v[36:39], v[164:167], v[200:203], v[36:39]
	v_mfma_f32_16x16x32_bf16 v[24:27], v[172:175], v[200:203], v[24:27]
	v_mfma_f32_16x16x32_bf16 v[16:19], v[164:167], v[208:211], v[16:19]
	v_mfma_f32_16x16x32_bf16 v[8:11], v[172:175], v[208:211], v[8:11]
	s_setprio 0
	s_barrier
	s_add_u32 s48, s48, 0x80080
	s_addc_u32 s49, s49, 0
	s_mov_b32 m0, s70
	v_lshl_add_u64 v[160:161], s[48:49], 0, v[130:131]
	global_load_lds_dwordx4 v[160:161], off
	v_lshl_add_u64 v[160:161], s[48:49], 0, v[128:129]
	s_mov_b32 m0, s71
	s_nop 0
	global_load_lds_dwordx4 v[160:161], off
	s_waitcnt vmcnt(6)
	s_barrier
	s_setprio 1
	v_mfma_f32_16x16x32_bf16 v[52:55], v[212:215], v[176:179], v[52:55]
	v_mfma_f32_16x16x32_bf16 v[40:43], v[220:223], v[176:179], v[40:43]
	v_mfma_f32_16x16x32_bf16 v[32:35], v[212:215], v[184:187], v[32:35]
	v_mfma_f32_16x16x32_bf16 v[28:31], v[220:223], v[184:187], v[28:31]
	v_mfma_f32_16x16x32_bf16 v[20:23], v[212:215], v[196:199], v[20:23]
	v_mfma_f32_16x16x32_bf16 v[12:15], v[220:223], v[196:199], v[12:15]
	v_mfma_f32_16x16x32_bf16 v[4:7], v[212:215], v[204:207], v[4:7]
	v_mfma_f32_16x16x32_bf16 v[0:3], v[220:223], v[204:207], v[0:3]
	v_mfma_f32_16x16x32_bf16 v[52:55], v[216:219], v[180:183], v[52:55]
	v_mfma_f32_16x16x32_bf16 v[40:43], v[224:227], v[180:183], v[40:43]
	v_mfma_f32_16x16x32_bf16 v[32:35], v[216:219], v[188:191], v[32:35]
	v_mfma_f32_16x16x32_bf16 v[28:31], v[224:227], v[188:191], v[28:31]
	v_mfma_f32_16x16x32_bf16 v[20:23], v[216:219], v[200:203], v[20:23]
	v_mfma_f32_16x16x32_bf16 v[12:15], v[224:227], v[200:203], v[12:15]
	v_mfma_f32_16x16x32_bf16 v[4:7], v[216:219], v[208:211], v[4:7]
	v_mfma_f32_16x16x32_bf16 v[0:3], v[224:227], v[208:211], v[0:3]
	s_setprio 0
	s_add_i32 s84, s84, 2
	s_add_u32 s46, s46, 0x100
	s_addc_u32 s47, s47, 0
	s_cmp_gt_u32 s84, 5
	s_barrier
	s_cbranch_scc0 .LBB0_1644
	s_and_b64 vcc, exec, s[20:21]
	s_cbranch_vccz .LBB0_1648
	s_barrier
	s_andn2_b64 vcc, exec, s[24:25]
	s_cbranch_vccz .LBB0_1649

.LBB0_1831:
	s_or_b64 exec, exec, s[4:5]
	s_add_u32 s54, s20, 0x4000000
	s_waitcnt lgkmcnt(0)
	s_barrier
	s_addc_u32 s55, s21, 0
	s_add_u32 s58, s20, 0xc000000
	v_ashrrev_i32_e32 v6, 4, v4
	v_and_b32_e32 v7, 15, v4
	v_lshlrev_b32_e32 v0, 5, v6
	v_lshlrev_b32_e32 v3, 2, v4
	s_addc_u32 s59, s21, 0
	s_lshr_b32 s1, s95, 8
	v_lshlrev_b32_e32 v2, 6, v7
	v_and_b32_e32 v0, 32, v0
	v_and_b32_e32 v3, 32, v3
	v_ashrrev_i32_e32 v1, 5, v4
	v_bitop3_b32 v0, v0, v3, v2 bitop3:0x36
	v_lshrrev_b32_e32 v2, 2, v4
	v_lshrrev_b32_e32 v3, 3, v4
	s_lshl_b32 s0, s1, 13
	v_xor_b32_e32 v2, v2, v3
	v_lshl_add_u32 v3, v1, 10, s0
	s_lshl_b32 s0, s3, 5
	s_and_b32 s12, s0, 0x60
	v_lshlrev_b32_e32 v2, 4, v2
	s_lshr_b32 s0, s12, 3
	v_and_b32_e32 v2, 16, v2
	v_add_lshl_u32 v1, v1, s0, 10
	v_or3_b32 v3, v2, v3, v0
	v_or3_b32 v0, v2, v1, v0
	s_add_i32 s0, 0, 0x10000
	v_add_u32_e32 v197, s0, v0
	v_xad_u32 v198, v0, 16, s0
	s_add_i32 s0, 0, 0x22140
	v_add_u32_e32 v195, 0, v3
	v_xad_u32 v196, v3, 16, 0
	v_mov_b32_e32 v0, s0
	ds_read_b32 v0, v0
	s_waitcnt lgkmcnt(0)
	v_readfirstlane_b32 s6, v0
	s_lshl_b32 s0, s6, 2
	s_cmp_lt_i32 s23, s0
	s_cselect_b64 s[4:5], -1, 0
	s_cmp_ge_i32 s23, s0
	s_cbranch_scc1 .LBB0_1835
	s_ashr_i32 s0, s23, 31
	s_lshr_b32 s0, s0, 30
	s_add_i32 s7, s23, s0
	s_ashr_i32 s0, s7, 2
	s_and_b32 s7, s7, -4
	s_sub_i32 s44, s23, s7
	s_cmp_ge_i32 s0, s6
	s_cbranch_scc0 .LBB0_1836
	s_ashr_i32 s45, s44, 31
	s_sub_i32 s8, s0, s6
	s_lshl_b64 s[6:7], s[44:45], 19
	s_add_u32 s16, s54, s6
	s_addc_u32 s17, s55, s7
	s_lshr_b32 s6, s8, 3
	s_mul_i32 s6, s6, 9
	s_and_b32 s7, s8, 7
	s_add_i32 s7, s7, s6
	s_lshl_b32 s6, s7, 8
	s_add_i32 s8, s6, 0xf41e0100
	s_cbranch_execz .LBB0_1837
	v_mov_b32_e32 v174, s8
	v_mov_b32_e32 v171, -1
	v_mov_b32_e32 v5, 0x100
	s_lshl_b32 s0, s0, 8
	s_andn2_b64 vcc, exec, s[4:5]
	s_cbranch_vccnz .LBB0_1878
	s_branch .LBB0_1838

.LBB0_1862:
	s_add_u32 s50, s20, s48
	s_addc_u32 s51, s21, s49
	ds_read_b128 v[186:189], v197
	ds_read_b128 v[202:205], v197 offset:2048
	ds_read_b128 v[190:193], v198
	ds_read_b128 v[206:209], v198 offset:2048
	s_add_u32 s52, s50, 0x14000100
	s_addc_u32 s53, s51, 0
	s_and_b64 s[50:51], s[16:17], exec
	s_cselect_b32 s53, s27, s53
	s_cselect_b32 s52, s26, s52
	s_add_u32 s79, s56, s48
	s_addc_u32 s80, s57, s49
	s_and_b64 s[50:51], s[16:17], exec
	s_cselect_b32 s51, s43, s80
	s_cselect_b32 s50, s42, s79
	ds_read_b128 v[210:213], v195
	ds_read_b128 v[218:221], v195 offset:2048
	ds_read_b128 v[214:217], v196
	ds_read_b128 v[222:225], v196 offset:2048
	ds_read_b128 v[226:229], v195 offset:4096
	ds_read_b128 v[234:237], v195 offset:6144
	ds_read_b128 v[230:233], v196 offset:4096
	ds_read_b128 v[238:241], v196 offset:6144
	s_waitcnt vmcnt(6)
	s_waitcnt lgkmcnt(8)
	s_barrier
	s_waitcnt lgkmcnt(0)
	s_setprio 1
	v_mfma_f32_16x16x128_f8f6f4 v[124:127], v[186:193], v[210:217], v[124:127]
	v_mfma_f32_16x16x128_f8f6f4 v[120:123], v[202:209], v[210:217], v[120:123]
	v_mfma_f32_16x16x128_f8f6f4 v[108:111], v[186:193], v[218:225], v[108:111]
	v_mfma_f32_16x16x128_f8f6f4 v[104:107], v[202:209], v[218:225], v[104:107]
	v_mfma_f32_16x16x128_f8f6f4 v[92:95], v[186:193], v[226:233], v[92:95]
	v_mfma_f32_16x16x128_f8f6f4 v[88:91], v[202:209], v[226:233], v[88:91]
	v_mfma_f32_16x16x128_f8f6f4 v[76:79], v[186:193], v[234:241], v[76:79]
	v_mfma_f32_16x16x128_f8f6f4 v[72:75], v[202:209], v[234:241], v[72:75]
	s_setprio 0
	s_barrier
	ds_read_b128 v[186:189], v197 offset:16384
	ds_read_b128 v[202:205], v197 offset:18432
	ds_read_b128 v[190:193], v198 offset:16384
	ds_read_b128 v[206:209], v198 offset:18432
	v_cndmask_b32_e64 v136, v175, v173, s[16:17]
	v_cndmask_b32_e64 v177, v176, v151, s[16:17]
	v_lshl_add_u64 v[242:243], v[184:185], 0, s[48:49]
	s_add_i32 m0, s45, 0xc000
	s_nop 0
	global_load_lds_dwordx4 v[242:243], off
	v_lshl_add_u64 v[242:243], v[182:183], 0, s[48:49]
	s_add_i32 m0, s45, 0xe000
	v_cndmask_b32_e64 v250, v178, v155, s[16:17]
	global_load_lds_dwordx4 v[242:243], off
	s_barrier
	s_waitcnt lgkmcnt(0)
	s_setprio 1
	v_mfma_f32_16x16x128_f8f6f4 v[116:119], v[186:193], v[210:217], v[116:119]
	v_mfma_f32_16x16x128_f8f6f4 v[112:115], v[202:209], v[210:217], v[112:115]
	v_mfma_f32_16x16x128_f8f6f4 v[100:103], v[186:193], v[218:225], v[100:103]
	v_mfma_f32_16x16x128_f8f6f4 v[96:99], v[202:209], v[218:225], v[96:99]
	v_mfma_f32_16x16x128_f8f6f4 v[84:87], v[186:193], v[226:233], v[84:87]
	v_mfma_f32_16x16x128_f8f6f4 v[80:83], v[202:209], v[226:233], v[80:83]
	v_mfma_f32_16x16x128_f8f6f4 v[68:71], v[186:193], v[234:241], v[68:71]
	v_mfma_f32_16x16x128_f8f6f4 v[64:67], v[202:209], v[234:241], v[64:67]
	s_setprio 0
	s_barrier
	ds_read_b128 v[202:205], v197
	ds_read_b128 v[210:213], v197 offset:2048
	ds_read_b128 v[206:209], v198
	ds_read_b128 v[214:217], v198 offset:2048
	s_mov_b32 m0, s45
	ds_read_b128 v[218:221], v195 offset:16384
	ds_read_b128 v[226:229], v195 offset:18432
	ds_read_b128 v[222:225], v196 offset:16384
	ds_read_b128 v[230:233], v196 offset:18432
	ds_read_b128 v[234:237], v195 offset:20480
	ds_read_b128 v[242:245], v195 offset:22528
	ds_read_b128 v[238:241], v196 offset:20480
	ds_read_b128 v[246:249], v196 offset:22528
	global_load_lds_dwordx4 v136, s[52:53]
	s_mov_b32 m0, s62
	v_mov_b32_e32 v251, v137
	global_load_lds_dwordx4 v250, s[52:53]
	s_waitcnt lgkmcnt(8)
	s_barrier
	s_waitcnt lgkmcnt(0)
	v_lshl_add_u64 v[192:193], s[52:53], 0, v[136:137]
	v_lshl_add_u64 v[190:191], s[52:53], 0, v[250:251]
	s_setprio 1
	s_waitcnt lgkmcnt(0)
	v_mfma_f32_16x16x128_f8f6f4 v[60:63], v[202:209], v[218:225], v[60:63]
	v_mfma_f32_16x16x128_f8f6f4 v[56:59], v[210:217], v[218:225], v[56:59]
	v_mfma_f32_16x16x128_f8f6f4 v[44:47], v[202:209], v[226:233], v[44:47]
	v_mfma_f32_16x16x128_f8f6f4 v[40:43], v[210:217], v[226:233], v[40:43]
	v_mfma_f32_16x16x128_f8f6f4 v[28:31], v[202:209], v[234:241], v[28:31]
	v_mfma_f32_16x16x128_f8f6f4 v[24:27], v[210:217], v[234:241], v[24:27]
	v_mfma_f32_16x16x128_f8f6f4 v[12:15], v[202:209], v[242:249], v[12:15]
	v_mfma_f32_16x16x128_f8f6f4 v[8:11], v[210:217], v[242:249], v[8:11]
	s_setprio 0
	s_barrier
	s_mov_b32 m0, s60
	v_lshl_add_u64 v[186:187], s[50:51], 0, v[138:139]
	ds_read_b128 v[202:205], v197 offset:16384
	ds_read_b128 v[210:213], v197 offset:18432
	ds_read_b128 v[206:209], v198 offset:16384
	ds_read_b128 v[214:217], v198 offset:18432
	global_load_lds_dwordx4 v[186:187], off
	v_lshl_add_u64 v[188:189], s[50:51], 0, v[140:141]
	s_mov_b32 m0, s61
	s_nop 0
	global_load_lds_dwordx4 v[188:189], off
	s_waitcnt vmcnt(8)
	s_waitcnt lgkmcnt(0)
	s_barrier
	s_setprio 1
	s_waitcnt lgkmcnt(0)
	v_mfma_f32_16x16x128_f8f6f4 v[52:55], v[202:209], v[218:225], v[52:55]
	v_mfma_f32_16x16x128_f8f6f4 v[48:51], v[210:217], v[218:225], v[48:51]
	v_mfma_f32_16x16x128_f8f6f4 v[36:39], v[202:209], v[226:233], v[36:39]
	v_mfma_f32_16x16x128_f8f6f4 v[32:35], v[210:217], v[226:233], v[32:35]
	v_mfma_f32_16x16x128_f8f6f4 v[20:23], v[202:209], v[234:241], v[20:23]
	v_mfma_f32_16x16x128_f8f6f4 v[16:19], v[210:217], v[234:241], v[16:19]
	v_mfma_f32_16x16x128_f8f6f4 v[4:7], v[202:209], v[242:249], v[4:7]
	v_mfma_f32_16x16x128_f8f6f4 v[0:3], v[210:217], v[242:249], v[0:3]
	s_setprio 0
	s_barrier
	ds_read_b128 v[202:205], v197 offset:32768
	ds_read_b128 v[210:213], v197 offset:34816
	ds_read_b128 v[206:209], v198 offset:32768
	ds_read_b128 v[214:217], v198 offset:34816
	s_mov_b32 m0, s65
	v_cndmask_b32_e64 v136, v180, v179, s[16:17]
	s_add_u32 s16, s50, 0x4000
	ds_read_b128 v[218:221], v195 offset:32768
	ds_read_b128 v[226:229], v195 offset:34816
	ds_read_b128 v[222:225], v196 offset:32768
	ds_read_b128 v[230:233], v196 offset:34816
	ds_read_b128 v[234:237], v195 offset:36864
	ds_read_b128 v[242:245], v195 offset:38912
	ds_read_b128 v[238:241], v196 offset:36864
	ds_read_b128 v[246:249], v196 offset:38912
	global_load_lds_dwordx4 v177, s[52:53]
	s_mov_b32 m0, s66
	s_addc_u32 s17, s51, 0
	global_load_lds_dwordx4 v136, s[52:53]
	s_waitcnt vmcnt(8)
	s_waitcnt lgkmcnt(8)
	s_barrier
	s_waitcnt lgkmcnt(0)
	s_setprio 1
	v_mfma_f32_16x16x128_f8f6f4 v[124:127], v[202:209], v[218:225], v[124:127]
	v_mfma_f32_16x16x128_f8f6f4 v[120:123], v[210:217], v[218:225], v[120:123]
	v_mfma_f32_16x16x128_f8f6f4 v[108:111], v[202:209], v[226:233], v[108:111]
	v_mfma_f32_16x16x128_f8f6f4 v[104:107], v[210:217], v[226:233], v[104:107]
	v_mfma_f32_16x16x128_f8f6f4 v[92:95], v[202:209], v[234:241], v[92:95]
	v_mfma_f32_16x16x128_f8f6f4 v[88:91], v[210:217], v[234:241], v[88:91]
	v_mfma_f32_16x16x128_f8f6f4 v[76:79], v[202:209], v[242:249], v[76:79]
	v_mfma_f32_16x16x128_f8f6f4 v[72:75], v[210:217], v[242:249], v[72:75]
	s_setprio 0
	s_barrier
	ds_read_b128 v[202:205], v197 offset:49152
	ds_read_b128 v[210:213], v197 offset:51200
	ds_read_b128 v[206:209], v198 offset:49152
	ds_read_b128 v[214:217], v198 offset:51200
	v_lshl_add_u64 v[250:251], s[16:17], 0, v[138:139]
	s_mov_b32 m0, s63
	s_nop 0
	global_load_lds_dwordx4 v[250:251], off
	v_lshl_add_u64 v[250:251], s[16:17], 0, v[140:141]
	s_mov_b32 m0, s64
	s_nop 0
	global_load_lds_dwordx4 v[250:251], off
	s_waitcnt vmcnt(8)
	s_barrier
	s_waitcnt lgkmcnt(0)
	s_setprio 1
	v_mfma_f32_16x16x128_f8f6f4 v[116:119], v[202:209], v[218:225], v[116:119]
	v_mfma_f32_16x16x128_f8f6f4 v[112:115], v[210:217], v[218:225], v[112:115]
	v_mfma_f32_16x16x128_f8f6f4 v[100:103], v[202:209], v[226:233], v[100:103]
	v_mfma_f32_16x16x128_f8f6f4 v[96:99], v[210:217], v[226:233], v[96:99]
	v_mfma_f32_16x16x128_f8f6f4 v[84:87], v[202:209], v[234:241], v[84:87]
	v_mfma_f32_16x16x128_f8f6f4 v[80:83], v[210:217], v[234:241], v[80:83]
	v_mfma_f32_16x16x128_f8f6f4 v[68:71], v[202:209], v[242:249], v[68:71]
	v_mfma_f32_16x16x128_f8f6f4 v[64:67], v[210:217], v[242:249], v[64:67]
	s_setprio 0
	s_barrier
	ds_read_b128 v[202:205], v197 offset:32768
	ds_read_b128 v[210:213], v197 offset:34816
	ds_read_b128 v[206:209], v198 offset:32768
	ds_read_b128 v[214:217], v198 offset:34816
	s_mov_b32 m0, s71
	v_lshl_add_u64 v[192:193], v[192:193], 0, s[34:35]
	ds_read_b128 v[218:221], v195 offset:49152
	ds_read_b128 v[226:229], v195 offset:51200
	ds_read_b128 v[222:225], v196 offset:49152
	ds_read_b128 v[230:233], v196 offset:51200
	ds_read_b128 v[234:237], v195 offset:53248
	ds_read_b128 v[242:245], v195 offset:55296
	ds_read_b128 v[238:241], v196 offset:53248
	ds_read_b128 v[246:249], v196 offset:55296
	global_load_lds_dwordx4 v[192:193], off
	v_lshl_add_u64 v[190:191], v[190:191], 0, s[34:35]
	s_mov_b32 m0, s72
	s_nop 0
	global_load_lds_dwordx4 v[190:191], off
	s_waitcnt lgkmcnt(8)
	s_barrier
	s_waitcnt lgkmcnt(0)
	s_setprio 1
	v_mfma_f32_16x16x128_f8f6f4 v[60:63], v[202:209], v[218:225], v[60:63]
	v_mfma_f32_16x16x128_f8f6f4 v[56:59], v[210:217], v[218:225], v[56:59]
	v_mfma_f32_16x16x128_f8f6f4 v[44:47], v[202:209], v[226:233], v[44:47]
	v_mfma_f32_16x16x128_f8f6f4 v[40:43], v[210:217], v[226:233], v[40:43]
	v_mfma_f32_16x16x128_f8f6f4 v[28:31], v[202:209], v[234:241], v[28:31]
	v_mfma_f32_16x16x128_f8f6f4 v[24:27], v[210:217], v[234:241], v[24:27]
	v_mfma_f32_16x16x128_f8f6f4 v[12:15], v[202:209], v[242:249], v[12:15]
	v_mfma_f32_16x16x128_f8f6f4 v[8:11], v[210:217], v[242:249], v[8:11]
	s_setprio 0
	s_barrier
	s_mov_b32 m0, s69
	v_lshl_add_u64 v[186:187], v[186:187], 0, s[34:35]
	ds_read_b128 v[202:205], v197 offset:49152
	ds_read_b128 v[210:213], v197 offset:51200
	ds_read_b128 v[206:209], v198 offset:49152
	ds_read_b128 v[214:217], v198 offset:51200
	global_load_lds_dwordx4 v[186:187], off
	v_lshl_add_u64 v[186:187], v[188:189], 0, s[34:35]
	s_mov_b32 m0, s70
	s_nop 0
	global_load_lds_dwordx4 v[186:187], off
	s_waitcnt vmcnt(8)
	s_waitcnt lgkmcnt(0)
	s_barrier
	s_setprio 1
	s_waitcnt lgkmcnt(0)
	v_mfma_f32_16x16x128_f8f6f4 v[52:55], v[202:209], v[218:225], v[52:55]
	v_mfma_f32_16x16x128_f8f6f4 v[48:51], v[210:217], v[218:225], v[48:51]
	v_mfma_f32_16x16x128_f8f6f4 v[36:39], v[202:209], v[226:233], v[36:39]
	v_mfma_f32_16x16x128_f8f6f4 v[32:35], v[210:217], v[226:233], v[32:35]
	v_mfma_f32_16x16x128_f8f6f4 v[20:23], v[202:209], v[234:241], v[20:23]
	v_mfma_f32_16x16x128_f8f6f4 v[16:19], v[210:217], v[234:241], v[16:19]
	v_mfma_f32_16x16x128_f8f6f4 v[4:7], v[202:209], v[242:249], v[4:7]
	v_mfma_f32_16x16x128_f8f6f4 v[0:3], v[210:217], v[242:249], v[0:3]
	s_setprio 0
	s_barrier
	s_add_u32 s16, s50, 0x4080
	s_addc_u32 s17, s51, 0
	s_mov_b32 m0, s73
	v_lshl_add_u64 v[186:187], s[16:17], 0, v[138:139]
	global_load_lds_dwordx4 v[186:187], off
	v_lshl_add_u64 v[186:187], s[16:17], 0, v[140:141]
	s_mov_b32 m0, s74
	s_add_i32 s78, s78, 2
	global_load_lds_dwordx4 v[186:187], off
	s_add_u32 s48, s48, 0x100
	s_addc_u32 s49, s49, 0
	s_cmp_gt_u32 s78, 13
	s_cbranch_scc1 .LBB0_1872

.LBB0_1945:
	s_or_b64 exec, exec, s[4:5]
	v_mov_b32_e32 v4, v144
	s_waitcnt lgkmcnt(0)
	s_barrier
	s_bfe_u32 s23, s95, 0x20006
	v_and_b32_e32 v5, 15, v4
	v_lshlrev_b32_e32 v0, 1, v4
	v_lshlrev_b32_e32 v2, 2, v4
	v_lshlrev_b32_e32 v1, 6, v5
	v_and_b32_e32 v0, 32, v0
	v_and_b32_e32 v2, 32, v2
	v_bitop3_b32 v0, v1, v2, v0 bitop3:0x36
	v_lshrrev_b32_e32 v1, 2, v4
	v_lshrrev_b32_e32 v2, 3, v4
	s_lshr_b32 s54, s95, 8
	v_xor_b32_e32 v1, v1, v2
	v_lshlrev_b32_e32 v2, 5, v4
	v_lshlrev_b32_e32 v1, 4, v1
	s_lshl_b32 s60, s54, 13
	v_and_b32_e32 v2, 0xfffffc00, v2
	s_lshl_b32 s58, s23, 12
	v_and_b32_e32 v1, 16, v1
	v_add_u32_e32 v3, s60, v2
	v_add_u32_e32 v2, s58, v2
	v_or3_b32 v3, v1, v3, v0
	v_or3_b32 v0, v1, v2, v0
	s_add_i32 s59, 0, 0x10000
	s_add_i32 s0, 0, 0x22140
	v_add_u32_e32 v145, 0, v3
	v_xad_u32 v146, v3, 16, 0
	v_add_u32_e32 v147, s59, v0
	v_xad_u32 v148, v0, 16, s59
	v_mov_b32_e32 v0, s0
	ds_read_b32 v0, v0
	s_lshl_b32 s55, s3, 10
	s_lshl_b32 s33, s54, 6
	s_lshl_b32 s61, s23, 5
	s_waitcnt lgkmcnt(0)
	v_lshlrev_b32_e32 v1, 3, v0
	v_cmp_ge_i32_e32 vcc, s27, v1
	s_cbranch_vccnz .LBB0_1968
	s_add_u32 s10, s8, 0x24000000
	s_addc_u32 s11, s9, 0
	s_add_u32 s62, s8, 0x28000000
	s_addc_u32 s63, s9, 0
	s_ashr_i32 s0, s27, 31
	s_lshr_b32 s0, s0, 29
	s_add_i32 s0, s27, s0
	s_ashr_i32 s0, s0, 3
	v_cmp_ge_i32_e32 vcc, s0, v0
	s_mov_b64 s[4:5], s[10:11]
	s_cbranch_vccnz .LBB0_1948
	s_lshl_b32 s1, s0, 1
	s_add_i32 s1, s1, 0
	s_add_i32 s1, s1, 0x22240
	v_mov_b32_e32 v0, s1
	ds_read_u16 v0, v0
	s_mov_b32 s5, 0
	s_waitcnt lgkmcnt(0)
	v_readfirstlane_b32 s1, v0
	s_and_b32 s4, s1, 0xffff
	s_lshl_b64 s[4:5], s[4:5], 20
	s_add_u32 s4, s62, s4
	s_addc_u32 s5, s63, s5

.LBB0_1960:
	v_mov_b32_e32 v137, v133
	v_mov_b32_e32 v139, v133
	s_mov_b64 s[44:45], 0
	s_mov_b64 s[40:41], -1
	s_mov_b64 s[42:43], 0
	s_add_u32 s52, s12, s44
	s_addc_u32 s53, s13, s45
	s_add_u32 s29, s52, 0x100
	s_addc_u32 s48, s53, 0
	s_and_b64 s[46:47], s[42:43], exec
	s_cselect_b32 s46, s12, s29
	s_cselect_b32 s47, s13, s48
	s_add_u32 s29, s38, s44
	s_addc_u32 s44, s39, s45
	s_add_u32 s29, s29, 0x100
	s_addc_u32 s48, s44, 0
	ds_read_b128 v[162:165], v147
	ds_read_b128 v[170:173], v147 offset:2048
	ds_read_b128 v[166:169], v148
	ds_read_b128 v[174:177], v148 offset:2048
	s_and_b64 s[44:45], s[42:43], exec
	s_cselect_b32 s51, s35, s48
	s_cselect_b32 s50, s34, s29
	ds_read_b128 v[178:181], v145
	ds_read_b128 v[186:189], v145 offset:2048
	ds_read_b128 v[182:185], v146
	ds_read_b128 v[190:193], v146 offset:2048
	ds_read_b128 v[196:199], v145 offset:4096
	ds_read_b128 v[204:207], v145 offset:6144
	ds_read_b128 v[200:203], v146 offset:4096
	ds_read_b128 v[208:211], v146 offset:6144
	s_waitcnt vmcnt(6)
	s_waitcnt lgkmcnt(8)
	s_barrier
	s_waitcnt lgkmcnt(0)
	v_cndmask_b32_e64 v140, v134, v158, s[42:43]
	s_setprio 1
	s_waitcnt lgkmcnt(0)
	v_mfma_f32_16x16x128_f8f6f4 v[124:127], v[162:169], v[178:185], 0
	v_mfma_f32_16x16x128_f8f6f4 v[120:123], v[170:177], v[178:185], 0
	v_mfma_f32_16x16x128_f8f6f4 v[108:111], v[162:169], v[186:193], 0
	v_mfma_f32_16x16x128_f8f6f4 v[104:107], v[170:177], v[186:193], 0
	v_mfma_f32_16x16x128_f8f6f4 v[92:95], v[162:169], v[196:203], 0
	v_mfma_f32_16x16x128_f8f6f4 v[88:91], v[170:177], v[196:203], 0
	v_mfma_f32_16x16x128_f8f6f4 v[76:79], v[162:169], v[204:211], 0
	v_mfma_f32_16x16x128_f8f6f4 v[72:75], v[170:177], v[204:211], 0
	s_setprio 0
	s_barrier
	ds_read_b128 v[218:221], v147 offset:16384
	ds_read_b128 v[226:229], v147 offset:18432
	ds_read_b128 v[222:225], v148 offset:16384
	ds_read_b128 v[230:233], v148 offset:18432
	s_add_i32 m0, s0, 0xc000
	s_add_i32 s29, s0, 0xe000
	s_add_u32 s48, s50, 0x1000
	s_addc_u32 s49, s51, 0
	s_add_u32 s44, s50, 0x1080
	s_addc_u32 s45, s51, 0
	v_cndmask_b32_e64 v132, v135, v157, s[42:43]
	v_cndmask_b32_e64 v161, v136, v159, s[42:43]
	v_lshl_add_u64 v[252:253], s[52:53], 0, v[136:137]
	v_lshl_add_u64 v[252:253], v[252:253], 0, s[20:21]
	global_load_lds_dwordx4 v[252:253], off
	v_lshl_add_u64 v[252:253], s[52:53], 0, v[138:139]
	v_lshl_add_u64 v[252:253], v[252:253], 0, s[20:21]
	s_mov_b32 m0, s29
	s_nop 0
	global_load_lds_dwordx4 v[252:253], off
	s_barrier
	s_waitcnt lgkmcnt(0)
	s_setprio 1
	v_mfma_f32_16x16x128_f8f6f4 v[116:119], v[218:225], v[178:185], 0
	v_mfma_f32_16x16x128_f8f6f4 v[112:115], v[226:233], v[178:185], 0
	v_mfma_f32_16x16x128_f8f6f4 v[100:103], v[218:225], v[186:193], 0
	v_mfma_f32_16x16x128_f8f6f4 v[96:99], v[226:233], v[186:193], 0
	v_mfma_f32_16x16x128_f8f6f4 v[84:87], v[218:225], v[196:203], 0
	v_mfma_f32_16x16x128_f8f6f4 v[80:83], v[226:233], v[196:203], 0
	v_mfma_f32_16x16x128_f8f6f4 v[68:71], v[218:225], v[204:211], 0
	v_mfma_f32_16x16x128_f8f6f4 v[64:67], v[226:233], v[204:211], 0
	s_setprio 0
	s_barrier
	s_mov_b32 m0, s0
	ds_read_b128 v[178:181], v145 offset:16384
	ds_read_b128 v[186:189], v145 offset:18432
	ds_read_b128 v[182:185], v146 offset:16384
	ds_read_b128 v[190:193], v146 offset:18432
	ds_read_b128 v[196:199], v145 offset:20480
	ds_read_b128 v[204:207], v145 offset:22528
	ds_read_b128 v[200:203], v146 offset:20480
	ds_read_b128 v[208:211], v146 offset:22528
	global_load_lds_dwordx4 v132, s[46:47]
	s_mov_b32 m0, s56
	v_mov_b32_e32 v141, v133
	global_load_lds_dwordx4 v140, s[46:47]
	s_waitcnt lgkmcnt(8)
	s_barrier
	s_waitcnt lgkmcnt(0)
	v_lshl_add_u64 v[212:213], s[46:47], 0, v[132:133]
	v_lshl_add_u64 v[214:215], s[46:47], 0, v[140:141]
	s_setprio 1
	s_waitcnt lgkmcnt(0)
	v_mfma_f32_16x16x128_f8f6f4 v[60:63], v[162:169], v[178:185], 0
	v_mfma_f32_16x16x128_f8f6f4 v[56:59], v[170:177], v[178:185], 0
	v_mfma_f32_16x16x128_f8f6f4 v[44:47], v[162:169], v[186:193], 0
	v_mfma_f32_16x16x128_f8f6f4 v[40:43], v[170:177], v[186:193], 0
	v_mfma_f32_16x16x128_f8f6f4 v[28:31], v[162:169], v[196:203], 0
	v_mfma_f32_16x16x128_f8f6f4 v[24:27], v[170:177], v[196:203], 0
	v_mfma_f32_16x16x128_f8f6f4 v[12:15], v[162:169], v[204:211], 0
	v_mfma_f32_16x16x128_f8f6f4 v[8:11], v[170:177], v[204:211], 0
	s_setprio 0
	s_barrier
	s_mov_b32 m0, s1
	v_lshl_add_u64 v[140:141], s[50:51], 0, v[128:129]
	global_load_lds_dwordx4 v[140:141], off
	v_lshl_add_u64 v[142:143], s[50:51], 0, v[130:131]
	s_mov_b32 m0, s37
	s_nop 0
	global_load_lds_dwordx4 v[142:143], off
	s_waitcnt vmcnt(8)
	s_waitcnt lgkmcnt(0)
	s_barrier
	s_setprio 1
	s_waitcnt lgkmcnt(0)
	v_mfma_f32_16x16x128_f8f6f4 v[52:55], v[218:225], v[178:185], 0
	v_mfma_f32_16x16x128_f8f6f4 v[48:51], v[226:233], v[178:185], 0
	v_mfma_f32_16x16x128_f8f6f4 v[36:39], v[218:225], v[186:193], 0
	v_mfma_f32_16x16x128_f8f6f4 v[32:35], v[226:233], v[186:193], 0
	v_mfma_f32_16x16x128_f8f6f4 v[20:23], v[218:225], v[196:203], 0
	v_mfma_f32_16x16x128_f8f6f4 v[16:19], v[226:233], v[196:203], 0
	v_mfma_f32_16x16x128_f8f6f4 v[4:7], v[218:225], v[204:211], 0
	v_mfma_f32_16x16x128_f8f6f4 v[0:3], v[226:233], v[204:211], 0
	s_setprio 0
	s_barrier
	ds_read_b128 v[162:165], v147 offset:32768
	ds_read_b128 v[170:173], v147 offset:34816
	ds_read_b128 v[166:169], v148 offset:32768
	ds_read_b128 v[174:177], v148 offset:34816
	s_mov_b32 m0, s65
	ds_read_b128 v[178:181], v145 offset:32768
	ds_read_b128 v[186:189], v145 offset:34816
	ds_read_b128 v[182:185], v146 offset:32768
	ds_read_b128 v[190:193], v146 offset:34816
	ds_read_b128 v[196:199], v145 offset:36864
	ds_read_b128 v[204:207], v145 offset:38912
	ds_read_b128 v[200:203], v146 offset:36864
	ds_read_b128 v[208:211], v146 offset:38912
	v_cndmask_b32_e64 v132, v138, v160, s[42:43]
	global_load_lds_dwordx4 v161, s[46:47]
	s_mov_b32 m0, s66
	s_nop 0
	global_load_lds_dwordx4 v132, s[46:47]
	s_waitcnt vmcnt(8)
	s_waitcnt lgkmcnt(8)
	s_barrier
	s_waitcnt lgkmcnt(0)
	s_setprio 1
	v_mfma_f32_16x16x128_f8f6f4 v[124:127], v[162:169], v[178:185], v[124:127]
	v_mfma_f32_16x16x128_f8f6f4 v[120:123], v[170:177], v[178:185], v[120:123]
	v_mfma_f32_16x16x128_f8f6f4 v[108:111], v[162:169], v[186:193], v[108:111]
	v_mfma_f32_16x16x128_f8f6f4 v[104:107], v[170:177], v[186:193], v[104:107]
	v_mfma_f32_16x16x128_f8f6f4 v[92:95], v[162:169], v[196:203], v[92:95]
	v_mfma_f32_16x16x128_f8f6f4 v[88:91], v[170:177], v[196:203], v[88:91]
	v_mfma_f32_16x16x128_f8f6f4 v[76:79], v[162:169], v[204:211], v[76:79]
	v_mfma_f32_16x16x128_f8f6f4 v[72:75], v[170:177], v[204:211], v[72:75]
	s_setprio 0
	s_barrier
	ds_read_b128 v[218:221], v147 offset:49152
	ds_read_b128 v[226:229], v147 offset:51200
	ds_read_b128 v[222:225], v148 offset:49152
	ds_read_b128 v[230:233], v148 offset:51200
	v_lshl_add_u64 v[216:217], s[48:49], 0, v[128:129]
	s_mov_b32 m0, s57
	s_nop 0
	global_load_lds_dwordx4 v[216:217], off
	v_lshl_add_u64 v[216:217], s[48:49], 0, v[130:131]
	s_mov_b32 m0, s64
	s_nop 0
	global_load_lds_dwordx4 v[216:217], off
	s_waitcnt vmcnt(8)
	s_barrier
	s_waitcnt lgkmcnt(0)
	s_setprio 1
	v_mfma_f32_16x16x128_f8f6f4 v[116:119], v[218:225], v[178:185], v[116:119]
	v_mfma_f32_16x16x128_f8f6f4 v[112:115], v[226:233], v[178:185], v[112:115]
	v_mfma_f32_16x16x128_f8f6f4 v[100:103], v[218:225], v[186:193], v[100:103]
	v_mfma_f32_16x16x128_f8f6f4 v[96:99], v[226:233], v[186:193], v[96:99]
	v_mfma_f32_16x16x128_f8f6f4 v[84:87], v[218:225], v[196:203], v[84:87]
	v_mfma_f32_16x16x128_f8f6f4 v[80:83], v[226:233], v[196:203], v[80:83]
	v_mfma_f32_16x16x128_f8f6f4 v[68:71], v[218:225], v[204:211], v[68:71]
	v_mfma_f32_16x16x128_f8f6f4 v[64:67], v[226:233], v[204:211], v[64:67]
	s_setprio 0
	s_barrier
	s_mov_b32 m0, s69
	v_lshl_add_u64 v[212:213], v[212:213], 0, s[20:21]
	ds_read_b128 v[178:181], v145 offset:49152
	ds_read_b128 v[186:189], v145 offset:51200
	ds_read_b128 v[182:185], v146 offset:49152
	ds_read_b128 v[190:193], v146 offset:51200
	ds_read_b128 v[196:199], v145 offset:53248
	ds_read_b128 v[204:207], v145 offset:55296
	ds_read_b128 v[200:203], v146 offset:53248
	ds_read_b128 v[208:211], v146 offset:55296
	global_load_lds_dwordx4 v[212:213], off
	v_lshl_add_u64 v[212:213], v[214:215], 0, s[20:21]
	s_mov_b32 m0, s70
	s_nop 0
	global_load_lds_dwordx4 v[212:213], off
	s_waitcnt lgkmcnt(8)
	s_barrier
	s_waitcnt lgkmcnt(0)
	s_setprio 1
	v_mfma_f32_16x16x128_f8f6f4 v[60:63], v[162:169], v[178:185], v[60:63]
	v_mfma_f32_16x16x128_f8f6f4 v[56:59], v[170:177], v[178:185], v[56:59]
	v_mfma_f32_16x16x128_f8f6f4 v[44:47], v[162:169], v[186:193], v[44:47]
	v_mfma_f32_16x16x128_f8f6f4 v[40:43], v[170:177], v[186:193], v[40:43]
	v_mfma_f32_16x16x128_f8f6f4 v[28:31], v[162:169], v[196:203], v[28:31]
	v_mfma_f32_16x16x128_f8f6f4 v[24:27], v[170:177], v[196:203], v[24:27]
	v_mfma_f32_16x16x128_f8f6f4 v[12:15], v[162:169], v[204:211], v[12:15]
	v_mfma_f32_16x16x128_f8f6f4 v[8:11], v[170:177], v[204:211], v[8:11]
	s_setprio 0
	s_barrier
	s_mov_b32 m0, s67
	v_lshl_add_u64 v[140:141], v[140:141], 0, s[20:21]
	global_load_lds_dwordx4 v[140:141], off
	v_lshl_add_u64 v[140:141], v[142:143], 0, s[20:21]
	s_mov_b32 m0, s68
	s_nop 0
	global_load_lds_dwordx4 v[140:141], off
	s_waitcnt vmcnt(8)
	s_waitcnt lgkmcnt(0)
	s_barrier
	s_setprio 1
	s_waitcnt lgkmcnt(0)
	v_mfma_f32_16x16x128_f8f6f4 v[52:55], v[218:225], v[178:185], v[52:55]
	v_mfma_f32_16x16x128_f8f6f4 v[48:51], v[226:233], v[178:185], v[48:51]
	v_mfma_f32_16x16x128_f8f6f4 v[36:39], v[218:225], v[186:193], v[36:39]
	v_mfma_f32_16x16x128_f8f6f4 v[32:35], v[226:233], v[186:193], v[32:35]
	v_mfma_f32_16x16x128_f8f6f4 v[20:23], v[218:225], v[196:203], v[20:23]
	v_mfma_f32_16x16x128_f8f6f4 v[16:19], v[226:233], v[196:203], v[16:19]
	v_mfma_f32_16x16x128_f8f6f4 v[4:7], v[218:225], v[204:211], v[4:7]
	v_mfma_f32_16x16x128_f8f6f4 v[0:3], v[226:233], v[204:211], v[0:3]
	s_setprio 0
	s_barrier
	s_mov_b32 m0, s71
	v_lshl_add_u64 v[140:141], s[44:45], 0, v[128:129]
	global_load_lds_dwordx4 v[140:141], off
	v_lshl_add_u64 v[140:141], s[44:45], 0, v[130:131]
	s_mov_b32 m0, s72
	s_andn2_b64 vcc, exec, s[40:41]
	global_load_lds_dwordx4 v[140:141], off
	s_mov_b64 s[42:43], -1
	s_mov_b64 s[40:41], 0
	s_mov_b64 s[44:45], 0x100
	s_cbranch_vccz .LBB0_1961
	s_branch .Lpeel_after_1961
.LBB0_1961:
	s_add_u32 s52, s12, s44
	s_addc_u32 s53, s13, s45
	s_add_u32 s29, s52, 0x100
	s_addc_u32 s48, s53, 0
	s_and_b64 s[46:47], s[42:43], exec
	s_cselect_b32 s46, s12, s29
	s_cselect_b32 s47, s13, s48
	s_add_u32 s29, s38, s44
	s_addc_u32 s44, s39, s45
	s_add_u32 s29, s29, 0x100
	s_addc_u32 s48, s44, 0
	ds_read_b128 v[162:165], v147
	ds_read_b128 v[170:173], v147 offset:2048
	ds_read_b128 v[166:169], v148
	ds_read_b128 v[174:177], v148 offset:2048
	s_and_b64 s[44:45], s[42:43], exec
	s_cselect_b32 s51, s35, s48
	s_cselect_b32 s50, s34, s29
	ds_read_b128 v[178:181], v145
	ds_read_b128 v[186:189], v145 offset:2048
	ds_read_b128 v[182:185], v146
	ds_read_b128 v[190:193], v146 offset:2048
	ds_read_b128 v[196:199], v145 offset:4096
	ds_read_b128 v[204:207], v145 offset:6144
	ds_read_b128 v[200:203], v146 offset:4096
	ds_read_b128 v[208:211], v146 offset:6144
	s_waitcnt vmcnt(6)
	s_waitcnt lgkmcnt(8)
	s_barrier
	s_waitcnt lgkmcnt(0)
	v_cndmask_b32_e64 v140, v134, v158, s[42:43]
	s_setprio 1
	s_waitcnt lgkmcnt(0)
	v_mfma_f32_16x16x128_f8f6f4 v[124:127], v[162:169], v[178:185], v[124:127]
	v_mfma_f32_16x16x128_f8f6f4 v[120:123], v[170:177], v[178:185], v[120:123]
	v_mfma_f32_16x16x128_f8f6f4 v[108:111], v[162:169], v[186:193], v[108:111]
	v_mfma_f32_16x16x128_f8f6f4 v[104:107], v[170:177], v[186:193], v[104:107]
	v_mfma_f32_16x16x128_f8f6f4 v[92:95], v[162:169], v[196:203], v[92:95]
	v_mfma_f32_16x16x128_f8f6f4 v[88:91], v[170:177], v[196:203], v[88:91]
	v_mfma_f32_16x16x128_f8f6f4 v[76:79], v[162:169], v[204:211], v[76:79]
	v_mfma_f32_16x16x128_f8f6f4 v[72:75], v[170:177], v[204:211], v[72:75]
	s_setprio 0
	s_barrier
	ds_read_b128 v[218:221], v147 offset:16384
	ds_read_b128 v[226:229], v147 offset:18432
	ds_read_b128 v[222:225], v148 offset:16384
	ds_read_b128 v[230:233], v148 offset:18432
	s_add_i32 m0, s0, 0xc000
	s_add_i32 s29, s0, 0xe000
	s_add_u32 s48, s50, 0x1000
	s_addc_u32 s49, s51, 0
	s_add_u32 s44, s50, 0x1080
	s_addc_u32 s45, s51, 0
	v_cndmask_b32_e64 v132, v135, v157, s[42:43]
	v_cndmask_b32_e64 v161, v136, v159, s[42:43]
	v_lshl_add_u64 v[252:253], s[52:53], 0, v[136:137]
	v_lshl_add_u64 v[252:253], v[252:253], 0, s[20:21]
	global_load_lds_dwordx4 v[252:253], off
	v_lshl_add_u64 v[252:253], s[52:53], 0, v[138:139]
	v_lshl_add_u64 v[252:253], v[252:253], 0, s[20:21]
	s_mov_b32 m0, s29
	s_nop 0
	global_load_lds_dwordx4 v[252:253], off
	s_barrier
	s_waitcnt lgkmcnt(0)
	s_setprio 1
	v_mfma_f32_16x16x128_f8f6f4 v[116:119], v[218:225], v[178:185], v[116:119]
	v_mfma_f32_16x16x128_f8f6f4 v[112:115], v[226:233], v[178:185], v[112:115]
	v_mfma_f32_16x16x128_f8f6f4 v[100:103], v[218:225], v[186:193], v[100:103]
	v_mfma_f32_16x16x128_f8f6f4 v[96:99], v[226:233], v[186:193], v[96:99]
	v_mfma_f32_16x16x128_f8f6f4 v[84:87], v[218:225], v[196:203], v[84:87]
	v_mfma_f32_16x16x128_f8f6f4 v[80:83], v[226:233], v[196:203], v[80:83]
	v_mfma_f32_16x16x128_f8f6f4 v[68:71], v[218:225], v[204:211], v[68:71]
	v_mfma_f32_16x16x128_f8f6f4 v[64:67], v[226:233], v[204:211], v[64:67]
	s_setprio 0
	s_barrier
	s_mov_b32 m0, s0
	ds_read_b128 v[178:181], v145 offset:16384
	ds_read_b128 v[186:189], v145 offset:18432
	ds_read_b128 v[182:185], v146 offset:16384
	ds_read_b128 v[190:193], v146 offset:18432
	ds_read_b128 v[196:199], v145 offset:20480
	ds_read_b128 v[204:207], v145 offset:22528
	ds_read_b128 v[200:203], v146 offset:20480
	ds_read_b128 v[208:211], v146 offset:22528
	global_load_lds_dwordx4 v132, s[46:47]
	s_mov_b32 m0, s56
	v_mov_b32_e32 v141, v133
	global_load_lds_dwordx4 v140, s[46:47]
	s_waitcnt lgkmcnt(8)
	s_barrier
	s_waitcnt lgkmcnt(0)
	v_lshl_add_u64 v[212:213], s[46:47], 0, v[132:133]
	v_lshl_add_u64 v[214:215], s[46:47], 0, v[140:141]
	s_setprio 1
	s_waitcnt lgkmcnt(0)
	v_mfma_f32_16x16x128_f8f6f4 v[60:63], v[162:169], v[178:185], v[60:63]
	v_mfma_f32_16x16x128_f8f6f4 v[56:59], v[170:177], v[178:185], v[56:59]
	v_mfma_f32_16x16x128_f8f6f4 v[44:47], v[162:169], v[186:193], v[44:47]
	v_mfma_f32_16x16x128_f8f6f4 v[40:43], v[170:177], v[186:193], v[40:43]
	v_mfma_f32_16x16x128_f8f6f4 v[28:31], v[162:169], v[196:203], v[28:31]
	v_mfma_f32_16x16x128_f8f6f4 v[24:27], v[170:177], v[196:203], v[24:27]
	v_mfma_f32_16x16x128_f8f6f4 v[12:15], v[162:169], v[204:211], v[12:15]
	v_mfma_f32_16x16x128_f8f6f4 v[8:11], v[170:177], v[204:211], v[8:11]
	s_setprio 0
	s_barrier
	s_mov_b32 m0, s1
	v_lshl_add_u64 v[140:141], s[50:51], 0, v[128:129]
	global_load_lds_dwordx4 v[140:141], off
	v_lshl_add_u64 v[142:143], s[50:51], 0, v[130:131]
	s_mov_b32 m0, s37
	s_nop 0
	global_load_lds_dwordx4 v[142:143], off
	s_waitcnt vmcnt(8)
	s_waitcnt lgkmcnt(0)
	s_barrier
	s_setprio 1
	s_waitcnt lgkmcnt(0)
	v_mfma_f32_16x16x128_f8f6f4 v[52:55], v[218:225], v[178:185], v[52:55]
	v_mfma_f32_16x16x128_f8f6f4 v[48:51], v[226:233], v[178:185], v[48:51]
	v_mfma_f32_16x16x128_f8f6f4 v[36:39], v[218:225], v[186:193], v[36:39]
	v_mfma_f32_16x16x128_f8f6f4 v[32:35], v[226:233], v[186:193], v[32:35]
	v_mfma_f32_16x16x128_f8f6f4 v[20:23], v[218:225], v[196:203], v[20:23]
	v_mfma_f32_16x16x128_f8f6f4 v[16:19], v[226:233], v[196:203], v[16:19]
	v_mfma_f32_16x16x128_f8f6f4 v[4:7], v[218:225], v[204:211], v[4:7]
	v_mfma_f32_16x16x128_f8f6f4 v[0:3], v[226:233], v[204:211], v[0:3]
	s_setprio 0
	s_barrier
	ds_read_b128 v[162:165], v147 offset:32768
	ds_read_b128 v[170:173], v147 offset:34816
	ds_read_b128 v[166:169], v148 offset:32768
	ds_read_b128 v[174:177], v148 offset:34816
	s_mov_b32 m0, s65
	ds_read_b128 v[178:181], v145 offset:32768
	ds_read_b128 v[186:189], v145 offset:34816
	ds_read_b128 v[182:185], v146 offset:32768
	ds_read_b128 v[190:193], v146 offset:34816
	ds_read_b128 v[196:199], v145 offset:36864
	ds_read_b128 v[204:207], v145 offset:38912
	ds_read_b128 v[200:203], v146 offset:36864
	ds_read_b128 v[208:211], v146 offset:38912
	v_cndmask_b32_e64 v132, v138, v160, s[42:43]
	global_load_lds_dwordx4 v161, s[46:47]
	s_mov_b32 m0, s66
	s_nop 0
	global_load_lds_dwordx4 v132, s[46:47]
	s_waitcnt vmcnt(8)
	s_waitcnt lgkmcnt(8)
	s_barrier
	s_waitcnt lgkmcnt(0)
	s_setprio 1
	v_mfma_f32_16x16x128_f8f6f4 v[124:127], v[162:169], v[178:185], v[124:127]
	v_mfma_f32_16x16x128_f8f6f4 v[120:123], v[170:177], v[178:185], v[120:123]
	v_mfma_f32_16x16x128_f8f6f4 v[108:111], v[162:169], v[186:193], v[108:111]
	v_mfma_f32_16x16x128_f8f6f4 v[104:107], v[170:177], v[186:193], v[104:107]
	v_mfma_f32_16x16x128_f8f6f4 v[92:95], v[162:169], v[196:203], v[92:95]
	v_mfma_f32_16x16x128_f8f6f4 v[88:91], v[170:177], v[196:203], v[88:91]
	v_mfma_f32_16x16x128_f8f6f4 v[76:79], v[162:169], v[204:211], v[76:79]
	v_mfma_f32_16x16x128_f8f6f4 v[72:75], v[170:177], v[204:211], v[72:75]
	s_setprio 0
	s_barrier
	ds_read_b128 v[218:221], v147 offset:49152
	ds_read_b128 v[226:229], v147 offset:51200
	ds_read_b128 v[222:225], v148 offset:49152
	ds_read_b128 v[230:233], v148 offset:51200
	v_lshl_add_u64 v[216:217], s[48:49], 0, v[128:129]
	s_mov_b32 m0, s57
	s_nop 0
	global_load_lds_dwordx4 v[216:217], off
	v_lshl_add_u64 v[216:217], s[48:49], 0, v[130:131]
	s_mov_b32 m0, s64
	s_nop 0
	global_load_lds_dwordx4 v[216:217], off
	s_waitcnt vmcnt(8)
	s_barrier
	s_waitcnt lgkmcnt(0)
	s_setprio 1
	v_mfma_f32_16x16x128_f8f6f4 v[116:119], v[218:225], v[178:185], v[116:119]
	v_mfma_f32_16x16x128_f8f6f4 v[112:115], v[226:233], v[178:185], v[112:115]
	v_mfma_f32_16x16x128_f8f6f4 v[100:103], v[218:225], v[186:193], v[100:103]
	v_mfma_f32_16x16x128_f8f6f4 v[96:99], v[226:233], v[186:193], v[96:99]
	v_mfma_f32_16x16x128_f8f6f4 v[84:87], v[218:225], v[196:203], v[84:87]
	v_mfma_f32_16x16x128_f8f6f4 v[80:83], v[226:233], v[196:203], v[80:83]
	v_mfma_f32_16x16x128_f8f6f4 v[68:71], v[218:225], v[204:211], v[68:71]
	v_mfma_f32_16x16x128_f8f6f4 v[64:67], v[226:233], v[204:211], v[64:67]
	s_setprio 0
	s_barrier
	s_mov_b32 m0, s69
	v_lshl_add_u64 v[212:213], v[212:213], 0, s[20:21]
	ds_read_b128 v[178:181], v145 offset:49152
	ds_read_b128 v[186:189], v145 offset:51200
	ds_read_b128 v[182:185], v146 offset:49152
	ds_read_b128 v[190:193], v146 offset:51200
	ds_read_b128 v[196:199], v145 offset:53248
	ds_read_b128 v[204:207], v145 offset:55296
	ds_read_b128 v[200:203], v146 offset:53248
	ds_read_b128 v[208:211], v146 offset:55296
	global_load_lds_dwordx4 v[212:213], off
	v_lshl_add_u64 v[212:213], v[214:215], 0, s[20:21]
	s_mov_b32 m0, s70
	s_nop 0
	global_load_lds_dwordx4 v[212:213], off
	s_waitcnt lgkmcnt(8)
	s_barrier
	s_waitcnt lgkmcnt(0)
	s_setprio 1
	v_mfma_f32_16x16x128_f8f6f4 v[60:63], v[162:169], v[178:185], v[60:63]
	v_mfma_f32_16x16x128_f8f6f4 v[56:59], v[170:177], v[178:185], v[56:59]
	v_mfma_f32_16x16x128_f8f6f4 v[44:47], v[162:169], v[186:193], v[44:47]
	v_mfma_f32_16x16x128_f8f6f4 v[40:43], v[170:177], v[186:193], v[40:43]
	v_mfma_f32_16x16x128_f8f6f4 v[28:31], v[162:169], v[196:203], v[28:31]
	v_mfma_f32_16x16x128_f8f6f4 v[24:27], v[170:177], v[196:203], v[24:27]
	v_mfma_f32_16x16x128_f8f6f4 v[12:15], v[162:169], v[204:211], v[12:15]
	v_mfma_f32_16x16x128_f8f6f4 v[8:11], v[170:177], v[204:211], v[8:11]
	s_setprio 0
	s_barrier
	s_mov_b32 m0, s67
	v_lshl_add_u64 v[140:141], v[140:141], 0, s[20:21]
	global_load_lds_dwordx4 v[140:141], off
	v_lshl_add_u64 v[140:141], v[142:143], 0, s[20:21]
	s_mov_b32 m0, s68
	s_nop 0
	global_load_lds_dwordx4 v[140:141], off
	s_waitcnt vmcnt(8)
	s_waitcnt lgkmcnt(0)
	s_barrier
	s_setprio 1
	s_waitcnt lgkmcnt(0)
	v_mfma_f32_16x16x128_f8f6f4 v[52:55], v[218:225], v[178:185], v[52:55]
	v_mfma_f32_16x16x128_f8f6f4 v[48:51], v[226:233], v[178:185], v[48:51]
	v_mfma_f32_16x16x128_f8f6f4 v[36:39], v[218:225], v[186:193], v[36:39]
	v_mfma_f32_16x16x128_f8f6f4 v[32:35], v[226:233], v[186:193], v[32:35]
	v_mfma_f32_16x16x128_f8f6f4 v[20:23], v[218:225], v[196:203], v[20:23]
	v_mfma_f32_16x16x128_f8f6f4 v[16:19], v[226:233], v[196:203], v[16:19]
	v_mfma_f32_16x16x128_f8f6f4 v[4:7], v[218:225], v[204:211], v[4:7]
	v_mfma_f32_16x16x128_f8f6f4 v[0:3], v[226:233], v[204:211], v[0:3]
	s_setprio 0
	s_barrier
	s_mov_b32 m0, s71
	v_lshl_add_u64 v[140:141], s[44:45], 0, v[128:129]
	global_load_lds_dwordx4 v[140:141], off
	v_lshl_add_u64 v[140:141], s[44:45], 0, v[130:131]
	s_mov_b32 m0, s72
	s_andn2_b64 vcc, exec, s[40:41]
	global_load_lds_dwordx4 v[140:141], off
	s_mov_b64 s[42:43], -1
	s_mov_b64 s[40:41], 0
	s_mov_b64 s[44:45], 0x100
	s_cbranch_vccz .LBB0_1961

.LBB0_1988:
	v_mov_b32_e32 v137, v133
	v_mov_b32_e32 v139, v133
	s_mov_b64 s[34:35], 0
	s_mov_b64 s[28:29], -1
	s_mov_b64 s[30:31], 0
	s_add_u32 s42, s10, s34
	s_addc_u32 s43, s11, s35
	s_add_u32 s38, s42, 0x100
	s_addc_u32 s39, s43, 0
	s_and_b64 s[36:37], s[30:31], exec
	s_cselect_b32 s36, s10, s38
	s_cselect_b32 s37, s11, s39
	s_add_u32 s34, s26, s34
	s_addc_u32 s35, s27, s35
	s_add_u32 s38, s34, 0x100
	s_addc_u32 s39, s35, 0
	ds_read_b128 v[160:163], v147
	ds_read_b128 v[168:171], v147 offset:2048
	ds_read_b128 v[164:167], v148
	ds_read_b128 v[172:175], v148 offset:2048
	s_and_b64 s[34:35], s[30:31], exec
	s_cselect_b32 s41, s25, s39
	s_cselect_b32 s40, s24, s38
	ds_read_b128 v[176:179], v145
	ds_read_b128 v[184:187], v145 offset:2048
	ds_read_b128 v[180:183], v146
	ds_read_b128 v[188:191], v146 offset:2048
	ds_read_b128 v[196:199], v145 offset:4096
	ds_read_b128 v[204:207], v145 offset:6144
	ds_read_b128 v[200:203], v146 offset:4096
	ds_read_b128 v[208:211], v146 offset:6144
	s_waitcnt vmcnt(6)
	s_waitcnt lgkmcnt(8)
	s_barrier
	s_waitcnt lgkmcnt(0)
	v_cndmask_b32_e64 v140, v134, v156, s[30:31]
	s_setprio 1
	s_waitcnt lgkmcnt(0)
	v_mfma_f32_16x16x128_f8f6f4 v[124:127], v[160:167], v[176:183], 0
	v_mfma_f32_16x16x128_f8f6f4 v[120:123], v[168:175], v[176:183], 0
	v_mfma_f32_16x16x128_f8f6f4 v[108:111], v[160:167], v[184:191], 0
	v_mfma_f32_16x16x128_f8f6f4 v[104:107], v[168:175], v[184:191], 0
	v_mfma_f32_16x16x128_f8f6f4 v[92:95], v[160:167], v[196:203], 0
	v_mfma_f32_16x16x128_f8f6f4 v[88:91], v[168:175], v[196:203], 0
	v_mfma_f32_16x16x128_f8f6f4 v[76:79], v[160:167], v[204:211], 0
	v_mfma_f32_16x16x128_f8f6f4 v[72:75], v[168:175], v[204:211], 0
	s_setprio 0
	s_barrier
	ds_read_b128 v[218:221], v147 offset:16384
	ds_read_b128 v[226:229], v147 offset:18432
	ds_read_b128 v[222:225], v148 offset:16384
	ds_read_b128 v[230:233], v148 offset:18432
	s_add_i32 m0, s0, 0xc000
	s_add_i32 s62, s0, 0xe000
	s_add_u32 s38, s40, 0x1000
	s_addc_u32 s39, s41, 0
	s_add_u32 s34, s40, 0x1080
	s_addc_u32 s35, s41, 0
	v_cndmask_b32_e64 v132, v135, v155, s[30:31]
	v_cndmask_b32_e64 v159, v136, v157, s[30:31]
	v_lshl_add_u64 v[252:253], s[42:43], 0, v[136:137]
	v_lshl_add_u64 v[252:253], v[252:253], 0, s[16:17]
	global_load_lds_dwordx4 v[252:253], off
	v_lshl_add_u64 v[252:253], s[42:43], 0, v[138:139]
	v_lshl_add_u64 v[252:253], v[252:253], 0, s[16:17]
	s_mov_b32 m0, s62
	s_nop 0
	global_load_lds_dwordx4 v[252:253], off
	s_barrier
	s_waitcnt lgkmcnt(0)
	s_setprio 1
	v_mfma_f32_16x16x128_f8f6f4 v[116:119], v[218:225], v[176:183], 0
	v_mfma_f32_16x16x128_f8f6f4 v[112:115], v[226:233], v[176:183], 0
	v_mfma_f32_16x16x128_f8f6f4 v[100:103], v[218:225], v[184:191], 0
	v_mfma_f32_16x16x128_f8f6f4 v[96:99], v[226:233], v[184:191], 0
	v_mfma_f32_16x16x128_f8f6f4 v[84:87], v[218:225], v[196:203], 0
	v_mfma_f32_16x16x128_f8f6f4 v[80:83], v[226:233], v[196:203], 0
	v_mfma_f32_16x16x128_f8f6f4 v[68:71], v[218:225], v[204:211], 0
	v_mfma_f32_16x16x128_f8f6f4 v[64:67], v[226:233], v[204:211], 0
	s_setprio 0
	s_barrier
	s_mov_b32 m0, s0
	ds_read_b128 v[176:179], v145 offset:16384
	ds_read_b128 v[184:187], v145 offset:18432
	ds_read_b128 v[180:183], v146 offset:16384
	ds_read_b128 v[188:191], v146 offset:18432
	ds_read_b128 v[196:199], v145 offset:20480
	ds_read_b128 v[204:207], v145 offset:22528
	ds_read_b128 v[200:203], v146 offset:20480
	ds_read_b128 v[208:211], v146 offset:22528
	global_load_lds_dwordx4 v132, s[36:37]
	s_mov_b32 m0, s47
	v_mov_b32_e32 v141, v133
	global_load_lds_dwordx4 v140, s[36:37]
	s_waitcnt lgkmcnt(8)
	s_barrier
	s_waitcnt lgkmcnt(0)
	v_lshl_add_u64 v[192:193], s[36:37], 0, v[132:133]
	v_lshl_add_u64 v[212:213], s[36:37], 0, v[140:141]
	s_setprio 1
	s_waitcnt lgkmcnt(0)
	v_mfma_f32_16x16x128_f8f6f4 v[60:63], v[160:167], v[176:183], 0
	v_mfma_f32_16x16x128_f8f6f4 v[56:59], v[168:175], v[176:183], 0
	v_mfma_f32_16x16x128_f8f6f4 v[44:47], v[160:167], v[184:191], 0
	v_mfma_f32_16x16x128_f8f6f4 v[40:43], v[168:175], v[184:191], 0
	v_mfma_f32_16x16x128_f8f6f4 v[28:31], v[160:167], v[196:203], 0
	v_mfma_f32_16x16x128_f8f6f4 v[24:27], v[168:175], v[196:203], 0
	v_mfma_f32_16x16x128_f8f6f4 v[12:15], v[160:167], v[204:211], 0
	v_mfma_f32_16x16x128_f8f6f4 v[8:11], v[168:175], v[204:211], 0
	s_setprio 0
	s_barrier
	s_mov_b32 m0, s1
	v_lshl_add_u64 v[140:141], s[40:41], 0, v[128:129]
	global_load_lds_dwordx4 v[140:141], off
	v_lshl_add_u64 v[142:143], s[40:41], 0, v[130:131]
	s_mov_b32 m0, s46
	s_nop 0
	global_load_lds_dwordx4 v[142:143], off
	s_waitcnt vmcnt(8)
	s_waitcnt lgkmcnt(0)
	s_barrier
	s_setprio 1
	s_waitcnt lgkmcnt(0)
	v_mfma_f32_16x16x128_f8f6f4 v[52:55], v[218:225], v[176:183], 0
	v_mfma_f32_16x16x128_f8f6f4 v[48:51], v[226:233], v[176:183], 0
	v_mfma_f32_16x16x128_f8f6f4 v[36:39], v[218:225], v[184:191], 0
	v_mfma_f32_16x16x128_f8f6f4 v[32:35], v[226:233], v[184:191], 0
	v_mfma_f32_16x16x128_f8f6f4 v[20:23], v[218:225], v[196:203], 0
	v_mfma_f32_16x16x128_f8f6f4 v[16:19], v[226:233], v[196:203], 0
	v_mfma_f32_16x16x128_f8f6f4 v[4:7], v[218:225], v[204:211], 0
	v_mfma_f32_16x16x128_f8f6f4 v[0:3], v[226:233], v[204:211], 0
	s_setprio 0
	s_barrier
	ds_read_b128 v[160:163], v147 offset:32768
	ds_read_b128 v[168:171], v147 offset:34816
	ds_read_b128 v[164:167], v148 offset:32768
	ds_read_b128 v[172:175], v148 offset:34816
	s_mov_b32 m0, s50
	ds_read_b128 v[176:179], v145 offset:32768
	ds_read_b128 v[184:187], v145 offset:34816
	ds_read_b128 v[180:183], v146 offset:32768
	ds_read_b128 v[188:191], v146 offset:34816
	ds_read_b128 v[196:199], v145 offset:36864
	ds_read_b128 v[204:207], v145 offset:38912
	ds_read_b128 v[200:203], v146 offset:36864
	ds_read_b128 v[208:211], v146 offset:38912
	v_cndmask_b32_e64 v132, v138, v158, s[30:31]
	global_load_lds_dwordx4 v159, s[36:37]
	s_mov_b32 m0, s51
	s_nop 0
	global_load_lds_dwordx4 v132, s[36:37]
	s_waitcnt vmcnt(8)
	s_waitcnt lgkmcnt(8)
	s_barrier
	s_waitcnt lgkmcnt(0)
	s_setprio 1
	v_mfma_f32_16x16x128_f8f6f4 v[124:127], v[160:167], v[176:183], v[124:127]
	v_mfma_f32_16x16x128_f8f6f4 v[120:123], v[168:175], v[176:183], v[120:123]
	v_mfma_f32_16x16x128_f8f6f4 v[108:111], v[160:167], v[184:191], v[108:111]
	v_mfma_f32_16x16x128_f8f6f4 v[104:107], v[168:175], v[184:191], v[104:107]
	v_mfma_f32_16x16x128_f8f6f4 v[92:95], v[160:167], v[196:203], v[92:95]
	v_mfma_f32_16x16x128_f8f6f4 v[88:91], v[168:175], v[196:203], v[88:91]
	v_mfma_f32_16x16x128_f8f6f4 v[76:79], v[160:167], v[204:211], v[76:79]
	v_mfma_f32_16x16x128_f8f6f4 v[72:75], v[168:175], v[204:211], v[72:75]
	s_setprio 0
	s_barrier
	ds_read_b128 v[218:221], v147 offset:49152
	ds_read_b128 v[226:229], v147 offset:51200
	ds_read_b128 v[222:225], v148 offset:49152
	ds_read_b128 v[230:233], v148 offset:51200
	v_lshl_add_u64 v[214:215], s[38:39], 0, v[128:129]
	s_mov_b32 m0, s48
	s_nop 0
	global_load_lds_dwordx4 v[214:215], off
	v_lshl_add_u64 v[214:215], s[38:39], 0, v[130:131]
	s_mov_b32 m0, s49
	s_nop 0
	global_load_lds_dwordx4 v[214:215], off
	s_waitcnt vmcnt(8)
	s_barrier
	s_waitcnt lgkmcnt(0)
	s_setprio 1
	v_mfma_f32_16x16x128_f8f6f4 v[116:119], v[218:225], v[176:183], v[116:119]
	v_mfma_f32_16x16x128_f8f6f4 v[112:115], v[226:233], v[176:183], v[112:115]
	v_mfma_f32_16x16x128_f8f6f4 v[100:103], v[218:225], v[184:191], v[100:103]
	v_mfma_f32_16x16x128_f8f6f4 v[96:99], v[226:233], v[184:191], v[96:99]
	v_mfma_f32_16x16x128_f8f6f4 v[84:87], v[218:225], v[196:203], v[84:87]
	v_mfma_f32_16x16x128_f8f6f4 v[80:83], v[226:233], v[196:203], v[80:83]
	v_mfma_f32_16x16x128_f8f6f4 v[68:71], v[218:225], v[204:211], v[68:71]
	v_mfma_f32_16x16x128_f8f6f4 v[64:67], v[226:233], v[204:211], v[64:67]
	s_setprio 0
	s_barrier
	s_mov_b32 m0, s55
	v_lshl_add_u64 v[192:193], v[192:193], 0, s[16:17]
	ds_read_b128 v[176:179], v145 offset:49152
	ds_read_b128 v[184:187], v145 offset:51200
	ds_read_b128 v[180:183], v146 offset:49152
	ds_read_b128 v[188:191], v146 offset:51200
	ds_read_b128 v[196:199], v145 offset:53248
	ds_read_b128 v[204:207], v145 offset:55296
	ds_read_b128 v[200:203], v146 offset:53248
	ds_read_b128 v[208:211], v146 offset:55296
	global_load_lds_dwordx4 v[192:193], off
	v_lshl_add_u64 v[192:193], v[212:213], 0, s[16:17]
	s_mov_b32 m0, s56
	s_nop 0
	global_load_lds_dwordx4 v[192:193], off
	s_waitcnt lgkmcnt(8)
	s_barrier
	s_waitcnt lgkmcnt(0)
	s_setprio 1
	v_mfma_f32_16x16x128_f8f6f4 v[60:63], v[160:167], v[176:183], v[60:63]
	v_mfma_f32_16x16x128_f8f6f4 v[56:59], v[168:175], v[176:183], v[56:59]
	v_mfma_f32_16x16x128_f8f6f4 v[44:47], v[160:167], v[184:191], v[44:47]
	v_mfma_f32_16x16x128_f8f6f4 v[40:43], v[168:175], v[184:191], v[40:43]
	v_mfma_f32_16x16x128_f8f6f4 v[28:31], v[160:167], v[196:203], v[28:31]
	v_mfma_f32_16x16x128_f8f6f4 v[24:27], v[168:175], v[196:203], v[24:27]
	v_mfma_f32_16x16x128_f8f6f4 v[12:15], v[160:167], v[204:211], v[12:15]
	v_mfma_f32_16x16x128_f8f6f4 v[8:11], v[168:175], v[204:211], v[8:11]
	s_setprio 0
	s_barrier
	s_mov_b32 m0, s53
	v_lshl_add_u64 v[140:141], v[140:141], 0, s[16:17]
	global_load_lds_dwordx4 v[140:141], off
	v_lshl_add_u64 v[140:141], v[142:143], 0, s[16:17]
	s_mov_b32 m0, s54
	s_nop 0
	global_load_lds_dwordx4 v[140:141], off
	s_waitcnt vmcnt(8)
	s_waitcnt lgkmcnt(0)
	s_barrier
	s_setprio 1
	s_waitcnt lgkmcnt(0)
	v_mfma_f32_16x16x128_f8f6f4 v[52:55], v[218:225], v[176:183], v[52:55]
	v_mfma_f32_16x16x128_f8f6f4 v[48:51], v[226:233], v[176:183], v[48:51]
	v_mfma_f32_16x16x128_f8f6f4 v[36:39], v[218:225], v[184:191], v[36:39]
	v_mfma_f32_16x16x128_f8f6f4 v[32:35], v[226:233], v[184:191], v[32:35]
	v_mfma_f32_16x16x128_f8f6f4 v[20:23], v[218:225], v[196:203], v[20:23]
	v_mfma_f32_16x16x128_f8f6f4 v[16:19], v[226:233], v[196:203], v[16:19]
	v_mfma_f32_16x16x128_f8f6f4 v[4:7], v[218:225], v[204:211], v[4:7]
	v_mfma_f32_16x16x128_f8f6f4 v[0:3], v[226:233], v[204:211], v[0:3]
	s_setprio 0
	s_barrier
	s_mov_b32 m0, s57
	v_lshl_add_u64 v[140:141], s[34:35], 0, v[128:129]
	global_load_lds_dwordx4 v[140:141], off
	v_lshl_add_u64 v[140:141], s[34:35], 0, v[130:131]
	s_mov_b32 m0, s58
	s_andn2_b64 vcc, exec, s[28:29]
	global_load_lds_dwordx4 v[140:141], off
	s_mov_b64 s[30:31], -1
	s_mov_b64 s[28:29], 0
	s_mov_b64 s[34:35], 0x100
	s_cbranch_vccz .LBB0_1989
	s_branch .Lpeel_after_1989
.LBB0_1989:
	s_add_u32 s42, s10, s34
	s_addc_u32 s43, s11, s35
	s_add_u32 s38, s42, 0x100
	s_addc_u32 s39, s43, 0
	s_and_b64 s[36:37], s[30:31], exec
	s_cselect_b32 s36, s10, s38
	s_cselect_b32 s37, s11, s39
	s_add_u32 s34, s26, s34
	s_addc_u32 s35, s27, s35
	s_add_u32 s38, s34, 0x100
	s_addc_u32 s39, s35, 0
	ds_read_b128 v[160:163], v147
	ds_read_b128 v[168:171], v147 offset:2048
	ds_read_b128 v[164:167], v148
	ds_read_b128 v[172:175], v148 offset:2048
	s_and_b64 s[34:35], s[30:31], exec
	s_cselect_b32 s41, s25, s39
	s_cselect_b32 s40, s24, s38
	ds_read_b128 v[176:179], v145
	ds_read_b128 v[184:187], v145 offset:2048
	ds_read_b128 v[180:183], v146
	ds_read_b128 v[188:191], v146 offset:2048
	ds_read_b128 v[196:199], v145 offset:4096
	ds_read_b128 v[204:207], v145 offset:6144
	ds_read_b128 v[200:203], v146 offset:4096
	ds_read_b128 v[208:211], v146 offset:6144
	s_waitcnt vmcnt(6)
	s_waitcnt lgkmcnt(8)
	s_barrier
	s_waitcnt lgkmcnt(0)
	v_cndmask_b32_e64 v140, v134, v156, s[30:31]
	s_setprio 1
	s_waitcnt lgkmcnt(0)
	v_mfma_f32_16x16x128_f8f6f4 v[124:127], v[160:167], v[176:183], v[124:127]
	v_mfma_f32_16x16x128_f8f6f4 v[120:123], v[168:175], v[176:183], v[120:123]
	v_mfma_f32_16x16x128_f8f6f4 v[108:111], v[160:167], v[184:191], v[108:111]
	v_mfma_f32_16x16x128_f8f6f4 v[104:107], v[168:175], v[184:191], v[104:107]
	v_mfma_f32_16x16x128_f8f6f4 v[92:95], v[160:167], v[196:203], v[92:95]
	v_mfma_f32_16x16x128_f8f6f4 v[88:91], v[168:175], v[196:203], v[88:91]
	v_mfma_f32_16x16x128_f8f6f4 v[76:79], v[160:167], v[204:211], v[76:79]
	v_mfma_f32_16x16x128_f8f6f4 v[72:75], v[168:175], v[204:211], v[72:75]
	s_setprio 0
	s_barrier
	ds_read_b128 v[218:221], v147 offset:16384
	ds_read_b128 v[226:229], v147 offset:18432
	ds_read_b128 v[222:225], v148 offset:16384
	ds_read_b128 v[230:233], v148 offset:18432
	s_add_i32 m0, s0, 0xc000
	s_add_i32 s62, s0, 0xe000
	s_add_u32 s38, s40, 0x1000
	s_addc_u32 s39, s41, 0
	s_add_u32 s34, s40, 0x1080
	s_addc_u32 s35, s41, 0
	v_cndmask_b32_e64 v132, v135, v155, s[30:31]
	v_cndmask_b32_e64 v159, v136, v157, s[30:31]
	v_lshl_add_u64 v[252:253], s[42:43], 0, v[136:137]
	v_lshl_add_u64 v[252:253], v[252:253], 0, s[16:17]
	global_load_lds_dwordx4 v[252:253], off
	v_lshl_add_u64 v[252:253], s[42:43], 0, v[138:139]
	v_lshl_add_u64 v[252:253], v[252:253], 0, s[16:17]
	s_mov_b32 m0, s62
	s_nop 0
	global_load_lds_dwordx4 v[252:253], off
	s_barrier
	s_waitcnt lgkmcnt(0)
	s_setprio 1
	v_mfma_f32_16x16x128_f8f6f4 v[116:119], v[218:225], v[176:183], v[116:119]
	v_mfma_f32_16x16x128_f8f6f4 v[112:115], v[226:233], v[176:183], v[112:115]
	v_mfma_f32_16x16x128_f8f6f4 v[100:103], v[218:225], v[184:191], v[100:103]
	v_mfma_f32_16x16x128_f8f6f4 v[96:99], v[226:233], v[184:191], v[96:99]
	v_mfma_f32_16x16x128_f8f6f4 v[84:87], v[218:225], v[196:203], v[84:87]
	v_mfma_f32_16x16x128_f8f6f4 v[80:83], v[226:233], v[196:203], v[80:83]
	v_mfma_f32_16x16x128_f8f6f4 v[68:71], v[218:225], v[204:211], v[68:71]
	v_mfma_f32_16x16x128_f8f6f4 v[64:67], v[226:233], v[204:211], v[64:67]
	s_setprio 0
	s_barrier
	s_mov_b32 m0, s0
	ds_read_b128 v[176:179], v145 offset:16384
	ds_read_b128 v[184:187], v145 offset:18432
	ds_read_b128 v[180:183], v146 offset:16384
	ds_read_b128 v[188:191], v146 offset:18432
	ds_read_b128 v[196:199], v145 offset:20480
	ds_read_b128 v[204:207], v145 offset:22528
	ds_read_b128 v[200:203], v146 offset:20480
	ds_read_b128 v[208:211], v146 offset:22528
	global_load_lds_dwordx4 v132, s[36:37]
	s_mov_b32 m0, s47
	v_mov_b32_e32 v141, v133
	global_load_lds_dwordx4 v140, s[36:37]
	s_waitcnt lgkmcnt(8)
	s_barrier
	s_waitcnt lgkmcnt(0)
	v_lshl_add_u64 v[192:193], s[36:37], 0, v[132:133]
	v_lshl_add_u64 v[212:213], s[36:37], 0, v[140:141]
	s_setprio 1
	s_waitcnt lgkmcnt(0)
	v_mfma_f32_16x16x128_f8f6f4 v[60:63], v[160:167], v[176:183], v[60:63]
	v_mfma_f32_16x16x128_f8f6f4 v[56:59], v[168:175], v[176:183], v[56:59]
	v_mfma_f32_16x16x128_f8f6f4 v[44:47], v[160:167], v[184:191], v[44:47]
	v_mfma_f32_16x16x128_f8f6f4 v[40:43], v[168:175], v[184:191], v[40:43]
	v_mfma_f32_16x16x128_f8f6f4 v[28:31], v[160:167], v[196:203], v[28:31]
	v_mfma_f32_16x16x128_f8f6f4 v[24:27], v[168:175], v[196:203], v[24:27]
	v_mfma_f32_16x16x128_f8f6f4 v[12:15], v[160:167], v[204:211], v[12:15]
	v_mfma_f32_16x16x128_f8f6f4 v[8:11], v[168:175], v[204:211], v[8:11]
	s_setprio 0
	s_barrier
	s_mov_b32 m0, s1
	v_lshl_add_u64 v[140:141], s[40:41], 0, v[128:129]
	global_load_lds_dwordx4 v[140:141], off
	v_lshl_add_u64 v[142:143], s[40:41], 0, v[130:131]
	s_mov_b32 m0, s46
	s_nop 0
	global_load_lds_dwordx4 v[142:143], off
	s_waitcnt vmcnt(8)
	s_waitcnt lgkmcnt(0)
	s_barrier
	s_setprio 1
	s_waitcnt lgkmcnt(0)
	v_mfma_f32_16x16x128_f8f6f4 v[52:55], v[218:225], v[176:183], v[52:55]
	v_mfma_f32_16x16x128_f8f6f4 v[48:51], v[226:233], v[176:183], v[48:51]
	v_mfma_f32_16x16x128_f8f6f4 v[36:39], v[218:225], v[184:191], v[36:39]
	v_mfma_f32_16x16x128_f8f6f4 v[32:35], v[226:233], v[184:191], v[32:35]
	v_mfma_f32_16x16x128_f8f6f4 v[20:23], v[218:225], v[196:203], v[20:23]
	v_mfma_f32_16x16x128_f8f6f4 v[16:19], v[226:233], v[196:203], v[16:19]
	v_mfma_f32_16x16x128_f8f6f4 v[4:7], v[218:225], v[204:211], v[4:7]
	v_mfma_f32_16x16x128_f8f6f4 v[0:3], v[226:233], v[204:211], v[0:3]
	s_setprio 0
	s_barrier
	ds_read_b128 v[160:163], v147 offset:32768
	ds_read_b128 v[168:171], v147 offset:34816
	ds_read_b128 v[164:167], v148 offset:32768
	ds_read_b128 v[172:175], v148 offset:34816
	s_mov_b32 m0, s50
	ds_read_b128 v[176:179], v145 offset:32768
	ds_read_b128 v[184:187], v145 offset:34816
	ds_read_b128 v[180:183], v146 offset:32768
	ds_read_b128 v[188:191], v146 offset:34816
	ds_read_b128 v[196:199], v145 offset:36864
	ds_read_b128 v[204:207], v145 offset:38912
	ds_read_b128 v[200:203], v146 offset:36864
	ds_read_b128 v[208:211], v146 offset:38912
	v_cndmask_b32_e64 v132, v138, v158, s[30:31]
	global_load_lds_dwordx4 v159, s[36:37]
	s_mov_b32 m0, s51
	s_nop 0
	global_load_lds_dwordx4 v132, s[36:37]
	s_waitcnt vmcnt(8)
	s_waitcnt lgkmcnt(8)
	s_barrier
	s_waitcnt lgkmcnt(0)
	s_setprio 1
	v_mfma_f32_16x16x128_f8f6f4 v[124:127], v[160:167], v[176:183], v[124:127]
	v_mfma_f32_16x16x128_f8f6f4 v[120:123], v[168:175], v[176:183], v[120:123]
	v_mfma_f32_16x16x128_f8f6f4 v[108:111], v[160:167], v[184:191], v[108:111]
	v_mfma_f32_16x16x128_f8f6f4 v[104:107], v[168:175], v[184:191], v[104:107]
	v_mfma_f32_16x16x128_f8f6f4 v[92:95], v[160:167], v[196:203], v[92:95]
	v_mfma_f32_16x16x128_f8f6f4 v[88:91], v[168:175], v[196:203], v[88:91]
	v_mfma_f32_16x16x128_f8f6f4 v[76:79], v[160:167], v[204:211], v[76:79]
	v_mfma_f32_16x16x128_f8f6f4 v[72:75], v[168:175], v[204:211], v[72:75]
	s_setprio 0
	s_barrier
	ds_read_b128 v[218:221], v147 offset:49152
	ds_read_b128 v[226:229], v147 offset:51200
	ds_read_b128 v[222:225], v148 offset:49152
	ds_read_b128 v[230:233], v148 offset:51200
	v_lshl_add_u64 v[214:215], s[38:39], 0, v[128:129]
	s_mov_b32 m0, s48
	s_nop 0
	global_load_lds_dwordx4 v[214:215], off
	v_lshl_add_u64 v[214:215], s[38:39], 0, v[130:131]
	s_mov_b32 m0, s49
	s_nop 0
	global_load_lds_dwordx4 v[214:215], off
	s_waitcnt vmcnt(8)
	s_barrier
	s_waitcnt lgkmcnt(0)
	s_setprio 1
	v_mfma_f32_16x16x128_f8f6f4 v[116:119], v[218:225], v[176:183], v[116:119]
	v_mfma_f32_16x16x128_f8f6f4 v[112:115], v[226:233], v[176:183], v[112:115]
	v_mfma_f32_16x16x128_f8f6f4 v[100:103], v[218:225], v[184:191], v[100:103]
	v_mfma_f32_16x16x128_f8f6f4 v[96:99], v[226:233], v[184:191], v[96:99]
	v_mfma_f32_16x16x128_f8f6f4 v[84:87], v[218:225], v[196:203], v[84:87]
	v_mfma_f32_16x16x128_f8f6f4 v[80:83], v[226:233], v[196:203], v[80:83]
	v_mfma_f32_16x16x128_f8f6f4 v[68:71], v[218:225], v[204:211], v[68:71]
	v_mfma_f32_16x16x128_f8f6f4 v[64:67], v[226:233], v[204:211], v[64:67]
	s_setprio 0
	s_barrier
	s_mov_b32 m0, s55
	v_lshl_add_u64 v[192:193], v[192:193], 0, s[16:17]
	ds_read_b128 v[176:179], v145 offset:49152
	ds_read_b128 v[184:187], v145 offset:51200
	ds_read_b128 v[180:183], v146 offset:49152
	ds_read_b128 v[188:191], v146 offset:51200
	ds_read_b128 v[196:199], v145 offset:53248
	ds_read_b128 v[204:207], v145 offset:55296
	ds_read_b128 v[200:203], v146 offset:53248
	ds_read_b128 v[208:211], v146 offset:55296
	global_load_lds_dwordx4 v[192:193], off
	v_lshl_add_u64 v[192:193], v[212:213], 0, s[16:17]
	s_mov_b32 m0, s56
	s_nop 0
	global_load_lds_dwordx4 v[192:193], off
	s_waitcnt lgkmcnt(8)
	s_barrier
	s_waitcnt lgkmcnt(0)
	s_setprio 1
	v_mfma_f32_16x16x128_f8f6f4 v[60:63], v[160:167], v[176:183], v[60:63]
	v_mfma_f32_16x16x128_f8f6f4 v[56:59], v[168:175], v[176:183], v[56:59]
	v_mfma_f32_16x16x128_f8f6f4 v[44:47], v[160:167], v[184:191], v[44:47]
	v_mfma_f32_16x16x128_f8f6f4 v[40:43], v[168:175], v[184:191], v[40:43]
	v_mfma_f32_16x16x128_f8f6f4 v[28:31], v[160:167], v[196:203], v[28:31]
	v_mfma_f32_16x16x128_f8f6f4 v[24:27], v[168:175], v[196:203], v[24:27]
	v_mfma_f32_16x16x128_f8f6f4 v[12:15], v[160:167], v[204:211], v[12:15]
	v_mfma_f32_16x16x128_f8f6f4 v[8:11], v[168:175], v[204:211], v[8:11]
	s_setprio 0
	s_barrier
	s_mov_b32 m0, s53
	v_lshl_add_u64 v[140:141], v[140:141], 0, s[16:17]
	global_load_lds_dwordx4 v[140:141], off
	v_lshl_add_u64 v[140:141], v[142:143], 0, s[16:17]
	s_mov_b32 m0, s54
	s_nop 0
	global_load_lds_dwordx4 v[140:141], off
	s_waitcnt vmcnt(8)
	s_waitcnt lgkmcnt(0)
	s_barrier
	s_setprio 1
	s_waitcnt lgkmcnt(0)
	v_mfma_f32_16x16x128_f8f6f4 v[52:55], v[218:225], v[176:183], v[52:55]
	v_mfma_f32_16x16x128_f8f6f4 v[48:51], v[226:233], v[176:183], v[48:51]
	v_mfma_f32_16x16x128_f8f6f4 v[36:39], v[218:225], v[184:191], v[36:39]
	v_mfma_f32_16x16x128_f8f6f4 v[32:35], v[226:233], v[184:191], v[32:35]
	v_mfma_f32_16x16x128_f8f6f4 v[20:23], v[218:225], v[196:203], v[20:23]
	v_mfma_f32_16x16x128_f8f6f4 v[16:19], v[226:233], v[196:203], v[16:19]
	v_mfma_f32_16x16x128_f8f6f4 v[4:7], v[218:225], v[204:211], v[4:7]
	v_mfma_f32_16x16x128_f8f6f4 v[0:3], v[226:233], v[204:211], v[0:3]
	s_setprio 0
	s_barrier
	s_mov_b32 m0, s57
	v_lshl_add_u64 v[140:141], s[34:35], 0, v[128:129]
	global_load_lds_dwordx4 v[140:141], off
	v_lshl_add_u64 v[140:141], s[34:35], 0, v[130:131]
	s_mov_b32 m0, s58
	s_andn2_b64 vcc, exec, s[28:29]
	global_load_lds_dwordx4 v[140:141], off
	s_mov_b64 s[30:31], -1
	s_mov_b64 s[28:29], 0
	s_mov_b64 s[34:35], 0x100
	s_cbranch_vccz .LBB0_1989

.LBB0_2058:
	s_or_b64 exec, exec, s[4:5]
	s_add_i32 s4, 0, 0x22140
	v_mov_b32_e32 v2, s4
	s_waitcnt lgkmcnt(0)
	s_barrier
	ds_read_b32 v2, v2
	s_waitcnt lgkmcnt(0)
	v_cmp_lt_i32_e32 vcc, v1, v2
	s_and_saveexec_b64 s[4:5], vcc
	s_cbranch_execz .LBB0_2063
	s_mov_b64 s[8:9], 0
